# speedup vs baseline: 1.1037x; 1.1037x over previous
.LBB2_16:
	s_or_b64 exec, exec, s[0:1]
	s_waitcnt lgkmcnt(0)
	s_barrier
	ds_read2_b32 v[2:3], v9 offset1:2
	ds_read2_b32 v[4:5], v11 offset1:2
	v_mov_b32_e32 v27, 0
	s_waitcnt lgkmcnt(0)
	v_mfma_f32_32x32x2_f32 a[0:15], v2, v4, a[0:15]
	s_movk_i32 s0, 0x2000
	s_movk_i32 s1, 0x3000
	v_lshlrev_b32_e32 v34, 3, v0
	v_mfma_f32_32x32x2_f32 a[0:15], v3, v5, a[0:15]
	ds_read2_b32 v[2:3], v9 offset0:4 offset1:6
	ds_read2_b32 v[4:5], v11 offset0:4 offset1:6
	ds_read2_b32 v[6:7], v9 offset0:8 offset1:10
	ds_read2_b32 v[24:25], v11 offset0:8 offset1:10
	s_waitcnt lgkmcnt(2)
	v_mfma_f32_32x32x2_f32 a[0:15], v2, v4, a[0:15]
	v_lshl_add_u32 v2, v12, 3, s11
	v_and_or_b32 v2, v10, 4, v2
	v_lshlrev_b32_e32 v26, 2, v2
	v_lshl_add_u64 v[20:21], s[2:3], 0, v[26:27]
	v_add_co_u32_e32 v22, vcc, s0, v20
	s_mov_b32 s0, 0xbfb8aa3b
	s_nop 0
	v_addc_co_u32_e32 v23, vcc, 0, v21, vcc
	v_add_co_u32_e32 v20, vcc, s1, v20
	s_lshl_b32 s1, s10, 12
	s_nop 0
	v_addc_co_u32_e32 v21, vcc, 0, v21, vcc
	v_mfma_f32_32x32x2_f32 a[0:15], v3, v5, a[0:15]
	global_load_dwordx4 v[2:5], v26, s[2:3]
	global_load_dwordx4 v[12:15], v[22:23], off offset:-4096
	global_load_dwordx4 v[16:19], v[22:23], off
	ds_read2_b32 v[8:9], v9 offset0:12 offset1:14
	global_load_dwordx4 v[20:23], v[20:21], off
	s_lshl_b32 s3, s9, 2
	s_lshl_b32 s2, s8, 7
	s_add_i32 s1, s3, s1
	s_add_i32 s1, s1, s2
	v_add_u32_e32 v10, s1, v1
	v_or_b32_e32 v26, 1, v10
	v_lshlrev_b64 v[28:29], 9, v[26:27]
	v_or_b32_e32 v26, 2, v10
	s_mov_b32 s2, 0xc038aa3b
	v_lshlrev_b64 v[30:31], 9, v[26:27]
	v_or_b32_e32 v28, v28, v34
	s_waitcnt lgkmcnt(1)
	v_mfma_f32_32x32x2_f32 a[0:15], v6, v24, a[0:15]
	v_or_b32_e32 v30, v30, v34
	v_or_b32_e32 v26, 3, v10
	v_lshl_add_u64 v[32:33], s[4:5], 0, v[30:31]
	v_lshl_add_u64 v[30:31], s[6:7], 0, v[30:31]
	v_mfma_f32_32x32x2_f32 a[0:15], v7, v25, a[0:15]
	ds_read2_b32 v[6:7], v11 offset0:12 offset1:14
	v_mov_b32_e32 v11, v27
	v_lshlrev_b64 v[0:1], 9, v[10:11]
	v_or_b32_e32 v0, v0, v34
	v_lshl_add_u64 v[24:25], s[4:5], 0, v[0:1]
	v_lshl_add_u64 v[10:11], s[4:5], 0, v[28:29]
	v_lshlrev_b64 v[26:27], 9, v[26:27]
	v_or_b32_e32 v26, v26, v34
	v_lshl_add_u64 v[0:1], s[6:7], 0, v[0:1]
	v_lshl_add_u64 v[34:35], s[4:5], 0, v[26:27]
	v_lshl_add_u64 v[28:29], s[6:7], 0, v[28:29]
	v_lshl_add_u64 v[26:27], s[6:7], 0, v[26:27]
	s_waitcnt lgkmcnt(0)
	v_mfma_f32_32x32x2_f32 a[0:15], v8, v6, a[0:15]
	v_mfma_f32_32x32x2_f32 a[0:15], v9, v7, a[0:15]
	s_nop 15
	s_nop 1
	v_accvgpr_read_b32 v47, a1
	v_accvgpr_read_b32 v45, a3
	v_accvgpr_read_b32 v44, a2
	v_accvgpr_read_b32 v46, a0
	v_accvgpr_read_b32 v7, a15
	v_accvgpr_read_b32 v6, a14
	v_accvgpr_read_b32 v9, a13
	v_accvgpr_read_b32 v8, a12
	v_accvgpr_read_b32 v37, a11
	v_accvgpr_read_b32 v36, a10
	v_accvgpr_read_b32 v39, a9
	v_accvgpr_read_b32 v38, a8
	v_accvgpr_read_b32 v41, a7
	v_accvgpr_read_b32 v40, a6
	v_accvgpr_read_b32 v43, a5
	v_accvgpr_read_b32 v42, a4
	s_waitcnt vmcnt(3)
	v_pk_add_f32 v[2:3], v[46:47], v[2:3]
	v_pk_add_f32 v[4:5], v[44:45], v[4:5]
	s_waitcnt vmcnt(2)
	v_pk_add_f32 v[12:13], v[42:43], v[12:13]
	v_pk_add_f32 v[14:15], v[40:41], v[14:15]
	s_waitcnt vmcnt(1)
	v_pk_add_f32 v[16:17], v[38:39], v[16:17]
	v_pk_add_f32 v[18:19], v[36:37], v[18:19]
	s_waitcnt vmcnt(0)
	v_pk_add_f32 v[8:9], v[8:9], v[20:21]
	v_pk_add_f32 v[6:7], v[6:7], v[22:23]
	v_pk_mul_f32 v[20:21], v[2:3], s[0:1] op_sel_hi:[1,0]
	v_pk_mul_f32 v[22:23], v[4:5], s[0:1] op_sel_hi:[1,0]
	v_pk_mul_f32 v[36:37], v[12:13], s[0:1] op_sel_hi:[1,0]
	v_pk_mul_f32 v[38:39], v[14:15], s[0:1] op_sel_hi:[1,0]
	v_pk_mul_f32 v[40:41], v[16:17], s[2:3] op_sel_hi:[1,0]
	v_pk_mul_f32 v[42:43], v[18:19], s[2:3] op_sel_hi:[1,0]
	v_pk_mul_f32 v[44:45], v[8:9], s[0:1] op_sel_hi:[1,0]
	v_pk_mul_f32 v[46:47], v[6:7], s[0:1] op_sel_hi:[1,0]
	v_mov_b32_e32 v2, s6
	v_mov_b32_e32 v3, s7
	v_sub_co_u32_e32 v0, vcc, v0, v2
	s_nop 1
	v_subb_co_u32_e32 v1, vcc, v1, v3, vcc
	s_nop 1
	v_add_co_u32_e32 v24, vcc, v24, v0
	s_nop 1
	v_addc_co_u32_e32 v25, vcc, v25, v1, vcc
	global_store_dwordx4 v[24:25], v[20:23], off
	v_sub_co_u32_e32 v28, vcc, v28, v2
	s_nop 1
	v_subb_co_u32_e32 v29, vcc, v29, v3, vcc
	s_nop 1
	v_add_co_u32_e32 v10, vcc, v10, v28
	s_nop 1
	v_addc_co_u32_e32 v11, vcc, v11, v29, vcc
	global_store_dwordx4 v[10:11], v[36:39], off
	v_sub_co_u32_e32 v30, vcc, v30, v2
	s_nop 1
	v_subb_co_u32_e32 v31, vcc, v31, v3, vcc
	s_nop 1
	v_add_co_u32_e32 v32, vcc, v32, v30
	s_nop 1
	v_addc_co_u32_e32 v33, vcc, v33, v31, vcc
	global_store_dwordx4 v[32:33], v[40:43], off
	v_sub_co_u32_e32 v26, vcc, v26, v2
	s_nop 1
	v_subb_co_u32_e32 v27, vcc, v27, v3, vcc
	s_nop 1
	v_add_co_u32_e32 v34, vcc, v34, v26
	s_nop 1
	v_addc_co_u32_e32 v35, vcc, v35, v27, vcc
	global_store_dwordx4 v[34:35], v[44:47], off
	s_endpgm

.LE_join7:
	s_waitcnt vmcnt(1)
	s_waitcnt vmcnt(0)
	s_barrier
	v_mov_b32_e32 v199, 1
	s_cmp_eq_u32 s31, 0
	s_cbranch_scc1 .LE_slow8
	global_store_dword v197, v199, s[40:41]
	s_branch .LE_join9

.LE_join9:
	s_mov_b32 s33, 1
	s_lshl_b32 s64, s33, 11
	s_lshl_b32 s65, s29, 8
	s_add_u32 s64, s64, s65
	s_lshl_b32 s64, s64, 3
	s_add_u32 s42, s12, s64
	s_addc_u32 s43, s13, 0
	global_load_dwordx2 v[228:229], v249, s[42:43] offset:0
	global_load_dwordx2 v[230:231], v249, s[42:43] offset:256
	global_load_dwordx2 v[232:233], v249, s[42:43] offset:512
	global_load_dwordx2 v[234:235], v249, s[42:43] offset:768
	ds_read_b128 v[236:239], v248 offset:0
	ds_read_b128 v[240:243], v248 offset:16
	ds_read_b128 v[244:247], v248 offset:32
	ds_read_b128 v[200:203], v248 offset:48
	ds_read_b128 v[204:207], v248 offset:64
	ds_read_b128 v[208:211], v248 offset:80
	s_waitcnt lgkmcnt(3)
	s_waitcnt vmcnt(0)
	v_fma_f32 v0, v229, v237, v244
	v_fma_f32 v1, v229, v239, v245
	v_fma_f32 v2, v229, v241, v246
	v_fma_f32 v3, v229, v243, v247
	v_fmac_f32_e32 v0, v228, v236
	v_fmac_f32_e32 v1, v228, v238
	v_fmac_f32_e32 v2, v228, v240
	v_fmac_f32_e32 v3, v228, v242
	v_fma_f32 v16, v231, v237, v244
	v_fma_f32 v17, v231, v239, v245
	v_fma_f32 v18, v231, v241, v246
	v_fma_f32 v19, v231, v243, v247
	v_fmac_f32_e32 v16, v230, v236
	v_fmac_f32_e32 v17, v230, v238
	v_fmac_f32_e32 v18, v230, v240
	v_fmac_f32_e32 v19, v230, v242
	v_fma_f32 v32, v233, v237, v244
	v_fma_f32 v33, v233, v239, v245
	v_fma_f32 v34, v233, v241, v246
	v_fma_f32 v35, v233, v243, v247
	v_fmac_f32_e32 v32, v232, v236
	v_fmac_f32_e32 v33, v232, v238
	v_fmac_f32_e32 v34, v232, v240
	v_fmac_f32_e32 v35, v232, v242
	v_fma_f32 v48, v235, v237, v244
	v_fma_f32 v49, v235, v239, v245
	v_fma_f32 v50, v235, v241, v246
	v_fma_f32 v51, v235, v243, v247
	v_fmac_f32_e32 v48, v234, v236
	v_fmac_f32_e32 v49, v234, v238
	v_fmac_f32_e32 v50, v234, v240
	v_fmac_f32_e32 v51, v234, v242
	ds_read_b128 v[236:239], v248 offset:96
	ds_read_b128 v[240:243], v248 offset:112
	ds_read_b128 v[244:247], v248 offset:128
	s_waitcnt lgkmcnt(3)
	v_fma_f32 v4, v229, v201, v208
	v_fma_f32 v5, v229, v203, v209
	v_fma_f32 v6, v229, v205, v210
	v_fma_f32 v7, v229, v207, v211
	v_fmac_f32_e32 v4, v228, v200
	v_fmac_f32_e32 v5, v228, v202
	v_fmac_f32_e32 v6, v228, v204
	v_fmac_f32_e32 v7, v228, v206
	v_fma_f32 v20, v231, v201, v208
	v_fma_f32 v21, v231, v203, v209
	v_fma_f32 v22, v231, v205, v210
	v_fma_f32 v23, v231, v207, v211
	v_fmac_f32_e32 v20, v230, v200
	v_fmac_f32_e32 v21, v230, v202
	v_fmac_f32_e32 v22, v230, v204
	v_fmac_f32_e32 v23, v230, v206
	v_fma_f32 v36, v233, v201, v208
	v_fma_f32 v37, v233, v203, v209
	v_fma_f32 v38, v233, v205, v210
	v_fma_f32 v39, v233, v207, v211
	v_fmac_f32_e32 v36, v232, v200
	v_fmac_f32_e32 v37, v232, v202
	v_fmac_f32_e32 v38, v232, v204
	v_fmac_f32_e32 v39, v232, v206
	v_fma_f32 v52, v235, v201, v208
	v_fma_f32 v53, v235, v203, v209
	v_fma_f32 v54, v235, v205, v210
	v_fma_f32 v55, v235, v207, v211
	v_fmac_f32_e32 v52, v234, v200
	v_fmac_f32_e32 v53, v234, v202
	v_fmac_f32_e32 v54, v234, v204
	v_fmac_f32_e32 v55, v234, v206
	ds_read_b128 v[200:203], v248 offset:144
	ds_read_b128 v[204:207], v248 offset:160
	ds_read_b128 v[208:211], v248 offset:176
	s_waitcnt lgkmcnt(3)
	v_fma_f32 v8, v229, v237, v244
	v_fma_f32 v9, v229, v239, v245
	v_fma_f32 v10, v229, v241, v246
	v_fma_f32 v11, v229, v243, v247
	v_fmac_f32_e32 v8, v228, v236
	v_fmac_f32_e32 v9, v228, v238
	v_fmac_f32_e32 v10, v228, v240
	v_fmac_f32_e32 v11, v228, v242
	v_fma_f32 v24, v231, v237, v244
	v_fma_f32 v25, v231, v239, v245
	v_fma_f32 v26, v231, v241, v246
	v_fma_f32 v27, v231, v243, v247
	v_fmac_f32_e32 v24, v230, v236
	v_fmac_f32_e32 v25, v230, v238
	v_fmac_f32_e32 v26, v230, v240
	v_fmac_f32_e32 v27, v230, v242
	v_fma_f32 v40, v233, v237, v244
	v_fma_f32 v41, v233, v239, v245
	v_fma_f32 v42, v233, v241, v246
	v_fma_f32 v43, v233, v243, v247
	v_fmac_f32_e32 v40, v232, v236
	v_fmac_f32_e32 v41, v232, v238
	v_fmac_f32_e32 v42, v232, v240
	v_fmac_f32_e32 v43, v232, v242
	v_fma_f32 v56, v235, v237, v244
	v_fma_f32 v57, v235, v239, v245
	v_fma_f32 v58, v235, v241, v246
	v_fma_f32 v59, v235, v243, v247
	v_fmac_f32_e32 v56, v234, v236
	v_fmac_f32_e32 v57, v234, v238
	v_fmac_f32_e32 v58, v234, v240
	v_fmac_f32_e32 v59, v234, v242
	s_waitcnt lgkmcnt(0)
	v_fma_f32 v12, v229, v201, v208
	v_fma_f32 v13, v229, v203, v209
	v_fma_f32 v14, v229, v205, v210
	v_fma_f32 v15, v229, v207, v211
	v_fmac_f32_e32 v12, v228, v200
	v_fmac_f32_e32 v13, v228, v202
	v_fmac_f32_e32 v14, v228, v204
	v_fmac_f32_e32 v15, v228, v206
	v_fma_f32 v28, v231, v201, v208
	v_fma_f32 v29, v231, v203, v209
	v_fma_f32 v30, v231, v205, v210
	v_fma_f32 v31, v231, v207, v211
	v_fmac_f32_e32 v28, v230, v200
	v_fmac_f32_e32 v29, v230, v202
	v_fmac_f32_e32 v30, v230, v204
	v_fmac_f32_e32 v31, v230, v206
	v_fma_f32 v44, v233, v201, v208
	v_fma_f32 v45, v233, v203, v209
	v_fma_f32 v46, v233, v205, v210
	v_fma_f32 v47, v233, v207, v211
	v_fmac_f32_e32 v44, v232, v200
	v_fmac_f32_e32 v45, v232, v202
	v_fmac_f32_e32 v46, v232, v204
	v_fmac_f32_e32 v47, v232, v206
	v_fma_f32 v60, v235, v201, v208
	v_fma_f32 v61, v235, v203, v209
	v_fma_f32 v62, v235, v205, v210
	v_fma_f32 v63, v235, v207, v211
	v_fmac_f32_e32 v60, v234, v200
	v_fmac_f32_e32 v61, v234, v202
	v_fmac_f32_e32 v62, v234, v204
	v_fmac_f32_e32 v63, v234, v206
	s_waitcnt vmcnt(0)
	s_waitcnt lgkmcnt(0)
	s_cmp_ge_u32 s33, s28
	s_cbranch_scc1 .LE_end11
	s_sub_u32 s71, s33, 1
	s_and_b32 s64, s71, 1
	s_lshl_b32 s64, s64, 22
	s_add_u32 s64, s64, s49
	s_add_u32 s34, s6, s64
	s_addc_u32 s35, s7, 0
	s_lshl_b32 s64, s71, 3
	s_add_u32 s64, s64, s29
	s_lshl_b32 s64, s64, 7
	s_add_u32 s38, s8, s64
	s_addc_u32 s39, s9, 0

.LE_pok13:
	s_waitcnt lgkmcnt(0)
	s_barrier
	s_add_u32 s44, s34, 0x0
	s_addc_u32 s45, s35, 0
	s_mov_b32 m0, s52
	s_nop 0
	global_load_lds_dwordx4 v192, s[44:45] sc1
	global_load_lds_dwordx4 v192, s[44:45] offset:1024 sc1
	global_load_lds_dwordx4 v192, s[44:45] offset:2048 sc1
	global_load_lds_dwordx4 v192, s[44:45] offset:3072 sc1
	s_add_u32 s44, s34, 0x1000
	s_addc_u32 s45, s35, 0
	s_mov_b32 m0, s53
	s_nop 0
	global_load_lds_dwordx4 v192, s[44:45] sc1
	global_load_lds_dwordx4 v192, s[44:45] offset:1024 sc1
	global_load_lds_dwordx4 v192, s[44:45] offset:2048 sc1
	global_load_lds_dwordx4 v192, s[44:45] offset:3072 sc1
	s_add_u32 s44, s34, 0x8000
	s_addc_u32 s45, s35, 0
	s_mov_b32 m0, s54
	s_nop 0
	global_load_lds_dwordx4 v192, s[44:45] sc1
	global_load_lds_dwordx4 v192, s[44:45] offset:1024 sc1
	global_load_lds_dwordx4 v192, s[44:45] offset:2048 sc1
	global_load_lds_dwordx4 v192, s[44:45] offset:3072 sc1
	s_add_u32 s44, s34, 0x9000
	s_addc_u32 s45, s35, 0
	s_mov_b32 m0, s55
	s_nop 0
	global_load_lds_dwordx4 v192, s[44:45] sc1
	global_load_lds_dwordx4 v192, s[44:45] offset:1024 sc1
	global_load_lds_dwordx4 v192, s[44:45] offset:2048 sc1
	global_load_lds_dwordx4 v192, s[44:45] offset:3072 sc1
	s_waitcnt vmcnt(8)
	s_barrier
	s_add_u32 s44, s34, 0x10000
	s_addc_u32 s45, s35, 0
	s_mov_b32 m0, s56
	s_nop 0
	global_load_lds_dwordx4 v192, s[44:45] sc1
	ds_read_b128 v[160:163], v192 offset:0
	ds_read_b128 v[164:167], v192 offset:1024
	ds_read_b128 v[168:171], v192 offset:2048
	ds_read_b128 v[172:175], v192 offset:3072
	ds_read_b128 v[176:179], v192 offset:4096
	ds_read_b128 v[180:183], v192 offset:5120
	ds_read_b128 v[184:187], v192 offset:6144
	ds_read_b128 v[188:191], v192 offset:7168
.LE_loop10:
	s_sub_u32 s71, s33, 1
	s_and_b32 s64, s71, 1
	s_lshl_b32 s64, s64, 22
	s_add_u32 s64, s64, s50
	s_add_u32 s64, s64, 0x40000
	s_add_u32 s36, s6, s64
	s_addc_u32 s37, s7, 0
	s_lshl_b32 s64, s71, 3
	s_add_u32 s64, s64, s29
	s_lshl_b32 s64, s64, 5
	s_add_u32 s64, s64, s30
	s_lshl_b32 s64, s64, 2
	s_add_u32 s40, s8, s64
	s_addc_u32 s41, s9, 0
	s_lshl_b32 s64, s33, 11
	s_lshl_b32 s65, s29, 8
	s_add_u32 s64, s64, s65
	s_add_u32 s64, s64, 128
	s_lshl_b32 s64, s64, 3
	s_add_u32 s42, s12, s64
	s_addc_u32 s43, s13, 0
	s_nop 11
	global_load_dwordx2 v[228:229], v249, s[42:43] offset:0
	global_load_dwordx2 v[230:231], v249, s[42:43] offset:256
	global_load_dwordx2 v[232:233], v249, s[42:43] offset:512
	global_load_dwordx2 v[234:235], v249, s[42:43] offset:768
	v_exp_f32_e32 v200, v64
	v_exp_f32_e32 v201, v65
	v_exp_f32_e32 v202, v66
	v_exp_f32_e32 v203, v67
	v_exp_f32_e32 v204, v68
	v_exp_f32_e32 v205, v69
	v_exp_f32_e32 v206, v70
	v_exp_f32_e32 v207, v71
	v_exp_f32_e32 v208, v72
	v_exp_f32_e32 v209, v73
	v_exp_f32_e32 v210, v74
	v_exp_f32_e32 v211, v75
	v_exp_f32_e32 v212, v76
	v_exp_f32_e32 v213, v77
	v_exp_f32_e32 v214, v78
	v_exp_f32_e32 v215, v79
	v_add_f32_e32 v200, 1.0, v200
	v_add_f32_e32 v201, 1.0, v201
	v_add_f32_e32 v202, 1.0, v202
	v_add_f32_e32 v203, 1.0, v203
	v_add_f32_e32 v204, 1.0, v204
	v_add_f32_e32 v205, 1.0, v205
	v_add_f32_e32 v206, 1.0, v206
	v_add_f32_e32 v207, 1.0, v207
	v_add_f32_e32 v208, 1.0, v208
	v_add_f32_e32 v209, 1.0, v209
	v_add_f32_e32 v210, 1.0, v210
	v_add_f32_e32 v211, 1.0, v211
	v_add_f32_e32 v212, 1.0, v212
	v_add_f32_e32 v213, 1.0, v213
	v_add_f32_e32 v214, 1.0, v214
	v_add_f32_e32 v215, 1.0, v215
	v_rcp_f32_e32 v200, v200
	v_rcp_f32_e32 v201, v201
	v_rcp_f32_e32 v202, v202
	v_rcp_f32_e32 v203, v203
	v_rcp_f32_e32 v204, v204
	v_rcp_f32_e32 v205, v205
	v_rcp_f32_e32 v206, v206
	v_rcp_f32_e32 v207, v207
	v_rcp_f32_e32 v208, v208
	v_rcp_f32_e32 v209, v209
	v_rcp_f32_e32 v210, v210
	v_rcp_f32_e32 v211, v211
	v_rcp_f32_e32 v212, v212
	v_rcp_f32_e32 v213, v213
	v_rcp_f32_e32 v214, v214
	v_rcp_f32_e32 v215, v215
	v_fmamk_f32 v208, v208, 0xc0b8aa3b, v198
	v_fmamk_f32 v209, v209, 0xc0b8aa3b, v198
	v_fmamk_f32 v210, v210, 0xc0b8aa3b, v198
	v_fmamk_f32 v211, v211, 0xc0b8aa3b, v198
	v_mul_f32_e32 v204, v204, v144
	v_mul_f32_e32 v205, v205, v145
	v_mul_f32_e32 v206, v206, v146
	v_mul_f32_e32 v207, v207, v147
	v_fma_f32 v144, v200, v208, v204
	v_fma_f32 v145, v201, v209, v205
	v_fma_f32 v146, v202, v210, v206
	v_fma_f32 v147, v203, v211, v207
	v_exp_f32_e32 v200, v144
	v_exp_f32_e32 v201, v145
	v_exp_f32_e32 v202, v146
	v_exp_f32_e32 v203, v147
	s_waitcnt lgkmcnt(7)
	v_mfma_f32_32x32x16_f16 v[0:15], a[0:3], v[160:163], v[0:15]
	ds_read_b128 v[160:163], v192 offset:8192
	v_add_f32_e32 v200, 1.0, v200
	v_add_f32_e32 v201, 1.0, v201
	v_add_f32_e32 v202, 1.0, v202
	v_add_f32_e32 v203, 1.0, v203
	s_waitcnt lgkmcnt(7)
	v_mfma_f32_32x32x16_f16 v[16:31], a[0:3], v[164:167], v[16:31]
	ds_read_b128 v[164:167], v192 offset:9216
	global_load_lds_dwordx4 v192, s[44:45] offset:1024 sc1
	v_rcp_f32_e32 v200, v200
	v_rcp_f32_e32 v201, v201
	s_waitcnt lgkmcnt(7)
	v_mfma_f32_32x32x16_f16 v[32:47], a[0:3], v[168:171], v[32:47]
	ds_read_b128 v[168:171], v192 offset:10240
	v_rcp_f32_e32 v202, v202
	v_rcp_f32_e32 v203, v203
	v_fma_f32 v200, v200, 2.0, -1.0
	s_waitcnt lgkmcnt(7)
	v_mfma_f32_32x32x16_f16 v[48:63], a[0:3], v[172:175], v[48:63]
	ds_read_b128 v[172:175], v192 offset:11264
	v_fma_f32 v201, v201, 2.0, -1.0
	v_fma_f32 v202, v202, 2.0, -1.0
	v_fma_f32 v203, v203, 2.0, -1.0
	v_mul_f32_e32 v216, v212, v200
	v_mul_f32_e32 v217, v213, v201
	s_waitcnt lgkmcnt(7)
	v_mfma_f32_32x32x16_f16 v[0:15], a[4:7], v[176:179], v[0:15]
	ds_read_b128 v[176:179], v192 offset:12288
	v_mul_f32_e32 v218, v214, v202
	v_mul_f32_e32 v219, v215, v203
	v_cvt_pk_f16_f32 v220, v216, v217
	v_cvt_pk_f16_f32 v221, v218, v219
	s_waitcnt lgkmcnt(7)
	v_mfma_f32_32x32x16_f16 v[16:31], a[4:7], v[180:183], v[16:31]
	ds_read_b128 v[180:183], v192 offset:13312
	global_load_lds_dwordx4 v192, s[44:45] offset:2048 sc1
	v_exp_f32_e32 v200, v80
	v_exp_f32_e32 v201, v81
	s_waitcnt lgkmcnt(7)
	v_mfma_f32_32x32x16_f16 v[32:47], a[4:7], v[184:187], v[32:47]
	ds_read_b128 v[184:187], v192 offset:14336
	v_exp_f32_e32 v202, v82
	v_exp_f32_e32 v203, v83
	s_waitcnt lgkmcnt(7)
	v_mfma_f32_32x32x16_f16 v[48:63], a[4:7], v[188:191], v[48:63]
	ds_read_b128 v[188:191], v192 offset:15360
	v_exp_f32_e32 v204, v84
	v_exp_f32_e32 v205, v85
	s_waitcnt lgkmcnt(7)
	v_mfma_f32_32x32x16_f16 v[0:15], a[8:11], v[160:163], v[0:15]
	ds_read_b128 v[160:163], v192 offset:16384
	v_exp_f32_e32 v206, v86
	v_exp_f32_e32 v207, v87
	s_waitcnt lgkmcnt(7)
	v_mfma_f32_32x32x16_f16 v[16:31], a[8:11], v[164:167], v[16:31]
	ds_read_b128 v[164:167], v192 offset:17408
	global_load_lds_dwordx4 v192, s[44:45] offset:3072 sc1
	v_exp_f32_e32 v208, v88
	v_exp_f32_e32 v209, v89
	s_waitcnt lgkmcnt(7)
	v_mfma_f32_32x32x16_f16 v[32:47], a[8:11], v[168:171], v[32:47]
	ds_read_b128 v[168:171], v192 offset:18432
	v_exp_f32_e32 v210, v90
	v_exp_f32_e32 v211, v91
	s_waitcnt lgkmcnt(7)
	v_mfma_f32_32x32x16_f16 v[48:63], a[8:11], v[172:175], v[48:63]
	ds_read_b128 v[172:175], v192 offset:19456
	v_exp_f32_e32 v212, v92
	v_exp_f32_e32 v213, v93
	s_waitcnt lgkmcnt(7)
	v_mfma_f32_32x32x16_f16 v[0:15], a[12:15], v[176:179], v[0:15]
	ds_read_b128 v[176:179], v192 offset:20480
	v_exp_f32_e32 v214, v94
	v_exp_f32_e32 v215, v95
	v_add_f32_e32 v200, 1.0, v200
	s_waitcnt lgkmcnt(7)
	v_mfma_f32_32x32x16_f16 v[16:31], a[12:15], v[180:183], v[16:31]
	ds_read_b128 v[180:183], v192 offset:21504
	s_add_u32 s44, s34, 0x11000
	s_addc_u32 s45, s35, 0
	s_mov_b32 m0, s57
	s_nop 0
	global_load_lds_dwordx4 v192, s[44:45] sc1
	v_add_f32_e32 v201, 1.0, v201
	v_add_f32_e32 v202, 1.0, v202
	v_add_f32_e32 v203, 1.0, v203
	v_add_f32_e32 v204, 1.0, v204
	v_add_f32_e32 v205, 1.0, v205
	s_waitcnt lgkmcnt(7)
	v_mfma_f32_32x32x16_f16 v[32:47], a[12:15], v[184:187], v[32:47]
	ds_read_b128 v[184:187], v192 offset:22528
	v_add_f32_e32 v206, 1.0, v206
	v_add_f32_e32 v207, 1.0, v207
	v_add_f32_e32 v208, 1.0, v208
	v_add_f32_e32 v209, 1.0, v209
	v_add_f32_e32 v210, 1.0, v210
	s_waitcnt lgkmcnt(7)
	v_mfma_f32_32x32x16_f16 v[48:63], a[12:15], v[188:191], v[48:63]
	ds_read_b128 v[188:191], v192 offset:23552
	v_add_f32_e32 v211, 1.0, v211
	v_add_f32_e32 v212, 1.0, v212
	v_add_f32_e32 v213, 1.0, v213
	v_add_f32_e32 v214, 1.0, v214
	v_add_f32_e32 v215, 1.0, v215
	s_waitcnt lgkmcnt(7)
	v_mfma_f32_32x32x16_f16 v[0:15], a[16:19], v[160:163], v[0:15]
	ds_read_b128 v[160:163], v192 offset:24576
	v_rcp_f32_e32 v200, v200
	v_rcp_f32_e32 v201, v201
	s_waitcnt lgkmcnt(7)
	v_mfma_f32_32x32x16_f16 v[16:31], a[16:19], v[164:167], v[16:31]
	ds_read_b128 v[164:167], v192 offset:25600
	global_load_lds_dwordx4 v192, s[44:45] offset:1024 sc1
	v_rcp_f32_e32 v202, v202
	v_rcp_f32_e32 v203, v203
	s_waitcnt lgkmcnt(7)
	v_mfma_f32_32x32x16_f16 v[32:47], a[16:19], v[168:171], v[32:47]
	ds_read_b128 v[168:171], v192 offset:26624
	v_rcp_f32_e32 v204, v204
	v_rcp_f32_e32 v205, v205
	s_waitcnt lgkmcnt(7)
	v_mfma_f32_32x32x16_f16 v[48:63], a[16:19], v[172:175], v[48:63]
	ds_read_b128 v[172:175], v192 offset:27648
	v_rcp_f32_e32 v206, v206
	v_rcp_f32_e32 v207, v207
	s_waitcnt lgkmcnt(7)
	v_mfma_f32_32x32x16_f16 v[0:15], a[20:23], v[176:179], v[0:15]
	ds_read_b128 v[176:179], v192 offset:28672
	v_rcp_f32_e32 v208, v208
	v_rcp_f32_e32 v209, v209
	s_waitcnt lgkmcnt(7)
	v_mfma_f32_32x32x16_f16 v[16:31], a[20:23], v[180:183], v[16:31]
	ds_read_b128 v[180:183], v192 offset:29696
	global_load_lds_dwordx4 v192, s[44:45] offset:2048 sc1
	v_rcp_f32_e32 v210, v210
	v_rcp_f32_e32 v211, v211
	s_waitcnt lgkmcnt(7)
	v_mfma_f32_32x32x16_f16 v[32:47], a[20:23], v[184:187], v[32:47]
	ds_read_b128 v[184:187], v192 offset:30720
	v_rcp_f32_e32 v212, v212
	v_rcp_f32_e32 v213, v213
	s_waitcnt lgkmcnt(7)
	v_mfma_f32_32x32x16_f16 v[48:63], a[20:23], v[188:191], v[48:63]
	ds_read_b128 v[188:191], v192 offset:31744
	v_rcp_f32_e32 v214, v214
	v_rcp_f32_e32 v215, v215
	v_fmamk_f32 v208, v208, 0xc0b8aa3b, v198
	s_waitcnt vmcnt(11)
	s_barrier
	s_waitcnt lgkmcnt(7)
	v_mfma_f32_32x32x16_f16 v[0:15], a[24:27], v[160:163], v[0:15]
	ds_read_b128 v[160:163], v192 offset:32768
	v_fmamk_f32 v209, v209, 0xc0b8aa3b, v198
	v_fmamk_f32 v210, v210, 0xc0b8aa3b, v198
	v_fmamk_f32 v211, v211, 0xc0b8aa3b, v198
	v_mul_f32_e32 v204, v204, v148
	v_mul_f32_e32 v205, v205, v149
	s_waitcnt lgkmcnt(7)
	v_mfma_f32_32x32x16_f16 v[16:31], a[24:27], v[164:167], v[16:31]
	ds_read_b128 v[164:167], v192 offset:33792
	global_load_lds_dwordx4 v192, s[44:45] offset:3072 sc1
	v_mul_f32_e32 v206, v206, v150
	v_mul_f32_e32 v207, v207, v151
	v_fma_f32 v148, v200, v208, v204
	v_fma_f32 v149, v201, v209, v205
	v_fma_f32 v150, v202, v210, v206
	s_waitcnt lgkmcnt(7)
	v_mfma_f32_32x32x16_f16 v[32:47], a[24:27], v[168:171], v[32:47]
	ds_read_b128 v[168:171], v192 offset:34816
	v_fma_f32 v151, v203, v211, v207
	v_exp_f32_e32 v200, v148
	v_exp_f32_e32 v201, v149
	s_waitcnt lgkmcnt(7)
	v_mfma_f32_32x32x16_f16 v[48:63], a[24:27], v[172:175], v[48:63]
	ds_read_b128 v[172:175], v192 offset:35840
	v_exp_f32_e32 v202, v150
	v_exp_f32_e32 v203, v151
	v_add_f32_e32 v200, 1.0, v200
	s_waitcnt lgkmcnt(7)
	v_mfma_f32_32x32x16_f16 v[0:15], a[28:31], v[176:179], v[0:15]
	ds_read_b128 v[176:179], v192 offset:36864
	v_add_f32_e32 v201, 1.0, v201
	v_add_f32_e32 v202, 1.0, v202
	v_add_f32_e32 v203, 1.0, v203
	v_rcp_f32_e32 v200, v200
	s_waitcnt lgkmcnt(7)
	v_mfma_f32_32x32x16_f16 v[16:31], a[28:31], v[180:183], v[16:31]
	ds_read_b128 v[180:183], v192 offset:37888
	s_add_u32 s44, s34, 0x18000
	s_addc_u32 s45, s35, 0
	s_mov_b32 m0, s58
	s_nop 0
	global_load_lds_dwordx4 v192, s[44:45] sc1
	v_rcp_f32_e32 v201, v201
	v_rcp_f32_e32 v202, v202
	s_waitcnt lgkmcnt(7)
	v_mfma_f32_32x32x16_f16 v[32:47], a[28:31], v[184:187], v[32:47]
	ds_read_b128 v[184:187], v192 offset:38912
	v_rcp_f32_e32 v203, v203
	v_fma_f32 v200, v200, 2.0, -1.0
	v_fma_f32 v201, v201, 2.0, -1.0
	v_fma_f32 v202, v202, 2.0, -1.0
	s_waitcnt lgkmcnt(7)
	v_mfma_f32_32x32x16_f16 v[48:63], a[28:31], v[188:191], v[48:63]
	ds_read_b128 v[188:191], v192 offset:39936
	v_fma_f32 v203, v203, 2.0, -1.0
	v_mul_f32_e32 v216, v212, v200
	v_mul_f32_e32 v217, v213, v201
	v_mul_f32_e32 v218, v214, v202
	v_mul_f32_e32 v219, v215, v203
	s_waitcnt lgkmcnt(7)
	v_mfma_f32_32x32x16_f16 v[0:15], a[32:35], v[160:163], v[0:15]
	ds_read_b128 v[160:163], v192 offset:40960
	v_cvt_pk_f16_f32 v222, v216, v217
	v_cvt_pk_f16_f32 v223, v218, v219
	s_waitcnt lgkmcnt(7)
	v_mfma_f32_32x32x16_f16 v[16:31], a[32:35], v[164:167], v[16:31]
	ds_read_b128 v[164:167], v192 offset:41984
	global_load_lds_dwordx4 v192, s[44:45] offset:1024 sc1
	s_nop 1
	v_permlane32_swap_b32_e32 v220, v222
	v_permlane32_swap_b32_e32 v221, v223
	s_cmp_eq_u32 s31, 0
	s_cbranch_scc1 .LE_slow14
	global_store_dwordx4 v195, v[220:223], s[36:37] offset:0
	s_branch .LE_join15

.LE_join15:
	s_waitcnt lgkmcnt(7)
	v_mfma_f32_32x32x16_f16 v[32:47], a[32:35], v[168:171], v[32:47]
	ds_read_b128 v[168:171], v192 offset:43008
	v_exp_f32_e32 v200, v96
	v_exp_f32_e32 v201, v97
	s_waitcnt lgkmcnt(7)
	v_mfma_f32_32x32x16_f16 v[48:63], a[32:35], v[172:175], v[48:63]
	ds_read_b128 v[172:175], v192 offset:44032
	v_exp_f32_e32 v202, v98
	v_exp_f32_e32 v203, v99
	s_waitcnt lgkmcnt(7)
	v_mfma_f32_32x32x16_f16 v[0:15], a[36:39], v[176:179], v[0:15]
	ds_read_b128 v[176:179], v192 offset:45056
	v_exp_f32_e32 v204, v100
	v_exp_f32_e32 v205, v101
	s_waitcnt lgkmcnt(7)
	v_mfma_f32_32x32x16_f16 v[16:31], a[36:39], v[180:183], v[16:31]
	ds_read_b128 v[180:183], v192 offset:46080
	global_load_lds_dwordx4 v192, s[44:45] offset:2048 sc1
	v_exp_f32_e32 v206, v102
	v_exp_f32_e32 v207, v103
	s_waitcnt lgkmcnt(7)
	v_mfma_f32_32x32x16_f16 v[32:47], a[36:39], v[184:187], v[32:47]
	ds_read_b128 v[184:187], v192 offset:47104
	v_exp_f32_e32 v208, v104
	v_exp_f32_e32 v209, v105
	s_waitcnt lgkmcnt(7)
	v_mfma_f32_32x32x16_f16 v[48:63], a[36:39], v[188:191], v[48:63]
	ds_read_b128 v[188:191], v192 offset:48128
	v_exp_f32_e32 v210, v106
	v_exp_f32_e32 v211, v107
	s_waitcnt lgkmcnt(7)
	v_mfma_f32_32x32x16_f16 v[0:15], a[40:43], v[160:163], v[0:15]
	ds_read_b128 v[160:163], v192 offset:49152
	v_exp_f32_e32 v212, v108
	v_exp_f32_e32 v213, v109
	s_waitcnt lgkmcnt(7)
	v_mfma_f32_32x32x16_f16 v[16:31], a[40:43], v[164:167], v[16:31]
	ds_read_b128 v[164:167], v192 offset:50176
	global_load_lds_dwordx4 v192, s[44:45] offset:3072 sc1
	v_exp_f32_e32 v214, v110
	v_exp_f32_e32 v215, v111
	v_add_f32_e32 v200, 1.0, v200
	s_waitcnt lgkmcnt(7)
	v_mfma_f32_32x32x16_f16 v[32:47], a[40:43], v[168:171], v[32:47]
	ds_read_b128 v[168:171], v192 offset:51200
	v_add_f32_e32 v201, 1.0, v201
	v_add_f32_e32 v202, 1.0, v202
	v_add_f32_e32 v203, 1.0, v203
	v_add_f32_e32 v204, 1.0, v204
	v_add_f32_e32 v205, 1.0, v205
	s_waitcnt lgkmcnt(7)
	v_mfma_f32_32x32x16_f16 v[48:63], a[40:43], v[172:175], v[48:63]
	ds_read_b128 v[172:175], v192 offset:52224
	v_add_f32_e32 v206, 1.0, v206
	v_add_f32_e32 v207, 1.0, v207
	v_add_f32_e32 v208, 1.0, v208
	v_add_f32_e32 v209, 1.0, v209
	v_add_f32_e32 v210, 1.0, v210
	s_waitcnt lgkmcnt(7)
	v_mfma_f32_32x32x16_f16 v[0:15], a[44:47], v[176:179], v[0:15]
	ds_read_b128 v[176:179], v192 offset:53248
	v_add_f32_e32 v211, 1.0, v211
	v_add_f32_e32 v212, 1.0, v212
	v_add_f32_e32 v213, 1.0, v213
	v_add_f32_e32 v214, 1.0, v214
	v_add_f32_e32 v215, 1.0, v215
	s_waitcnt lgkmcnt(7)
	v_mfma_f32_32x32x16_f16 v[16:31], a[44:47], v[180:183], v[16:31]
	ds_read_b128 v[180:183], v192 offset:54272
	s_add_u32 s44, s34, 0x19000
	s_addc_u32 s45, s35, 0
	s_mov_b32 m0, s59
	s_nop 0
	global_load_lds_dwordx4 v192, s[44:45] sc1
	v_rcp_f32_e32 v200, v200
	v_rcp_f32_e32 v201, v201
	s_waitcnt lgkmcnt(7)
	v_mfma_f32_32x32x16_f16 v[32:47], a[44:47], v[184:187], v[32:47]
	ds_read_b128 v[184:187], v192 offset:55296
	v_rcp_f32_e32 v202, v202
	v_rcp_f32_e32 v203, v203
	s_waitcnt lgkmcnt(7)
	v_mfma_f32_32x32x16_f16 v[48:63], a[44:47], v[188:191], v[48:63]
	ds_read_b128 v[188:191], v192 offset:56320
	v_rcp_f32_e32 v204, v204
	v_rcp_f32_e32 v205, v205
	s_waitcnt lgkmcnt(7)
	v_mfma_f32_32x32x16_f16 v[0:15], a[48:51], v[160:163], v[0:15]
	ds_read_b128 v[160:163], v192 offset:57344
	v_rcp_f32_e32 v206, v206
	v_rcp_f32_e32 v207, v207
	s_waitcnt lgkmcnt(7)
	v_mfma_f32_32x32x16_f16 v[16:31], a[48:51], v[164:167], v[16:31]
	ds_read_b128 v[164:167], v192 offset:58368
	global_load_lds_dwordx4 v192, s[44:45] offset:1024 sc1
	v_rcp_f32_e32 v208, v208
	v_rcp_f32_e32 v209, v209
	s_waitcnt lgkmcnt(7)
	v_mfma_f32_32x32x16_f16 v[32:47], a[48:51], v[168:171], v[32:47]
	ds_read_b128 v[168:171], v192 offset:59392
	v_rcp_f32_e32 v210, v210
	v_rcp_f32_e32 v211, v211
	s_waitcnt lgkmcnt(7)
	v_mfma_f32_32x32x16_f16 v[48:63], a[48:51], v[172:175], v[48:63]
	ds_read_b128 v[172:175], v192 offset:60416
	v_rcp_f32_e32 v212, v212
	v_rcp_f32_e32 v213, v213
	s_waitcnt lgkmcnt(7)
	v_mfma_f32_32x32x16_f16 v[0:15], a[52:55], v[176:179], v[0:15]
	ds_read_b128 v[176:179], v192 offset:61440
	v_rcp_f32_e32 v214, v214
	v_rcp_f32_e32 v215, v215
	v_fmamk_f32 v208, v208, 0xc0b8aa3b, v198
	s_waitcnt lgkmcnt(7)
	v_mfma_f32_32x32x16_f16 v[16:31], a[52:55], v[180:183], v[16:31]
	ds_read_b128 v[180:183], v192 offset:62464
	global_load_lds_dwordx4 v192, s[44:45] offset:2048 sc1
	v_fmamk_f32 v209, v209, 0xc0b8aa3b, v198
	v_fmamk_f32 v210, v210, 0xc0b8aa3b, v198
	v_fmamk_f32 v211, v211, 0xc0b8aa3b, v198
	v_mul_f32_e32 v204, v204, v152
	v_mul_f32_e32 v205, v205, v153
	s_waitcnt lgkmcnt(7)
	v_mfma_f32_32x32x16_f16 v[32:47], a[52:55], v[184:187], v[32:47]
	ds_read_b128 v[184:187], v192 offset:63488
	v_mul_f32_e32 v206, v206, v154
	v_mul_f32_e32 v207, v207, v155
	v_fma_f32 v152, v200, v208, v204
	v_fma_f32 v153, v201, v209, v205
	v_fma_f32 v154, v202, v210, v206
	s_waitcnt lgkmcnt(7)
	v_mfma_f32_32x32x16_f16 v[48:63], a[52:55], v[188:191], v[48:63]
	ds_read_b128 v[188:191], v192 offset:64512
	v_fma_f32 v155, v203, v211, v207
	v_exp_f32_e32 v200, v152
	v_exp_f32_e32 v201, v153
	s_waitcnt vmcnt(8)
	s_barrier
	s_waitcnt lgkmcnt(7)
	v_mfma_f32_32x32x16_f16 v[0:15], a[56:59], v[160:163], v[0:15]
	ds_read_b128 v[160:163], v193 offset:0
	v_exp_f32_e32 v202, v154
	v_exp_f32_e32 v203, v155
	v_add_f32_e32 v200, 1.0, v200
	s_waitcnt lgkmcnt(7)
	v_mfma_f32_32x32x16_f16 v[16:31], a[56:59], v[164:167], v[16:31]
	ds_read_b128 v[164:167], v193 offset:1024
	global_load_lds_dwordx4 v192, s[44:45] offset:3072 sc1
	v_add_f32_e32 v201, 1.0, v201
	v_add_f32_e32 v202, 1.0, v202
	v_add_f32_e32 v203, 1.0, v203
	v_rcp_f32_e32 v200, v200
	s_waitcnt lgkmcnt(7)
	v_mfma_f32_32x32x16_f16 v[32:47], a[56:59], v[168:171], v[32:47]
	ds_read_b128 v[168:171], v193 offset:2048
	v_rcp_f32_e32 v201, v201
	v_rcp_f32_e32 v202, v202
	s_waitcnt lgkmcnt(7)
	v_mfma_f32_32x32x16_f16 v[48:63], a[56:59], v[172:175], v[48:63]
	ds_read_b128 v[172:175], v193 offset:3072
	v_rcp_f32_e32 v203, v203
	v_fma_f32 v200, v200, 2.0, -1.0
	v_fma_f32 v201, v201, 2.0, -1.0
	v_fma_f32 v202, v202, 2.0, -1.0
	s_waitcnt lgkmcnt(7)
	v_mfma_f32_32x32x16_f16 v[0:15], a[60:63], v[176:179], v[0:15]
	ds_read_b128 v[176:179], v193 offset:4096
	v_fma_f32 v203, v203, 2.0, -1.0
	v_mul_f32_e32 v216, v212, v200
	v_mul_f32_e32 v217, v213, v201
	v_mul_f32_e32 v218, v214, v202
	v_mul_f32_e32 v219, v215, v203
	s_waitcnt lgkmcnt(7)
	v_mfma_f32_32x32x16_f16 v[16:31], a[60:63], v[180:183], v[16:31]
	ds_read_b128 v[180:183], v193 offset:5120
	s_add_u32 s44, s34, 0x20000
	s_addc_u32 s45, s35, 0
	s_mov_b32 m0, s52
	s_nop 0
	global_load_lds_dwordx4 v192, s[44:45] sc1
	v_cvt_pk_f16_f32 v224, v216, v217
	v_cvt_pk_f16_f32 v225, v218, v219
	v_exp_f32_e32 v200, v112
	s_waitcnt lgkmcnt(7)
	v_mfma_f32_32x32x16_f16 v[32:47], a[60:63], v[184:187], v[32:47]
	ds_read_b128 v[184:187], v193 offset:6144
	v_exp_f32_e32 v201, v113
	v_exp_f32_e32 v202, v114
	s_waitcnt lgkmcnt(7)
	v_mfma_f32_32x32x16_f16 v[48:63], a[60:63], v[188:191], v[48:63]
	ds_read_b128 v[188:191], v193 offset:7168
	v_exp_f32_e32 v203, v115
	v_exp_f32_e32 v204, v116
	s_waitcnt lgkmcnt(7)
	v_mfma_f32_32x32x16_f16 v[0:15], a[64:67], v[160:163], v[0:15]
	ds_read_b128 v[160:163], v193 offset:8192
	v_exp_f32_e32 v205, v117
	v_exp_f32_e32 v206, v118
	s_waitcnt lgkmcnt(7)
	v_mfma_f32_32x32x16_f16 v[16:31], a[64:67], v[164:167], v[16:31]
	ds_read_b128 v[164:167], v193 offset:9216
	global_load_lds_dwordx4 v192, s[44:45] offset:1024 sc1
	v_exp_f32_e32 v207, v119
	v_exp_f32_e32 v208, v120
	s_waitcnt lgkmcnt(7)
	v_mfma_f32_32x32x16_f16 v[32:47], a[64:67], v[168:171], v[32:47]
	ds_read_b128 v[168:171], v193 offset:10240
	v_exp_f32_e32 v209, v121
	v_exp_f32_e32 v210, v122
	s_waitcnt lgkmcnt(7)
	v_mfma_f32_32x32x16_f16 v[48:63], a[64:67], v[172:175], v[48:63]
	ds_read_b128 v[172:175], v193 offset:11264
	v_exp_f32_e32 v211, v123
	v_exp_f32_e32 v212, v124
	s_waitcnt lgkmcnt(7)
	v_mfma_f32_32x32x16_f16 v[0:15], a[68:71], v[176:179], v[0:15]
	ds_read_b128 v[176:179], v193 offset:12288
	v_exp_f32_e32 v213, v125
	v_exp_f32_e32 v214, v126
	s_waitcnt lgkmcnt(7)
	v_mfma_f32_32x32x16_f16 v[16:31], a[68:71], v[180:183], v[16:31]
	ds_read_b128 v[180:183], v193 offset:13312
	global_load_lds_dwordx4 v192, s[44:45] offset:2048 sc1
	v_exp_f32_e32 v215, v127
	v_add_f32_e32 v200, 1.0, v200
	v_add_f32_e32 v201, 1.0, v201
	v_add_f32_e32 v202, 1.0, v202
	s_waitcnt lgkmcnt(7)
	v_mfma_f32_32x32x16_f16 v[32:47], a[68:71], v[184:187], v[32:47]
	ds_read_b128 v[184:187], v193 offset:14336
	v_add_f32_e32 v203, 1.0, v203
	v_add_f32_e32 v204, 1.0, v204
	v_add_f32_e32 v205, 1.0, v205
	v_add_f32_e32 v206, 1.0, v206
	v_add_f32_e32 v207, 1.0, v207
	s_waitcnt lgkmcnt(7)
	v_mfma_f32_32x32x16_f16 v[48:63], a[68:71], v[188:191], v[48:63]
	ds_read_b128 v[188:191], v193 offset:15360
	v_add_f32_e32 v208, 1.0, v208
	v_add_f32_e32 v209, 1.0, v209
	v_add_f32_e32 v210, 1.0, v210
	v_add_f32_e32 v211, 1.0, v211
	v_add_f32_e32 v212, 1.0, v212
	s_waitcnt lgkmcnt(7)
	v_mfma_f32_32x32x16_f16 v[0:15], a[72:75], v[160:163], v[0:15]
	ds_read_b128 v[160:163], v193 offset:16384
	v_add_f32_e32 v213, 1.0, v213
	v_add_f32_e32 v214, 1.0, v214
	v_add_f32_e32 v215, 1.0, v215
	v_rcp_f32_e32 v200, v200
	s_waitcnt lgkmcnt(7)
	v_mfma_f32_32x32x16_f16 v[16:31], a[72:75], v[164:167], v[16:31]
	ds_read_b128 v[164:167], v193 offset:17408
	global_load_lds_dwordx4 v192, s[44:45] offset:3072 sc1
	v_rcp_f32_e32 v201, v201
	v_rcp_f32_e32 v202, v202
	s_waitcnt lgkmcnt(7)
	v_mfma_f32_32x32x16_f16 v[32:47], a[72:75], v[168:171], v[32:47]
	ds_read_b128 v[168:171], v193 offset:18432
	v_rcp_f32_e32 v203, v203
	v_rcp_f32_e32 v204, v204
	s_waitcnt lgkmcnt(7)
	v_mfma_f32_32x32x16_f16 v[48:63], a[72:75], v[172:175], v[48:63]
	ds_read_b128 v[172:175], v193 offset:19456
	v_rcp_f32_e32 v205, v205
	v_rcp_f32_e32 v206, v206
	s_waitcnt lgkmcnt(7)
	v_mfma_f32_32x32x16_f16 v[0:15], a[76:79], v[176:179], v[0:15]
	ds_read_b128 v[176:179], v193 offset:20480
	v_rcp_f32_e32 v207, v207
	v_rcp_f32_e32 v208, v208
	s_waitcnt lgkmcnt(7)
	v_mfma_f32_32x32x16_f16 v[16:31], a[76:79], v[180:183], v[16:31]
	ds_read_b128 v[180:183], v193 offset:21504
	s_add_u32 s44, s34, 0x21000
	s_addc_u32 s45, s35, 0
	s_mov_b32 m0, s53
	s_nop 0
	global_load_lds_dwordx4 v192, s[44:45] sc1
	v_rcp_f32_e32 v209, v209
	v_rcp_f32_e32 v210, v210
	s_waitcnt lgkmcnt(7)
	v_mfma_f32_32x32x16_f16 v[32:47], a[76:79], v[184:187], v[32:47]
	ds_read_b128 v[184:187], v193 offset:22528
	v_rcp_f32_e32 v211, v211
	v_rcp_f32_e32 v212, v212
	s_waitcnt lgkmcnt(7)
	v_mfma_f32_32x32x16_f16 v[48:63], a[76:79], v[188:191], v[48:63]
	ds_read_b128 v[188:191], v193 offset:23552
	v_rcp_f32_e32 v213, v213
	v_rcp_f32_e32 v214, v214
	s_waitcnt lgkmcnt(7)
	v_mfma_f32_32x32x16_f16 v[0:15], a[80:83], v[160:163], v[0:15]
	ds_read_b128 v[160:163], v193 offset:24576
	v_rcp_f32_e32 v215, v215
	v_fmamk_f32 v208, v208, 0xc0b8aa3b, v198
	v_fmamk_f32 v209, v209, 0xc0b8aa3b, v198
	v_fmamk_f32 v210, v210, 0xc0b8aa3b, v198
	s_waitcnt lgkmcnt(7)
	v_mfma_f32_32x32x16_f16 v[16:31], a[80:83], v[164:167], v[16:31]
	ds_read_b128 v[164:167], v193 offset:25600
	global_load_lds_dwordx4 v192, s[44:45] offset:1024 sc1
	v_fmamk_f32 v211, v211, 0xc0b8aa3b, v198
	v_mul_f32_e32 v204, v204, v156
	v_mul_f32_e32 v205, v205, v157
	v_mul_f32_e32 v206, v206, v158
	v_mul_f32_e32 v207, v207, v159
	s_waitcnt lgkmcnt(7)
	v_mfma_f32_32x32x16_f16 v[32:47], a[80:83], v[168:171], v[32:47]
	ds_read_b128 v[168:171], v193 offset:26624
	v_fma_f32 v156, v200, v208, v204
	v_fma_f32 v157, v201, v209, v205
	v_fma_f32 v158, v202, v210, v206
	v_fma_f32 v159, v203, v211, v207
	s_waitcnt lgkmcnt(7)
	v_mfma_f32_32x32x16_f16 v[48:63], a[80:83], v[172:175], v[48:63]
	ds_read_b128 v[172:175], v193 offset:27648
	v_exp_f32_e32 v200, v156
	v_exp_f32_e32 v201, v157
	s_waitcnt lgkmcnt(7)
	v_mfma_f32_32x32x16_f16 v[0:15], a[84:87], v[176:179], v[0:15]
	ds_read_b128 v[176:179], v193 offset:28672
	v_exp_f32_e32 v202, v158
	v_exp_f32_e32 v203, v159
	v_add_f32_e32 v200, 1.0, v200
	s_waitcnt lgkmcnt(7)
	v_mfma_f32_32x32x16_f16 v[16:31], a[84:87], v[180:183], v[16:31]
	ds_read_b128 v[180:183], v193 offset:29696
	global_load_lds_dwordx4 v192, s[44:45] offset:2048 sc1
	v_add_f32_e32 v201, 1.0, v201
	v_add_f32_e32 v202, 1.0, v202
	v_add_f32_e32 v203, 1.0, v203
	v_rcp_f32_e32 v200, v200
	s_waitcnt lgkmcnt(7)
	v_mfma_f32_32x32x16_f16 v[32:47], a[84:87], v[184:187], v[32:47]
	ds_read_b128 v[184:187], v193 offset:30720
	v_rcp_f32_e32 v201, v201
	v_rcp_f32_e32 v202, v202
	s_waitcnt lgkmcnt(7)
	v_mfma_f32_32x32x16_f16 v[48:63], a[84:87], v[188:191], v[48:63]
	ds_read_b128 v[188:191], v193 offset:31744
	v_rcp_f32_e32 v203, v203
	v_fma_f32 v200, v200, 2.0, -1.0
	v_fma_f32 v201, v201, 2.0, -1.0
	v_fma_f32 v202, v202, 2.0, -1.0
	s_waitcnt vmcnt(7)
	s_barrier
	s_waitcnt lgkmcnt(7)
	v_mfma_f32_32x32x16_f16 v[0:15], a[88:91], v[160:163], v[0:15]
	ds_read_b128 v[160:163], v193 offset:32768
	v_fma_f32 v203, v203, 2.0, -1.0
	v_mul_f32_e32 v216, v212, v200
	v_mul_f32_e32 v217, v213, v201
	v_mul_f32_e32 v218, v214, v202
	v_mul_f32_e32 v219, v215, v203
	s_waitcnt lgkmcnt(7)
	v_mfma_f32_32x32x16_f16 v[16:31], a[88:91], v[164:167], v[16:31]
	ds_read_b128 v[164:167], v193 offset:33792
	global_load_lds_dwordx4 v192, s[44:45] offset:3072 sc1
	v_cvt_pk_f16_f32 v226, v216, v217
	v_cvt_pk_f16_f32 v227, v218, v219
	s_waitcnt lgkmcnt(7)
	v_mfma_f32_32x32x16_f16 v[32:47], a[88:91], v[168:171], v[32:47]
	ds_read_b128 v[168:171], v193 offset:34816
	s_nop 1
	v_permlane32_swap_b32_e32 v224, v226
	v_permlane32_swap_b32_e32 v225, v227
	s_cmp_eq_u32 s31, 0
	s_cbranch_scc1 .LE_slow16
	global_store_dwordx4 v195, v[224:227], s[36:37] offset:2048
	s_branch .LE_join17

.LE_join17:
	s_waitcnt lgkmcnt(7)
	v_mfma_f32_32x32x16_f16 v[48:63], a[88:91], v[172:175], v[48:63]
	ds_read_b128 v[172:175], v193 offset:35840
	ds_read_b128 v[236:239], v248 offset:0
	ds_read_b128 v[240:243], v248 offset:16
	ds_read_b128 v[244:247], v248 offset:32
	s_waitcnt lgkmcnt(10)
	v_mfma_f32_32x32x16_f16 v[0:15], a[92:95], v[176:179], v[0:15]
	ds_read_b128 v[176:179], v193 offset:36864
	ds_read_b128 v[200:203], v248 offset:48
	ds_read_b128 v[204:207], v248 offset:64
	ds_read_b128 v[208:211], v248 offset:80
	s_waitcnt lgkmcnt(4)
	v_fma_f32 v64, v229, v237, v244
	v_mfma_f32_32x32x16_f16 v[16:31], a[92:95], v[180:183], v[16:31]
	ds_read_b128 v[180:183], v193 offset:37888
	s_add_u32 s44, s34, 0x28000
	s_addc_u32 s45, s35, 0
	s_mov_b32 m0, s54
	s_nop 0
	global_load_lds_dwordx4 v192, s[44:45] sc1
	v_fma_f32 v65, v229, v239, v245
	v_fma_f32 v66, v229, v241, v246
	v_fma_f32 v67, v229, v243, v247
	v_fmac_f32_e32 v64, v228, v236
	v_fmac_f32_e32 v65, v228, v238
	v_mfma_f32_32x32x16_f16 v[32:47], a[92:95], v[184:187], v[32:47]
	ds_read_b128 v[184:187], v193 offset:38912
	v_fmac_f32_e32 v66, v228, v240
	v_fmac_f32_e32 v67, v228, v242
	v_fma_f32 v80, v231, v237, v244
	v_fma_f32 v81, v231, v239, v245
	v_fma_f32 v82, v231, v241, v246
	v_mfma_f32_32x32x16_f16 v[48:63], a[92:95], v[188:191], v[48:63]
	ds_read_b128 v[188:191], v193 offset:39936
	v_fma_f32 v83, v231, v243, v247
	v_fmac_f32_e32 v80, v230, v236
	v_fmac_f32_e32 v81, v230, v238
	v_fmac_f32_e32 v82, v230, v240
	v_fmac_f32_e32 v83, v230, v242
	v_mfma_f32_32x32x16_f16 v[0:15], a[96:99], v[160:163], v[0:15]
	ds_read_b128 v[160:163], v193 offset:40960
	v_fma_f32 v96, v233, v237, v244
	v_fma_f32 v97, v233, v239, v245
	v_fma_f32 v98, v233, v241, v246
	v_fma_f32 v99, v233, v243, v247
	v_fmac_f32_e32 v96, v232, v236
	v_mfma_f32_32x32x16_f16 v[16:31], a[96:99], v[164:167], v[16:31]
	ds_read_b128 v[164:167], v193 offset:41984
	global_load_lds_dwordx4 v192, s[44:45] offset:1024 sc1
	v_fmac_f32_e32 v97, v232, v238
	v_fmac_f32_e32 v98, v232, v240
	v_fmac_f32_e32 v99, v232, v242
	v_fma_f32 v112, v235, v237, v244
	v_fma_f32 v113, v235, v239, v245
	v_mfma_f32_32x32x16_f16 v[32:47], a[96:99], v[168:171], v[32:47]
	ds_read_b128 v[168:171], v193 offset:43008
	v_fma_f32 v114, v235, v241, v246
	v_fma_f32 v115, v235, v243, v247
	v_fmac_f32_e32 v112, v234, v236
	v_fmac_f32_e32 v113, v234, v238
	v_fmac_f32_e32 v114, v234, v240
	v_mfma_f32_32x32x16_f16 v[48:63], a[96:99], v[172:175], v[48:63]
	ds_read_b128 v[172:175], v193 offset:44032
	v_fmac_f32_e32 v115, v234, v242
	ds_read_b128 v[236:239], v248 offset:96
	ds_read_b128 v[240:243], v248 offset:112
	ds_read_b128 v[244:247], v248 offset:128
	s_waitcnt lgkmcnt(10)
	v_mfma_f32_32x32x16_f16 v[0:15], a[100:103], v[176:179], v[0:15]
	ds_read_b128 v[176:179], v193 offset:45056
	v_fma_f32 v68, v229, v201, v208
	v_fma_f32 v69, v229, v203, v209
	v_fma_f32 v70, v229, v205, v210
	v_fma_f32 v71, v229, v207, v211
	v_fmac_f32_e32 v68, v228, v200
	s_waitcnt lgkmcnt(10)
	v_mfma_f32_32x32x16_f16 v[16:31], a[100:103], v[180:183], v[16:31]
	ds_read_b128 v[180:183], v193 offset:46080
	global_load_lds_dwordx4 v192, s[44:45] offset:2048 sc1
	v_fmac_f32_e32 v69, v228, v202
	v_fmac_f32_e32 v70, v228, v204
	v_fmac_f32_e32 v71, v228, v206
	v_fma_f32 v84, v231, v201, v208
	v_fma_f32 v85, v231, v203, v209
	s_waitcnt lgkmcnt(10)
	v_mfma_f32_32x32x16_f16 v[32:47], a[100:103], v[184:187], v[32:47]
	ds_read_b128 v[184:187], v193 offset:47104
	v_fma_f32 v86, v231, v205, v210
	s_waitcnt vmcnt(3)
	s_barrier
	v_mov_b32_e32 v199, 2
	s_cmp_eq_u32 s31, 0
	s_cbranch_scc1 .LE_slow18
	global_store_dword v197, v199, s[40:41]
	s_branch .LE_join19

.LE_join19:
	v_fma_f32 v87, v231, v207, v211
	s_waitcnt lgkmcnt(10)
	v_mfma_f32_32x32x16_f16 v[48:63], a[100:103], v[188:191], v[48:63]
	ds_read_b128 v[188:191], v193 offset:48128
	v_fmac_f32_e32 v84, v230, v200
	v_fmac_f32_e32 v85, v230, v202
	v_fmac_f32_e32 v86, v230, v204
	s_waitcnt lgkmcnt(10)
	v_mfma_f32_32x32x16_f16 v[0:15], a[104:107], v[160:163], v[0:15]
	ds_read_b128 v[160:163], v193 offset:49152
	v_fmac_f32_e32 v87, v230, v206
	v_fma_f32 v100, v233, v201, v208
	v_fma_f32 v101, v233, v203, v209
	s_waitcnt lgkmcnt(10)
	v_mfma_f32_32x32x16_f16 v[16:31], a[104:107], v[164:167], v[16:31]
	ds_read_b128 v[164:167], v193 offset:50176
	global_load_lds_dwordx4 v192, s[44:45] offset:3072 sc1
	v_fma_f32 v102, v233, v205, v210
	v_fma_f32 v103, v233, v207, v211
	v_fmac_f32_e32 v100, v232, v200
	s_waitcnt lgkmcnt(10)
	v_mfma_f32_32x32x16_f16 v[32:47], a[104:107], v[168:171], v[32:47]
	ds_read_b128 v[168:171], v193 offset:51200
	v_fmac_f32_e32 v101, v232, v202
	v_fmac_f32_e32 v102, v232, v204
	v_fmac_f32_e32 v103, v232, v206
	s_waitcnt lgkmcnt(10)
	v_mfma_f32_32x32x16_f16 v[48:63], a[104:107], v[172:175], v[48:63]
	ds_read_b128 v[172:175], v193 offset:52224
	v_fma_f32 v116, v235, v201, v208
	v_fma_f32 v117, v235, v203, v209
	v_fma_f32 v118, v235, v205, v210
	s_waitcnt lgkmcnt(7)
	v_mfma_f32_32x32x16_f16 v[0:15], a[108:111], v[176:179], v[0:15]
	ds_read_b128 v[176:179], v193 offset:53248
	v_fma_f32 v119, v235, v207, v211
	v_fmac_f32_e32 v116, v234, v200
	v_fmac_f32_e32 v117, v234, v202
	s_waitcnt lgkmcnt(7)
	v_mfma_f32_32x32x16_f16 v[16:31], a[108:111], v[180:183], v[16:31]
	ds_read_b128 v[180:183], v193 offset:54272
	s_add_u32 s44, s34, 0x29000
	s_addc_u32 s45, s35, 0
	s_mov_b32 m0, s55
	s_nop 0
	global_load_lds_dwordx4 v192, s[44:45] sc1
	v_fmac_f32_e32 v118, v234, v204
	v_fmac_f32_e32 v119, v234, v206
	s_waitcnt lgkmcnt(7)
	v_mfma_f32_32x32x16_f16 v[32:47], a[108:111], v[184:187], v[32:47]
	ds_read_b128 v[184:187], v193 offset:55296
	ds_read_b128 v[200:203], v248 offset:144
	ds_read_b128 v[204:207], v248 offset:160
	ds_read_b128 v[208:211], v248 offset:176
	s_waitcnt lgkmcnt(10)
	v_mfma_f32_32x32x16_f16 v[48:63], a[108:111], v[188:191], v[48:63]
	ds_read_b128 v[188:191], v193 offset:56320
	v_fma_f32 v72, v229, v237, v244
	v_fma_f32 v73, v229, v239, v245
	s_waitcnt lgkmcnt(10)
	v_mfma_f32_32x32x16_f16 v[0:15], a[112:115], v[160:163], v[0:15]
	ds_read_b128 v[160:163], v193 offset:57344
	v_fma_f32 v74, v229, v241, v246
	v_fma_f32 v75, v229, v243, v247
	v_fmac_f32_e32 v72, v228, v236
	s_waitcnt lgkmcnt(10)
	v_mfma_f32_32x32x16_f16 v[16:31], a[112:115], v[164:167], v[16:31]
	ds_read_b128 v[164:167], v193 offset:58368
	global_load_lds_dwordx4 v192, s[44:45] offset:1024 sc1
	v_fmac_f32_e32 v73, v228, v238
	v_fmac_f32_e32 v74, v228, v240
	v_fmac_f32_e32 v75, v228, v242
	s_waitcnt lgkmcnt(10)
	v_mfma_f32_32x32x16_f16 v[32:47], a[112:115], v[168:171], v[32:47]
	ds_read_b128 v[168:171], v193 offset:59392
	v_fma_f32 v88, v231, v237, v244
	v_fma_f32 v89, v231, v239, v245
	v_fma_f32 v90, v231, v241, v246
	s_waitcnt lgkmcnt(10)
	v_mfma_f32_32x32x16_f16 v[48:63], a[112:115], v[172:175], v[48:63]
	ds_read_b128 v[172:175], v193 offset:60416
	v_fma_f32 v91, v231, v243, v247
	v_fmac_f32_e32 v88, v230, v236
	v_fmac_f32_e32 v89, v230, v238
	s_waitcnt lgkmcnt(10)
	v_mfma_f32_32x32x16_f16 v[0:15], a[116:119], v[176:179], v[0:15]
	ds_read_b128 v[176:179], v193 offset:61440
	v_fmac_f32_e32 v90, v230, v240
	v_fmac_f32_e32 v91, v230, v242
	v_fma_f32 v104, v233, v237, v244
	s_waitcnt lgkmcnt(10)
	v_mfma_f32_32x32x16_f16 v[16:31], a[116:119], v[180:183], v[16:31]
	ds_read_b128 v[180:183], v193 offset:62464
	global_load_lds_dwordx4 v192, s[44:45] offset:2048 sc1
	v_fma_f32 v105, v233, v239, v245
	v_fma_f32 v106, v233, v241, v246
	v_fma_f32 v107, v233, v243, v247
	s_waitcnt lgkmcnt(10)
	v_mfma_f32_32x32x16_f16 v[32:47], a[116:119], v[184:187], v[32:47]
	ds_read_b128 v[184:187], v193 offset:63488
	v_fmac_f32_e32 v104, v232, v236
	v_fmac_f32_e32 v105, v232, v238
	v_fmac_f32_e32 v106, v232, v240
	s_waitcnt lgkmcnt(7)
	v_mfma_f32_32x32x16_f16 v[48:63], a[116:119], v[188:191], v[48:63]
	ds_read_b128 v[188:191], v193 offset:64512
	v_fmac_f32_e32 v107, v232, v242
	v_fma_f32 v120, v235, v237, v244
	v_fma_f32 v121, v235, v239, v245
	s_barrier
	s_waitcnt lgkmcnt(7)
	v_mfma_f32_32x32x16_f16 v[0:15], a[120:123], v[160:163], v[0:15]
	ds_read_b128 v[160:163], v192 offset:0
	v_fma_f32 v122, v235, v241, v246
	v_fma_f32 v123, v235, v243, v247
	v_fmac_f32_e32 v120, v234, v236
	s_waitcnt lgkmcnt(7)
	v_mfma_f32_32x32x16_f16 v[16:31], a[120:123], v[164:167], v[16:31]
	ds_read_b128 v[164:167], v192 offset:1024
	global_load_lds_dwordx4 v192, s[44:45] offset:3072 sc1
	v_fmac_f32_e32 v121, v234, v238
	v_fmac_f32_e32 v122, v234, v240
	v_fmac_f32_e32 v123, v234, v242
	s_waitcnt lgkmcnt(7)
	v_mfma_f32_32x32x16_f16 v[32:47], a[120:123], v[168:171], v[32:47]
	ds_read_b128 v[168:171], v192 offset:2048
	v_fma_f32 v76, v229, v201, v208
	v_fma_f32 v77, v229, v203, v209
	s_waitcnt lgkmcnt(7)
	v_mfma_f32_32x32x16_f16 v[48:63], a[120:123], v[172:175], v[48:63]
	ds_read_b128 v[172:175], v192 offset:3072
	v_fma_f32 v78, v229, v205, v210
	v_fma_f32 v79, v229, v207, v211
	v_fmac_f32_e32 v76, v228, v200
	s_waitcnt lgkmcnt(7)
	v_mfma_f32_32x32x16_f16 v[0:15], a[124:127], v[176:179], v[0:15]
	ds_read_b128 v[176:179], v192 offset:4096
	v_fmac_f32_e32 v77, v228, v202
	v_fmac_f32_e32 v78, v228, v204
	v_fmac_f32_e32 v79, v228, v206
	s_waitcnt lgkmcnt(7)
	v_mfma_f32_32x32x16_f16 v[16:31], a[124:127], v[180:183], v[16:31]
	ds_read_b128 v[180:183], v192 offset:5120
	s_add_u32 s44, s34, 0x30000
	s_addc_u32 s45, s35, 0
	s_mov_b32 m0, s56
	s_nop 0
	global_load_lds_dwordx4 v192, s[44:45] sc1
	v_fma_f32 v92, v231, v201, v208
	v_fma_f32 v93, v231, v203, v209
	v_fma_f32 v94, v231, v205, v210
	s_waitcnt lgkmcnt(7)
	v_mfma_f32_32x32x16_f16 v[32:47], a[124:127], v[184:187], v[32:47]
	ds_read_b128 v[184:187], v192 offset:6144
	v_fma_f32 v95, v231, v207, v211
	v_fmac_f32_e32 v92, v230, v200
	v_fmac_f32_e32 v93, v230, v202
	s_waitcnt lgkmcnt(7)
	v_mfma_f32_32x32x16_f16 v[48:63], a[124:127], v[188:191], v[48:63]
	ds_read_b128 v[188:191], v192 offset:7168
	v_fmac_f32_e32 v94, v230, v204
	v_fmac_f32_e32 v95, v230, v206
	v_fma_f32 v108, v233, v201, v208
	s_waitcnt lgkmcnt(7)
	v_mfma_f32_32x32x16_f16 v[0:15], a[128:131], v[160:163], v[0:15]
	ds_read_b128 v[160:163], v192 offset:8192
	v_fma_f32 v109, v233, v203, v209
	v_fma_f32 v110, v233, v205, v210
	v_fma_f32 v111, v233, v207, v211
	s_waitcnt lgkmcnt(7)
	v_mfma_f32_32x32x16_f16 v[16:31], a[128:131], v[164:167], v[16:31]
	ds_read_b128 v[164:167], v192 offset:9216
	global_load_lds_dwordx4 v192, s[44:45] offset:1024 sc1
	v_fmac_f32_e32 v108, v232, v200
	v_fmac_f32_e32 v109, v232, v202
	v_fmac_f32_e32 v110, v232, v204
	s_waitcnt lgkmcnt(7)
	v_mfma_f32_32x32x16_f16 v[32:47], a[128:131], v[168:171], v[32:47]
	ds_read_b128 v[168:171], v192 offset:10240
	v_fmac_f32_e32 v111, v232, v206
	v_fma_f32 v124, v235, v201, v208
	v_fma_f32 v125, v235, v203, v209
	s_waitcnt lgkmcnt(7)
	v_mfma_f32_32x32x16_f16 v[48:63], a[128:131], v[172:175], v[48:63]
	ds_read_b128 v[172:175], v192 offset:11264
	v_fma_f32 v126, v235, v205, v210
	v_fma_f32 v127, v235, v207, v211
	v_fmac_f32_e32 v124, v234, v200
	s_waitcnt lgkmcnt(7)
	v_mfma_f32_32x32x16_f16 v[0:15], a[132:135], v[176:179], v[0:15]
	ds_read_b128 v[176:179], v192 offset:12288
	v_fmac_f32_e32 v125, v234, v202
	v_fmac_f32_e32 v126, v234, v204
	v_fmac_f32_e32 v127, v234, v206
	s_waitcnt lgkmcnt(7)
	v_mfma_f32_32x32x16_f16 v[16:31], a[132:135], v[180:183], v[16:31]
	ds_read_b128 v[180:183], v192 offset:13312
	global_load_lds_dwordx4 v192, s[44:45] offset:2048 sc1
	s_waitcnt lgkmcnt(7)
	v_mfma_f32_32x32x16_f16 v[32:47], a[132:135], v[184:187], v[32:47]
	ds_read_b128 v[184:187], v192 offset:14336
	s_waitcnt lgkmcnt(7)
	v_mfma_f32_32x32x16_f16 v[48:63], a[132:135], v[188:191], v[48:63]
	ds_read_b128 v[188:191], v192 offset:15360
	s_waitcnt lgkmcnt(7)
	v_mfma_f32_32x32x16_f16 v[0:15], a[136:139], v[160:163], v[0:15]
	ds_read_b128 v[160:163], v192 offset:16384
	s_waitcnt lgkmcnt(7)
	v_mfma_f32_32x32x16_f16 v[16:31], a[136:139], v[164:167], v[16:31]
	ds_read_b128 v[164:167], v192 offset:17408
	global_load_lds_dwordx4 v192, s[44:45] offset:3072 sc1
	s_waitcnt lgkmcnt(7)
	v_mfma_f32_32x32x16_f16 v[32:47], a[136:139], v[168:171], v[32:47]
	ds_read_b128 v[168:171], v192 offset:18432
	s_waitcnt lgkmcnt(7)
	v_mfma_f32_32x32x16_f16 v[48:63], a[136:139], v[172:175], v[48:63]
	ds_read_b128 v[172:175], v192 offset:19456
	s_waitcnt lgkmcnt(7)
	v_mfma_f32_32x32x16_f16 v[0:15], a[140:143], v[176:179], v[0:15]
	ds_read_b128 v[176:179], v192 offset:20480
	s_waitcnt lgkmcnt(7)
	v_mfma_f32_32x32x16_f16 v[16:31], a[140:143], v[180:183], v[16:31]
	ds_read_b128 v[180:183], v192 offset:21504
	s_add_u32 s44, s34, 0x31000
	s_addc_u32 s45, s35, 0
	s_mov_b32 m0, s57
	s_nop 0
	global_load_lds_dwordx4 v192, s[44:45] sc1
	s_waitcnt lgkmcnt(7)
	v_mfma_f32_32x32x16_f16 v[32:47], a[140:143], v[184:187], v[32:47]
	ds_read_b128 v[184:187], v192 offset:22528
	s_waitcnt lgkmcnt(7)
	v_mfma_f32_32x32x16_f16 v[48:63], a[140:143], v[188:191], v[48:63]
	ds_read_b128 v[188:191], v192 offset:23552
	s_waitcnt lgkmcnt(7)
	v_mfma_f32_32x32x16_f16 v[0:15], a[144:147], v[160:163], v[0:15]
	ds_read_b128 v[160:163], v192 offset:24576
	s_waitcnt lgkmcnt(7)
	v_mfma_f32_32x32x16_f16 v[16:31], a[144:147], v[164:167], v[16:31]
	ds_read_b128 v[164:167], v192 offset:25600
	global_load_lds_dwordx4 v192, s[44:45] offset:1024 sc1
	s_waitcnt lgkmcnt(7)
	v_mfma_f32_32x32x16_f16 v[32:47], a[144:147], v[168:171], v[32:47]
	ds_read_b128 v[168:171], v192 offset:26624
	s_waitcnt lgkmcnt(7)
	v_mfma_f32_32x32x16_f16 v[48:63], a[144:147], v[172:175], v[48:63]
	ds_read_b128 v[172:175], v192 offset:27648
	s_waitcnt lgkmcnt(7)
	v_mfma_f32_32x32x16_f16 v[0:15], a[148:151], v[176:179], v[0:15]
	ds_read_b128 v[176:179], v192 offset:28672
	s_waitcnt lgkmcnt(7)
	v_mfma_f32_32x32x16_f16 v[16:31], a[148:151], v[180:183], v[16:31]
	ds_read_b128 v[180:183], v192 offset:29696
	global_load_lds_dwordx4 v192, s[44:45] offset:2048 sc1
	s_waitcnt lgkmcnt(7)
	v_mfma_f32_32x32x16_f16 v[32:47], a[148:151], v[184:187], v[32:47]
	ds_read_b128 v[184:187], v192 offset:30720
	s_waitcnt lgkmcnt(7)
	v_mfma_f32_32x32x16_f16 v[48:63], a[148:151], v[188:191], v[48:63]
	ds_read_b128 v[188:191], v192 offset:31744
	s_waitcnt vmcnt(7)
	s_barrier
	s_waitcnt lgkmcnt(7)
	v_mfma_f32_32x32x16_f16 v[0:15], a[152:155], v[160:163], v[0:15]
	ds_read_b128 v[160:163], v192 offset:32768
	s_waitcnt lgkmcnt(7)
	v_mfma_f32_32x32x16_f16 v[16:31], a[152:155], v[164:167], v[16:31]
	ds_read_b128 v[164:167], v192 offset:33792
	global_load_lds_dwordx4 v192, s[44:45] offset:3072 sc1
	s_waitcnt lgkmcnt(7)
	v_mfma_f32_32x32x16_f16 v[32:47], a[152:155], v[168:171], v[32:47]
	ds_read_b128 v[168:171], v192 offset:34816
	s_waitcnt lgkmcnt(7)
	v_mfma_f32_32x32x16_f16 v[48:63], a[152:155], v[172:175], v[48:63]
	ds_read_b128 v[172:175], v192 offset:35840
	s_waitcnt lgkmcnt(7)
	v_mfma_f32_32x32x16_f16 v[0:15], a[156:159], v[176:179], v[0:15]
	ds_read_b128 v[176:179], v192 offset:36864
	s_waitcnt lgkmcnt(7)
	v_mfma_f32_32x32x16_f16 v[16:31], a[156:159], v[180:183], v[16:31]
	ds_read_b128 v[180:183], v192 offset:37888
	s_add_u32 s44, s34, 0x38000
	s_addc_u32 s45, s35, 0
	s_mov_b32 m0, s58
	s_nop 0
	global_load_lds_dwordx4 v192, s[44:45] sc1
	s_waitcnt lgkmcnt(7)
	v_mfma_f32_32x32x16_f16 v[32:47], a[156:159], v[184:187], v[32:47]
	ds_read_b128 v[184:187], v192 offset:38912
	s_waitcnt lgkmcnt(7)
	v_mfma_f32_32x32x16_f16 v[48:63], a[156:159], v[188:191], v[48:63]
	ds_read_b128 v[188:191], v192 offset:39936
	s_lshl_b32 s64, s71, 3
	s_add_u32 s64, s64, s29
	s_lshl_b32 s64, s64, 7
	s_add_u32 s38, s8, s64
	s_addc_u32 s39, s9, 0
	global_load_dword v251, v196, s[38:39] sc1
	s_waitcnt lgkmcnt(7)
	v_mfma_f32_32x32x16_f16 v[0:15], a[160:163], v[160:163], v[0:15]
	ds_read_b128 v[160:163], v192 offset:40960
	s_waitcnt lgkmcnt(7)
	v_mfma_f32_32x32x16_f16 v[16:31], a[160:163], v[164:167], v[16:31]
	ds_read_b128 v[164:167], v192 offset:41984
	global_load_lds_dwordx4 v192, s[44:45] offset:1024 sc1
	s_waitcnt lgkmcnt(7)
	v_mfma_f32_32x32x16_f16 v[32:47], a[160:163], v[168:171], v[32:47]
	ds_read_b128 v[168:171], v192 offset:43008
	s_waitcnt lgkmcnt(7)
	v_mfma_f32_32x32x16_f16 v[48:63], a[160:163], v[172:175], v[48:63]
	ds_read_b128 v[172:175], v192 offset:44032
	s_waitcnt lgkmcnt(7)
	v_mfma_f32_32x32x16_f16 v[0:15], a[164:167], v[176:179], v[0:15]
	ds_read_b128 v[176:179], v192 offset:45056
	s_waitcnt lgkmcnt(7)
	v_mfma_f32_32x32x16_f16 v[16:31], a[164:167], v[180:183], v[16:31]
	ds_read_b128 v[180:183], v192 offset:46080
	global_load_lds_dwordx4 v192, s[44:45] offset:2048 sc1
	s_waitcnt lgkmcnt(7)
	v_mfma_f32_32x32x16_f16 v[32:47], a[164:167], v[184:187], v[32:47]
	ds_read_b128 v[184:187], v192 offset:47104
	s_waitcnt lgkmcnt(7)
	v_mfma_f32_32x32x16_f16 v[48:63], a[164:167], v[188:191], v[48:63]
	ds_read_b128 v[188:191], v192 offset:48128
	s_waitcnt lgkmcnt(7)
	v_mfma_f32_32x32x16_f16 v[0:15], a[168:171], v[160:163], v[0:15]
	ds_read_b128 v[160:163], v192 offset:49152
	s_waitcnt lgkmcnt(7)
	v_mfma_f32_32x32x16_f16 v[16:31], a[168:171], v[164:167], v[16:31]
	ds_read_b128 v[164:167], v192 offset:50176
	global_load_lds_dwordx4 v192, s[44:45] offset:3072 sc1
	s_waitcnt lgkmcnt(7)
	v_mfma_f32_32x32x16_f16 v[32:47], a[168:171], v[168:171], v[32:47]
	ds_read_b128 v[168:171], v192 offset:51200
	s_waitcnt lgkmcnt(7)
	v_mfma_f32_32x32x16_f16 v[48:63], a[168:171], v[172:175], v[48:63]
	ds_read_b128 v[172:175], v192 offset:52224
	s_waitcnt lgkmcnt(7)
	v_mfma_f32_32x32x16_f16 v[0:15], a[172:175], v[176:179], v[0:15]
	ds_read_b128 v[176:179], v192 offset:53248
	s_waitcnt lgkmcnt(7)
	v_mfma_f32_32x32x16_f16 v[16:31], a[172:175], v[180:183], v[16:31]
	ds_read_b128 v[180:183], v192 offset:54272
	s_add_u32 s44, s34, 0x39000
	s_addc_u32 s45, s35, 0
	s_mov_b32 m0, s59
	s_nop 0
	global_load_lds_dwordx4 v192, s[44:45] sc1
	s_waitcnt lgkmcnt(7)
	v_mfma_f32_32x32x16_f16 v[32:47], a[172:175], v[184:187], v[32:47]
	ds_read_b128 v[184:187], v192 offset:55296
	s_waitcnt lgkmcnt(7)
	v_mfma_f32_32x32x16_f16 v[48:63], a[172:175], v[188:191], v[48:63]
	ds_read_b128 v[188:191], v192 offset:56320
	s_waitcnt lgkmcnt(7)
	v_mfma_f32_32x32x16_f16 v[0:15], a[176:179], v[160:163], v[0:15]
	ds_read_b128 v[160:163], v192 offset:57344
	s_waitcnt lgkmcnt(7)
	v_mfma_f32_32x32x16_f16 v[16:31], a[176:179], v[164:167], v[16:31]
	ds_read_b128 v[164:167], v192 offset:58368
	global_load_lds_dwordx4 v192, s[44:45] offset:1024 sc1
	s_waitcnt lgkmcnt(7)
	v_mfma_f32_32x32x16_f16 v[32:47], a[176:179], v[168:171], v[32:47]
	ds_read_b128 v[168:171], v192 offset:59392
	s_waitcnt lgkmcnt(7)
	v_mfma_f32_32x32x16_f16 v[48:63], a[176:179], v[172:175], v[48:63]
	ds_read_b128 v[172:175], v192 offset:60416
	s_waitcnt lgkmcnt(7)
	v_mfma_f32_32x32x16_f16 v[0:15], a[180:183], v[176:179], v[0:15]
	ds_read_b128 v[176:179], v192 offset:61440
	s_waitcnt lgkmcnt(7)
	v_mfma_f32_32x32x16_f16 v[16:31], a[180:183], v[180:183], v[16:31]
	ds_read_b128 v[180:183], v192 offset:62464
	global_load_lds_dwordx4 v192, s[44:45] offset:2048 sc1
	s_waitcnt lgkmcnt(7)
	v_mfma_f32_32x32x16_f16 v[32:47], a[180:183], v[184:187], v[32:47]
	ds_read_b128 v[184:187], v192 offset:63488
	s_waitcnt lgkmcnt(7)
	v_mfma_f32_32x32x16_f16 v[48:63], a[180:183], v[188:191], v[48:63]
	ds_read_b128 v[188:191], v192 offset:64512
	s_waitcnt vmcnt(8)
	s_barrier
	s_waitcnt lgkmcnt(7)
	v_mfma_f32_32x32x16_f16 v[0:15], a[184:187], v[160:163], v[0:15]
	ds_read_b128 v[160:163], v193 offset:0
	s_waitcnt lgkmcnt(7)
	v_mfma_f32_32x32x16_f16 v[16:31], a[184:187], v[164:167], v[16:31]
	ds_read_b128 v[164:167], v193 offset:1024
	global_load_lds_dwordx4 v192, s[44:45] offset:3072 sc1
	s_waitcnt lgkmcnt(7)
	v_mfma_f32_32x32x16_f16 v[32:47], a[184:187], v[168:171], v[32:47]
	ds_read_b128 v[168:171], v193 offset:2048
	s_waitcnt lgkmcnt(7)
	v_mfma_f32_32x32x16_f16 v[48:63], a[184:187], v[172:175], v[48:63]
	ds_read_b128 v[172:175], v193 offset:3072
	s_waitcnt lgkmcnt(7)
	v_mfma_f32_32x32x16_f16 v[0:15], a[188:191], v[176:179], v[0:15]
	ds_read_b128 v[176:179], v193 offset:4096
	s_waitcnt lgkmcnt(7)
	v_mfma_f32_32x32x16_f16 v[16:31], a[188:191], v[180:183], v[16:31]
	ds_read_b128 v[180:183], v193 offset:5120
	s_waitcnt vmcnt(7)
	v_cmp_gt_u32_e32 vcc, 2, v251
	s_cbranch_vccz .LE_tok20
.LE_tpoll21:
	s_cmp_eq_u32 s48, 0
	s_cbranch_scc1 .LE_tok20
	s_sub_u32 s48, s48, 1
	s_sleep 1
	global_load_dword v251, v196, s[38:39] sc1
	s_waitcnt vmcnt(0)
	v_cmp_gt_u32_e32 vcc, 2, v251
	s_cbranch_vccnz .LE_tpoll21
.LE_tok20:
	s_and_b32 s64, s71, 1
	s_lshl_b32 s64, s64, 22
	s_add_u32 s64, s64, s49
	s_add_u32 s64, s64, 0x40000
	s_add_u32 s34, s6, s64
	s_addc_u32 s35, s7, 0
	s_add_u32 s44, s34, 0x0
	s_addc_u32 s45, s35, 0
	s_mov_b32 m0, s52
	s_nop 0
	global_load_lds_dwordx4 v192, s[44:45] sc1
	s_waitcnt lgkmcnt(7)
	v_mfma_f32_32x32x16_f16 v[32:47], a[188:191], v[184:187], v[32:47]
	ds_read_b128 v[184:187], v193 offset:6144
	s_waitcnt lgkmcnt(7)
	v_mfma_f32_32x32x16_f16 v[48:63], a[188:191], v[188:191], v[48:63]
	ds_read_b128 v[188:191], v193 offset:7168
	s_waitcnt lgkmcnt(7)
	v_mfma_f32_32x32x16_f16 v[0:15], a[192:195], v[160:163], v[0:15]
	ds_read_b128 v[160:163], v193 offset:8192
	s_waitcnt lgkmcnt(7)
	v_mfma_f32_32x32x16_f16 v[16:31], a[192:195], v[164:167], v[16:31]
	ds_read_b128 v[164:167], v193 offset:9216
	global_load_lds_dwordx4 v192, s[44:45] offset:1024 sc1
	s_waitcnt lgkmcnt(7)
	v_mfma_f32_32x32x16_f16 v[32:47], a[192:195], v[168:171], v[32:47]
	ds_read_b128 v[168:171], v193 offset:10240
	s_waitcnt lgkmcnt(7)
	v_mfma_f32_32x32x16_f16 v[48:63], a[192:195], v[172:175], v[48:63]
	ds_read_b128 v[172:175], v193 offset:11264
	s_waitcnt lgkmcnt(7)
	v_mfma_f32_32x32x16_f16 v[0:15], a[196:199], v[176:179], v[0:15]
	ds_read_b128 v[176:179], v193 offset:12288
	s_waitcnt lgkmcnt(7)
	v_mfma_f32_32x32x16_f16 v[16:31], a[196:199], v[180:183], v[16:31]
	ds_read_b128 v[180:183], v193 offset:13312
	global_load_lds_dwordx4 v192, s[44:45] offset:2048 sc1
	s_waitcnt lgkmcnt(7)
	v_mfma_f32_32x32x16_f16 v[32:47], a[196:199], v[184:187], v[32:47]
	ds_read_b128 v[184:187], v193 offset:14336
	s_waitcnt lgkmcnt(7)
	v_mfma_f32_32x32x16_f16 v[48:63], a[196:199], v[188:191], v[48:63]
	ds_read_b128 v[188:191], v193 offset:15360
	s_waitcnt lgkmcnt(7)
	v_mfma_f32_32x32x16_f16 v[0:15], a[200:203], v[160:163], v[0:15]
	ds_read_b128 v[160:163], v193 offset:16384
	s_waitcnt lgkmcnt(7)
	v_mfma_f32_32x32x16_f16 v[16:31], a[200:203], v[164:167], v[16:31]
	ds_read_b128 v[164:167], v193 offset:17408
	global_load_lds_dwordx4 v192, s[44:45] offset:3072 sc1
	s_waitcnt lgkmcnt(7)
	v_mfma_f32_32x32x16_f16 v[32:47], a[200:203], v[168:171], v[32:47]
	ds_read_b128 v[168:171], v193 offset:18432
	s_waitcnt lgkmcnt(7)
	v_mfma_f32_32x32x16_f16 v[48:63], a[200:203], v[172:175], v[48:63]
	ds_read_b128 v[172:175], v193 offset:19456
	s_waitcnt lgkmcnt(7)
	v_mfma_f32_32x32x16_f16 v[0:15], a[204:207], v[176:179], v[0:15]
	ds_read_b128 v[176:179], v193 offset:20480
	s_waitcnt lgkmcnt(7)
	v_mfma_f32_32x32x16_f16 v[16:31], a[204:207], v[180:183], v[16:31]
	ds_read_b128 v[180:183], v193 offset:21504
	s_add_u32 s44, s34, 0x1000
	s_addc_u32 s45, s35, 0
	s_mov_b32 m0, s53
	s_nop 0
	global_load_lds_dwordx4 v192, s[44:45] sc1
	s_waitcnt lgkmcnt(7)
	v_mfma_f32_32x32x16_f16 v[32:47], a[204:207], v[184:187], v[32:47]
	ds_read_b128 v[184:187], v193 offset:22528
	s_waitcnt lgkmcnt(7)
	v_mfma_f32_32x32x16_f16 v[48:63], a[204:207], v[188:191], v[48:63]
	ds_read_b128 v[188:191], v193 offset:23552
	s_waitcnt lgkmcnt(7)
	v_mfma_f32_32x32x16_f16 v[0:15], a[208:211], v[160:163], v[0:15]
	ds_read_b128 v[160:163], v193 offset:24576
	s_waitcnt lgkmcnt(7)
	v_mfma_f32_32x32x16_f16 v[16:31], a[208:211], v[164:167], v[16:31]
	ds_read_b128 v[164:167], v193 offset:25600
	global_load_lds_dwordx4 v192, s[44:45] offset:1024 sc1
	s_waitcnt lgkmcnt(7)
	v_mfma_f32_32x32x16_f16 v[32:47], a[208:211], v[168:171], v[32:47]
	ds_read_b128 v[168:171], v193 offset:26624
	s_waitcnt lgkmcnt(7)
	v_mfma_f32_32x32x16_f16 v[48:63], a[208:211], v[172:175], v[48:63]
	ds_read_b128 v[172:175], v193 offset:27648
	s_waitcnt lgkmcnt(7)
	v_mfma_f32_32x32x16_f16 v[0:15], a[212:215], v[176:179], v[0:15]
	ds_read_b128 v[176:179], v193 offset:28672
	s_waitcnt lgkmcnt(7)
	v_mfma_f32_32x32x16_f16 v[16:31], a[212:215], v[180:183], v[16:31]
	ds_read_b128 v[180:183], v193 offset:29696
	global_load_lds_dwordx4 v192, s[44:45] offset:2048 sc1
	s_waitcnt lgkmcnt(7)
	v_mfma_f32_32x32x16_f16 v[32:47], a[212:215], v[184:187], v[32:47]
	ds_read_b128 v[184:187], v193 offset:30720
	s_waitcnt lgkmcnt(7)
	v_mfma_f32_32x32x16_f16 v[48:63], a[212:215], v[188:191], v[48:63]
	ds_read_b128 v[188:191], v193 offset:31744
	s_waitcnt vmcnt(7)
	s_barrier
	s_waitcnt lgkmcnt(7)
	v_mfma_f32_32x32x16_f16 v[0:15], a[216:219], v[160:163], v[0:15]
	ds_read_b128 v[160:163], v193 offset:32768
	s_waitcnt lgkmcnt(7)
	v_mfma_f32_32x32x16_f16 v[16:31], a[216:219], v[164:167], v[16:31]
	ds_read_b128 v[164:167], v193 offset:33792
	global_load_lds_dwordx4 v192, s[44:45] offset:3072 sc1
	s_waitcnt lgkmcnt(7)
	v_mfma_f32_32x32x16_f16 v[32:47], a[216:219], v[168:171], v[32:47]
	ds_read_b128 v[168:171], v193 offset:34816
	s_waitcnt lgkmcnt(7)
	v_mfma_f32_32x32x16_f16 v[48:63], a[216:219], v[172:175], v[48:63]
	ds_read_b128 v[172:175], v193 offset:35840
	s_waitcnt lgkmcnt(7)
	v_mfma_f32_32x32x16_f16 v[0:15], a[220:223], v[176:179], v[0:15]
	ds_read_b128 v[176:179], v193 offset:36864
	s_waitcnt lgkmcnt(7)
	v_mfma_f32_32x32x16_f16 v[16:31], a[220:223], v[180:183], v[16:31]
	ds_read_b128 v[180:183], v193 offset:37888
	s_add_u32 s44, s34, 0x8000
	s_addc_u32 s45, s35, 0
	s_mov_b32 m0, s54
	s_nop 0
	global_load_lds_dwordx4 v192, s[44:45] sc1
	s_waitcnt lgkmcnt(7)
	v_mfma_f32_32x32x16_f16 v[32:47], a[220:223], v[184:187], v[32:47]
	ds_read_b128 v[184:187], v193 offset:38912
	s_waitcnt lgkmcnt(7)
	v_mfma_f32_32x32x16_f16 v[48:63], a[220:223], v[188:191], v[48:63]
	ds_read_b128 v[188:191], v193 offset:39936
	s_waitcnt lgkmcnt(7)
	v_mfma_f32_32x32x16_f16 v[0:15], a[224:227], v[160:163], v[0:15]
	ds_read_b128 v[160:163], v193 offset:40960
	s_waitcnt lgkmcnt(7)
	v_mfma_f32_32x32x16_f16 v[16:31], a[224:227], v[164:167], v[16:31]
	ds_read_b128 v[164:167], v193 offset:41984
	global_load_lds_dwordx4 v192, s[44:45] offset:1024 sc1
	s_waitcnt lgkmcnt(7)
	v_mfma_f32_32x32x16_f16 v[32:47], a[224:227], v[168:171], v[32:47]
	ds_read_b128 v[168:171], v193 offset:43008
	s_waitcnt lgkmcnt(7)
	v_mfma_f32_32x32x16_f16 v[48:63], a[224:227], v[172:175], v[48:63]
	ds_read_b128 v[172:175], v193 offset:44032
	s_waitcnt lgkmcnt(7)
	v_mfma_f32_32x32x16_f16 v[0:15], a[228:231], v[176:179], v[0:15]
	ds_read_b128 v[176:179], v193 offset:45056
	s_waitcnt lgkmcnt(7)
	v_mfma_f32_32x32x16_f16 v[16:31], a[228:231], v[180:183], v[16:31]
	ds_read_b128 v[180:183], v193 offset:46080
	global_load_lds_dwordx4 v192, s[44:45] offset:2048 sc1
	s_waitcnt lgkmcnt(7)
	v_mfma_f32_32x32x16_f16 v[32:47], a[228:231], v[184:187], v[32:47]
	ds_read_b128 v[184:187], v193 offset:47104
	s_waitcnt lgkmcnt(7)
	v_mfma_f32_32x32x16_f16 v[48:63], a[228:231], v[188:191], v[48:63]
	ds_read_b128 v[188:191], v193 offset:48128
	s_waitcnt lgkmcnt(7)
	v_mfma_f32_32x32x16_f16 v[0:15], a[232:235], v[160:163], v[0:15]
	ds_read_b128 v[160:163], v193 offset:49152
	s_waitcnt lgkmcnt(7)
	v_mfma_f32_32x32x16_f16 v[16:31], a[232:235], v[164:167], v[16:31]
	ds_read_b128 v[164:167], v193 offset:50176
	global_load_lds_dwordx4 v192, s[44:45] offset:3072 sc1
	s_waitcnt lgkmcnt(7)
	v_mfma_f32_32x32x16_f16 v[32:47], a[232:235], v[168:171], v[32:47]
	ds_read_b128 v[168:171], v193 offset:51200
	s_waitcnt lgkmcnt(7)
	v_mfma_f32_32x32x16_f16 v[48:63], a[232:235], v[172:175], v[48:63]
	ds_read_b128 v[172:175], v193 offset:52224
	s_waitcnt lgkmcnt(7)
	v_mfma_f32_32x32x16_f16 v[0:15], a[236:239], v[176:179], v[0:15]
	ds_read_b128 v[176:179], v193 offset:53248
	s_waitcnt lgkmcnt(7)
	v_mfma_f32_32x32x16_f16 v[16:31], a[236:239], v[180:183], v[16:31]
	ds_read_b128 v[180:183], v193 offset:54272
	s_add_u32 s44, s34, 0x9000
	s_addc_u32 s45, s35, 0
	s_mov_b32 m0, s55
	s_nop 0
	global_load_lds_dwordx4 v192, s[44:45] sc1
	s_waitcnt lgkmcnt(7)
	v_mfma_f32_32x32x16_f16 v[32:47], a[236:239], v[184:187], v[32:47]
	ds_read_b128 v[184:187], v193 offset:55296
	s_waitcnt lgkmcnt(7)
	v_mfma_f32_32x32x16_f16 v[48:63], a[236:239], v[188:191], v[48:63]
	ds_read_b128 v[188:191], v193 offset:56320
	s_waitcnt lgkmcnt(7)
	v_mfma_f32_32x32x16_f16 v[0:15], a[240:243], v[160:163], v[0:15]
	ds_read_b128 v[160:163], v193 offset:57344
	s_waitcnt lgkmcnt(7)
	v_mfma_f32_32x32x16_f16 v[16:31], a[240:243], v[164:167], v[16:31]
	ds_read_b128 v[164:167], v193 offset:58368
	global_load_lds_dwordx4 v192, s[44:45] offset:1024 sc1
	s_waitcnt lgkmcnt(7)
	v_mfma_f32_32x32x16_f16 v[32:47], a[240:243], v[168:171], v[32:47]
	ds_read_b128 v[168:171], v193 offset:59392
	s_waitcnt lgkmcnt(7)
	v_mfma_f32_32x32x16_f16 v[48:63], a[240:243], v[172:175], v[48:63]
	ds_read_b128 v[172:175], v193 offset:60416
	s_waitcnt lgkmcnt(7)
	v_mfma_f32_32x32x16_f16 v[0:15], a[244:247], v[176:179], v[0:15]
	ds_read_b128 v[176:179], v193 offset:61440
	s_waitcnt lgkmcnt(7)
	v_mfma_f32_32x32x16_f16 v[16:31], a[244:247], v[180:183], v[16:31]
	ds_read_b128 v[180:183], v193 offset:62464
	global_load_lds_dwordx4 v192, s[44:45] offset:2048 sc1
	s_waitcnt lgkmcnt(7)
	v_mfma_f32_32x32x16_f16 v[32:47], a[244:247], v[184:187], v[32:47]
	ds_read_b128 v[184:187], v193 offset:63488
	s_waitcnt lgkmcnt(7)
	v_mfma_f32_32x32x16_f16 v[48:63], a[244:247], v[188:191], v[48:63]
	ds_read_b128 v[188:191], v193 offset:64512
	s_waitcnt vmcnt(7)
	s_barrier
	s_waitcnt lgkmcnt(7)
	v_mfma_f32_32x32x16_f16 v[0:15], a[248:251], v[160:163], v[0:15]
	ds_read_b128 v[160:163], v192 offset:0
	s_waitcnt lgkmcnt(7)
	v_mfma_f32_32x32x16_f16 v[16:31], a[248:251], v[164:167], v[16:31]
	ds_read_b128 v[164:167], v192 offset:1024
	global_load_lds_dwordx4 v192, s[44:45] offset:3072 sc1
	s_waitcnt lgkmcnt(7)
	v_mfma_f32_32x32x16_f16 v[32:47], a[248:251], v[168:171], v[32:47]
	ds_read_b128 v[168:171], v192 offset:2048
	s_waitcnt lgkmcnt(7)
	v_mfma_f32_32x32x16_f16 v[48:63], a[248:251], v[172:175], v[48:63]
	ds_read_b128 v[172:175], v192 offset:3072
	s_waitcnt lgkmcnt(7)
	v_mfma_f32_32x32x16_f16 v[0:15], a[252:255], v[176:179], v[0:15]
	ds_read_b128 v[176:179], v192 offset:4096
	s_waitcnt lgkmcnt(7)
	v_mfma_f32_32x32x16_f16 v[16:31], a[252:255], v[180:183], v[16:31]
	ds_read_b128 v[180:183], v192 offset:5120
	s_add_u32 s44, s34, 0x10000
	s_addc_u32 s45, s35, 0
	s_mov_b32 m0, s56
	s_nop 0
	global_load_lds_dwordx4 v192, s[44:45] sc1
	s_waitcnt lgkmcnt(7)
	v_mfma_f32_32x32x16_f16 v[32:47], a[252:255], v[184:187], v[32:47]
	ds_read_b128 v[184:187], v192 offset:6144
	s_waitcnt lgkmcnt(7)
	v_mfma_f32_32x32x16_f16 v[48:63], a[252:255], v[188:191], v[48:63]
	ds_read_b128 v[188:191], v192 offset:7168
	s_and_b32 s64, s33, 1
	s_lshl_b32 s64, s64, 22
	s_add_u32 s64, s64, s50
	s_add_u32 s36, s6, s64
	s_addc_u32 s37, s7, 0
	s_lshl_b32 s64, s33, 3
	s_add_u32 s64, s64, s29
	s_lshl_b32 s64, s64, 5
	s_add_u32 s64, s64, s30
	s_lshl_b32 s64, s64, 2
	s_add_u32 s40, s8, s64
	s_addc_u32 s41, s9, 0
	s_add_u32 s61, s33, 1
	s_min_u32 s61, s61, s60
	s_lshl_b32 s64, s61, 11
	s_lshl_b32 s65, s29, 8
	s_add_u32 s64, s64, s65
	s_lshl_b32 s64, s64, 3
	s_add_u32 s42, s12, s64
	s_addc_u32 s43, s13, 0
	s_nop 11
	global_load_dwordx2 v[228:229], v249, s[42:43] offset:0
	global_load_dwordx2 v[230:231], v249, s[42:43] offset:256
	global_load_dwordx2 v[232:233], v249, s[42:43] offset:512
	global_load_dwordx2 v[234:235], v249, s[42:43] offset:768
	v_exp_f32_e32 v200, v0
	v_exp_f32_e32 v201, v1
	v_exp_f32_e32 v202, v2
	v_exp_f32_e32 v203, v3
	v_exp_f32_e32 v204, v4
	v_exp_f32_e32 v205, v5
	v_exp_f32_e32 v206, v6
	v_exp_f32_e32 v207, v7
	v_exp_f32_e32 v208, v8
	v_exp_f32_e32 v209, v9
	v_exp_f32_e32 v210, v10
	v_exp_f32_e32 v211, v11
	v_exp_f32_e32 v212, v12
	v_exp_f32_e32 v213, v13
	v_exp_f32_e32 v214, v14
	v_exp_f32_e32 v215, v15
	v_add_f32_e32 v200, 1.0, v200
	v_add_f32_e32 v201, 1.0, v201
	v_add_f32_e32 v202, 1.0, v202
	v_add_f32_e32 v203, 1.0, v203
	v_add_f32_e32 v204, 1.0, v204
	v_add_f32_e32 v205, 1.0, v205
	v_add_f32_e32 v206, 1.0, v206
	v_add_f32_e32 v207, 1.0, v207
	v_add_f32_e32 v208, 1.0, v208
	v_add_f32_e32 v209, 1.0, v209
	v_add_f32_e32 v210, 1.0, v210
	v_add_f32_e32 v211, 1.0, v211
	v_add_f32_e32 v212, 1.0, v212
	v_add_f32_e32 v213, 1.0, v213
	v_add_f32_e32 v214, 1.0, v214
	v_add_f32_e32 v215, 1.0, v215
	v_rcp_f32_e32 v200, v200
	v_rcp_f32_e32 v201, v201
	v_rcp_f32_e32 v202, v202
	v_rcp_f32_e32 v203, v203
	v_rcp_f32_e32 v204, v204
	v_rcp_f32_e32 v205, v205
	v_rcp_f32_e32 v206, v206
	v_rcp_f32_e32 v207, v207
	v_rcp_f32_e32 v208, v208
	v_rcp_f32_e32 v209, v209
	v_rcp_f32_e32 v210, v210
	v_rcp_f32_e32 v211, v211
	v_rcp_f32_e32 v212, v212
	v_rcp_f32_e32 v213, v213
	v_rcp_f32_e32 v214, v214
	v_rcp_f32_e32 v215, v215
	v_fmamk_f32 v208, v208, 0xc0b8aa3b, v198
	v_fmamk_f32 v209, v209, 0xc0b8aa3b, v198
	v_fmamk_f32 v210, v210, 0xc0b8aa3b, v198
	v_fmamk_f32 v211, v211, 0xc0b8aa3b, v198
	v_mul_f32_e32 v204, v204, v128
	v_mul_f32_e32 v205, v205, v129
	v_mul_f32_e32 v206, v206, v130
	v_mul_f32_e32 v207, v207, v131
	v_fma_f32 v128, v200, v208, v204
	v_fma_f32 v129, v201, v209, v205
	v_fma_f32 v130, v202, v210, v206
	v_fma_f32 v131, v203, v211, v207
	v_exp_f32_e32 v200, v128
	v_exp_f32_e32 v201, v129
	v_exp_f32_e32 v202, v130
	v_exp_f32_e32 v203, v131
	s_waitcnt lgkmcnt(7)
	v_mfma_f32_32x32x16_f16 v[64:79], a[0:3], v[160:163], v[64:79]
	ds_read_b128 v[160:163], v192 offset:8192
	v_add_f32_e32 v200, 1.0, v200
	v_add_f32_e32 v201, 1.0, v201
	v_add_f32_e32 v202, 1.0, v202
	v_add_f32_e32 v203, 1.0, v203
	s_waitcnt lgkmcnt(7)
	v_mfma_f32_32x32x16_f16 v[80:95], a[0:3], v[164:167], v[80:95]
	ds_read_b128 v[164:167], v192 offset:9216
	global_load_lds_dwordx4 v192, s[44:45] offset:1024 sc1
	v_rcp_f32_e32 v200, v200
	v_rcp_f32_e32 v201, v201
	s_waitcnt lgkmcnt(7)
	v_mfma_f32_32x32x16_f16 v[96:111], a[0:3], v[168:171], v[96:111]
	ds_read_b128 v[168:171], v192 offset:10240
	v_rcp_f32_e32 v202, v202
	v_rcp_f32_e32 v203, v203
	v_fma_f32 v200, v200, 2.0, -1.0
	s_waitcnt lgkmcnt(7)
	v_mfma_f32_32x32x16_f16 v[112:127], a[0:3], v[172:175], v[112:127]
	ds_read_b128 v[172:175], v192 offset:11264
	v_fma_f32 v201, v201, 2.0, -1.0
	v_fma_f32 v202, v202, 2.0, -1.0
	v_fma_f32 v203, v203, 2.0, -1.0
	v_mul_f32_e32 v216, v212, v200
	v_mul_f32_e32 v217, v213, v201
	s_waitcnt lgkmcnt(7)
	v_mfma_f32_32x32x16_f16 v[64:79], a[4:7], v[176:179], v[64:79]
	ds_read_b128 v[176:179], v192 offset:12288
	v_mul_f32_e32 v218, v214, v202
	v_mul_f32_e32 v219, v215, v203
	v_cvt_pk_f16_f32 v220, v216, v217
	v_cvt_pk_f16_f32 v221, v218, v219
	s_waitcnt lgkmcnt(7)
	v_mfma_f32_32x32x16_f16 v[80:95], a[4:7], v[180:183], v[80:95]
	ds_read_b128 v[180:183], v192 offset:13312
	global_load_lds_dwordx4 v192, s[44:45] offset:2048 sc1
	s_cmp_lg_u32 s33, s60
	s_cbranch_scc1 .LE_nht22
	s_add_u32 s46, s62, 0x0
	s_addc_u32 s47, s63, 0
	global_store_dwordx4 v250, v[216:219], s[46:47]
	s_waitcnt vmcnt(0)
.LE_nht22:
	v_exp_f32_e32 v200, v16
	s_waitcnt lgkmcnt(7)
	v_mfma_f32_32x32x16_f16 v[96:111], a[4:7], v[184:187], v[96:111]
	ds_read_b128 v[184:187], v192 offset:14336
	v_exp_f32_e32 v201, v17
	v_exp_f32_e32 v202, v18
	s_waitcnt lgkmcnt(7)
	v_mfma_f32_32x32x16_f16 v[112:127], a[4:7], v[188:191], v[112:127]
	ds_read_b128 v[188:191], v192 offset:15360
	v_exp_f32_e32 v203, v19
	v_exp_f32_e32 v204, v20
	s_waitcnt lgkmcnt(7)
	v_mfma_f32_32x32x16_f16 v[64:79], a[8:11], v[160:163], v[64:79]
	ds_read_b128 v[160:163], v192 offset:16384
	v_exp_f32_e32 v205, v21
	v_exp_f32_e32 v206, v22
	s_waitcnt lgkmcnt(7)
	v_mfma_f32_32x32x16_f16 v[80:95], a[8:11], v[164:167], v[80:95]
	ds_read_b128 v[164:167], v192 offset:17408
	global_load_lds_dwordx4 v192, s[44:45] offset:3072 sc1
	v_exp_f32_e32 v207, v23
	v_exp_f32_e32 v208, v24
	s_waitcnt lgkmcnt(7)
	v_mfma_f32_32x32x16_f16 v[96:111], a[8:11], v[168:171], v[96:111]
	ds_read_b128 v[168:171], v192 offset:18432
	v_exp_f32_e32 v209, v25
	v_exp_f32_e32 v210, v26
	s_waitcnt lgkmcnt(7)
	v_mfma_f32_32x32x16_f16 v[112:127], a[8:11], v[172:175], v[112:127]
	ds_read_b128 v[172:175], v192 offset:19456
	v_exp_f32_e32 v211, v27
	v_exp_f32_e32 v212, v28
	s_waitcnt lgkmcnt(7)
	v_mfma_f32_32x32x16_f16 v[64:79], a[12:15], v[176:179], v[64:79]
	ds_read_b128 v[176:179], v192 offset:20480
	v_exp_f32_e32 v213, v29
	v_exp_f32_e32 v214, v30
	s_waitcnt lgkmcnt(7)
	v_mfma_f32_32x32x16_f16 v[80:95], a[12:15], v[180:183], v[80:95]
	ds_read_b128 v[180:183], v192 offset:21504
	s_add_u32 s44, s34, 0x11000
	s_addc_u32 s45, s35, 0
	s_mov_b32 m0, s57
	s_nop 0
	global_load_lds_dwordx4 v192, s[44:45] sc1
	v_exp_f32_e32 v215, v31
	v_add_f32_e32 v200, 1.0, v200
	v_add_f32_e32 v201, 1.0, v201
	v_add_f32_e32 v202, 1.0, v202
	s_waitcnt lgkmcnt(7)
	v_mfma_f32_32x32x16_f16 v[96:111], a[12:15], v[184:187], v[96:111]
	ds_read_b128 v[184:187], v192 offset:22528
	v_add_f32_e32 v203, 1.0, v203
	v_add_f32_e32 v204, 1.0, v204
	v_add_f32_e32 v205, 1.0, v205
	v_add_f32_e32 v206, 1.0, v206
	v_add_f32_e32 v207, 1.0, v207
	s_waitcnt lgkmcnt(7)
	v_mfma_f32_32x32x16_f16 v[112:127], a[12:15], v[188:191], v[112:127]
	ds_read_b128 v[188:191], v192 offset:23552
	v_add_f32_e32 v208, 1.0, v208
	v_add_f32_e32 v209, 1.0, v209
	v_add_f32_e32 v210, 1.0, v210
	v_add_f32_e32 v211, 1.0, v211
	v_add_f32_e32 v212, 1.0, v212
	s_waitcnt lgkmcnt(7)
	v_mfma_f32_32x32x16_f16 v[64:79], a[16:19], v[160:163], v[64:79]
	ds_read_b128 v[160:163], v192 offset:24576
	v_add_f32_e32 v213, 1.0, v213
	v_add_f32_e32 v214, 1.0, v214
	v_add_f32_e32 v215, 1.0, v215
	v_rcp_f32_e32 v200, v200
	s_waitcnt lgkmcnt(7)
	v_mfma_f32_32x32x16_f16 v[80:95], a[16:19], v[164:167], v[80:95]
	ds_read_b128 v[164:167], v192 offset:25600
	global_load_lds_dwordx4 v192, s[44:45] offset:1024 sc1
	v_rcp_f32_e32 v201, v201
	v_rcp_f32_e32 v202, v202
	s_waitcnt lgkmcnt(7)
	v_mfma_f32_32x32x16_f16 v[96:111], a[16:19], v[168:171], v[96:111]
	ds_read_b128 v[168:171], v192 offset:26624
	v_rcp_f32_e32 v203, v203
	v_rcp_f32_e32 v204, v204
	s_waitcnt lgkmcnt(7)
	v_mfma_f32_32x32x16_f16 v[112:127], a[16:19], v[172:175], v[112:127]
	ds_read_b128 v[172:175], v192 offset:27648
	v_rcp_f32_e32 v205, v205
	v_rcp_f32_e32 v206, v206
	s_waitcnt lgkmcnt(7)
	v_mfma_f32_32x32x16_f16 v[64:79], a[20:23], v[176:179], v[64:79]
	ds_read_b128 v[176:179], v192 offset:28672
	v_rcp_f32_e32 v207, v207
	v_rcp_f32_e32 v208, v208
	s_waitcnt lgkmcnt(7)
	v_mfma_f32_32x32x16_f16 v[80:95], a[20:23], v[180:183], v[80:95]
	ds_read_b128 v[180:183], v192 offset:29696
	global_load_lds_dwordx4 v192, s[44:45] offset:2048 sc1
	v_rcp_f32_e32 v209, v209
	v_rcp_f32_e32 v210, v210
	s_waitcnt lgkmcnt(7)
	v_mfma_f32_32x32x16_f16 v[96:111], a[20:23], v[184:187], v[96:111]
	ds_read_b128 v[184:187], v192 offset:30720
	v_rcp_f32_e32 v211, v211
	v_rcp_f32_e32 v212, v212
	s_waitcnt lgkmcnt(7)
	v_mfma_f32_32x32x16_f16 v[112:127], a[20:23], v[188:191], v[112:127]
	ds_read_b128 v[188:191], v192 offset:31744
	v_rcp_f32_e32 v213, v213
	v_rcp_f32_e32 v214, v214
	s_waitcnt vmcnt(11)
	s_barrier
	s_waitcnt lgkmcnt(7)
	v_mfma_f32_32x32x16_f16 v[64:79], a[24:27], v[160:163], v[64:79]
	ds_read_b128 v[160:163], v192 offset:32768
	v_rcp_f32_e32 v215, v215
	v_fmamk_f32 v208, v208, 0xc0b8aa3b, v198
	v_fmamk_f32 v209, v209, 0xc0b8aa3b, v198
	v_fmamk_f32 v210, v210, 0xc0b8aa3b, v198
	s_waitcnt lgkmcnt(7)
	v_mfma_f32_32x32x16_f16 v[80:95], a[24:27], v[164:167], v[80:95]
	ds_read_b128 v[164:167], v192 offset:33792
	global_load_lds_dwordx4 v192, s[44:45] offset:3072 sc1
	v_fmamk_f32 v211, v211, 0xc0b8aa3b, v198
	v_mul_f32_e32 v204, v204, v132
	v_mul_f32_e32 v205, v205, v133
	v_mul_f32_e32 v206, v206, v134
	v_mul_f32_e32 v207, v207, v135
	s_waitcnt lgkmcnt(7)
	v_mfma_f32_32x32x16_f16 v[96:111], a[24:27], v[168:171], v[96:111]
	ds_read_b128 v[168:171], v192 offset:34816
	v_fma_f32 v132, v200, v208, v204
	v_fma_f32 v133, v201, v209, v205
	v_fma_f32 v134, v202, v210, v206
	v_fma_f32 v135, v203, v211, v207
	s_waitcnt lgkmcnt(7)
	v_mfma_f32_32x32x16_f16 v[112:127], a[24:27], v[172:175], v[112:127]
	ds_read_b128 v[172:175], v192 offset:35840
	v_exp_f32_e32 v200, v132
	v_exp_f32_e32 v201, v133
	s_waitcnt lgkmcnt(7)
	v_mfma_f32_32x32x16_f16 v[64:79], a[28:31], v[176:179], v[64:79]
	ds_read_b128 v[176:179], v192 offset:36864
	v_exp_f32_e32 v202, v134
	v_exp_f32_e32 v203, v135
	v_add_f32_e32 v200, 1.0, v200
	s_waitcnt lgkmcnt(7)
	v_mfma_f32_32x32x16_f16 v[80:95], a[28:31], v[180:183], v[80:95]
	ds_read_b128 v[180:183], v192 offset:37888
	s_add_u32 s44, s34, 0x18000
	s_addc_u32 s45, s35, 0
	s_mov_b32 m0, s58
	s_nop 0
	global_load_lds_dwordx4 v192, s[44:45] sc1
	v_add_f32_e32 v201, 1.0, v201
	v_add_f32_e32 v202, 1.0, v202
	v_add_f32_e32 v203, 1.0, v203
	v_rcp_f32_e32 v200, v200
	s_waitcnt lgkmcnt(7)
	v_mfma_f32_32x32x16_f16 v[96:111], a[28:31], v[184:187], v[96:111]
	ds_read_b128 v[184:187], v192 offset:38912
	v_rcp_f32_e32 v201, v201
	v_rcp_f32_e32 v202, v202
	s_waitcnt lgkmcnt(7)
	v_mfma_f32_32x32x16_f16 v[112:127], a[28:31], v[188:191], v[112:127]
	ds_read_b128 v[188:191], v192 offset:39936
	v_rcp_f32_e32 v203, v203
	v_fma_f32 v200, v200, 2.0, -1.0
	v_fma_f32 v201, v201, 2.0, -1.0
	v_fma_f32 v202, v202, 2.0, -1.0
	s_waitcnt lgkmcnt(7)
	v_mfma_f32_32x32x16_f16 v[64:79], a[32:35], v[160:163], v[64:79]
	ds_read_b128 v[160:163], v192 offset:40960
	v_fma_f32 v203, v203, 2.0, -1.0
	v_mul_f32_e32 v216, v212, v200
	v_mul_f32_e32 v217, v213, v201
	v_mul_f32_e32 v218, v214, v202
	v_mul_f32_e32 v219, v215, v203
	s_waitcnt lgkmcnt(7)
	v_mfma_f32_32x32x16_f16 v[80:95], a[32:35], v[164:167], v[80:95]
	ds_read_b128 v[164:167], v192 offset:41984
	global_load_lds_dwordx4 v192, s[44:45] offset:1024 sc1
	v_cvt_pk_f16_f32 v222, v216, v217
	v_cvt_pk_f16_f32 v223, v218, v219
	s_cmp_lg_u32 s33, s60
	s_cbranch_scc1 .LE_nht23
	s_add_u32 s46, s62, 0x20000
	s_addc_u32 s47, s63, 0
	global_store_dwordx4 v250, v[216:219], s[46:47]
	s_waitcnt vmcnt(0)
.LE_nht23:
	s_waitcnt lgkmcnt(7)
	v_mfma_f32_32x32x16_f16 v[96:111], a[32:35], v[168:171], v[96:111]
	ds_read_b128 v[168:171], v192 offset:43008
	s_nop 1
	v_permlane32_swap_b32_e32 v220, v222
	v_permlane32_swap_b32_e32 v221, v223
	s_cmp_eq_u32 s31, 0
	s_cbranch_scc1 .LE_slow24
	global_store_dwordx4 v195, v[220:223], s[36:37] offset:0
	s_branch .LE_join25

.LE_join25:
	s_waitcnt lgkmcnt(7)
	v_mfma_f32_32x32x16_f16 v[112:127], a[32:35], v[172:175], v[112:127]
	ds_read_b128 v[172:175], v192 offset:44032
	v_exp_f32_e32 v200, v32
	v_exp_f32_e32 v201, v33
	s_waitcnt lgkmcnt(7)
	v_mfma_f32_32x32x16_f16 v[64:79], a[36:39], v[176:179], v[64:79]
	ds_read_b128 v[176:179], v192 offset:45056
	v_exp_f32_e32 v202, v34
	v_exp_f32_e32 v203, v35
	s_waitcnt lgkmcnt(7)
	v_mfma_f32_32x32x16_f16 v[80:95], a[36:39], v[180:183], v[80:95]
	ds_read_b128 v[180:183], v192 offset:46080
	global_load_lds_dwordx4 v192, s[44:45] offset:2048 sc1
	v_exp_f32_e32 v204, v36
	v_exp_f32_e32 v205, v37
	s_waitcnt lgkmcnt(7)
	v_mfma_f32_32x32x16_f16 v[96:111], a[36:39], v[184:187], v[96:111]
	ds_read_b128 v[184:187], v192 offset:47104
	v_exp_f32_e32 v206, v38
	v_exp_f32_e32 v207, v39
	s_waitcnt lgkmcnt(7)
	v_mfma_f32_32x32x16_f16 v[112:127], a[36:39], v[188:191], v[112:127]
	ds_read_b128 v[188:191], v192 offset:48128
	v_exp_f32_e32 v208, v40
	v_exp_f32_e32 v209, v41
	s_waitcnt lgkmcnt(7)
	v_mfma_f32_32x32x16_f16 v[64:79], a[40:43], v[160:163], v[64:79]
	ds_read_b128 v[160:163], v192 offset:49152
	v_exp_f32_e32 v210, v42
	v_exp_f32_e32 v211, v43
	s_waitcnt lgkmcnt(7)
	v_mfma_f32_32x32x16_f16 v[80:95], a[40:43], v[164:167], v[80:95]
	ds_read_b128 v[164:167], v192 offset:50176
	global_load_lds_dwordx4 v192, s[44:45] offset:3072 sc1
	v_exp_f32_e32 v212, v44
	v_exp_f32_e32 v213, v45
	s_waitcnt lgkmcnt(7)
	v_mfma_f32_32x32x16_f16 v[96:111], a[40:43], v[168:171], v[96:111]
	ds_read_b128 v[168:171], v192 offset:51200
	v_exp_f32_e32 v214, v46
	v_exp_f32_e32 v215, v47
	v_add_f32_e32 v200, 1.0, v200
	s_waitcnt lgkmcnt(7)
	v_mfma_f32_32x32x16_f16 v[112:127], a[40:43], v[172:175], v[112:127]
	ds_read_b128 v[172:175], v192 offset:52224
	v_add_f32_e32 v201, 1.0, v201
	v_add_f32_e32 v202, 1.0, v202
	v_add_f32_e32 v203, 1.0, v203
	v_add_f32_e32 v204, 1.0, v204
	v_add_f32_e32 v205, 1.0, v205
	s_waitcnt lgkmcnt(7)
	v_mfma_f32_32x32x16_f16 v[64:79], a[44:47], v[176:179], v[64:79]
	ds_read_b128 v[176:179], v192 offset:53248
	v_add_f32_e32 v206, 1.0, v206
	v_add_f32_e32 v207, 1.0, v207
	v_add_f32_e32 v208, 1.0, v208
	v_add_f32_e32 v209, 1.0, v209
	v_add_f32_e32 v210, 1.0, v210
	s_waitcnt lgkmcnt(7)
	v_mfma_f32_32x32x16_f16 v[80:95], a[44:47], v[180:183], v[80:95]
	ds_read_b128 v[180:183], v192 offset:54272
	s_add_u32 s44, s34, 0x19000
	s_addc_u32 s45, s35, 0
	s_mov_b32 m0, s59
	s_nop 0
	global_load_lds_dwordx4 v192, s[44:45] sc1
	v_add_f32_e32 v211, 1.0, v211
	v_add_f32_e32 v212, 1.0, v212
	v_add_f32_e32 v213, 1.0, v213
	v_add_f32_e32 v214, 1.0, v214
	v_add_f32_e32 v215, 1.0, v215
	s_waitcnt lgkmcnt(7)
	v_mfma_f32_32x32x16_f16 v[96:111], a[44:47], v[184:187], v[96:111]
	ds_read_b128 v[184:187], v192 offset:55296
	v_rcp_f32_e32 v200, v200
	v_rcp_f32_e32 v201, v201
	s_waitcnt lgkmcnt(7)
	v_mfma_f32_32x32x16_f16 v[112:127], a[44:47], v[188:191], v[112:127]
	ds_read_b128 v[188:191], v192 offset:56320
	v_rcp_f32_e32 v202, v202
	v_rcp_f32_e32 v203, v203
	s_waitcnt lgkmcnt(7)
	v_mfma_f32_32x32x16_f16 v[64:79], a[48:51], v[160:163], v[64:79]
	ds_read_b128 v[160:163], v192 offset:57344
	v_rcp_f32_e32 v204, v204
	v_rcp_f32_e32 v205, v205
	s_waitcnt lgkmcnt(7)
	v_mfma_f32_32x32x16_f16 v[80:95], a[48:51], v[164:167], v[80:95]
	ds_read_b128 v[164:167], v192 offset:58368
	global_load_lds_dwordx4 v192, s[44:45] offset:1024 sc1
	v_rcp_f32_e32 v206, v206
	v_rcp_f32_e32 v207, v207
	s_waitcnt lgkmcnt(7)
	v_mfma_f32_32x32x16_f16 v[96:111], a[48:51], v[168:171], v[96:111]
	ds_read_b128 v[168:171], v192 offset:59392
	v_rcp_f32_e32 v208, v208
	v_rcp_f32_e32 v209, v209
	s_waitcnt lgkmcnt(7)
	v_mfma_f32_32x32x16_f16 v[112:127], a[48:51], v[172:175], v[112:127]
	ds_read_b128 v[172:175], v192 offset:60416
	v_rcp_f32_e32 v210, v210
	v_rcp_f32_e32 v211, v211
	s_waitcnt lgkmcnt(7)
	v_mfma_f32_32x32x16_f16 v[64:79], a[52:55], v[176:179], v[64:79]
	ds_read_b128 v[176:179], v192 offset:61440
	v_rcp_f32_e32 v212, v212
	v_rcp_f32_e32 v213, v213
	s_waitcnt lgkmcnt(7)
	v_mfma_f32_32x32x16_f16 v[80:95], a[52:55], v[180:183], v[80:95]
	ds_read_b128 v[180:183], v192 offset:62464
	global_load_lds_dwordx4 v192, s[44:45] offset:2048 sc1
	v_rcp_f32_e32 v214, v214
	v_rcp_f32_e32 v215, v215
	v_fmamk_f32 v208, v208, 0xc0b8aa3b, v198
	s_waitcnt lgkmcnt(7)
	v_mfma_f32_32x32x16_f16 v[96:111], a[52:55], v[184:187], v[96:111]
	ds_read_b128 v[184:187], v192 offset:63488
	v_fmamk_f32 v209, v209, 0xc0b8aa3b, v198
	v_fmamk_f32 v210, v210, 0xc0b8aa3b, v198
	v_fmamk_f32 v211, v211, 0xc0b8aa3b, v198
	v_mul_f32_e32 v204, v204, v136
	v_mul_f32_e32 v205, v205, v137
	s_waitcnt lgkmcnt(7)
	v_mfma_f32_32x32x16_f16 v[112:127], a[52:55], v[188:191], v[112:127]
	ds_read_b128 v[188:191], v192 offset:64512
	v_mul_f32_e32 v206, v206, v138
	v_mul_f32_e32 v207, v207, v139
	v_fma_f32 v136, v200, v208, v204
	v_fma_f32 v137, v201, v209, v205
	v_fma_f32 v138, v202, v210, v206
	s_waitcnt vmcnt(8)
	s_barrier
	s_waitcnt lgkmcnt(7)
	v_mfma_f32_32x32x16_f16 v[64:79], a[56:59], v[160:163], v[64:79]
	ds_read_b128 v[160:163], v193 offset:0
	v_fma_f32 v139, v203, v211, v207
	v_exp_f32_e32 v200, v136
	v_exp_f32_e32 v201, v137
	s_waitcnt lgkmcnt(7)
	v_mfma_f32_32x32x16_f16 v[80:95], a[56:59], v[164:167], v[80:95]
	ds_read_b128 v[164:167], v193 offset:1024
	global_load_lds_dwordx4 v192, s[44:45] offset:3072 sc1
	v_exp_f32_e32 v202, v138
	v_exp_f32_e32 v203, v139
	v_add_f32_e32 v200, 1.0, v200
	s_waitcnt lgkmcnt(7)
	v_mfma_f32_32x32x16_f16 v[96:111], a[56:59], v[168:171], v[96:111]
	ds_read_b128 v[168:171], v193 offset:2048
	v_add_f32_e32 v201, 1.0, v201
	v_add_f32_e32 v202, 1.0, v202
	v_add_f32_e32 v203, 1.0, v203
	v_rcp_f32_e32 v200, v200
	s_waitcnt lgkmcnt(7)
	v_mfma_f32_32x32x16_f16 v[112:127], a[56:59], v[172:175], v[112:127]
	ds_read_b128 v[172:175], v193 offset:3072
	v_rcp_f32_e32 v201, v201
	v_rcp_f32_e32 v202, v202
	s_waitcnt lgkmcnt(7)
	v_mfma_f32_32x32x16_f16 v[64:79], a[60:63], v[176:179], v[64:79]
	ds_read_b128 v[176:179], v193 offset:4096
	v_rcp_f32_e32 v203, v203
	v_fma_f32 v200, v200, 2.0, -1.0
	v_fma_f32 v201, v201, 2.0, -1.0
	v_fma_f32 v202, v202, 2.0, -1.0
	s_waitcnt lgkmcnt(7)
	v_mfma_f32_32x32x16_f16 v[80:95], a[60:63], v[180:183], v[80:95]
	ds_read_b128 v[180:183], v193 offset:5120
	s_add_u32 s44, s34, 0x20000
	s_addc_u32 s45, s35, 0
	s_mov_b32 m0, s52
	s_nop 0
	global_load_lds_dwordx4 v192, s[44:45] sc1
	v_fma_f32 v203, v203, 2.0, -1.0
	v_mul_f32_e32 v216, v212, v200
	v_mul_f32_e32 v217, v213, v201
	v_mul_f32_e32 v218, v214, v202
	v_mul_f32_e32 v219, v215, v203
	s_waitcnt lgkmcnt(7)
	v_mfma_f32_32x32x16_f16 v[96:111], a[60:63], v[184:187], v[96:111]
	ds_read_b128 v[184:187], v193 offset:6144
	v_cvt_pk_f16_f32 v224, v216, v217
	v_cvt_pk_f16_f32 v225, v218, v219
	s_cmp_lg_u32 s33, s60
	s_cbranch_scc1 .LE_nht26
	s_add_u32 s46, s62, 0x40000
	s_addc_u32 s47, s63, 0
	global_store_dwordx4 v250, v[216:219], s[46:47]
	s_waitcnt vmcnt(0)
.LE_nht26:
	s_waitcnt lgkmcnt(7)
	v_mfma_f32_32x32x16_f16 v[112:127], a[60:63], v[188:191], v[112:127]
	ds_read_b128 v[188:191], v193 offset:7168
	v_exp_f32_e32 v200, v48
	v_exp_f32_e32 v201, v49
	s_waitcnt lgkmcnt(7)
	v_mfma_f32_32x32x16_f16 v[64:79], a[64:67], v[160:163], v[64:79]
	ds_read_b128 v[160:163], v193 offset:8192
	v_exp_f32_e32 v202, v50
	v_exp_f32_e32 v203, v51
	s_waitcnt lgkmcnt(7)
	v_mfma_f32_32x32x16_f16 v[80:95], a[64:67], v[164:167], v[80:95]
	ds_read_b128 v[164:167], v193 offset:9216
	global_load_lds_dwordx4 v192, s[44:45] offset:1024 sc1
	v_exp_f32_e32 v204, v52
	v_exp_f32_e32 v205, v53
	s_waitcnt lgkmcnt(7)
	v_mfma_f32_32x32x16_f16 v[96:111], a[64:67], v[168:171], v[96:111]
	ds_read_b128 v[168:171], v193 offset:10240
	v_exp_f32_e32 v206, v54
	v_exp_f32_e32 v207, v55
	s_waitcnt lgkmcnt(7)
	v_mfma_f32_32x32x16_f16 v[112:127], a[64:67], v[172:175], v[112:127]
	ds_read_b128 v[172:175], v193 offset:11264
	v_exp_f32_e32 v208, v56
	v_exp_f32_e32 v209, v57
	s_waitcnt lgkmcnt(7)
	v_mfma_f32_32x32x16_f16 v[64:79], a[68:71], v[176:179], v[64:79]
	ds_read_b128 v[176:179], v193 offset:12288
	v_exp_f32_e32 v210, v58
	v_exp_f32_e32 v211, v59
	s_waitcnt lgkmcnt(7)
	v_mfma_f32_32x32x16_f16 v[80:95], a[68:71], v[180:183], v[80:95]
	ds_read_b128 v[180:183], v193 offset:13312
	global_load_lds_dwordx4 v192, s[44:45] offset:2048 sc1
	v_exp_f32_e32 v212, v60
	v_exp_f32_e32 v213, v61
	s_waitcnt lgkmcnt(7)
	v_mfma_f32_32x32x16_f16 v[96:111], a[68:71], v[184:187], v[96:111]
	ds_read_b128 v[184:187], v193 offset:14336
	v_exp_f32_e32 v214, v62
	v_exp_f32_e32 v215, v63
	v_add_f32_e32 v200, 1.0, v200
	s_waitcnt lgkmcnt(7)
	v_mfma_f32_32x32x16_f16 v[112:127], a[68:71], v[188:191], v[112:127]
	ds_read_b128 v[188:191], v193 offset:15360
	v_add_f32_e32 v201, 1.0, v201
	v_add_f32_e32 v202, 1.0, v202
	v_add_f32_e32 v203, 1.0, v203
	v_add_f32_e32 v204, 1.0, v204
	v_add_f32_e32 v205, 1.0, v205
	s_waitcnt lgkmcnt(7)
	v_mfma_f32_32x32x16_f16 v[64:79], a[72:75], v[160:163], v[64:79]
	ds_read_b128 v[160:163], v193 offset:16384
	v_add_f32_e32 v206, 1.0, v206
	v_add_f32_e32 v207, 1.0, v207
	v_add_f32_e32 v208, 1.0, v208
	v_add_f32_e32 v209, 1.0, v209
	v_add_f32_e32 v210, 1.0, v210
	s_waitcnt lgkmcnt(7)
	v_mfma_f32_32x32x16_f16 v[80:95], a[72:75], v[164:167], v[80:95]
	ds_read_b128 v[164:167], v193 offset:17408
	global_load_lds_dwordx4 v192, s[44:45] offset:3072 sc1
	v_add_f32_e32 v211, 1.0, v211
	v_add_f32_e32 v212, 1.0, v212
	v_add_f32_e32 v213, 1.0, v213
	v_add_f32_e32 v214, 1.0, v214
	v_add_f32_e32 v215, 1.0, v215
	s_waitcnt lgkmcnt(7)
	v_mfma_f32_32x32x16_f16 v[96:111], a[72:75], v[168:171], v[96:111]
	ds_read_b128 v[168:171], v193 offset:18432
	v_rcp_f32_e32 v200, v200
	v_rcp_f32_e32 v201, v201
	s_waitcnt lgkmcnt(7)
	v_mfma_f32_32x32x16_f16 v[112:127], a[72:75], v[172:175], v[112:127]
	ds_read_b128 v[172:175], v193 offset:19456
	v_rcp_f32_e32 v202, v202
	v_rcp_f32_e32 v203, v203
	s_waitcnt lgkmcnt(7)
	v_mfma_f32_32x32x16_f16 v[64:79], a[76:79], v[176:179], v[64:79]
	ds_read_b128 v[176:179], v193 offset:20480
	v_rcp_f32_e32 v204, v204
	v_rcp_f32_e32 v205, v205
	s_waitcnt lgkmcnt(7)
	v_mfma_f32_32x32x16_f16 v[80:95], a[76:79], v[180:183], v[80:95]
	ds_read_b128 v[180:183], v193 offset:21504
	s_add_u32 s44, s34, 0x21000
	s_addc_u32 s45, s35, 0
	s_mov_b32 m0, s53
	s_nop 0
	global_load_lds_dwordx4 v192, s[44:45] sc1
	v_rcp_f32_e32 v206, v206
	v_rcp_f32_e32 v207, v207
	s_waitcnt lgkmcnt(7)
	v_mfma_f32_32x32x16_f16 v[96:111], a[76:79], v[184:187], v[96:111]
	ds_read_b128 v[184:187], v193 offset:22528
	v_rcp_f32_e32 v208, v208
	v_rcp_f32_e32 v209, v209
	s_waitcnt lgkmcnt(7)
	v_mfma_f32_32x32x16_f16 v[112:127], a[76:79], v[188:191], v[112:127]
	ds_read_b128 v[188:191], v193 offset:23552
	v_rcp_f32_e32 v210, v210
	v_rcp_f32_e32 v211, v211
	s_waitcnt lgkmcnt(7)
	v_mfma_f32_32x32x16_f16 v[64:79], a[80:83], v[160:163], v[64:79]
	ds_read_b128 v[160:163], v193 offset:24576
	v_rcp_f32_e32 v212, v212
	v_rcp_f32_e32 v213, v213
	s_waitcnt lgkmcnt(7)
	v_mfma_f32_32x32x16_f16 v[80:95], a[80:83], v[164:167], v[80:95]
	ds_read_b128 v[164:167], v193 offset:25600
	global_load_lds_dwordx4 v192, s[44:45] offset:1024 sc1
	v_rcp_f32_e32 v214, v214
	v_rcp_f32_e32 v215, v215
	v_fmamk_f32 v208, v208, 0xc0b8aa3b, v198
	s_waitcnt lgkmcnt(7)
	v_mfma_f32_32x32x16_f16 v[96:111], a[80:83], v[168:171], v[96:111]
	ds_read_b128 v[168:171], v193 offset:26624
	v_fmamk_f32 v209, v209, 0xc0b8aa3b, v198
	v_fmamk_f32 v210, v210, 0xc0b8aa3b, v198
	v_fmamk_f32 v211, v211, 0xc0b8aa3b, v198
	v_mul_f32_e32 v204, v204, v140
	v_mul_f32_e32 v205, v205, v141
	s_waitcnt lgkmcnt(7)
	v_mfma_f32_32x32x16_f16 v[112:127], a[80:83], v[172:175], v[112:127]
	ds_read_b128 v[172:175], v193 offset:27648
	v_mul_f32_e32 v206, v206, v142
	v_mul_f32_e32 v207, v207, v143
	v_fma_f32 v140, v200, v208, v204
	v_fma_f32 v141, v201, v209, v205
	v_fma_f32 v142, v202, v210, v206
	s_waitcnt lgkmcnt(7)
	v_mfma_f32_32x32x16_f16 v[64:79], a[84:87], v[176:179], v[64:79]
	ds_read_b128 v[176:179], v193 offset:28672
	v_fma_f32 v143, v203, v211, v207
	v_exp_f32_e32 v200, v140
	v_exp_f32_e32 v201, v141
	s_waitcnt lgkmcnt(7)
	v_mfma_f32_32x32x16_f16 v[80:95], a[84:87], v[180:183], v[80:95]
	ds_read_b128 v[180:183], v193 offset:29696
	global_load_lds_dwordx4 v192, s[44:45] offset:2048 sc1
	v_exp_f32_e32 v202, v142
	v_exp_f32_e32 v203, v143
	v_add_f32_e32 v200, 1.0, v200
	s_waitcnt lgkmcnt(7)
	v_mfma_f32_32x32x16_f16 v[96:111], a[84:87], v[184:187], v[96:111]
	ds_read_b128 v[184:187], v193 offset:30720
	v_add_f32_e32 v201, 1.0, v201
	v_add_f32_e32 v202, 1.0, v202
	v_add_f32_e32 v203, 1.0, v203
	v_rcp_f32_e32 v200, v200
	s_waitcnt lgkmcnt(7)
	v_mfma_f32_32x32x16_f16 v[112:127], a[84:87], v[188:191], v[112:127]
	ds_read_b128 v[188:191], v193 offset:31744
	v_rcp_f32_e32 v201, v201
	v_rcp_f32_e32 v202, v202
	s_waitcnt vmcnt(7)
	s_barrier
	s_waitcnt lgkmcnt(7)
	v_mfma_f32_32x32x16_f16 v[64:79], a[88:91], v[160:163], v[64:79]
	ds_read_b128 v[160:163], v193 offset:32768
	v_rcp_f32_e32 v203, v203
	v_fma_f32 v200, v200, 2.0, -1.0
	v_fma_f32 v201, v201, 2.0, -1.0
	v_fma_f32 v202, v202, 2.0, -1.0
	s_waitcnt lgkmcnt(7)
	v_mfma_f32_32x32x16_f16 v[80:95], a[88:91], v[164:167], v[80:95]
	ds_read_b128 v[164:167], v193 offset:33792
	global_load_lds_dwordx4 v192, s[44:45] offset:3072 sc1
	v_fma_f32 v203, v203, 2.0, -1.0
	v_mul_f32_e32 v216, v212, v200
	v_mul_f32_e32 v217, v213, v201
	v_mul_f32_e32 v218, v214, v202
	v_mul_f32_e32 v219, v215, v203
	s_waitcnt lgkmcnt(7)
	v_mfma_f32_32x32x16_f16 v[96:111], a[88:91], v[168:171], v[96:111]
	ds_read_b128 v[168:171], v193 offset:34816
	v_cvt_pk_f16_f32 v226, v216, v217
	v_cvt_pk_f16_f32 v227, v218, v219
	s_cmp_lg_u32 s33, s60
	s_cbranch_scc1 .LE_nht27
	s_add_u32 s46, s62, 0x60000
	s_addc_u32 s47, s63, 0
	global_store_dwordx4 v250, v[216:219], s[46:47]
	s_waitcnt vmcnt(0)
.LE_nht27:
	s_waitcnt lgkmcnt(7)
	v_mfma_f32_32x32x16_f16 v[112:127], a[88:91], v[172:175], v[112:127]
	ds_read_b128 v[172:175], v193 offset:35840
	s_nop 1
	v_permlane32_swap_b32_e32 v224, v226
	v_permlane32_swap_b32_e32 v225, v227
	s_cmp_eq_u32 s31, 0
	s_cbranch_scc1 .LE_slow28
	global_store_dwordx4 v195, v[224:227], s[36:37] offset:2048
	s_branch .LE_join29

.LE_join29:
	s_waitcnt lgkmcnt(7)
	v_mfma_f32_32x32x16_f16 v[64:79], a[92:95], v[176:179], v[64:79]
	ds_read_b128 v[176:179], v193 offset:36864
	ds_read_b128 v[236:239], v248 offset:0
	ds_read_b128 v[240:243], v248 offset:16
	ds_read_b128 v[244:247], v248 offset:32
	s_waitcnt lgkmcnt(10)
	v_mfma_f32_32x32x16_f16 v[80:95], a[92:95], v[180:183], v[80:95]
	ds_read_b128 v[180:183], v193 offset:37888
	s_add_u32 s44, s34, 0x28000
	s_addc_u32 s45, s35, 0
	s_mov_b32 m0, s54
	s_nop 0
	global_load_lds_dwordx4 v192, s[44:45] sc1
	ds_read_b128 v[200:203], v248 offset:48
	ds_read_b128 v[204:207], v248 offset:64
	ds_read_b128 v[208:211], v248 offset:80
	s_waitcnt lgkmcnt(4)
	v_fma_f32 v0, v229, v237, v244
	v_mfma_f32_32x32x16_f16 v[96:111], a[92:95], v[184:187], v[96:111]
	ds_read_b128 v[184:187], v193 offset:38912
	v_fma_f32 v1, v229, v239, v245
	v_fma_f32 v2, v229, v241, v246
	v_fma_f32 v3, v229, v243, v247
	v_fmac_f32_e32 v0, v228, v236
	v_fmac_f32_e32 v1, v228, v238
	v_mfma_f32_32x32x16_f16 v[112:127], a[92:95], v[188:191], v[112:127]
	ds_read_b128 v[188:191], v193 offset:39936
	v_fmac_f32_e32 v2, v228, v240
	v_fmac_f32_e32 v3, v228, v242
	v_fma_f32 v16, v231, v237, v244
	v_fma_f32 v17, v231, v239, v245
	v_fma_f32 v18, v231, v241, v246
	v_mfma_f32_32x32x16_f16 v[64:79], a[96:99], v[160:163], v[64:79]
	ds_read_b128 v[160:163], v193 offset:40960
	v_fma_f32 v19, v231, v243, v247
	v_fmac_f32_e32 v16, v230, v236
	v_fmac_f32_e32 v17, v230, v238
	v_fmac_f32_e32 v18, v230, v240
	v_fmac_f32_e32 v19, v230, v242
	v_mfma_f32_32x32x16_f16 v[80:95], a[96:99], v[164:167], v[80:95]
	ds_read_b128 v[164:167], v193 offset:41984
	global_load_lds_dwordx4 v192, s[44:45] offset:1024 sc1
	v_fma_f32 v32, v233, v237, v244
	v_fma_f32 v33, v233, v239, v245
	v_fma_f32 v34, v233, v241, v246
	v_fma_f32 v35, v233, v243, v247
	v_fmac_f32_e32 v32, v232, v236
	v_mfma_f32_32x32x16_f16 v[96:111], a[96:99], v[168:171], v[96:111]
	ds_read_b128 v[168:171], v193 offset:43008
	v_fmac_f32_e32 v33, v232, v238
	v_fmac_f32_e32 v34, v232, v240
	v_fmac_f32_e32 v35, v232, v242
	v_fma_f32 v48, v235, v237, v244
	v_fma_f32 v49, v235, v239, v245
	v_mfma_f32_32x32x16_f16 v[112:127], a[96:99], v[172:175], v[112:127]
	ds_read_b128 v[172:175], v193 offset:44032
	v_fma_f32 v50, v235, v241, v246
	v_fma_f32 v51, v235, v243, v247
	v_fmac_f32_e32 v48, v234, v236
	v_fmac_f32_e32 v49, v234, v238
	v_fmac_f32_e32 v50, v234, v240
	v_mfma_f32_32x32x16_f16 v[64:79], a[100:103], v[176:179], v[64:79]
	ds_read_b128 v[176:179], v193 offset:45056
	v_fmac_f32_e32 v51, v234, v242
	ds_read_b128 v[236:239], v248 offset:96
	ds_read_b128 v[240:243], v248 offset:112
	ds_read_b128 v[244:247], v248 offset:128
	s_waitcnt lgkmcnt(10)
	v_mfma_f32_32x32x16_f16 v[80:95], a[100:103], v[180:183], v[80:95]
	ds_read_b128 v[180:183], v193 offset:46080
	global_load_lds_dwordx4 v192, s[44:45] offset:2048 sc1
	v_fma_f32 v4, v229, v201, v208
	v_fma_f32 v5, v229, v203, v209
	v_fma_f32 v6, v229, v205, v210
	v_fma_f32 v7, v229, v207, v211
	v_fmac_f32_e32 v4, v228, v200
	s_waitcnt lgkmcnt(10)
	v_mfma_f32_32x32x16_f16 v[96:111], a[100:103], v[184:187], v[96:111]
	ds_read_b128 v[184:187], v193 offset:47104
	v_fmac_f32_e32 v5, v228, v202
	v_fmac_f32_e32 v6, v228, v204
	v_fmac_f32_e32 v7, v228, v206
	v_fma_f32 v20, v231, v201, v208
	v_fma_f32 v21, v231, v203, v209
	s_waitcnt lgkmcnt(10)
	v_mfma_f32_32x32x16_f16 v[112:127], a[100:103], v[188:191], v[112:127]
	ds_read_b128 v[188:191], v193 offset:48128
	v_fma_f32 v22, v231, v205, v210
	s_waitcnt vmcnt(3)
	s_barrier
	v_mov_b32_e32 v199, 1
	s_cmp_eq_u32 s31, 0
	s_cbranch_scc1 .LE_slow30
	global_store_dword v197, v199, s[40:41]
	s_branch .LE_join31

.LE_join31:
	v_fma_f32 v23, v231, v207, v211
	s_waitcnt lgkmcnt(10)
	v_mfma_f32_32x32x16_f16 v[64:79], a[104:107], v[160:163], v[64:79]
	ds_read_b128 v[160:163], v193 offset:49152
	v_fmac_f32_e32 v20, v230, v200
	v_fmac_f32_e32 v21, v230, v202
	v_fmac_f32_e32 v22, v230, v204
	s_waitcnt lgkmcnt(10)
	v_mfma_f32_32x32x16_f16 v[80:95], a[104:107], v[164:167], v[80:95]
	ds_read_b128 v[164:167], v193 offset:50176
	global_load_lds_dwordx4 v192, s[44:45] offset:3072 sc1
	v_fmac_f32_e32 v23, v230, v206
	v_fma_f32 v36, v233, v201, v208
	v_fma_f32 v37, v233, v203, v209
	s_waitcnt lgkmcnt(10)
	v_mfma_f32_32x32x16_f16 v[96:111], a[104:107], v[168:171], v[96:111]
	ds_read_b128 v[168:171], v193 offset:51200
	v_fma_f32 v38, v233, v205, v210
	v_fma_f32 v39, v233, v207, v211
	v_fmac_f32_e32 v36, v232, v200
	s_waitcnt lgkmcnt(10)
	v_mfma_f32_32x32x16_f16 v[112:127], a[104:107], v[172:175], v[112:127]
	ds_read_b128 v[172:175], v193 offset:52224
	v_fmac_f32_e32 v37, v232, v202
	v_fmac_f32_e32 v38, v232, v204
	v_fmac_f32_e32 v39, v232, v206
	s_waitcnt lgkmcnt(10)
	v_mfma_f32_32x32x16_f16 v[64:79], a[108:111], v[176:179], v[64:79]
	ds_read_b128 v[176:179], v193 offset:53248
	v_fma_f32 v52, v235, v201, v208
	v_fma_f32 v53, v235, v203, v209
	v_fma_f32 v54, v235, v205, v210
	s_waitcnt lgkmcnt(7)
	v_mfma_f32_32x32x16_f16 v[80:95], a[108:111], v[180:183], v[80:95]
	ds_read_b128 v[180:183], v193 offset:54272
	s_add_u32 s44, s34, 0x29000
	s_addc_u32 s45, s35, 0
	s_mov_b32 m0, s55
	s_nop 0
	global_load_lds_dwordx4 v192, s[44:45] sc1
	v_fma_f32 v55, v235, v207, v211
	v_fmac_f32_e32 v52, v234, v200
	v_fmac_f32_e32 v53, v234, v202
	s_waitcnt lgkmcnt(7)
	v_mfma_f32_32x32x16_f16 v[96:111], a[108:111], v[184:187], v[96:111]
	ds_read_b128 v[184:187], v193 offset:55296
	v_fmac_f32_e32 v54, v234, v204
	v_fmac_f32_e32 v55, v234, v206
	s_waitcnt lgkmcnt(7)
	v_mfma_f32_32x32x16_f16 v[112:127], a[108:111], v[188:191], v[112:127]
	ds_read_b128 v[188:191], v193 offset:56320
	ds_read_b128 v[200:203], v248 offset:144
	ds_read_b128 v[204:207], v248 offset:160
	ds_read_b128 v[208:211], v248 offset:176
	s_waitcnt lgkmcnt(10)
	v_mfma_f32_32x32x16_f16 v[64:79], a[112:115], v[160:163], v[64:79]
	ds_read_b128 v[160:163], v193 offset:57344
	v_fma_f32 v8, v229, v237, v244
	v_fma_f32 v9, v229, v239, v245
	s_waitcnt lgkmcnt(10)
	v_mfma_f32_32x32x16_f16 v[80:95], a[112:115], v[164:167], v[80:95]
	ds_read_b128 v[164:167], v193 offset:58368
	global_load_lds_dwordx4 v192, s[44:45] offset:1024 sc1
	v_fma_f32 v10, v229, v241, v246
	v_fma_f32 v11, v229, v243, v247
	v_fmac_f32_e32 v8, v228, v236
	s_waitcnt lgkmcnt(10)
	v_mfma_f32_32x32x16_f16 v[96:111], a[112:115], v[168:171], v[96:111]
	ds_read_b128 v[168:171], v193 offset:59392
	v_fmac_f32_e32 v9, v228, v238
	v_fmac_f32_e32 v10, v228, v240
	v_fmac_f32_e32 v11, v228, v242
	s_waitcnt lgkmcnt(10)
	v_mfma_f32_32x32x16_f16 v[112:127], a[112:115], v[172:175], v[112:127]
	ds_read_b128 v[172:175], v193 offset:60416
	v_fma_f32 v24, v231, v237, v244
	v_fma_f32 v25, v231, v239, v245
	v_fma_f32 v26, v231, v241, v246
	s_waitcnt lgkmcnt(10)
	v_mfma_f32_32x32x16_f16 v[64:79], a[116:119], v[176:179], v[64:79]
	ds_read_b128 v[176:179], v193 offset:61440
	v_fma_f32 v27, v231, v243, v247
	v_fmac_f32_e32 v24, v230, v236
	v_fmac_f32_e32 v25, v230, v238
	s_waitcnt lgkmcnt(10)
	v_mfma_f32_32x32x16_f16 v[80:95], a[116:119], v[180:183], v[80:95]
	ds_read_b128 v[180:183], v193 offset:62464
	global_load_lds_dwordx4 v192, s[44:45] offset:2048 sc1
	v_fmac_f32_e32 v26, v230, v240
	v_fmac_f32_e32 v27, v230, v242
	v_fma_f32 v40, v233, v237, v244
	s_waitcnt lgkmcnt(10)
	v_mfma_f32_32x32x16_f16 v[96:111], a[116:119], v[184:187], v[96:111]
	ds_read_b128 v[184:187], v193 offset:63488
	v_fma_f32 v41, v233, v239, v245
	v_fma_f32 v42, v233, v241, v246
	v_fma_f32 v43, v233, v243, v247
	s_waitcnt lgkmcnt(10)
	v_mfma_f32_32x32x16_f16 v[112:127], a[116:119], v[188:191], v[112:127]
	ds_read_b128 v[188:191], v193 offset:64512
	v_fmac_f32_e32 v40, v232, v236
	v_fmac_f32_e32 v41, v232, v238
	v_fmac_f32_e32 v42, v232, v240
	s_barrier
	s_waitcnt lgkmcnt(7)
	v_mfma_f32_32x32x16_f16 v[64:79], a[120:123], v[160:163], v[64:79]
	ds_read_b128 v[160:163], v192 offset:0
	v_fmac_f32_e32 v43, v232, v242
	v_fma_f32 v56, v235, v237, v244
	v_fma_f32 v57, v235, v239, v245
	s_waitcnt lgkmcnt(7)
	v_mfma_f32_32x32x16_f16 v[80:95], a[120:123], v[164:167], v[80:95]
	ds_read_b128 v[164:167], v192 offset:1024
	global_load_lds_dwordx4 v192, s[44:45] offset:3072 sc1
	v_fma_f32 v58, v235, v241, v246
	v_fma_f32 v59, v235, v243, v247
	v_fmac_f32_e32 v56, v234, v236
	s_waitcnt lgkmcnt(7)
	v_mfma_f32_32x32x16_f16 v[96:111], a[120:123], v[168:171], v[96:111]
	ds_read_b128 v[168:171], v192 offset:2048
	v_fmac_f32_e32 v57, v234, v238
	v_fmac_f32_e32 v58, v234, v240
	v_fmac_f32_e32 v59, v234, v242
	s_waitcnt lgkmcnt(7)
	v_mfma_f32_32x32x16_f16 v[112:127], a[120:123], v[172:175], v[112:127]
	ds_read_b128 v[172:175], v192 offset:3072
	v_fma_f32 v12, v229, v201, v208
	v_fma_f32 v13, v229, v203, v209
	s_waitcnt lgkmcnt(7)
	v_mfma_f32_32x32x16_f16 v[64:79], a[124:127], v[176:179], v[64:79]
	ds_read_b128 v[176:179], v192 offset:4096
	v_fma_f32 v14, v229, v205, v210
	v_fma_f32 v15, v229, v207, v211
	v_fmac_f32_e32 v12, v228, v200
	s_waitcnt lgkmcnt(7)
	v_mfma_f32_32x32x16_f16 v[80:95], a[124:127], v[180:183], v[80:95]
	ds_read_b128 v[180:183], v192 offset:5120
	s_add_u32 s44, s34, 0x30000
	s_addc_u32 s45, s35, 0
	s_mov_b32 m0, s56
	s_nop 0
	global_load_lds_dwordx4 v192, s[44:45] sc1
	v_fmac_f32_e32 v13, v228, v202
	v_fmac_f32_e32 v14, v228, v204
	v_fmac_f32_e32 v15, v228, v206
	s_waitcnt lgkmcnt(7)
	v_mfma_f32_32x32x16_f16 v[96:111], a[124:127], v[184:187], v[96:111]
	ds_read_b128 v[184:187], v192 offset:6144
	v_fma_f32 v28, v231, v201, v208
	v_fma_f32 v29, v231, v203, v209
	v_fma_f32 v30, v231, v205, v210
	s_waitcnt lgkmcnt(7)
	v_mfma_f32_32x32x16_f16 v[112:127], a[124:127], v[188:191], v[112:127]
	ds_read_b128 v[188:191], v192 offset:7168
	v_fma_f32 v31, v231, v207, v211
	v_fmac_f32_e32 v28, v230, v200
	v_fmac_f32_e32 v29, v230, v202
	s_waitcnt lgkmcnt(7)
	v_mfma_f32_32x32x16_f16 v[64:79], a[128:131], v[160:163], v[64:79]
	ds_read_b128 v[160:163], v192 offset:8192
	v_fmac_f32_e32 v30, v230, v204
	v_fmac_f32_e32 v31, v230, v206
	v_fma_f32 v44, v233, v201, v208
	s_waitcnt lgkmcnt(7)
	v_mfma_f32_32x32x16_f16 v[80:95], a[128:131], v[164:167], v[80:95]
	ds_read_b128 v[164:167], v192 offset:9216
	global_load_lds_dwordx4 v192, s[44:45] offset:1024 sc1
	v_fma_f32 v45, v233, v203, v209
	v_fma_f32 v46, v233, v205, v210
	v_fma_f32 v47, v233, v207, v211
	s_waitcnt lgkmcnt(7)
	v_mfma_f32_32x32x16_f16 v[96:111], a[128:131], v[168:171], v[96:111]
	ds_read_b128 v[168:171], v192 offset:10240
	v_fmac_f32_e32 v44, v232, v200
	v_fmac_f32_e32 v45, v232, v202
	v_fmac_f32_e32 v46, v232, v204
	s_waitcnt lgkmcnt(7)
	v_mfma_f32_32x32x16_f16 v[112:127], a[128:131], v[172:175], v[112:127]
	ds_read_b128 v[172:175], v192 offset:11264
	v_fmac_f32_e32 v47, v232, v206
	v_fma_f32 v60, v235, v201, v208
	v_fma_f32 v61, v235, v203, v209
	s_waitcnt lgkmcnt(7)
	v_mfma_f32_32x32x16_f16 v[64:79], a[132:135], v[176:179], v[64:79]
	ds_read_b128 v[176:179], v192 offset:12288
	v_fma_f32 v62, v235, v205, v210
	v_fma_f32 v63, v235, v207, v211
	v_fmac_f32_e32 v60, v234, v200
	s_waitcnt lgkmcnt(7)
	v_mfma_f32_32x32x16_f16 v[80:95], a[132:135], v[180:183], v[80:95]
	ds_read_b128 v[180:183], v192 offset:13312
	global_load_lds_dwordx4 v192, s[44:45] offset:2048 sc1
	v_fmac_f32_e32 v61, v234, v202
	v_fmac_f32_e32 v62, v234, v204
	v_fmac_f32_e32 v63, v234, v206
	s_waitcnt lgkmcnt(7)
	v_mfma_f32_32x32x16_f16 v[96:111], a[132:135], v[184:187], v[96:111]
	ds_read_b128 v[184:187], v192 offset:14336
	s_waitcnt lgkmcnt(7)
	v_mfma_f32_32x32x16_f16 v[112:127], a[132:135], v[188:191], v[112:127]
	ds_read_b128 v[188:191], v192 offset:15360
	s_waitcnt lgkmcnt(7)
	v_mfma_f32_32x32x16_f16 v[64:79], a[136:139], v[160:163], v[64:79]
	ds_read_b128 v[160:163], v192 offset:16384
	s_waitcnt lgkmcnt(7)
	v_mfma_f32_32x32x16_f16 v[80:95], a[136:139], v[164:167], v[80:95]
	ds_read_b128 v[164:167], v192 offset:17408
	global_load_lds_dwordx4 v192, s[44:45] offset:3072 sc1
	s_waitcnt lgkmcnt(7)
	v_mfma_f32_32x32x16_f16 v[96:111], a[136:139], v[168:171], v[96:111]
	ds_read_b128 v[168:171], v192 offset:18432
	s_waitcnt lgkmcnt(7)
	v_mfma_f32_32x32x16_f16 v[112:127], a[136:139], v[172:175], v[112:127]
	ds_read_b128 v[172:175], v192 offset:19456
	s_waitcnt lgkmcnt(7)
	v_mfma_f32_32x32x16_f16 v[64:79], a[140:143], v[176:179], v[64:79]
	ds_read_b128 v[176:179], v192 offset:20480
	s_waitcnt lgkmcnt(7)
	v_mfma_f32_32x32x16_f16 v[80:95], a[140:143], v[180:183], v[80:95]
	ds_read_b128 v[180:183], v192 offset:21504
	s_add_u32 s44, s34, 0x31000
	s_addc_u32 s45, s35, 0
	s_mov_b32 m0, s57
	s_nop 0
	global_load_lds_dwordx4 v192, s[44:45] sc1
	s_waitcnt lgkmcnt(7)
	v_mfma_f32_32x32x16_f16 v[96:111], a[140:143], v[184:187], v[96:111]
	ds_read_b128 v[184:187], v192 offset:22528
	s_waitcnt lgkmcnt(7)
	v_mfma_f32_32x32x16_f16 v[112:127], a[140:143], v[188:191], v[112:127]
	ds_read_b128 v[188:191], v192 offset:23552
	s_waitcnt lgkmcnt(7)
	v_mfma_f32_32x32x16_f16 v[64:79], a[144:147], v[160:163], v[64:79]
	ds_read_b128 v[160:163], v192 offset:24576
	s_waitcnt lgkmcnt(7)
	v_mfma_f32_32x32x16_f16 v[80:95], a[144:147], v[164:167], v[80:95]
	ds_read_b128 v[164:167], v192 offset:25600
	global_load_lds_dwordx4 v192, s[44:45] offset:1024 sc1
	s_waitcnt lgkmcnt(7)
	v_mfma_f32_32x32x16_f16 v[96:111], a[144:147], v[168:171], v[96:111]
	ds_read_b128 v[168:171], v192 offset:26624
	s_waitcnt lgkmcnt(7)
	v_mfma_f32_32x32x16_f16 v[112:127], a[144:147], v[172:175], v[112:127]
	ds_read_b128 v[172:175], v192 offset:27648
	s_waitcnt lgkmcnt(7)
	v_mfma_f32_32x32x16_f16 v[64:79], a[148:151], v[176:179], v[64:79]
	ds_read_b128 v[176:179], v192 offset:28672
	s_waitcnt lgkmcnt(7)
	v_mfma_f32_32x32x16_f16 v[80:95], a[148:151], v[180:183], v[80:95]
	ds_read_b128 v[180:183], v192 offset:29696
	global_load_lds_dwordx4 v192, s[44:45] offset:2048 sc1
	s_waitcnt lgkmcnt(7)
	v_mfma_f32_32x32x16_f16 v[96:111], a[148:151], v[184:187], v[96:111]
	ds_read_b128 v[184:187], v192 offset:30720
	s_waitcnt lgkmcnt(7)
	v_mfma_f32_32x32x16_f16 v[112:127], a[148:151], v[188:191], v[112:127]
	ds_read_b128 v[188:191], v192 offset:31744
	s_waitcnt vmcnt(7)
	s_barrier
	s_waitcnt lgkmcnt(7)
	v_mfma_f32_32x32x16_f16 v[64:79], a[152:155], v[160:163], v[64:79]
	ds_read_b128 v[160:163], v192 offset:32768
	s_waitcnt lgkmcnt(7)
	v_mfma_f32_32x32x16_f16 v[80:95], a[152:155], v[164:167], v[80:95]
	ds_read_b128 v[164:167], v192 offset:33792
	global_load_lds_dwordx4 v192, s[44:45] offset:3072 sc1
	s_waitcnt lgkmcnt(7)
	v_mfma_f32_32x32x16_f16 v[96:111], a[152:155], v[168:171], v[96:111]
	ds_read_b128 v[168:171], v192 offset:34816
	s_waitcnt lgkmcnt(7)
	v_mfma_f32_32x32x16_f16 v[112:127], a[152:155], v[172:175], v[112:127]
	ds_read_b128 v[172:175], v192 offset:35840
	s_waitcnt lgkmcnt(7)
	v_mfma_f32_32x32x16_f16 v[64:79], a[156:159], v[176:179], v[64:79]
	ds_read_b128 v[176:179], v192 offset:36864
	s_waitcnt lgkmcnt(7)
	v_mfma_f32_32x32x16_f16 v[80:95], a[156:159], v[180:183], v[80:95]
	ds_read_b128 v[180:183], v192 offset:37888
	s_add_u32 s44, s34, 0x38000
	s_addc_u32 s45, s35, 0
	s_mov_b32 m0, s58
	s_nop 0
	global_load_lds_dwordx4 v192, s[44:45] sc1
	s_waitcnt lgkmcnt(7)
	v_mfma_f32_32x32x16_f16 v[96:111], a[156:159], v[184:187], v[96:111]
	ds_read_b128 v[184:187], v192 offset:38912
	s_waitcnt lgkmcnt(7)
	v_mfma_f32_32x32x16_f16 v[112:127], a[156:159], v[188:191], v[112:127]
	ds_read_b128 v[188:191], v192 offset:39936
	s_lshl_b32 s64, s33, 3
	s_add_u32 s64, s64, s29
	s_lshl_b32 s64, s64, 7
	s_add_u32 s38, s8, s64
	s_addc_u32 s39, s9, 0
	global_load_dword v251, v196, s[38:39] sc1
	s_waitcnt lgkmcnt(7)
	v_mfma_f32_32x32x16_f16 v[64:79], a[160:163], v[160:163], v[64:79]
	ds_read_b128 v[160:163], v192 offset:40960
	s_waitcnt lgkmcnt(7)
	v_mfma_f32_32x32x16_f16 v[80:95], a[160:163], v[164:167], v[80:95]
	ds_read_b128 v[164:167], v192 offset:41984
	global_load_lds_dwordx4 v192, s[44:45] offset:1024 sc1
	s_waitcnt lgkmcnt(7)
	v_mfma_f32_32x32x16_f16 v[96:111], a[160:163], v[168:171], v[96:111]
	ds_read_b128 v[168:171], v192 offset:43008
	s_waitcnt lgkmcnt(7)
	v_mfma_f32_32x32x16_f16 v[112:127], a[160:163], v[172:175], v[112:127]
	ds_read_b128 v[172:175], v192 offset:44032
	s_waitcnt lgkmcnt(7)
	v_mfma_f32_32x32x16_f16 v[64:79], a[164:167], v[176:179], v[64:79]
	ds_read_b128 v[176:179], v192 offset:45056
	s_waitcnt lgkmcnt(7)
	v_mfma_f32_32x32x16_f16 v[80:95], a[164:167], v[180:183], v[80:95]
	ds_read_b128 v[180:183], v192 offset:46080
	global_load_lds_dwordx4 v192, s[44:45] offset:2048 sc1
	s_waitcnt lgkmcnt(7)
	v_mfma_f32_32x32x16_f16 v[96:111], a[164:167], v[184:187], v[96:111]
	ds_read_b128 v[184:187], v192 offset:47104
	s_waitcnt lgkmcnt(7)
	v_mfma_f32_32x32x16_f16 v[112:127], a[164:167], v[188:191], v[112:127]
	ds_read_b128 v[188:191], v192 offset:48128
	s_waitcnt lgkmcnt(7)
	v_mfma_f32_32x32x16_f16 v[64:79], a[168:171], v[160:163], v[64:79]
	ds_read_b128 v[160:163], v192 offset:49152
	s_waitcnt lgkmcnt(7)
	v_mfma_f32_32x32x16_f16 v[80:95], a[168:171], v[164:167], v[80:95]
	ds_read_b128 v[164:167], v192 offset:50176
	global_load_lds_dwordx4 v192, s[44:45] offset:3072 sc1
	s_waitcnt lgkmcnt(7)
	v_mfma_f32_32x32x16_f16 v[96:111], a[168:171], v[168:171], v[96:111]
	ds_read_b128 v[168:171], v192 offset:51200
	s_waitcnt lgkmcnt(7)
	v_mfma_f32_32x32x16_f16 v[112:127], a[168:171], v[172:175], v[112:127]
	ds_read_b128 v[172:175], v192 offset:52224
	s_waitcnt lgkmcnt(7)
	v_mfma_f32_32x32x16_f16 v[64:79], a[172:175], v[176:179], v[64:79]
	ds_read_b128 v[176:179], v192 offset:53248
	s_waitcnt lgkmcnt(7)
	v_mfma_f32_32x32x16_f16 v[80:95], a[172:175], v[180:183], v[80:95]
	ds_read_b128 v[180:183], v192 offset:54272
	s_add_u32 s44, s34, 0x39000
	s_addc_u32 s45, s35, 0
	s_mov_b32 m0, s59
	s_nop 0
	global_load_lds_dwordx4 v192, s[44:45] sc1
	s_waitcnt lgkmcnt(7)
	v_mfma_f32_32x32x16_f16 v[96:111], a[172:175], v[184:187], v[96:111]
	ds_read_b128 v[184:187], v192 offset:55296
	s_waitcnt lgkmcnt(7)
	v_mfma_f32_32x32x16_f16 v[112:127], a[172:175], v[188:191], v[112:127]
	ds_read_b128 v[188:191], v192 offset:56320
	s_waitcnt lgkmcnt(7)
	v_mfma_f32_32x32x16_f16 v[64:79], a[176:179], v[160:163], v[64:79]
	ds_read_b128 v[160:163], v192 offset:57344
	s_waitcnt lgkmcnt(7)
	v_mfma_f32_32x32x16_f16 v[80:95], a[176:179], v[164:167], v[80:95]
	ds_read_b128 v[164:167], v192 offset:58368
	global_load_lds_dwordx4 v192, s[44:45] offset:1024 sc1
	s_waitcnt lgkmcnt(7)
	v_mfma_f32_32x32x16_f16 v[96:111], a[176:179], v[168:171], v[96:111]
	ds_read_b128 v[168:171], v192 offset:59392
	s_waitcnt lgkmcnt(7)
	v_mfma_f32_32x32x16_f16 v[112:127], a[176:179], v[172:175], v[112:127]
	ds_read_b128 v[172:175], v192 offset:60416
	s_waitcnt lgkmcnt(7)
	v_mfma_f32_32x32x16_f16 v[64:79], a[180:183], v[176:179], v[64:79]
	ds_read_b128 v[176:179], v192 offset:61440
	s_waitcnt lgkmcnt(7)
	v_mfma_f32_32x32x16_f16 v[80:95], a[180:183], v[180:183], v[80:95]
	ds_read_b128 v[180:183], v192 offset:62464
	global_load_lds_dwordx4 v192, s[44:45] offset:2048 sc1
	s_waitcnt lgkmcnt(7)
	v_mfma_f32_32x32x16_f16 v[96:111], a[180:183], v[184:187], v[96:111]
	ds_read_b128 v[184:187], v192 offset:63488
	s_waitcnt lgkmcnt(7)
	v_mfma_f32_32x32x16_f16 v[112:127], a[180:183], v[188:191], v[112:127]
	ds_read_b128 v[188:191], v192 offset:64512
	s_waitcnt vmcnt(8)
	s_barrier
	s_waitcnt lgkmcnt(7)
	v_mfma_f32_32x32x16_f16 v[64:79], a[184:187], v[160:163], v[64:79]
	ds_read_b128 v[160:163], v193 offset:0
	s_waitcnt lgkmcnt(7)
	v_mfma_f32_32x32x16_f16 v[80:95], a[184:187], v[164:167], v[80:95]
	ds_read_b128 v[164:167], v193 offset:1024
	global_load_lds_dwordx4 v192, s[44:45] offset:3072 sc1
	s_waitcnt lgkmcnt(7)
	v_mfma_f32_32x32x16_f16 v[96:111], a[184:187], v[168:171], v[96:111]
	ds_read_b128 v[168:171], v193 offset:2048
	s_waitcnt lgkmcnt(7)
	v_mfma_f32_32x32x16_f16 v[112:127], a[184:187], v[172:175], v[112:127]
	ds_read_b128 v[172:175], v193 offset:3072
	s_waitcnt lgkmcnt(7)
	v_mfma_f32_32x32x16_f16 v[64:79], a[188:191], v[176:179], v[64:79]
	ds_read_b128 v[176:179], v193 offset:4096
	s_waitcnt lgkmcnt(7)
	v_mfma_f32_32x32x16_f16 v[80:95], a[188:191], v[180:183], v[80:95]
	ds_read_b128 v[180:183], v193 offset:5120
	s_waitcnt vmcnt(7)
	v_cmp_gt_u32_e32 vcc, 1, v251
	s_cbranch_vccz .LE_tok32
.LE_tpoll33:
	s_cmp_eq_u32 s48, 0
	s_cbranch_scc1 .LE_tok32
	s_sub_u32 s48, s48, 1
	s_sleep 1
	global_load_dword v251, v196, s[38:39] sc1
	s_waitcnt vmcnt(0)
	v_cmp_gt_u32_e32 vcc, 1, v251
	s_cbranch_vccnz .LE_tpoll33
.LE_tok32:
	s_and_b32 s64, s33, 1
	s_lshl_b32 s64, s64, 22
	s_add_u32 s64, s64, s49
	s_add_u32 s34, s6, s64
	s_addc_u32 s35, s7, 0
	s_add_u32 s44, s34, 0x0
	s_addc_u32 s45, s35, 0
	s_mov_b32 m0, s52
	s_nop 0
	global_load_lds_dwordx4 v192, s[44:45] sc1
	s_waitcnt lgkmcnt(7)
	v_mfma_f32_32x32x16_f16 v[96:111], a[188:191], v[184:187], v[96:111]
	ds_read_b128 v[184:187], v193 offset:6144
	s_waitcnt lgkmcnt(7)
	v_mfma_f32_32x32x16_f16 v[112:127], a[188:191], v[188:191], v[112:127]
	ds_read_b128 v[188:191], v193 offset:7168
	s_waitcnt lgkmcnt(7)
	v_mfma_f32_32x32x16_f16 v[64:79], a[192:195], v[160:163], v[64:79]
	ds_read_b128 v[160:163], v193 offset:8192
	s_waitcnt lgkmcnt(7)
	v_mfma_f32_32x32x16_f16 v[80:95], a[192:195], v[164:167], v[80:95]
	ds_read_b128 v[164:167], v193 offset:9216
	global_load_lds_dwordx4 v192, s[44:45] offset:1024 sc1
	s_waitcnt lgkmcnt(7)
	v_mfma_f32_32x32x16_f16 v[96:111], a[192:195], v[168:171], v[96:111]
	ds_read_b128 v[168:171], v193 offset:10240
	s_waitcnt lgkmcnt(7)
	v_mfma_f32_32x32x16_f16 v[112:127], a[192:195], v[172:175], v[112:127]
	ds_read_b128 v[172:175], v193 offset:11264
	s_waitcnt lgkmcnt(7)
	v_mfma_f32_32x32x16_f16 v[64:79], a[196:199], v[176:179], v[64:79]
	ds_read_b128 v[176:179], v193 offset:12288
	s_waitcnt lgkmcnt(7)
	v_mfma_f32_32x32x16_f16 v[80:95], a[196:199], v[180:183], v[80:95]
	ds_read_b128 v[180:183], v193 offset:13312
	global_load_lds_dwordx4 v192, s[44:45] offset:2048 sc1
	s_waitcnt lgkmcnt(7)
	v_mfma_f32_32x32x16_f16 v[96:111], a[196:199], v[184:187], v[96:111]
	ds_read_b128 v[184:187], v193 offset:14336
	s_waitcnt lgkmcnt(7)
	v_mfma_f32_32x32x16_f16 v[112:127], a[196:199], v[188:191], v[112:127]
	ds_read_b128 v[188:191], v193 offset:15360
	s_waitcnt lgkmcnt(7)
	v_mfma_f32_32x32x16_f16 v[64:79], a[200:203], v[160:163], v[64:79]
	ds_read_b128 v[160:163], v193 offset:16384
	s_waitcnt lgkmcnt(7)
	v_mfma_f32_32x32x16_f16 v[80:95], a[200:203], v[164:167], v[80:95]
	ds_read_b128 v[164:167], v193 offset:17408
	global_load_lds_dwordx4 v192, s[44:45] offset:3072 sc1
	s_waitcnt lgkmcnt(7)
	v_mfma_f32_32x32x16_f16 v[96:111], a[200:203], v[168:171], v[96:111]
	ds_read_b128 v[168:171], v193 offset:18432
	s_waitcnt lgkmcnt(7)
	v_mfma_f32_32x32x16_f16 v[112:127], a[200:203], v[172:175], v[112:127]
	ds_read_b128 v[172:175], v193 offset:19456
	s_waitcnt lgkmcnt(7)
	v_mfma_f32_32x32x16_f16 v[64:79], a[204:207], v[176:179], v[64:79]
	ds_read_b128 v[176:179], v193 offset:20480
	s_waitcnt lgkmcnt(7)
	v_mfma_f32_32x32x16_f16 v[80:95], a[204:207], v[180:183], v[80:95]
	ds_read_b128 v[180:183], v193 offset:21504
	s_add_u32 s44, s34, 0x1000
	s_addc_u32 s45, s35, 0
	s_mov_b32 m0, s53
	s_nop 0
	global_load_lds_dwordx4 v192, s[44:45] sc1
	s_waitcnt lgkmcnt(7)
	v_mfma_f32_32x32x16_f16 v[96:111], a[204:207], v[184:187], v[96:111]
	ds_read_b128 v[184:187], v193 offset:22528
	s_waitcnt lgkmcnt(7)
	v_mfma_f32_32x32x16_f16 v[112:127], a[204:207], v[188:191], v[112:127]
	ds_read_b128 v[188:191], v193 offset:23552
	s_waitcnt lgkmcnt(7)
	v_mfma_f32_32x32x16_f16 v[64:79], a[208:211], v[160:163], v[64:79]
	ds_read_b128 v[160:163], v193 offset:24576
	s_waitcnt lgkmcnt(7)
	v_mfma_f32_32x32x16_f16 v[80:95], a[208:211], v[164:167], v[80:95]
	ds_read_b128 v[164:167], v193 offset:25600
	global_load_lds_dwordx4 v192, s[44:45] offset:1024 sc1
	s_waitcnt lgkmcnt(7)
	v_mfma_f32_32x32x16_f16 v[96:111], a[208:211], v[168:171], v[96:111]
	ds_read_b128 v[168:171], v193 offset:26624
	s_waitcnt lgkmcnt(7)
	v_mfma_f32_32x32x16_f16 v[112:127], a[208:211], v[172:175], v[112:127]
	ds_read_b128 v[172:175], v193 offset:27648
	s_waitcnt lgkmcnt(7)
	v_mfma_f32_32x32x16_f16 v[64:79], a[212:215], v[176:179], v[64:79]
	ds_read_b128 v[176:179], v193 offset:28672
	s_waitcnt lgkmcnt(7)
	v_mfma_f32_32x32x16_f16 v[80:95], a[212:215], v[180:183], v[80:95]
	ds_read_b128 v[180:183], v193 offset:29696
	global_load_lds_dwordx4 v192, s[44:45] offset:2048 sc1
	s_waitcnt lgkmcnt(7)
	v_mfma_f32_32x32x16_f16 v[96:111], a[212:215], v[184:187], v[96:111]
	ds_read_b128 v[184:187], v193 offset:30720
	s_waitcnt lgkmcnt(7)
	v_mfma_f32_32x32x16_f16 v[112:127], a[212:215], v[188:191], v[112:127]
	ds_read_b128 v[188:191], v193 offset:31744
	s_waitcnt vmcnt(7)
	s_barrier
	s_waitcnt lgkmcnt(7)
	v_mfma_f32_32x32x16_f16 v[64:79], a[216:219], v[160:163], v[64:79]
	ds_read_b128 v[160:163], v193 offset:32768
	s_waitcnt lgkmcnt(7)
	v_mfma_f32_32x32x16_f16 v[80:95], a[216:219], v[164:167], v[80:95]
	ds_read_b128 v[164:167], v193 offset:33792
	global_load_lds_dwordx4 v192, s[44:45] offset:3072 sc1
	s_waitcnt lgkmcnt(7)
	v_mfma_f32_32x32x16_f16 v[96:111], a[216:219], v[168:171], v[96:111]
	ds_read_b128 v[168:171], v193 offset:34816
	s_waitcnt lgkmcnt(7)
	v_mfma_f32_32x32x16_f16 v[112:127], a[216:219], v[172:175], v[112:127]
	ds_read_b128 v[172:175], v193 offset:35840
	s_waitcnt lgkmcnt(7)
	v_mfma_f32_32x32x16_f16 v[64:79], a[220:223], v[176:179], v[64:79]
	ds_read_b128 v[176:179], v193 offset:36864
	s_waitcnt lgkmcnt(7)
	v_mfma_f32_32x32x16_f16 v[80:95], a[220:223], v[180:183], v[80:95]
	ds_read_b128 v[180:183], v193 offset:37888
	s_add_u32 s44, s34, 0x8000
	s_addc_u32 s45, s35, 0
	s_mov_b32 m0, s54
	s_nop 0
	global_load_lds_dwordx4 v192, s[44:45] sc1
	s_waitcnt lgkmcnt(7)
	v_mfma_f32_32x32x16_f16 v[96:111], a[220:223], v[184:187], v[96:111]
	ds_read_b128 v[184:187], v193 offset:38912
	s_waitcnt lgkmcnt(7)
	v_mfma_f32_32x32x16_f16 v[112:127], a[220:223], v[188:191], v[112:127]
	ds_read_b128 v[188:191], v193 offset:39936
	s_waitcnt lgkmcnt(7)
	v_mfma_f32_32x32x16_f16 v[64:79], a[224:227], v[160:163], v[64:79]
	ds_read_b128 v[160:163], v193 offset:40960
	s_waitcnt lgkmcnt(7)
	v_mfma_f32_32x32x16_f16 v[80:95], a[224:227], v[164:167], v[80:95]
	ds_read_b128 v[164:167], v193 offset:41984
	global_load_lds_dwordx4 v192, s[44:45] offset:1024 sc1
	s_waitcnt lgkmcnt(7)
	v_mfma_f32_32x32x16_f16 v[96:111], a[224:227], v[168:171], v[96:111]
	ds_read_b128 v[168:171], v193 offset:43008
	s_waitcnt lgkmcnt(7)
	v_mfma_f32_32x32x16_f16 v[112:127], a[224:227], v[172:175], v[112:127]
	ds_read_b128 v[172:175], v193 offset:44032
	s_waitcnt lgkmcnt(7)
	v_mfma_f32_32x32x16_f16 v[64:79], a[228:231], v[176:179], v[64:79]
	ds_read_b128 v[176:179], v193 offset:45056
	s_waitcnt lgkmcnt(7)
	v_mfma_f32_32x32x16_f16 v[80:95], a[228:231], v[180:183], v[80:95]
	ds_read_b128 v[180:183], v193 offset:46080
	global_load_lds_dwordx4 v192, s[44:45] offset:2048 sc1
	s_waitcnt lgkmcnt(7)
	v_mfma_f32_32x32x16_f16 v[96:111], a[228:231], v[184:187], v[96:111]
	ds_read_b128 v[184:187], v193 offset:47104
	s_waitcnt lgkmcnt(7)
	v_mfma_f32_32x32x16_f16 v[112:127], a[228:231], v[188:191], v[112:127]
	ds_read_b128 v[188:191], v193 offset:48128
	s_waitcnt lgkmcnt(7)
	v_mfma_f32_32x32x16_f16 v[64:79], a[232:235], v[160:163], v[64:79]
	ds_read_b128 v[160:163], v193 offset:49152
	s_waitcnt lgkmcnt(7)
	v_mfma_f32_32x32x16_f16 v[80:95], a[232:235], v[164:167], v[80:95]
	ds_read_b128 v[164:167], v193 offset:50176
	global_load_lds_dwordx4 v192, s[44:45] offset:3072 sc1
	s_waitcnt lgkmcnt(7)
	v_mfma_f32_32x32x16_f16 v[96:111], a[232:235], v[168:171], v[96:111]
	ds_read_b128 v[168:171], v193 offset:51200
	s_waitcnt lgkmcnt(7)
	v_mfma_f32_32x32x16_f16 v[112:127], a[232:235], v[172:175], v[112:127]
	ds_read_b128 v[172:175], v193 offset:52224
	s_waitcnt lgkmcnt(7)
	v_mfma_f32_32x32x16_f16 v[64:79], a[236:239], v[176:179], v[64:79]
	ds_read_b128 v[176:179], v193 offset:53248
	s_waitcnt lgkmcnt(7)
	v_mfma_f32_32x32x16_f16 v[80:95], a[236:239], v[180:183], v[80:95]
	ds_read_b128 v[180:183], v193 offset:54272
	s_add_u32 s44, s34, 0x9000
	s_addc_u32 s45, s35, 0
	s_mov_b32 m0, s55
	s_nop 0
	global_load_lds_dwordx4 v192, s[44:45] sc1
	s_waitcnt lgkmcnt(7)
	v_mfma_f32_32x32x16_f16 v[96:111], a[236:239], v[184:187], v[96:111]
	ds_read_b128 v[184:187], v193 offset:55296
	s_waitcnt lgkmcnt(7)
	v_mfma_f32_32x32x16_f16 v[112:127], a[236:239], v[188:191], v[112:127]
	ds_read_b128 v[188:191], v193 offset:56320
	s_waitcnt lgkmcnt(7)
	v_mfma_f32_32x32x16_f16 v[64:79], a[240:243], v[160:163], v[64:79]
	ds_read_b128 v[160:163], v193 offset:57344
	s_waitcnt lgkmcnt(7)
	v_mfma_f32_32x32x16_f16 v[80:95], a[240:243], v[164:167], v[80:95]
	ds_read_b128 v[164:167], v193 offset:58368
	global_load_lds_dwordx4 v192, s[44:45] offset:1024 sc1
	s_waitcnt lgkmcnt(7)
	v_mfma_f32_32x32x16_f16 v[96:111], a[240:243], v[168:171], v[96:111]
	ds_read_b128 v[168:171], v193 offset:59392
	s_waitcnt lgkmcnt(7)
	v_mfma_f32_32x32x16_f16 v[112:127], a[240:243], v[172:175], v[112:127]
	ds_read_b128 v[172:175], v193 offset:60416
	s_waitcnt lgkmcnt(7)
	v_mfma_f32_32x32x16_f16 v[64:79], a[244:247], v[176:179], v[64:79]
	ds_read_b128 v[176:179], v193 offset:61440
	s_waitcnt lgkmcnt(7)
	v_mfma_f32_32x32x16_f16 v[80:95], a[244:247], v[180:183], v[80:95]
	ds_read_b128 v[180:183], v193 offset:62464
	global_load_lds_dwordx4 v192, s[44:45] offset:2048 sc1
	s_waitcnt lgkmcnt(7)
	v_mfma_f32_32x32x16_f16 v[96:111], a[244:247], v[184:187], v[96:111]
	ds_read_b128 v[184:187], v193 offset:63488
	s_waitcnt lgkmcnt(7)
	v_mfma_f32_32x32x16_f16 v[112:127], a[244:247], v[188:191], v[112:127]
	ds_read_b128 v[188:191], v193 offset:64512
	s_waitcnt vmcnt(7)
	s_barrier
	s_waitcnt lgkmcnt(7)
	v_mfma_f32_32x32x16_f16 v[64:79], a[248:251], v[160:163], v[64:79]
	ds_read_b128 v[160:163], v192 offset:0
	s_waitcnt lgkmcnt(7)
	v_mfma_f32_32x32x16_f16 v[80:95], a[248:251], v[164:167], v[80:95]
	ds_read_b128 v[164:167], v192 offset:1024
	global_load_lds_dwordx4 v192, s[44:45] offset:3072 sc1
	s_waitcnt lgkmcnt(7)
	v_mfma_f32_32x32x16_f16 v[96:111], a[248:251], v[168:171], v[96:111]
	ds_read_b128 v[168:171], v192 offset:2048
	s_waitcnt lgkmcnt(7)
	v_mfma_f32_32x32x16_f16 v[112:127], a[248:251], v[172:175], v[112:127]
	ds_read_b128 v[172:175], v192 offset:3072
	s_waitcnt lgkmcnt(7)
	v_mfma_f32_32x32x16_f16 v[64:79], a[252:255], v[176:179], v[64:79]
	ds_read_b128 v[176:179], v192 offset:4096
	s_waitcnt lgkmcnt(7)
	v_mfma_f32_32x32x16_f16 v[80:95], a[252:255], v[180:183], v[80:95]
	ds_read_b128 v[180:183], v192 offset:5120
	s_add_u32 s44, s34, 0x10000
	s_addc_u32 s45, s35, 0
	s_mov_b32 m0, s56
	s_nop 0
	global_load_lds_dwordx4 v192, s[44:45] sc1
	s_waitcnt lgkmcnt(7)
	v_mfma_f32_32x32x16_f16 v[96:111], a[252:255], v[184:187], v[96:111]
	ds_read_b128 v[184:187], v192 offset:6144
	s_waitcnt lgkmcnt(7)
	v_mfma_f32_32x32x16_f16 v[112:127], a[252:255], v[188:191], v[112:127]
	ds_read_b128 v[188:191], v192 offset:7168
	s_add_u32 s33, s33, 1
	s_cmp_lt_u32 s33, s28
	s_cbranch_scc1 .LE_loop10

_Z12lstm_persistILi0EEvPKDv8_DF16_PhPjS4_PKfS6_S6_PKDv4_DF16_S9_S6_PfSA_i:
	s_load_dwordx8 s[4:11], s[0:1], 0x0
	s_load_dwordx8 s[12:19], s[0:1], 0x20
	s_load_dwordx8 s[20:27], s[0:1], 0x40
	s_load_dword s28, s[0:1], 0x60
	v_and_b32_e32 v194, 63, v0
	v_lshrrev_b32_e32 v252, 6, v0
	v_lshlrev_b32_e32 v192, 4, v194
	v_add_u32_e32 v193, 0x10000, v192
	v_readfirstlane_b32 s32, v252
	v_and_b32_e32 v253, 31, v194
	v_lshrrev_b32_e32 v254, 5, v194
	v_mov_b32_e32 v197, 0
	v_mov_b32_e32 v198, 0x4038aa3b
	v_lshlrev_b32_e32 v196, 2, v253
	v_lshlrev_b32_e32 v195, 4, v253
	v_lshl_add_u32 v195, v254, 10, v195
	s_mov_b32 s48, 0x100000
	s_waitcnt lgkmcnt(0)
	s_cmp_lg_u32 s32, 0
	s_cbranch_scc1 .LD_cdone1
	s_mov_b64 exec, 1
	s_getreg_b32 s64, hwreg(HW_REG_XCC_ID, 0, 4)
	s_and_b32 s64, s64, 7
	s_lshl_b32 s65, s64, 2
	v_mov_b32_e32 v252, s65
	v_mov_b32_e32 v251, 1
	global_atomic_add v250, v252, v251, s[10:11] sc0
	s_waitcnt vmcnt(0)
	s_mov_b32 s66, 0

.LD_cgot3:
	v_xor_b32_e32 v200, 32, v200
	v_xor_b32_e32 v201, 32, v201
	v_xor_b32_e32 v202, 32, v202
	v_xor_b32_e32 v203, 32, v203
	v_xor_b32_e32 v204, 32, v204
	v_xor_b32_e32 v205, 32, v205
	v_xor_b32_e32 v206, 32, v206
	v_xor_b32_e32 v207, 32, v207
	v_or_b32_e32 v200, v200, v201
	v_or_b32_e32 v202, v202, v203
	v_or_b32_e32 v204, v204, v205
	v_or_b32_e32 v206, v206, v207
	v_or_b32_e32 v200, v200, v202
	v_or_b32_e32 v204, v204, v206
	v_or_b32_e32 v200, v200, v204
	s_nop 1
	v_readfirstlane_b32 s67, v200
	v_readfirstlane_b32 s68, v250
	s_nop 1
	s_and_b32 s69, s2, 7
	s_lshr_b32 s70, s2, 3
	s_cmp_eq_u32 s67, 0
	s_cselect_b32 s31, 1, 0
	s_cselect_b32 s29, s64, s69
	s_cselect_b32 s30, s68, s70
	v_mov_b32_e32 v200, s31
	v_mov_b32_e32 v201, s29
	v_mov_b32_e32 v202, s30
	v_mov_b32_e32 v252, 0x22000
	ds_write_b32 v252, v200
	ds_write_b32 v252, v201 offset:4
	ds_write_b32 v252, v202 offset:8
	s_mov_b64 exec, -1
.LD_cdone1:
	s_waitcnt lgkmcnt(0)
	s_barrier
	v_mov_b32_e32 v252, 0x22000
	ds_read_b32 v200, v252
	ds_read_b32 v201, v252 offset:4
	ds_read_b32 v202, v252 offset:8
	s_waitcnt lgkmcnt(0)
	s_nop 1
	v_readfirstlane_b32 s31, v200
	v_readfirstlane_b32 s29, v201
	v_readfirstlane_b32 s30, v202
	s_nop 3
	s_barrier
	s_lshl_b32 s49, s29, 19
	s_lshl_b32 s64, s32, 13
	s_add_u32 s49, s49, s64
	s_mov_b32 s51, s64
	s_add_u32 s52, s51, 0x0
	s_add_u32 s53, s51, 0x1000
	s_add_u32 s54, s51, 0x8000
	s_add_u32 s55, s51, 0x9000
	s_add_u32 s56, s51, 0x10000
	s_add_u32 s57, s51, 0x11000
	s_add_u32 s58, s51, 0x18000
	s_add_u32 s59, s51, 0x19000
	s_lshl_b32 s64, s29, 7
	s_lshl_b32 s65, s30, 1
	s_add_u32 s64, s64, s65
	s_lshr_b32 s65, s32, 1
	s_add_u32 s64, s64, s65
	s_lshl_b32 s64, s64, 12
	s_and_b32 s65, s32, 1
	s_lshl_b32 s65, s65, 9
	s_add_u32 s50, s64, s65
	s_sub_u32 s60, s28, 1
	s_lshl_b32 s64, s30, 2
	s_add_u32 s64, s64, s32
	s_lshl_b32 s64, s64, 16
	s_add_u32 s44, s4, s64
	s_addc_u32 s45, s5, 0
	global_load_dwordx4 a[0:3], v192, s[44:45] offset:0
	global_load_dwordx4 a[4:7], v192, s[44:45] offset:1024
	global_load_dwordx4 a[8:11], v192, s[44:45] offset:2048
	global_load_dwordx4 a[12:15], v192, s[44:45] offset:3072
	s_add_u32 s44, s44, 0x1000
	s_addc_u32 s45, s45, 0
	global_load_dwordx4 a[16:19], v192, s[44:45] offset:0
	global_load_dwordx4 a[20:23], v192, s[44:45] offset:1024
	global_load_dwordx4 a[24:27], v192, s[44:45] offset:2048
	global_load_dwordx4 a[28:31], v192, s[44:45] offset:3072
	s_add_u32 s44, s44, 0x1000
	s_addc_u32 s45, s45, 0
	global_load_dwordx4 a[32:35], v192, s[44:45] offset:0
	global_load_dwordx4 a[36:39], v192, s[44:45] offset:1024
	global_load_dwordx4 a[40:43], v192, s[44:45] offset:2048
	global_load_dwordx4 a[44:47], v192, s[44:45] offset:3072
	s_add_u32 s44, s44, 0x1000
	s_addc_u32 s45, s45, 0
	global_load_dwordx4 a[48:51], v192, s[44:45] offset:0
	global_load_dwordx4 a[52:55], v192, s[44:45] offset:1024
	global_load_dwordx4 a[56:59], v192, s[44:45] offset:2048
	global_load_dwordx4 a[60:63], v192, s[44:45] offset:3072
	s_add_u32 s44, s44, 0x1000
	s_addc_u32 s45, s45, 0
	global_load_dwordx4 a[64:67], v192, s[44:45] offset:0
	global_load_dwordx4 a[68:71], v192, s[44:45] offset:1024
	global_load_dwordx4 a[72:75], v192, s[44:45] offset:2048
	global_load_dwordx4 a[76:79], v192, s[44:45] offset:3072
	s_add_u32 s44, s44, 0x1000
	s_addc_u32 s45, s45, 0
	global_load_dwordx4 a[80:83], v192, s[44:45] offset:0
	global_load_dwordx4 a[84:87], v192, s[44:45] offset:1024
	global_load_dwordx4 a[88:91], v192, s[44:45] offset:2048
	global_load_dwordx4 a[92:95], v192, s[44:45] offset:3072
	s_add_u32 s44, s44, 0x1000
	s_addc_u32 s45, s45, 0
	global_load_dwordx4 a[96:99], v192, s[44:45] offset:0
	global_load_dwordx4 a[100:103], v192, s[44:45] offset:1024
	global_load_dwordx4 a[104:107], v192, s[44:45] offset:2048
	global_load_dwordx4 a[108:111], v192, s[44:45] offset:3072
	s_add_u32 s44, s44, 0x1000
	s_addc_u32 s45, s45, 0
	global_load_dwordx4 a[112:115], v192, s[44:45] offset:0
	global_load_dwordx4 a[116:119], v192, s[44:45] offset:1024
	global_load_dwordx4 a[120:123], v192, s[44:45] offset:2048
	global_load_dwordx4 a[124:127], v192, s[44:45] offset:3072
	s_add_u32 s44, s44, 0x1000
	s_addc_u32 s45, s45, 0
	s_waitcnt vmcnt(16)
	global_load_dwordx4 a[128:131], v192, s[44:45] offset:0
	global_load_dwordx4 a[132:135], v192, s[44:45] offset:1024
	global_load_dwordx4 a[136:139], v192, s[44:45] offset:2048
	global_load_dwordx4 a[140:143], v192, s[44:45] offset:3072
	s_add_u32 s44, s44, 0x1000
	s_addc_u32 s45, s45, 0
	global_load_dwordx4 a[144:147], v192, s[44:45] offset:0
	global_load_dwordx4 a[148:151], v192, s[44:45] offset:1024
	global_load_dwordx4 a[152:155], v192, s[44:45] offset:2048
	global_load_dwordx4 a[156:159], v192, s[44:45] offset:3072
	s_add_u32 s44, s44, 0x1000
	s_addc_u32 s45, s45, 0
	global_load_dwordx4 a[160:163], v192, s[44:45] offset:0
	global_load_dwordx4 a[164:167], v192, s[44:45] offset:1024
	global_load_dwordx4 a[168:171], v192, s[44:45] offset:2048
	global_load_dwordx4 a[172:175], v192, s[44:45] offset:3072
	s_add_u32 s44, s44, 0x1000
	s_addc_u32 s45, s45, 0
	global_load_dwordx4 a[176:179], v192, s[44:45] offset:0
	global_load_dwordx4 a[180:183], v192, s[44:45] offset:1024
	global_load_dwordx4 a[184:187], v192, s[44:45] offset:2048
	global_load_dwordx4 a[188:191], v192, s[44:45] offset:3072
	s_add_u32 s44, s44, 0x1000
	s_addc_u32 s45, s45, 0
	global_load_dwordx4 a[192:195], v192, s[44:45] offset:0
	global_load_dwordx4 a[196:199], v192, s[44:45] offset:1024
	global_load_dwordx4 a[200:203], v192, s[44:45] offset:2048
	global_load_dwordx4 a[204:207], v192, s[44:45] offset:3072
	s_add_u32 s44, s44, 0x1000
	s_addc_u32 s45, s45, 0
	global_load_dwordx4 a[208:211], v192, s[44:45] offset:0
	global_load_dwordx4 a[212:215], v192, s[44:45] offset:1024
	global_load_dwordx4 a[216:219], v192, s[44:45] offset:2048
	global_load_dwordx4 a[220:223], v192, s[44:45] offset:3072
	s_add_u32 s44, s44, 0x1000
	s_addc_u32 s45, s45, 0
	global_load_dwordx4 a[224:227], v192, s[44:45] offset:0
	global_load_dwordx4 a[228:231], v192, s[44:45] offset:1024
	global_load_dwordx4 a[232:235], v192, s[44:45] offset:2048
	global_load_dwordx4 a[236:239], v192, s[44:45] offset:3072
	s_add_u32 s44, s44, 0x1000
	s_addc_u32 s45, s45, 0
	global_load_dwordx4 a[240:243], v192, s[44:45] offset:0
	global_load_dwordx4 a[244:247], v192, s[44:45] offset:1024
	global_load_dwordx4 a[248:251], v192, s[44:45] offset:2048
	global_load_dwordx4 a[252:255], v192, s[44:45] offset:3072
	s_add_u32 s44, s44, 0x1000
	s_addc_u32 s45, s45, 0
	v_mov_b32_e32 v128, 0
	v_mov_b32_e32 v129, 0
	v_mov_b32_e32 v130, 0
	v_mov_b32_e32 v131, 0
	v_mov_b32_e32 v132, 0
	v_mov_b32_e32 v133, 0
	v_mov_b32_e32 v134, 0
	v_mov_b32_e32 v135, 0
	v_mov_b32_e32 v136, 0
	v_mov_b32_e32 v137, 0
	v_mov_b32_e32 v138, 0
	v_mov_b32_e32 v139, 0
	v_mov_b32_e32 v140, 0
	v_mov_b32_e32 v141, 0
	v_mov_b32_e32 v142, 0
	v_mov_b32_e32 v143, 0
	v_mov_b32_e32 v144, 0
	v_mov_b32_e32 v145, 0
	v_mov_b32_e32 v146, 0
	v_mov_b32_e32 v147, 0
	v_mov_b32_e32 v148, 0
	v_mov_b32_e32 v149, 0
	v_mov_b32_e32 v150, 0
	v_mov_b32_e32 v151, 0
	v_mov_b32_e32 v152, 0
	v_mov_b32_e32 v153, 0
	v_mov_b32_e32 v154, 0
	v_mov_b32_e32 v155, 0
	v_mov_b32_e32 v156, 0
	v_mov_b32_e32 v157, 0
	v_mov_b32_e32 v158, 0
	v_mov_b32_e32 v159, 0
	s_lshl_b32 s64, s30, 5
	s_lshl_b32 s65, s32, 3
	s_add_u32 s64, s64, s65
	v_lshlrev_b32_e32 v255, 2, v254
	v_add_u32_e32 v255, s64, v255
	v_lshlrev_b32_e32 v200, 2, v255
	global_load_dwordx4 v[228:231], v200, s[22:23]
	v_add_u32_e32 v201, 0x1000, v200
	global_load_dwordx4 v[232:235], v201, s[22:23]
	s_lshl_b32 s65, s32, 11
	v_lshl_add_u32 v248, v253, 3, s65
	v_add_u32_e32 v248, 0x20000, v248
	s_lshl_b32 s65, s32, 8
	v_lshl_add_u32 v249, v253, 3, s65
	v_add_u32_e32 v249, 0x20000, v249
	v_lshlrev_b32_e32 v250, 3, v253
	s_lshl_b32 s65, s30, 11
	s_lshl_b32 s66, s29, 8
	s_add_u32 s65, s65, s66
	s_lshl_b32 s66, s32, 5
	s_add_u32 s65, s65, s66
	s_lshl_b32 s65, s65, 3
	s_add_u32 s62, s24, s65
	s_addc_u32 s63, s25, 0
	s_lshl_b32 s65, s29, 5
	s_add_u32 s65, s65, s30
	s_lshl_b32 s65, s65, 2
	s_add_u32 s65, s65, s32
	s_lshl_b32 s65, s65, 15
	s_add_u32 s42, s18, s65
	s_addc_u32 s43, s19, 0
	s_waitcnt vmcnt(0)
	s_waitcnt vmcnt(0)
	s_mov_b32 s33, 0
	s_add_u32 s46, s42, 0x0
	s_addc_u32 s47, s43, 0
	global_load_dwordx4 v[0:3], v192, s[46:47] offset:0
	global_load_dwordx4 v[4:7], v192, s[46:47] offset:1024
	global_load_dwordx4 v[8:11], v192, s[46:47] offset:2048
	global_load_dwordx4 v[12:15], v192, s[46:47] offset:3072
	s_add_u32 s46, s42, 0x1000
	s_addc_u32 s47, s43, 0
	global_load_dwordx4 v[16:19], v192, s[46:47] offset:0
	global_load_dwordx4 v[20:23], v192, s[46:47] offset:1024
	global_load_dwordx4 v[24:27], v192, s[46:47] offset:2048
	global_load_dwordx4 v[28:31], v192, s[46:47] offset:3072
	s_add_u32 s46, s42, 0x2000
	s_addc_u32 s47, s43, 0
	global_load_dwordx4 v[32:35], v192, s[46:47] offset:0
	global_load_dwordx4 v[36:39], v192, s[46:47] offset:1024
	global_load_dwordx4 v[40:43], v192, s[46:47] offset:2048
	global_load_dwordx4 v[44:47], v192, s[46:47] offset:3072
	s_add_u32 s46, s42, 0x3000
	s_addc_u32 s47, s43, 0
	global_load_dwordx4 v[48:51], v192, s[46:47] offset:0
	global_load_dwordx4 v[52:55], v192, s[46:47] offset:1024
	global_load_dwordx4 v[56:59], v192, s[46:47] offset:2048
	global_load_dwordx4 v[60:63], v192, s[46:47] offset:3072
	s_add_u32 s46, s42, 0x4000
	s_addc_u32 s47, s43, 0
	global_load_dwordx4 v[64:67], v192, s[46:47] offset:0
	global_load_dwordx4 v[68:71], v192, s[46:47] offset:1024
	global_load_dwordx4 v[72:75], v192, s[46:47] offset:2048
	global_load_dwordx4 v[76:79], v192, s[46:47] offset:3072
	s_add_u32 s46, s42, 0x5000
	s_addc_u32 s47, s43, 0
	global_load_dwordx4 v[80:83], v192, s[46:47] offset:0
	global_load_dwordx4 v[84:87], v192, s[46:47] offset:1024
	global_load_dwordx4 v[88:91], v192, s[46:47] offset:2048
	global_load_dwordx4 v[92:95], v192, s[46:47] offset:3072
	s_add_u32 s46, s42, 0x6000
	s_addc_u32 s47, s43, 0
	global_load_dwordx4 v[96:99], v192, s[46:47] offset:0
	global_load_dwordx4 v[100:103], v192, s[46:47] offset:1024
	global_load_dwordx4 v[104:107], v192, s[46:47] offset:2048
	global_load_dwordx4 v[108:111], v192, s[46:47] offset:3072
	s_add_u32 s46, s42, 0x7000
	s_addc_u32 s47, s43, 0
	global_load_dwordx4 v[112:115], v192, s[46:47] offset:0
	global_load_dwordx4 v[116:119], v192, s[46:47] offset:1024
	global_load_dwordx4 v[120:123], v192, s[46:47] offset:2048
	global_load_dwordx4 v[124:127], v192, s[46:47] offset:3072
	s_waitcnt vmcnt(0)
	s_and_b32 s64, s33, 1
	s_lshl_b32 s64, s64, 22
	s_add_u32 s64, s64, s50
	s_add_u32 s36, s6, s64
	s_addc_u32 s37, s7, 0
	s_lshl_b32 s64, s33, 3
	s_add_u32 s64, s64, s29
	s_lshl_b32 s64, s64, 5
	s_add_u32 s64, s64, s30
	s_lshl_b32 s64, s64, 2
	s_add_u32 s40, s8, s64
	s_addc_u32 s41, s9, 0
	s_lshl_b32 s64, s33, 19
	s_add_u32 s72, s62, s64
	s_addc_u32 s73, s63, 0
	v_exp_f32_e32 v200, v0
	v_exp_f32_e32 v201, v1
	v_exp_f32_e32 v202, v2
	v_exp_f32_e32 v203, v3
	v_exp_f32_e32 v204, v4
	v_exp_f32_e32 v205, v5
	v_exp_f32_e32 v206, v6
	v_exp_f32_e32 v207, v7
	v_exp_f32_e32 v208, v8
	v_exp_f32_e32 v209, v9
	v_exp_f32_e32 v210, v10
	v_exp_f32_e32 v211, v11
	v_exp_f32_e32 v212, v12
	v_exp_f32_e32 v213, v13
	v_exp_f32_e32 v214, v14
	v_exp_f32_e32 v215, v15
	v_add_f32_e32 v200, 1.0, v200
	v_add_f32_e32 v201, 1.0, v201
	v_add_f32_e32 v202, 1.0, v202
	v_add_f32_e32 v203, 1.0, v203
	v_add_f32_e32 v204, 1.0, v204
	v_add_f32_e32 v205, 1.0, v205
	v_add_f32_e32 v206, 1.0, v206
	v_add_f32_e32 v207, 1.0, v207
	v_add_f32_e32 v208, 1.0, v208
	v_add_f32_e32 v209, 1.0, v209
	v_add_f32_e32 v210, 1.0, v210
	v_add_f32_e32 v211, 1.0, v211
	v_add_f32_e32 v212, 1.0, v212
	v_add_f32_e32 v213, 1.0, v213
	v_add_f32_e32 v214, 1.0, v214
	v_add_f32_e32 v215, 1.0, v215
	v_rcp_f32_e32 v200, v200
	v_rcp_f32_e32 v201, v201
	v_rcp_f32_e32 v202, v202
	v_rcp_f32_e32 v203, v203
	v_rcp_f32_e32 v204, v204
	v_rcp_f32_e32 v205, v205
	v_rcp_f32_e32 v206, v206
	v_rcp_f32_e32 v207, v207
	v_rcp_f32_e32 v208, v208
	v_rcp_f32_e32 v209, v209
	v_rcp_f32_e32 v210, v210
	v_rcp_f32_e32 v211, v211
	v_rcp_f32_e32 v212, v212
	v_rcp_f32_e32 v213, v213
	v_rcp_f32_e32 v214, v214
	v_rcp_f32_e32 v215, v215
	v_fmamk_f32 v208, v208, 0xc0b8aa3b, v198
	v_fmamk_f32 v209, v209, 0xc0b8aa3b, v198
	v_fmamk_f32 v210, v210, 0xc0b8aa3b, v198
	v_fmamk_f32 v211, v211, 0xc0b8aa3b, v198
	v_mul_f32_e32 v204, v204, v128
	v_mul_f32_e32 v205, v205, v129
	v_mul_f32_e32 v206, v206, v130
	v_mul_f32_e32 v207, v207, v131
	v_fma_f32 v128, v200, v208, v204
	v_fma_f32 v129, v201, v209, v205
	v_fma_f32 v130, v202, v210, v206
	v_fma_f32 v131, v203, v211, v207
	v_exp_f32_e32 v200, v128
	v_exp_f32_e32 v201, v129
	v_exp_f32_e32 v202, v130
	v_exp_f32_e32 v203, v131
	v_add_f32_e32 v200, 1.0, v200
	v_add_f32_e32 v201, 1.0, v201
	v_add_f32_e32 v202, 1.0, v202
	v_add_f32_e32 v203, 1.0, v203
	v_rcp_f32_e32 v200, v200
	v_rcp_f32_e32 v201, v201
	v_rcp_f32_e32 v202, v202
	v_rcp_f32_e32 v203, v203
	v_fma_f32 v200, v200, 2.0, -1.0
	v_fma_f32 v201, v201, 2.0, -1.0
	v_fma_f32 v202, v202, 2.0, -1.0
	v_fma_f32 v203, v203, 2.0, -1.0
	v_mul_f32_e32 v216, v212, v200
	v_mul_f32_e32 v217, v213, v201
	v_mul_f32_e32 v218, v214, v202
	v_mul_f32_e32 v219, v215, v203
	v_mul_f32_e32 v236, v216, v228
	v_mul_f32_e32 v237, v216, v232
	v_fmac_f32_e32 v236, v217, v229
	v_fmac_f32_e32 v237, v217, v233
	v_fmac_f32_e32 v236, v218, v230
	v_fmac_f32_e32 v237, v218, v234
	v_fmac_f32_e32 v236, v219, v231
	v_fmac_f32_e32 v237, v219, v235
	v_mov_b32_e32 v238, v236
	v_mov_b32_e32 v239, v236
	v_mov_b32_e32 v240, v237
	v_mov_b32_e32 v241, v237
	s_nop 1
	v_permlane32_swap_b32_e32 v238, v239
	v_permlane32_swap_b32_e32 v240, v241
	v_add_f32_e32 v238, v238, v239
	v_add_f32_e32 v239, v240, v241
	ds_write_b64 v248, v[238:239] offset:0
	v_cvt_pk_f16_f32 v220, v216, v217
	v_cvt_pk_f16_f32 v221, v218, v219
	v_exp_f32_e32 v200, v16
	v_exp_f32_e32 v201, v17
	v_exp_f32_e32 v202, v18
	v_exp_f32_e32 v203, v19
	v_exp_f32_e32 v204, v20
	v_exp_f32_e32 v205, v21
	v_exp_f32_e32 v206, v22
	v_exp_f32_e32 v207, v23
	v_exp_f32_e32 v208, v24
	v_exp_f32_e32 v209, v25
	v_exp_f32_e32 v210, v26
	v_exp_f32_e32 v211, v27
	v_exp_f32_e32 v212, v28
	v_exp_f32_e32 v213, v29
	v_exp_f32_e32 v214, v30
	v_exp_f32_e32 v215, v31
	v_add_f32_e32 v200, 1.0, v200
	v_add_f32_e32 v201, 1.0, v201
	v_add_f32_e32 v202, 1.0, v202
	v_add_f32_e32 v203, 1.0, v203
	v_add_f32_e32 v204, 1.0, v204
	v_add_f32_e32 v205, 1.0, v205
	v_add_f32_e32 v206, 1.0, v206
	v_add_f32_e32 v207, 1.0, v207
	v_add_f32_e32 v208, 1.0, v208
	v_add_f32_e32 v209, 1.0, v209
	v_add_f32_e32 v210, 1.0, v210
	v_add_f32_e32 v211, 1.0, v211
	v_add_f32_e32 v212, 1.0, v212
	v_add_f32_e32 v213, 1.0, v213
	v_add_f32_e32 v214, 1.0, v214
	v_add_f32_e32 v215, 1.0, v215
	v_rcp_f32_e32 v200, v200
	v_rcp_f32_e32 v201, v201
	v_rcp_f32_e32 v202, v202
	v_rcp_f32_e32 v203, v203
	v_rcp_f32_e32 v204, v204
	v_rcp_f32_e32 v205, v205
	v_rcp_f32_e32 v206, v206
	v_rcp_f32_e32 v207, v207
	v_rcp_f32_e32 v208, v208
	v_rcp_f32_e32 v209, v209
	v_rcp_f32_e32 v210, v210
	v_rcp_f32_e32 v211, v211
	v_rcp_f32_e32 v212, v212
	v_rcp_f32_e32 v213, v213
	v_rcp_f32_e32 v214, v214
	v_rcp_f32_e32 v215, v215
	v_fmamk_f32 v208, v208, 0xc0b8aa3b, v198
	v_fmamk_f32 v209, v209, 0xc0b8aa3b, v198
	v_fmamk_f32 v210, v210, 0xc0b8aa3b, v198
	v_fmamk_f32 v211, v211, 0xc0b8aa3b, v198
	v_mul_f32_e32 v204, v204, v132
	v_mul_f32_e32 v205, v205, v133
	v_mul_f32_e32 v206, v206, v134
	v_mul_f32_e32 v207, v207, v135
	v_fma_f32 v132, v200, v208, v204
	v_fma_f32 v133, v201, v209, v205
	v_fma_f32 v134, v202, v210, v206
	v_fma_f32 v135, v203, v211, v207
	v_exp_f32_e32 v200, v132
	v_exp_f32_e32 v201, v133
	v_exp_f32_e32 v202, v134
	v_exp_f32_e32 v203, v135
	v_add_f32_e32 v200, 1.0, v200
	v_add_f32_e32 v201, 1.0, v201
	v_add_f32_e32 v202, 1.0, v202
	v_add_f32_e32 v203, 1.0, v203
	v_rcp_f32_e32 v200, v200
	v_rcp_f32_e32 v201, v201
	v_rcp_f32_e32 v202, v202
	v_rcp_f32_e32 v203, v203
	v_fma_f32 v200, v200, 2.0, -1.0
	v_fma_f32 v201, v201, 2.0, -1.0
	v_fma_f32 v202, v202, 2.0, -1.0
	v_fma_f32 v203, v203, 2.0, -1.0
	v_mul_f32_e32 v216, v212, v200
	v_mul_f32_e32 v217, v213, v201
	v_mul_f32_e32 v218, v214, v202
	v_mul_f32_e32 v219, v215, v203
	v_mul_f32_e32 v236, v216, v228
	v_mul_f32_e32 v237, v216, v232
	v_fmac_f32_e32 v236, v217, v229
	v_fmac_f32_e32 v237, v217, v233
	v_fmac_f32_e32 v236, v218, v230
	v_fmac_f32_e32 v237, v218, v234
	v_fmac_f32_e32 v236, v219, v231
	v_fmac_f32_e32 v237, v219, v235
	v_mov_b32_e32 v238, v236
	v_mov_b32_e32 v239, v236
	v_mov_b32_e32 v240, v237
	v_mov_b32_e32 v241, v237
	s_nop 1
	v_permlane32_swap_b32_e32 v238, v239
	v_permlane32_swap_b32_e32 v240, v241
	v_add_f32_e32 v238, v238, v239
	v_add_f32_e32 v239, v240, v241
	ds_write_b64 v248, v[238:239] offset:256
	v_cvt_pk_f16_f32 v222, v216, v217
	v_cvt_pk_f16_f32 v223, v218, v219
	s_nop 1
	v_permlane32_swap_b32_e32 v220, v222
	v_permlane32_swap_b32_e32 v221, v223
	s_cmp_eq_u32 s31, 0
	s_cbranch_scc1 .LD_slow4
	global_store_dwordx4 v195, v[220:223], s[36:37] offset:0
	s_branch .LD_join5

.LD_join5:
	v_exp_f32_e32 v200, v32
	v_exp_f32_e32 v201, v33
	v_exp_f32_e32 v202, v34
	v_exp_f32_e32 v203, v35
	v_exp_f32_e32 v204, v36
	v_exp_f32_e32 v205, v37
	v_exp_f32_e32 v206, v38
	v_exp_f32_e32 v207, v39
	v_exp_f32_e32 v208, v40
	v_exp_f32_e32 v209, v41
	v_exp_f32_e32 v210, v42
	v_exp_f32_e32 v211, v43
	v_exp_f32_e32 v212, v44
	v_exp_f32_e32 v213, v45
	v_exp_f32_e32 v214, v46
	v_exp_f32_e32 v215, v47
	v_add_f32_e32 v200, 1.0, v200
	v_add_f32_e32 v201, 1.0, v201
	v_add_f32_e32 v202, 1.0, v202
	v_add_f32_e32 v203, 1.0, v203
	v_add_f32_e32 v204, 1.0, v204
	v_add_f32_e32 v205, 1.0, v205
	v_add_f32_e32 v206, 1.0, v206
	v_add_f32_e32 v207, 1.0, v207
	v_add_f32_e32 v208, 1.0, v208
	v_add_f32_e32 v209, 1.0, v209
	v_add_f32_e32 v210, 1.0, v210
	v_add_f32_e32 v211, 1.0, v211
	v_add_f32_e32 v212, 1.0, v212
	v_add_f32_e32 v213, 1.0, v213
	v_add_f32_e32 v214, 1.0, v214
	v_add_f32_e32 v215, 1.0, v215
	v_rcp_f32_e32 v200, v200
	v_rcp_f32_e32 v201, v201
	v_rcp_f32_e32 v202, v202
	v_rcp_f32_e32 v203, v203
	v_rcp_f32_e32 v204, v204
	v_rcp_f32_e32 v205, v205
	v_rcp_f32_e32 v206, v206
	v_rcp_f32_e32 v207, v207
	v_rcp_f32_e32 v208, v208
	v_rcp_f32_e32 v209, v209
	v_rcp_f32_e32 v210, v210
	v_rcp_f32_e32 v211, v211
	v_rcp_f32_e32 v212, v212
	v_rcp_f32_e32 v213, v213
	v_rcp_f32_e32 v214, v214
	v_rcp_f32_e32 v215, v215
	v_fmamk_f32 v208, v208, 0xc0b8aa3b, v198
	v_fmamk_f32 v209, v209, 0xc0b8aa3b, v198
	v_fmamk_f32 v210, v210, 0xc0b8aa3b, v198
	v_fmamk_f32 v211, v211, 0xc0b8aa3b, v198
	v_mul_f32_e32 v204, v204, v136
	v_mul_f32_e32 v205, v205, v137
	v_mul_f32_e32 v206, v206, v138
	v_mul_f32_e32 v207, v207, v139
	v_fma_f32 v136, v200, v208, v204
	v_fma_f32 v137, v201, v209, v205
	v_fma_f32 v138, v202, v210, v206
	v_fma_f32 v139, v203, v211, v207
	v_exp_f32_e32 v200, v136
	v_exp_f32_e32 v201, v137
	v_exp_f32_e32 v202, v138
	v_exp_f32_e32 v203, v139
	v_add_f32_e32 v200, 1.0, v200
	v_add_f32_e32 v201, 1.0, v201
	v_add_f32_e32 v202, 1.0, v202
	v_add_f32_e32 v203, 1.0, v203
	v_rcp_f32_e32 v200, v200
	v_rcp_f32_e32 v201, v201
	v_rcp_f32_e32 v202, v202
	v_rcp_f32_e32 v203, v203
	v_fma_f32 v200, v200, 2.0, -1.0
	v_fma_f32 v201, v201, 2.0, -1.0
	v_fma_f32 v202, v202, 2.0, -1.0
	v_fma_f32 v203, v203, 2.0, -1.0
	v_mul_f32_e32 v216, v212, v200
	v_mul_f32_e32 v217, v213, v201
	v_mul_f32_e32 v218, v214, v202
	v_mul_f32_e32 v219, v215, v203
	v_mul_f32_e32 v236, v216, v228
	v_mul_f32_e32 v237, v216, v232
	v_fmac_f32_e32 v236, v217, v229
	v_fmac_f32_e32 v237, v217, v233
	v_fmac_f32_e32 v236, v218, v230
	v_fmac_f32_e32 v237, v218, v234
	v_fmac_f32_e32 v236, v219, v231
	v_fmac_f32_e32 v237, v219, v235
	v_mov_b32_e32 v238, v236
	v_mov_b32_e32 v239, v236
	v_mov_b32_e32 v240, v237
	v_mov_b32_e32 v241, v237
	s_nop 1
	v_permlane32_swap_b32_e32 v238, v239
	v_permlane32_swap_b32_e32 v240, v241
	v_add_f32_e32 v238, v238, v239
	v_add_f32_e32 v239, v240, v241
	ds_write_b64 v248, v[238:239] offset:512
	v_cvt_pk_f16_f32 v224, v216, v217
	v_cvt_pk_f16_f32 v225, v218, v219
	v_exp_f32_e32 v200, v48
	v_exp_f32_e32 v201, v49
	v_exp_f32_e32 v202, v50
	v_exp_f32_e32 v203, v51
	v_exp_f32_e32 v204, v52
	v_exp_f32_e32 v205, v53
	v_exp_f32_e32 v206, v54
	v_exp_f32_e32 v207, v55
	v_exp_f32_e32 v208, v56
	v_exp_f32_e32 v209, v57
	v_exp_f32_e32 v210, v58
	v_exp_f32_e32 v211, v59
	v_exp_f32_e32 v212, v60
	v_exp_f32_e32 v213, v61
	v_exp_f32_e32 v214, v62
	v_exp_f32_e32 v215, v63
	v_add_f32_e32 v200, 1.0, v200
	v_add_f32_e32 v201, 1.0, v201
	v_add_f32_e32 v202, 1.0, v202
	v_add_f32_e32 v203, 1.0, v203
	v_add_f32_e32 v204, 1.0, v204
	v_add_f32_e32 v205, 1.0, v205
	v_add_f32_e32 v206, 1.0, v206
	v_add_f32_e32 v207, 1.0, v207
	v_add_f32_e32 v208, 1.0, v208
	v_add_f32_e32 v209, 1.0, v209
	v_add_f32_e32 v210, 1.0, v210
	v_add_f32_e32 v211, 1.0, v211
	v_add_f32_e32 v212, 1.0, v212
	v_add_f32_e32 v213, 1.0, v213
	v_add_f32_e32 v214, 1.0, v214
	v_add_f32_e32 v215, 1.0, v215
	v_rcp_f32_e32 v200, v200
	v_rcp_f32_e32 v201, v201
	v_rcp_f32_e32 v202, v202
	v_rcp_f32_e32 v203, v203
	v_rcp_f32_e32 v204, v204
	v_rcp_f32_e32 v205, v205
	v_rcp_f32_e32 v206, v206
	v_rcp_f32_e32 v207, v207
	v_rcp_f32_e32 v208, v208
	v_rcp_f32_e32 v209, v209
	v_rcp_f32_e32 v210, v210
	v_rcp_f32_e32 v211, v211
	v_rcp_f32_e32 v212, v212
	v_rcp_f32_e32 v213, v213
	v_rcp_f32_e32 v214, v214
	v_rcp_f32_e32 v215, v215
	v_fmamk_f32 v208, v208, 0xc0b8aa3b, v198
	v_fmamk_f32 v209, v209, 0xc0b8aa3b, v198
	v_fmamk_f32 v210, v210, 0xc0b8aa3b, v198
	v_fmamk_f32 v211, v211, 0xc0b8aa3b, v198
	v_mul_f32_e32 v204, v204, v140
	v_mul_f32_e32 v205, v205, v141
	v_mul_f32_e32 v206, v206, v142
	v_mul_f32_e32 v207, v207, v143
	v_fma_f32 v140, v200, v208, v204
	v_fma_f32 v141, v201, v209, v205
	v_fma_f32 v142, v202, v210, v206
	v_fma_f32 v143, v203, v211, v207
	v_exp_f32_e32 v200, v140
	v_exp_f32_e32 v201, v141
	v_exp_f32_e32 v202, v142
	v_exp_f32_e32 v203, v143
	v_add_f32_e32 v200, 1.0, v200
	v_add_f32_e32 v201, 1.0, v201
	v_add_f32_e32 v202, 1.0, v202
	v_add_f32_e32 v203, 1.0, v203
	v_rcp_f32_e32 v200, v200
	v_rcp_f32_e32 v201, v201
	v_rcp_f32_e32 v202, v202
	v_rcp_f32_e32 v203, v203
	v_fma_f32 v200, v200, 2.0, -1.0
	v_fma_f32 v201, v201, 2.0, -1.0
	v_fma_f32 v202, v202, 2.0, -1.0
	v_fma_f32 v203, v203, 2.0, -1.0
	v_mul_f32_e32 v216, v212, v200
	v_mul_f32_e32 v217, v213, v201
	v_mul_f32_e32 v218, v214, v202
	v_mul_f32_e32 v219, v215, v203
	v_mul_f32_e32 v236, v216, v228
	v_mul_f32_e32 v237, v216, v232
	v_fmac_f32_e32 v236, v217, v229
	v_fmac_f32_e32 v237, v217, v233
	v_fmac_f32_e32 v236, v218, v230
	v_fmac_f32_e32 v237, v218, v234
	v_fmac_f32_e32 v236, v219, v231
	v_fmac_f32_e32 v237, v219, v235
	v_mov_b32_e32 v238, v236
	v_mov_b32_e32 v239, v236
	v_mov_b32_e32 v240, v237
	v_mov_b32_e32 v241, v237
	s_nop 1
	v_permlane32_swap_b32_e32 v238, v239
	v_permlane32_swap_b32_e32 v240, v241
	v_add_f32_e32 v238, v238, v239
	v_add_f32_e32 v239, v240, v241
	ds_write_b64 v248, v[238:239] offset:768
	v_cvt_pk_f16_f32 v226, v216, v217
	v_cvt_pk_f16_f32 v227, v218, v219
	s_nop 1
	v_permlane32_swap_b32_e32 v224, v226
	v_permlane32_swap_b32_e32 v225, v227
	s_cmp_eq_u32 s31, 0
	s_cbranch_scc1 .LD_slow6
	global_store_dwordx4 v195, v[224:227], s[36:37] offset:2048
	s_branch .LD_join7

.LD_join9:
	ds_read_b64 v[200:201], v249 offset:0
	ds_read_b64 v[202:203], v249 offset:2048
	ds_read_b64 v[204:205], v249 offset:4096
	ds_read_b64 v[206:207], v249 offset:6144
	s_waitcnt lgkmcnt(0)
	v_add_f32_e32 v200, v200, v202
	v_add_f32_e32 v201, v201, v203
	v_add_f32_e32 v200, v200, v204
	v_add_f32_e32 v201, v201, v205
	v_add_f32_e32 v200, v200, v206
	v_add_f32_e32 v201, v201, v207
	global_store_dwordx2 v250, v[200:201], s[72:73]
	s_mov_b32 s33, 1
	s_add_u32 s46, s42, 0x0
	s_addc_u32 s47, s43, 0
	global_load_dwordx4 v[0:3], v192, s[46:47] offset:0
	global_load_dwordx4 v[4:7], v192, s[46:47] offset:1024
	global_load_dwordx4 v[8:11], v192, s[46:47] offset:2048
	global_load_dwordx4 v[12:15], v192, s[46:47] offset:3072
	s_add_u32 s46, s42, 0x1000
	s_addc_u32 s47, s43, 0
	global_load_dwordx4 v[16:19], v192, s[46:47] offset:0
	global_load_dwordx4 v[20:23], v192, s[46:47] offset:1024
	global_load_dwordx4 v[24:27], v192, s[46:47] offset:2048
	global_load_dwordx4 v[28:31], v192, s[46:47] offset:3072
	s_add_u32 s46, s42, 0x2000
	s_addc_u32 s47, s43, 0
	global_load_dwordx4 v[32:35], v192, s[46:47] offset:0
	global_load_dwordx4 v[36:39], v192, s[46:47] offset:1024
	global_load_dwordx4 v[40:43], v192, s[46:47] offset:2048
	global_load_dwordx4 v[44:47], v192, s[46:47] offset:3072
	s_add_u32 s46, s42, 0x3000
	s_addc_u32 s47, s43, 0
	global_load_dwordx4 v[48:51], v192, s[46:47] offset:0
	global_load_dwordx4 v[52:55], v192, s[46:47] offset:1024
	global_load_dwordx4 v[56:59], v192, s[46:47] offset:2048
	global_load_dwordx4 v[60:63], v192, s[46:47] offset:3072
	s_waitcnt vmcnt(0)
	s_waitcnt lgkmcnt(0)
	s_cmp_ge_u32 s33, s28
	s_cbranch_scc1 .LD_end11
	s_sub_u32 s71, s33, 1
	s_and_b32 s64, s71, 1
	s_lshl_b32 s64, s64, 22
	s_add_u32 s64, s64, s49
	s_add_u32 s34, s6, s64
	s_addc_u32 s35, s7, 0
	s_lshl_b32 s64, s71, 3
	s_add_u32 s64, s64, s29
	s_lshl_b32 s64, s64, 7
	s_add_u32 s38, s8, s64
	s_addc_u32 s39, s9, 0

.LD_loop10:
	s_sub_u32 s71, s33, 1
	s_and_b32 s64, s71, 1
	s_lshl_b32 s64, s64, 22
	s_add_u32 s64, s64, s50
	s_add_u32 s64, s64, 0x40000
	s_add_u32 s36, s6, s64
	s_addc_u32 s37, s7, 0
	s_lshl_b32 s64, s71, 3
	s_add_u32 s64, s64, s29
	s_lshl_b32 s64, s64, 5
	s_add_u32 s64, s64, s30
	s_lshl_b32 s64, s64, 2
	s_add_u32 s40, s8, s64
	s_addc_u32 s41, s9, 0
	s_lshl_b32 s64, s71, 19
	s_add_u32 s64, s64, 0x400
	s_add_u32 s72, s62, s64
	s_addc_u32 s73, s63, 0
	s_nop 11
	v_exp_f32_e32 v200, v64
	v_exp_f32_e32 v201, v65
	v_exp_f32_e32 v202, v66
	v_exp_f32_e32 v203, v67
	v_exp_f32_e32 v204, v68
	v_exp_f32_e32 v205, v69
	v_exp_f32_e32 v206, v70
	v_exp_f32_e32 v207, v71
	v_exp_f32_e32 v208, v72
	v_exp_f32_e32 v209, v73
	v_exp_f32_e32 v210, v74
	v_exp_f32_e32 v211, v75
	v_exp_f32_e32 v212, v76
	v_exp_f32_e32 v213, v77
	v_exp_f32_e32 v214, v78
	v_exp_f32_e32 v215, v79
	v_add_f32_e32 v200, 1.0, v200
	v_add_f32_e32 v201, 1.0, v201
	v_add_f32_e32 v202, 1.0, v202
	v_add_f32_e32 v203, 1.0, v203
	v_add_f32_e32 v204, 1.0, v204
	v_add_f32_e32 v205, 1.0, v205
	v_add_f32_e32 v206, 1.0, v206
	v_add_f32_e32 v207, 1.0, v207
	v_add_f32_e32 v208, 1.0, v208
	v_add_f32_e32 v209, 1.0, v209
	v_add_f32_e32 v210, 1.0, v210
	v_add_f32_e32 v211, 1.0, v211
	v_add_f32_e32 v212, 1.0, v212
	v_add_f32_e32 v213, 1.0, v213
	v_add_f32_e32 v214, 1.0, v214
	v_add_f32_e32 v215, 1.0, v215
	v_rcp_f32_e32 v200, v200
	v_rcp_f32_e32 v201, v201
	v_rcp_f32_e32 v202, v202
	v_rcp_f32_e32 v203, v203
	v_rcp_f32_e32 v204, v204
	v_rcp_f32_e32 v205, v205
	v_rcp_f32_e32 v206, v206
	v_rcp_f32_e32 v207, v207
	v_rcp_f32_e32 v208, v208
	v_rcp_f32_e32 v209, v209
	v_rcp_f32_e32 v210, v210
	v_rcp_f32_e32 v211, v211
	v_rcp_f32_e32 v212, v212
	v_rcp_f32_e32 v213, v213
	v_rcp_f32_e32 v214, v214
	v_rcp_f32_e32 v215, v215
	v_fmamk_f32 v208, v208, 0xc0b8aa3b, v198
	v_fmamk_f32 v209, v209, 0xc0b8aa3b, v198
	v_fmamk_f32 v210, v210, 0xc0b8aa3b, v198
	v_fmamk_f32 v211, v211, 0xc0b8aa3b, v198
	v_mul_f32_e32 v204, v204, v144
	v_mul_f32_e32 v205, v205, v145
	v_mul_f32_e32 v206, v206, v146
	v_mul_f32_e32 v207, v207, v147
	v_fma_f32 v144, v200, v208, v204
	v_fma_f32 v145, v201, v209, v205
	v_fma_f32 v146, v202, v210, v206
	v_fma_f32 v147, v203, v211, v207
	v_exp_f32_e32 v200, v144
	v_exp_f32_e32 v201, v145
	v_exp_f32_e32 v202, v146
	v_exp_f32_e32 v203, v147
	s_waitcnt lgkmcnt(7)
	v_mfma_f32_32x32x16_f16 v[0:15], a[0:3], v[160:163], v[0:15]
	ds_read_b128 v[160:163], v192 offset:8192
	v_add_f32_e32 v200, 1.0, v200
	v_add_f32_e32 v201, 1.0, v201
	v_add_f32_e32 v202, 1.0, v202
	v_add_f32_e32 v203, 1.0, v203
	s_waitcnt lgkmcnt(7)
	v_mfma_f32_32x32x16_f16 v[16:31], a[0:3], v[164:167], v[16:31]
	ds_read_b128 v[164:167], v192 offset:9216
	global_load_lds_dwordx4 v192, s[44:45] offset:1024 sc1
	v_rcp_f32_e32 v200, v200
	v_rcp_f32_e32 v201, v201
	s_waitcnt lgkmcnt(7)
	v_mfma_f32_32x32x16_f16 v[32:47], a[0:3], v[168:171], v[32:47]
	ds_read_b128 v[168:171], v192 offset:10240
	v_rcp_f32_e32 v202, v202
	v_rcp_f32_e32 v203, v203
	v_fma_f32 v200, v200, 2.0, -1.0
	s_waitcnt lgkmcnt(7)
	v_mfma_f32_32x32x16_f16 v[48:63], a[0:3], v[172:175], v[48:63]
	ds_read_b128 v[172:175], v192 offset:11264
	v_fma_f32 v201, v201, 2.0, -1.0
	v_fma_f32 v202, v202, 2.0, -1.0
	v_fma_f32 v203, v203, 2.0, -1.0
	v_mul_f32_e32 v216, v212, v200
	v_mul_f32_e32 v217, v213, v201
	s_waitcnt lgkmcnt(7)
	v_mfma_f32_32x32x16_f16 v[0:15], a[4:7], v[176:179], v[0:15]
	ds_read_b128 v[176:179], v192 offset:12288
	v_mul_f32_e32 v218, v214, v202
	v_mul_f32_e32 v219, v215, v203
	v_mul_f32_e32 v236, v216, v228
	v_mul_f32_e32 v237, v216, v232
	v_fmac_f32_e32 v236, v217, v229
	s_waitcnt lgkmcnt(7)
	v_mfma_f32_32x32x16_f16 v[16:31], a[4:7], v[180:183], v[16:31]
	ds_read_b128 v[180:183], v192 offset:13312
	global_load_lds_dwordx4 v192, s[44:45] offset:2048 sc1
	v_fmac_f32_e32 v237, v217, v233
	v_fmac_f32_e32 v236, v218, v230
	v_fmac_f32_e32 v237, v218, v234
	v_fmac_f32_e32 v236, v219, v231
	v_fmac_f32_e32 v237, v219, v235
	s_waitcnt lgkmcnt(7)
	v_mfma_f32_32x32x16_f16 v[32:47], a[4:7], v[184:187], v[32:47]
	ds_read_b128 v[184:187], v192 offset:14336
	v_mov_b32_e32 v238, v236
	v_mov_b32_e32 v239, v236
	v_mov_b32_e32 v240, v237
	v_mov_b32_e32 v241, v237
	s_waitcnt lgkmcnt(7)
	v_mfma_f32_32x32x16_f16 v[48:63], a[4:7], v[188:191], v[48:63]
	ds_read_b128 v[188:191], v192 offset:15360
	s_nop 1
	v_permlane32_swap_b32_e32 v238, v239
	v_permlane32_swap_b32_e32 v240, v241
	v_add_f32_e32 v238, v238, v239
	v_add_f32_e32 v239, v240, v241
	ds_write_b64 v248, v[238:239] offset:1024
	s_waitcnt lgkmcnt(8)
	v_mfma_f32_32x32x16_f16 v[0:15], a[8:11], v[160:163], v[0:15]
	ds_read_b128 v[160:163], v192 offset:16384
	v_cvt_pk_f16_f32 v220, v216, v217
	v_cvt_pk_f16_f32 v221, v218, v219
	v_exp_f32_e32 v200, v80
	s_waitcnt lgkmcnt(8)
	v_mfma_f32_32x32x16_f16 v[16:31], a[8:11], v[164:167], v[16:31]
	ds_read_b128 v[164:167], v192 offset:17408
	global_load_lds_dwordx4 v192, s[44:45] offset:3072 sc1
	v_exp_f32_e32 v201, v81
	v_exp_f32_e32 v202, v82
	s_waitcnt lgkmcnt(8)
	v_mfma_f32_32x32x16_f16 v[32:47], a[8:11], v[168:171], v[32:47]
	ds_read_b128 v[168:171], v192 offset:18432
	v_exp_f32_e32 v203, v83
	v_exp_f32_e32 v204, v84
	s_waitcnt lgkmcnt(8)
	v_mfma_f32_32x32x16_f16 v[48:63], a[8:11], v[172:175], v[48:63]
	ds_read_b128 v[172:175], v192 offset:19456
	v_exp_f32_e32 v205, v85
	v_exp_f32_e32 v206, v86
	s_waitcnt lgkmcnt(8)
	v_mfma_f32_32x32x16_f16 v[0:15], a[12:15], v[176:179], v[0:15]
	ds_read_b128 v[176:179], v192 offset:20480
	v_exp_f32_e32 v207, v87
	v_exp_f32_e32 v208, v88
	s_waitcnt lgkmcnt(8)
	v_mfma_f32_32x32x16_f16 v[16:31], a[12:15], v[180:183], v[16:31]
	ds_read_b128 v[180:183], v192 offset:21504
	s_add_u32 s44, s34, 0x11000
	s_addc_u32 s45, s35, 0
	s_mov_b32 m0, s57
	s_nop 0
	global_load_lds_dwordx4 v192, s[44:45] sc1
	v_exp_f32_e32 v209, v89
	v_exp_f32_e32 v210, v90
	s_waitcnt lgkmcnt(8)
	v_mfma_f32_32x32x16_f16 v[32:47], a[12:15], v[184:187], v[32:47]
	ds_read_b128 v[184:187], v192 offset:22528
	v_exp_f32_e32 v211, v91
	v_exp_f32_e32 v212, v92
	s_waitcnt lgkmcnt(8)
	v_mfma_f32_32x32x16_f16 v[48:63], a[12:15], v[188:191], v[48:63]
	ds_read_b128 v[188:191], v192 offset:23552
	v_exp_f32_e32 v213, v93
	v_exp_f32_e32 v214, v94
	s_waitcnt lgkmcnt(7)
	v_mfma_f32_32x32x16_f16 v[0:15], a[16:19], v[160:163], v[0:15]
	ds_read_b128 v[160:163], v192 offset:24576
	v_exp_f32_e32 v215, v95
	v_add_f32_e32 v200, 1.0, v200
	v_add_f32_e32 v201, 1.0, v201
	v_add_f32_e32 v202, 1.0, v202
	s_waitcnt lgkmcnt(7)
	v_mfma_f32_32x32x16_f16 v[16:31], a[16:19], v[164:167], v[16:31]
	ds_read_b128 v[164:167], v192 offset:25600
	global_load_lds_dwordx4 v192, s[44:45] offset:1024 sc1
	v_add_f32_e32 v203, 1.0, v203
	v_add_f32_e32 v204, 1.0, v204
	v_add_f32_e32 v205, 1.0, v205
	v_add_f32_e32 v206, 1.0, v206
	v_add_f32_e32 v207, 1.0, v207
	s_waitcnt lgkmcnt(7)
	v_mfma_f32_32x32x16_f16 v[32:47], a[16:19], v[168:171], v[32:47]
	ds_read_b128 v[168:171], v192 offset:26624
	v_add_f32_e32 v208, 1.0, v208
	v_add_f32_e32 v209, 1.0, v209
	v_add_f32_e32 v210, 1.0, v210
	v_add_f32_e32 v211, 1.0, v211
	v_add_f32_e32 v212, 1.0, v212
	s_waitcnt lgkmcnt(7)
	v_mfma_f32_32x32x16_f16 v[48:63], a[16:19], v[172:175], v[48:63]
	ds_read_b128 v[172:175], v192 offset:27648
	v_add_f32_e32 v213, 1.0, v213
	v_add_f32_e32 v214, 1.0, v214
	v_add_f32_e32 v215, 1.0, v215
	v_rcp_f32_e32 v200, v200
	s_waitcnt lgkmcnt(7)
	v_mfma_f32_32x32x16_f16 v[0:15], a[20:23], v[176:179], v[0:15]
	ds_read_b128 v[176:179], v192 offset:28672
	v_rcp_f32_e32 v201, v201
	v_rcp_f32_e32 v202, v202
	s_waitcnt lgkmcnt(7)
	v_mfma_f32_32x32x16_f16 v[16:31], a[20:23], v[180:183], v[16:31]
	ds_read_b128 v[180:183], v192 offset:29696
	global_load_lds_dwordx4 v192, s[44:45] offset:2048 sc1
	v_rcp_f32_e32 v203, v203
	v_rcp_f32_e32 v204, v204
	s_waitcnt lgkmcnt(7)
	v_mfma_f32_32x32x16_f16 v[32:47], a[20:23], v[184:187], v[32:47]
	ds_read_b128 v[184:187], v192 offset:30720
	v_rcp_f32_e32 v205, v205
	v_rcp_f32_e32 v206, v206
	s_waitcnt lgkmcnt(7)
	v_mfma_f32_32x32x16_f16 v[48:63], a[20:23], v[188:191], v[48:63]
	ds_read_b128 v[188:191], v192 offset:31744
	v_rcp_f32_e32 v207, v207
	v_rcp_f32_e32 v208, v208
	s_waitcnt vmcnt(7)
	s_barrier
	s_waitcnt lgkmcnt(7)
	v_mfma_f32_32x32x16_f16 v[0:15], a[24:27], v[160:163], v[0:15]
	ds_read_b128 v[160:163], v192 offset:32768
	v_rcp_f32_e32 v209, v209
	v_rcp_f32_e32 v210, v210
	s_waitcnt lgkmcnt(7)
	v_mfma_f32_32x32x16_f16 v[16:31], a[24:27], v[164:167], v[16:31]
	ds_read_b128 v[164:167], v192 offset:33792
	global_load_lds_dwordx4 v192, s[44:45] offset:3072 sc1
	v_rcp_f32_e32 v211, v211
	v_rcp_f32_e32 v212, v212
	s_waitcnt lgkmcnt(7)
	v_mfma_f32_32x32x16_f16 v[32:47], a[24:27], v[168:171], v[32:47]
	ds_read_b128 v[168:171], v192 offset:34816
	v_rcp_f32_e32 v213, v213
	v_rcp_f32_e32 v214, v214
	s_waitcnt lgkmcnt(7)
	v_mfma_f32_32x32x16_f16 v[48:63], a[24:27], v[172:175], v[48:63]
	ds_read_b128 v[172:175], v192 offset:35840
	v_rcp_f32_e32 v215, v215
	v_fmamk_f32 v208, v208, 0xc0b8aa3b, v198
	v_fmamk_f32 v209, v209, 0xc0b8aa3b, v198
	v_fmamk_f32 v210, v210, 0xc0b8aa3b, v198
	s_waitcnt lgkmcnt(7)
	v_mfma_f32_32x32x16_f16 v[0:15], a[28:31], v[176:179], v[0:15]
	ds_read_b128 v[176:179], v192 offset:36864
	v_fmamk_f32 v211, v211, 0xc0b8aa3b, v198
	v_mul_f32_e32 v204, v204, v148
	v_mul_f32_e32 v205, v205, v149
	v_mul_f32_e32 v206, v206, v150
	v_mul_f32_e32 v207, v207, v151
	s_waitcnt lgkmcnt(7)
	v_mfma_f32_32x32x16_f16 v[16:31], a[28:31], v[180:183], v[16:31]
	ds_read_b128 v[180:183], v192 offset:37888
	s_add_u32 s44, s34, 0x18000
	s_addc_u32 s45, s35, 0
	s_mov_b32 m0, s58
	s_nop 0
	global_load_lds_dwordx4 v192, s[44:45] sc1
	v_fma_f32 v148, v200, v208, v204
	v_fma_f32 v149, v201, v209, v205
	v_fma_f32 v150, v202, v210, v206
	v_fma_f32 v151, v203, v211, v207
	s_waitcnt lgkmcnt(7)
	v_mfma_f32_32x32x16_f16 v[32:47], a[28:31], v[184:187], v[32:47]
	ds_read_b128 v[184:187], v192 offset:38912
	v_exp_f32_e32 v200, v148
	v_exp_f32_e32 v201, v149
	s_waitcnt lgkmcnt(7)
	v_mfma_f32_32x32x16_f16 v[48:63], a[28:31], v[188:191], v[48:63]
	ds_read_b128 v[188:191], v192 offset:39936
	v_exp_f32_e32 v202, v150
	v_exp_f32_e32 v203, v151
	v_add_f32_e32 v200, 1.0, v200
	s_waitcnt lgkmcnt(7)
	v_mfma_f32_32x32x16_f16 v[0:15], a[32:35], v[160:163], v[0:15]
	ds_read_b128 v[160:163], v192 offset:40960
	v_add_f32_e32 v201, 1.0, v201
	v_add_f32_e32 v202, 1.0, v202
	v_add_f32_e32 v203, 1.0, v203
	v_rcp_f32_e32 v200, v200
	s_waitcnt lgkmcnt(7)
	v_mfma_f32_32x32x16_f16 v[16:31], a[32:35], v[164:167], v[16:31]
	ds_read_b128 v[164:167], v192 offset:41984
	global_load_lds_dwordx4 v192, s[44:45] offset:1024 sc1
	v_rcp_f32_e32 v201, v201
	v_rcp_f32_e32 v202, v202
	s_waitcnt lgkmcnt(7)
	v_mfma_f32_32x32x16_f16 v[32:47], a[32:35], v[168:171], v[32:47]
	ds_read_b128 v[168:171], v192 offset:43008
	v_rcp_f32_e32 v203, v203
	v_fma_f32 v200, v200, 2.0, -1.0
	v_fma_f32 v201, v201, 2.0, -1.0
	v_fma_f32 v202, v202, 2.0, -1.0
	s_waitcnt lgkmcnt(7)
	v_mfma_f32_32x32x16_f16 v[48:63], a[32:35], v[172:175], v[48:63]
	ds_read_b128 v[172:175], v192 offset:44032
	v_fma_f32 v203, v203, 2.0, -1.0
	v_mul_f32_e32 v216, v212, v200
	v_mul_f32_e32 v217, v213, v201
	v_mul_f32_e32 v218, v214, v202
	v_mul_f32_e32 v219, v215, v203
	s_waitcnt lgkmcnt(7)
	v_mfma_f32_32x32x16_f16 v[0:15], a[36:39], v[176:179], v[0:15]
	ds_read_b128 v[176:179], v192 offset:45056
	v_mul_f32_e32 v236, v216, v228
	v_mul_f32_e32 v237, v216, v232
	v_fmac_f32_e32 v236, v217, v229
	v_fmac_f32_e32 v237, v217, v233
	v_fmac_f32_e32 v236, v218, v230
	s_waitcnt lgkmcnt(7)
	v_mfma_f32_32x32x16_f16 v[16:31], a[36:39], v[180:183], v[16:31]
	ds_read_b128 v[180:183], v192 offset:46080
	global_load_lds_dwordx4 v192, s[44:45] offset:2048 sc1
	v_fmac_f32_e32 v237, v218, v234
	v_fmac_f32_e32 v236, v219, v231
	v_fmac_f32_e32 v237, v219, v235
	v_mov_b32_e32 v238, v236
	v_mov_b32_e32 v239, v236
	s_waitcnt lgkmcnt(7)
	v_mfma_f32_32x32x16_f16 v[32:47], a[36:39], v[184:187], v[32:47]
	ds_read_b128 v[184:187], v192 offset:47104
	v_mov_b32_e32 v240, v237
	v_mov_b32_e32 v241, v237
	s_waitcnt lgkmcnt(7)
	v_mfma_f32_32x32x16_f16 v[48:63], a[36:39], v[188:191], v[48:63]
	ds_read_b128 v[188:191], v192 offset:48128
	s_nop 1
	v_permlane32_swap_b32_e32 v238, v239
	v_permlane32_swap_b32_e32 v240, v241
	v_add_f32_e32 v238, v238, v239
	v_add_f32_e32 v239, v240, v241
	ds_write_b64 v248, v[238:239] offset:1280
	s_waitcnt lgkmcnt(8)
	v_mfma_f32_32x32x16_f16 v[0:15], a[40:43], v[160:163], v[0:15]
	ds_read_b128 v[160:163], v192 offset:49152
	v_cvt_pk_f16_f32 v222, v216, v217
	v_cvt_pk_f16_f32 v223, v218, v219
	s_waitcnt lgkmcnt(8)
	v_mfma_f32_32x32x16_f16 v[16:31], a[40:43], v[164:167], v[16:31]
	ds_read_b128 v[164:167], v192 offset:50176
	global_load_lds_dwordx4 v192, s[44:45] offset:3072 sc1
	s_nop 1
	v_permlane32_swap_b32_e32 v220, v222
	v_permlane32_swap_b32_e32 v221, v223
	s_cmp_eq_u32 s31, 0
	s_cbranch_scc1 .LD_slow14
	global_store_dwordx4 v195, v[220:223], s[36:37] offset:0
	s_branch .LD_join15

.LD_join15:
	s_waitcnt lgkmcnt(8)
	v_mfma_f32_32x32x16_f16 v[32:47], a[40:43], v[168:171], v[32:47]
	ds_read_b128 v[168:171], v192 offset:51200
	v_exp_f32_e32 v200, v96
	v_exp_f32_e32 v201, v97
	s_waitcnt lgkmcnt(8)
	v_mfma_f32_32x32x16_f16 v[48:63], a[40:43], v[172:175], v[48:63]
	ds_read_b128 v[172:175], v192 offset:52224
	v_exp_f32_e32 v202, v98
	v_exp_f32_e32 v203, v99
	s_waitcnt lgkmcnt(8)
	v_mfma_f32_32x32x16_f16 v[0:15], a[44:47], v[176:179], v[0:15]
	ds_read_b128 v[176:179], v192 offset:53248
	v_exp_f32_e32 v204, v100
	v_exp_f32_e32 v205, v101
	s_waitcnt lgkmcnt(8)
	v_mfma_f32_32x32x16_f16 v[16:31], a[44:47], v[180:183], v[16:31]
	ds_read_b128 v[180:183], v192 offset:54272
	s_add_u32 s44, s34, 0x19000
	s_addc_u32 s45, s35, 0
	s_mov_b32 m0, s59
	s_nop 0
	global_load_lds_dwordx4 v192, s[44:45] sc1
	v_exp_f32_e32 v206, v102
	v_exp_f32_e32 v207, v103
	s_waitcnt lgkmcnt(8)
	v_mfma_f32_32x32x16_f16 v[32:47], a[44:47], v[184:187], v[32:47]
	ds_read_b128 v[184:187], v192 offset:55296
	v_exp_f32_e32 v208, v104
	v_exp_f32_e32 v209, v105
	s_waitcnt lgkmcnt(8)
	v_mfma_f32_32x32x16_f16 v[48:63], a[44:47], v[188:191], v[48:63]
	ds_read_b128 v[188:191], v192 offset:56320
	v_exp_f32_e32 v210, v106
	v_exp_f32_e32 v211, v107
	s_waitcnt lgkmcnt(7)
	v_mfma_f32_32x32x16_f16 v[0:15], a[48:51], v[160:163], v[0:15]
	ds_read_b128 v[160:163], v192 offset:57344
	v_exp_f32_e32 v212, v108
	v_exp_f32_e32 v213, v109
	s_waitcnt lgkmcnt(7)
	v_mfma_f32_32x32x16_f16 v[16:31], a[48:51], v[164:167], v[16:31]
	ds_read_b128 v[164:167], v192 offset:58368
	global_load_lds_dwordx4 v192, s[44:45] offset:1024 sc1
	v_exp_f32_e32 v214, v110
	v_exp_f32_e32 v215, v111
	v_add_f32_e32 v200, 1.0, v200
	s_waitcnt lgkmcnt(7)
	v_mfma_f32_32x32x16_f16 v[32:47], a[48:51], v[168:171], v[32:47]
	ds_read_b128 v[168:171], v192 offset:59392
	v_add_f32_e32 v201, 1.0, v201
	v_add_f32_e32 v202, 1.0, v202
	v_add_f32_e32 v203, 1.0, v203
	v_add_f32_e32 v204, 1.0, v204
	v_add_f32_e32 v205, 1.0, v205
	s_waitcnt lgkmcnt(7)
	v_mfma_f32_32x32x16_f16 v[48:63], a[48:51], v[172:175], v[48:63]
	ds_read_b128 v[172:175], v192 offset:60416
	v_add_f32_e32 v206, 1.0, v206
	v_add_f32_e32 v207, 1.0, v207
	v_add_f32_e32 v208, 1.0, v208
	v_add_f32_e32 v209, 1.0, v209
	v_add_f32_e32 v210, 1.0, v210
	s_waitcnt lgkmcnt(7)
	v_mfma_f32_32x32x16_f16 v[0:15], a[52:55], v[176:179], v[0:15]
	ds_read_b128 v[176:179], v192 offset:61440
	v_add_f32_e32 v211, 1.0, v211
	v_add_f32_e32 v212, 1.0, v212
	v_add_f32_e32 v213, 1.0, v213
	v_add_f32_e32 v214, 1.0, v214
	v_add_f32_e32 v215, 1.0, v215
	s_waitcnt lgkmcnt(7)
	v_mfma_f32_32x32x16_f16 v[16:31], a[52:55], v[180:183], v[16:31]
	ds_read_b128 v[180:183], v192 offset:62464
	global_load_lds_dwordx4 v192, s[44:45] offset:2048 sc1
	v_rcp_f32_e32 v200, v200
	v_rcp_f32_e32 v201, v201
	s_waitcnt lgkmcnt(7)
	v_mfma_f32_32x32x16_f16 v[32:47], a[52:55], v[184:187], v[32:47]
	ds_read_b128 v[184:187], v192 offset:63488
	v_rcp_f32_e32 v202, v202
	v_rcp_f32_e32 v203, v203
	s_waitcnt lgkmcnt(7)
	v_mfma_f32_32x32x16_f16 v[48:63], a[52:55], v[188:191], v[48:63]
	ds_read_b128 v[188:191], v192 offset:64512
	v_rcp_f32_e32 v204, v204
	v_rcp_f32_e32 v205, v205
	s_waitcnt vmcnt(8)
	s_barrier
	s_waitcnt lgkmcnt(7)
	v_mfma_f32_32x32x16_f16 v[0:15], a[56:59], v[160:163], v[0:15]
	ds_read_b128 v[160:163], v193 offset:0
	v_rcp_f32_e32 v206, v206
	v_rcp_f32_e32 v207, v207
	s_waitcnt lgkmcnt(7)
	v_mfma_f32_32x32x16_f16 v[16:31], a[56:59], v[164:167], v[16:31]
	ds_read_b128 v[164:167], v193 offset:1024
	global_load_lds_dwordx4 v192, s[44:45] offset:3072 sc1
	v_rcp_f32_e32 v208, v208
	v_rcp_f32_e32 v209, v209
	s_waitcnt lgkmcnt(7)
	v_mfma_f32_32x32x16_f16 v[32:47], a[56:59], v[168:171], v[32:47]
	ds_read_b128 v[168:171], v193 offset:2048
	v_rcp_f32_e32 v210, v210
	v_rcp_f32_e32 v211, v211
	s_waitcnt lgkmcnt(7)
	v_mfma_f32_32x32x16_f16 v[48:63], a[56:59], v[172:175], v[48:63]
	ds_read_b128 v[172:175], v193 offset:3072
	v_rcp_f32_e32 v212, v212
	v_rcp_f32_e32 v213, v213
	s_waitcnt lgkmcnt(7)
	v_mfma_f32_32x32x16_f16 v[0:15], a[60:63], v[176:179], v[0:15]
	ds_read_b128 v[176:179], v193 offset:4096
	v_rcp_f32_e32 v214, v214
	v_rcp_f32_e32 v215, v215
	v_fmamk_f32 v208, v208, 0xc0b8aa3b, v198
	s_waitcnt lgkmcnt(7)
	v_mfma_f32_32x32x16_f16 v[16:31], a[60:63], v[180:183], v[16:31]
	ds_read_b128 v[180:183], v193 offset:5120
	s_add_u32 s44, s34, 0x20000
	s_addc_u32 s45, s35, 0
	s_mov_b32 m0, s52
	s_nop 0
	global_load_lds_dwordx4 v192, s[44:45] sc1
	v_fmamk_f32 v209, v209, 0xc0b8aa3b, v198
	v_fmamk_f32 v210, v210, 0xc0b8aa3b, v198
	v_fmamk_f32 v211, v211, 0xc0b8aa3b, v198
	v_mul_f32_e32 v204, v204, v152
	v_mul_f32_e32 v205, v205, v153
	s_waitcnt lgkmcnt(7)
	v_mfma_f32_32x32x16_f16 v[32:47], a[60:63], v[184:187], v[32:47]
	ds_read_b128 v[184:187], v193 offset:6144
	v_mul_f32_e32 v206, v206, v154
	v_mul_f32_e32 v207, v207, v155
	v_fma_f32 v152, v200, v208, v204
	v_fma_f32 v153, v201, v209, v205
	v_fma_f32 v154, v202, v210, v206
	s_waitcnt lgkmcnt(7)
	v_mfma_f32_32x32x16_f16 v[48:63], a[60:63], v[188:191], v[48:63]
	ds_read_b128 v[188:191], v193 offset:7168
	v_fma_f32 v155, v203, v211, v207
	v_exp_f32_e32 v200, v152
	v_exp_f32_e32 v201, v153
	s_waitcnt lgkmcnt(7)
	v_mfma_f32_32x32x16_f16 v[0:15], a[64:67], v[160:163], v[0:15]
	ds_read_b128 v[160:163], v193 offset:8192
	v_exp_f32_e32 v202, v154
	v_exp_f32_e32 v203, v155
	v_add_f32_e32 v200, 1.0, v200
	s_waitcnt lgkmcnt(7)
	v_mfma_f32_32x32x16_f16 v[16:31], a[64:67], v[164:167], v[16:31]
	ds_read_b128 v[164:167], v193 offset:9216
	global_load_lds_dwordx4 v192, s[44:45] offset:1024 sc1
	v_add_f32_e32 v201, 1.0, v201
	v_add_f32_e32 v202, 1.0, v202
	v_add_f32_e32 v203, 1.0, v203
	v_rcp_f32_e32 v200, v200
	s_waitcnt lgkmcnt(7)
	v_mfma_f32_32x32x16_f16 v[32:47], a[64:67], v[168:171], v[32:47]
	ds_read_b128 v[168:171], v193 offset:10240
	v_rcp_f32_e32 v201, v201
	v_rcp_f32_e32 v202, v202
	s_waitcnt lgkmcnt(7)
	v_mfma_f32_32x32x16_f16 v[48:63], a[64:67], v[172:175], v[48:63]
	ds_read_b128 v[172:175], v193 offset:11264
	v_rcp_f32_e32 v203, v203
	v_fma_f32 v200, v200, 2.0, -1.0
	v_fma_f32 v201, v201, 2.0, -1.0
	v_fma_f32 v202, v202, 2.0, -1.0
	s_waitcnt lgkmcnt(7)
	v_mfma_f32_32x32x16_f16 v[0:15], a[68:71], v[176:179], v[0:15]
	ds_read_b128 v[176:179], v193 offset:12288
	v_fma_f32 v203, v203, 2.0, -1.0
	v_mul_f32_e32 v216, v212, v200
	v_mul_f32_e32 v217, v213, v201
	v_mul_f32_e32 v218, v214, v202
	v_mul_f32_e32 v219, v215, v203
	s_waitcnt lgkmcnt(7)
	v_mfma_f32_32x32x16_f16 v[16:31], a[68:71], v[180:183], v[16:31]
	ds_read_b128 v[180:183], v193 offset:13312
	global_load_lds_dwordx4 v192, s[44:45] offset:2048 sc1
	v_mul_f32_e32 v236, v216, v228
	v_mul_f32_e32 v237, v216, v232
	v_fmac_f32_e32 v236, v217, v229
	v_fmac_f32_e32 v237, v217, v233
	v_fmac_f32_e32 v236, v218, v230
	s_waitcnt lgkmcnt(7)
	v_mfma_f32_32x32x16_f16 v[32:47], a[68:71], v[184:187], v[32:47]
	ds_read_b128 v[184:187], v193 offset:14336
	v_fmac_f32_e32 v237, v218, v234
	v_fmac_f32_e32 v236, v219, v231
	v_fmac_f32_e32 v237, v219, v235
	v_mov_b32_e32 v238, v236
	v_mov_b32_e32 v239, v236
	s_waitcnt lgkmcnt(7)
	v_mfma_f32_32x32x16_f16 v[48:63], a[68:71], v[188:191], v[48:63]
	ds_read_b128 v[188:191], v193 offset:15360
	v_mov_b32_e32 v240, v237
	v_mov_b32_e32 v241, v237
	s_waitcnt lgkmcnt(7)
	v_mfma_f32_32x32x16_f16 v[0:15], a[72:75], v[160:163], v[0:15]
	ds_read_b128 v[160:163], v193 offset:16384
	s_nop 1
	v_permlane32_swap_b32_e32 v238, v239
	v_permlane32_swap_b32_e32 v240, v241
	v_add_f32_e32 v238, v238, v239
	v_add_f32_e32 v239, v240, v241
	ds_write_b64 v248, v[238:239] offset:1536
	s_waitcnt lgkmcnt(8)
	v_mfma_f32_32x32x16_f16 v[16:31], a[72:75], v[164:167], v[16:31]
	ds_read_b128 v[164:167], v193 offset:17408
	global_load_lds_dwordx4 v192, s[44:45] offset:3072 sc1
	v_cvt_pk_f16_f32 v224, v216, v217
	v_cvt_pk_f16_f32 v225, v218, v219
	v_exp_f32_e32 v200, v112
	s_waitcnt lgkmcnt(8)
	v_mfma_f32_32x32x16_f16 v[32:47], a[72:75], v[168:171], v[32:47]
	ds_read_b128 v[168:171], v193 offset:18432
	v_exp_f32_e32 v201, v113
	v_exp_f32_e32 v202, v114
	s_waitcnt lgkmcnt(8)
	v_mfma_f32_32x32x16_f16 v[48:63], a[72:75], v[172:175], v[48:63]
	ds_read_b128 v[172:175], v193 offset:19456
	v_exp_f32_e32 v203, v115
	v_exp_f32_e32 v204, v116
	s_waitcnt lgkmcnt(8)
	v_mfma_f32_32x32x16_f16 v[0:15], a[76:79], v[176:179], v[0:15]
	ds_read_b128 v[176:179], v193 offset:20480
	v_exp_f32_e32 v205, v117
	v_exp_f32_e32 v206, v118
	s_waitcnt lgkmcnt(8)
	v_mfma_f32_32x32x16_f16 v[16:31], a[76:79], v[180:183], v[16:31]
	ds_read_b128 v[180:183], v193 offset:21504
	s_add_u32 s44, s34, 0x21000
	s_addc_u32 s45, s35, 0
	s_mov_b32 m0, s53
	s_nop 0
	global_load_lds_dwordx4 v192, s[44:45] sc1
	v_exp_f32_e32 v207, v119
	v_exp_f32_e32 v208, v120
	s_waitcnt lgkmcnt(8)
	v_mfma_f32_32x32x16_f16 v[32:47], a[76:79], v[184:187], v[32:47]
	ds_read_b128 v[184:187], v193 offset:22528
	v_exp_f32_e32 v209, v121
	v_exp_f32_e32 v210, v122
	s_waitcnt lgkmcnt(8)
	v_mfma_f32_32x32x16_f16 v[48:63], a[76:79], v[188:191], v[48:63]
	ds_read_b128 v[188:191], v193 offset:23552
	v_exp_f32_e32 v211, v123
	v_exp_f32_e32 v212, v124
	s_waitcnt lgkmcnt(8)
	v_mfma_f32_32x32x16_f16 v[0:15], a[80:83], v[160:163], v[0:15]
	ds_read_b128 v[160:163], v193 offset:24576
	v_exp_f32_e32 v213, v125
	v_exp_f32_e32 v214, v126
	s_waitcnt lgkmcnt(7)
	v_mfma_f32_32x32x16_f16 v[16:31], a[80:83], v[164:167], v[16:31]
	ds_read_b128 v[164:167], v193 offset:25600
	global_load_lds_dwordx4 v192, s[44:45] offset:1024 sc1
	v_exp_f32_e32 v215, v127
	v_add_f32_e32 v200, 1.0, v200
	v_add_f32_e32 v201, 1.0, v201
	v_add_f32_e32 v202, 1.0, v202
	s_waitcnt lgkmcnt(7)
	v_mfma_f32_32x32x16_f16 v[32:47], a[80:83], v[168:171], v[32:47]
	ds_read_b128 v[168:171], v193 offset:26624
	v_add_f32_e32 v203, 1.0, v203
	v_add_f32_e32 v204, 1.0, v204
	v_add_f32_e32 v205, 1.0, v205
	v_add_f32_e32 v206, 1.0, v206
	v_add_f32_e32 v207, 1.0, v207
	s_waitcnt lgkmcnt(7)
	v_mfma_f32_32x32x16_f16 v[48:63], a[80:83], v[172:175], v[48:63]
	ds_read_b128 v[172:175], v193 offset:27648
	v_add_f32_e32 v208, 1.0, v208
	v_add_f32_e32 v209, 1.0, v209
	v_add_f32_e32 v210, 1.0, v210
	v_add_f32_e32 v211, 1.0, v211
	v_add_f32_e32 v212, 1.0, v212
	s_waitcnt lgkmcnt(7)
	v_mfma_f32_32x32x16_f16 v[0:15], a[84:87], v[176:179], v[0:15]
	ds_read_b128 v[176:179], v193 offset:28672
	v_add_f32_e32 v213, 1.0, v213
	v_add_f32_e32 v214, 1.0, v214
	v_add_f32_e32 v215, 1.0, v215
	v_rcp_f32_e32 v200, v200
	s_waitcnt lgkmcnt(7)
	v_mfma_f32_32x32x16_f16 v[16:31], a[84:87], v[180:183], v[16:31]
	ds_read_b128 v[180:183], v193 offset:29696
	global_load_lds_dwordx4 v192, s[44:45] offset:2048 sc1
	v_rcp_f32_e32 v201, v201
	v_rcp_f32_e32 v202, v202
	s_waitcnt lgkmcnt(7)
	v_mfma_f32_32x32x16_f16 v[32:47], a[84:87], v[184:187], v[32:47]
	ds_read_b128 v[184:187], v193 offset:30720
	v_rcp_f32_e32 v203, v203
	v_rcp_f32_e32 v204, v204
	s_waitcnt lgkmcnt(7)
	v_mfma_f32_32x32x16_f16 v[48:63], a[84:87], v[188:191], v[48:63]
	ds_read_b128 v[188:191], v193 offset:31744
	v_rcp_f32_e32 v205, v205
	v_rcp_f32_e32 v206, v206
	s_waitcnt vmcnt(7)
	s_barrier
	s_waitcnt lgkmcnt(7)
	v_mfma_f32_32x32x16_f16 v[0:15], a[88:91], v[160:163], v[0:15]
	ds_read_b128 v[160:163], v193 offset:32768
	v_rcp_f32_e32 v207, v207
	v_rcp_f32_e32 v208, v208
	s_waitcnt lgkmcnt(7)
	v_mfma_f32_32x32x16_f16 v[16:31], a[88:91], v[164:167], v[16:31]
	ds_read_b128 v[164:167], v193 offset:33792
	global_load_lds_dwordx4 v192, s[44:45] offset:3072 sc1
	v_rcp_f32_e32 v209, v209
	v_rcp_f32_e32 v210, v210
	s_waitcnt lgkmcnt(7)
	v_mfma_f32_32x32x16_f16 v[32:47], a[88:91], v[168:171], v[32:47]
	ds_read_b128 v[168:171], v193 offset:34816
	v_rcp_f32_e32 v211, v211
	v_rcp_f32_e32 v212, v212
	s_waitcnt lgkmcnt(7)
	v_mfma_f32_32x32x16_f16 v[48:63], a[88:91], v[172:175], v[48:63]
	ds_read_b128 v[172:175], v193 offset:35840
	v_rcp_f32_e32 v213, v213
	v_rcp_f32_e32 v214, v214
	s_waitcnt lgkmcnt(7)
	v_mfma_f32_32x32x16_f16 v[0:15], a[92:95], v[176:179], v[0:15]
	ds_read_b128 v[176:179], v193 offset:36864
	v_rcp_f32_e32 v215, v215
	v_fmamk_f32 v208, v208, 0xc0b8aa3b, v198
	v_fmamk_f32 v209, v209, 0xc0b8aa3b, v198
	v_fmamk_f32 v210, v210, 0xc0b8aa3b, v198
	s_waitcnt lgkmcnt(7)
	v_mfma_f32_32x32x16_f16 v[16:31], a[92:95], v[180:183], v[16:31]
	ds_read_b128 v[180:183], v193 offset:37888
	s_add_u32 s44, s34, 0x28000
	s_addc_u32 s45, s35, 0
	s_mov_b32 m0, s54
	s_nop 0
	global_load_lds_dwordx4 v192, s[44:45] sc1
	v_fmamk_f32 v211, v211, 0xc0b8aa3b, v198
	v_mul_f32_e32 v204, v204, v156
	v_mul_f32_e32 v205, v205, v157
	v_mul_f32_e32 v206, v206, v158
	v_mul_f32_e32 v207, v207, v159
	s_waitcnt lgkmcnt(7)
	v_mfma_f32_32x32x16_f16 v[32:47], a[92:95], v[184:187], v[32:47]
	ds_read_b128 v[184:187], v193 offset:38912
	v_fma_f32 v156, v200, v208, v204
	v_fma_f32 v157, v201, v209, v205
	v_fma_f32 v158, v202, v210, v206
	v_fma_f32 v159, v203, v211, v207
	s_waitcnt lgkmcnt(7)
	v_mfma_f32_32x32x16_f16 v[48:63], a[92:95], v[188:191], v[48:63]
	ds_read_b128 v[188:191], v193 offset:39936
	v_exp_f32_e32 v200, v156
	v_exp_f32_e32 v201, v157
	s_waitcnt lgkmcnt(7)
	v_mfma_f32_32x32x16_f16 v[0:15], a[96:99], v[160:163], v[0:15]
	ds_read_b128 v[160:163], v193 offset:40960
	v_exp_f32_e32 v202, v158
	v_exp_f32_e32 v203, v159
	v_add_f32_e32 v200, 1.0, v200
	s_waitcnt lgkmcnt(7)
	v_mfma_f32_32x32x16_f16 v[16:31], a[96:99], v[164:167], v[16:31]
	ds_read_b128 v[164:167], v193 offset:41984
	global_load_lds_dwordx4 v192, s[44:45] offset:1024 sc1
	v_add_f32_e32 v201, 1.0, v201
	v_add_f32_e32 v202, 1.0, v202
	v_add_f32_e32 v203, 1.0, v203
	v_rcp_f32_e32 v200, v200
	s_waitcnt lgkmcnt(7)
	v_mfma_f32_32x32x16_f16 v[32:47], a[96:99], v[168:171], v[32:47]
	ds_read_b128 v[168:171], v193 offset:43008
	v_rcp_f32_e32 v201, v201
	v_rcp_f32_e32 v202, v202
	s_waitcnt lgkmcnt(7)
	v_mfma_f32_32x32x16_f16 v[48:63], a[96:99], v[172:175], v[48:63]
	ds_read_b128 v[172:175], v193 offset:44032
	v_rcp_f32_e32 v203, v203
	v_fma_f32 v200, v200, 2.0, -1.0
	v_fma_f32 v201, v201, 2.0, -1.0
	v_fma_f32 v202, v202, 2.0, -1.0
	s_waitcnt lgkmcnt(7)
	v_mfma_f32_32x32x16_f16 v[0:15], a[100:103], v[176:179], v[0:15]
	ds_read_b128 v[176:179], v193 offset:45056
	v_fma_f32 v203, v203, 2.0, -1.0
	v_mul_f32_e32 v216, v212, v200
	v_mul_f32_e32 v217, v213, v201
	v_mul_f32_e32 v218, v214, v202
	v_mul_f32_e32 v219, v215, v203
	s_waitcnt lgkmcnt(7)
	v_mfma_f32_32x32x16_f16 v[16:31], a[100:103], v[180:183], v[16:31]
	ds_read_b128 v[180:183], v193 offset:46080
	global_load_lds_dwordx4 v192, s[44:45] offset:2048 sc1
	v_mul_f32_e32 v236, v216, v228
	v_mul_f32_e32 v237, v216, v232
	v_fmac_f32_e32 v236, v217, v229
	v_fmac_f32_e32 v237, v217, v233
	v_fmac_f32_e32 v236, v218, v230
	s_waitcnt lgkmcnt(7)
	v_mfma_f32_32x32x16_f16 v[32:47], a[100:103], v[184:187], v[32:47]
	ds_read_b128 v[184:187], v193 offset:47104
	v_fmac_f32_e32 v237, v218, v234
	v_fmac_f32_e32 v236, v219, v231
	v_fmac_f32_e32 v237, v219, v235
	v_mov_b32_e32 v238, v236
	v_mov_b32_e32 v239, v236
	s_waitcnt lgkmcnt(7)
	v_mfma_f32_32x32x16_f16 v[48:63], a[100:103], v[188:191], v[48:63]
	ds_read_b128 v[188:191], v193 offset:48128
	v_mov_b32_e32 v240, v237
	v_mov_b32_e32 v241, v237
	s_waitcnt lgkmcnt(7)
	v_mfma_f32_32x32x16_f16 v[0:15], a[104:107], v[160:163], v[0:15]
	ds_read_b128 v[160:163], v193 offset:49152
	s_nop 1
	v_permlane32_swap_b32_e32 v238, v239
	v_permlane32_swap_b32_e32 v240, v241
	v_add_f32_e32 v238, v238, v239
	v_add_f32_e32 v239, v240, v241
	ds_write_b64 v248, v[238:239] offset:1792
	s_waitcnt lgkmcnt(8)
	v_mfma_f32_32x32x16_f16 v[16:31], a[104:107], v[164:167], v[16:31]
	ds_read_b128 v[164:167], v193 offset:50176
	global_load_lds_dwordx4 v192, s[44:45] offset:3072 sc1
	v_cvt_pk_f16_f32 v226, v216, v217
	v_cvt_pk_f16_f32 v227, v218, v219
	s_waitcnt lgkmcnt(8)
	v_mfma_f32_32x32x16_f16 v[32:47], a[104:107], v[168:171], v[32:47]
	ds_read_b128 v[168:171], v193 offset:51200
	s_nop 1
	v_permlane32_swap_b32_e32 v224, v226
	v_permlane32_swap_b32_e32 v225, v227
	s_cmp_eq_u32 s31, 0
	s_cbranch_scc1 .LD_slow16
	global_store_dwordx4 v195, v[224:227], s[36:37] offset:2048
	s_branch .LD_join17

.LD_join17:
	s_waitcnt lgkmcnt(8)
	v_mfma_f32_32x32x16_f16 v[48:63], a[104:107], v[172:175], v[48:63]
	ds_read_b128 v[172:175], v193 offset:52224
	s_add_u32 s46, s42, 0x4000
	s_addc_u32 s47, s43, 0
	global_load_dwordx4 v[64:67], v192, s[46:47] offset:0
	global_load_dwordx4 v[68:71], v192, s[46:47] offset:1024
	s_waitcnt lgkmcnt(8)
	v_mfma_f32_32x32x16_f16 v[0:15], a[108:111], v[176:179], v[0:15]
	ds_read_b128 v[176:179], v193 offset:53248
	global_load_dwordx4 v[72:75], v192, s[46:47] offset:2048
	global_load_dwordx4 v[76:79], v192, s[46:47] offset:3072
	s_add_u32 s46, s42, 0x5000
	s_addc_u32 s47, s43, 0
	s_waitcnt lgkmcnt(8)
	v_mfma_f32_32x32x16_f16 v[16:31], a[108:111], v[180:183], v[16:31]
	ds_read_b128 v[180:183], v193 offset:54272
	s_add_u32 s44, s34, 0x29000
	s_addc_u32 s45, s35, 0
	s_mov_b32 m0, s55
	s_nop 0
	global_load_lds_dwordx4 v192, s[44:45] sc1
	global_load_dwordx4 v[80:83], v192, s[46:47] offset:0
	global_load_dwordx4 v[84:87], v192, s[46:47] offset:1024
	global_load_dwordx4 v[88:91], v192, s[46:47] offset:2048
	s_waitcnt lgkmcnt(8)
	v_mfma_f32_32x32x16_f16 v[32:47], a[108:111], v[184:187], v[32:47]
	ds_read_b128 v[184:187], v193 offset:55296
	global_load_dwordx4 v[92:95], v192, s[46:47] offset:3072
	s_add_u32 s46, s42, 0x6000
	s_addc_u32 s47, s43, 0
	global_load_dwordx4 v[96:99], v192, s[46:47] offset:0
	s_waitcnt lgkmcnt(8)
	v_mfma_f32_32x32x16_f16 v[48:63], a[108:111], v[188:191], v[48:63]
	ds_read_b128 v[188:191], v193 offset:56320
	global_load_dwordx4 v[100:103], v192, s[46:47] offset:1024
	global_load_dwordx4 v[104:107], v192, s[46:47] offset:2048
	global_load_dwordx4 v[108:111], v192, s[46:47] offset:3072
	s_waitcnt lgkmcnt(8)
	v_mfma_f32_32x32x16_f16 v[0:15], a[112:115], v[160:163], v[0:15]
	ds_read_b128 v[160:163], v193 offset:57344
	s_add_u32 s46, s42, 0x7000
	s_addc_u32 s47, s43, 0
	global_load_dwordx4 v[112:115], v192, s[46:47] offset:0
	global_load_dwordx4 v[116:119], v192, s[46:47] offset:1024
	s_waitcnt lgkmcnt(7)
	v_mfma_f32_32x32x16_f16 v[16:31], a[112:115], v[164:167], v[16:31]
	ds_read_b128 v[164:167], v193 offset:58368
	global_load_lds_dwordx4 v192, s[44:45] offset:1024 sc1
	global_load_dwordx4 v[120:123], v192, s[46:47] offset:2048
	global_load_dwordx4 v[124:127], v192, s[46:47] offset:3072
	s_waitcnt lgkmcnt(7)
	v_mfma_f32_32x32x16_f16 v[32:47], a[112:115], v[168:171], v[32:47]
	ds_read_b128 v[168:171], v193 offset:59392
	s_waitcnt vmcnt(18)
	s_barrier
	v_mov_b32_e32 v199, 2
	s_cmp_eq_u32 s31, 0
	s_cbranch_scc1 .LD_slow18
	global_store_dword v197, v199, s[40:41]
	s_branch .LD_join19

.LD_join19:
	ds_read_b64 v[200:201], v249 offset:1024
	ds_read_b64 v[202:203], v249 offset:3072
	ds_read_b64 v[204:205], v249 offset:5120
	ds_read_b64 v[206:207], v249 offset:7168
	s_waitcnt lgkmcnt(11)
	v_mfma_f32_32x32x16_f16 v[48:63], a[112:115], v[172:175], v[48:63]
	ds_read_b128 v[172:175], v193 offset:60416
	s_waitcnt lgkmcnt(11)
	v_mfma_f32_32x32x16_f16 v[0:15], a[116:119], v[176:179], v[0:15]
	ds_read_b128 v[176:179], v193 offset:61440
	s_waitcnt lgkmcnt(11)
	v_mfma_f32_32x32x16_f16 v[16:31], a[116:119], v[180:183], v[16:31]
	ds_read_b128 v[180:183], v193 offset:62464
	global_load_lds_dwordx4 v192, s[44:45] offset:2048 sc1
	s_waitcnt lgkmcnt(3)
	v_add_f32_e32 v200, v200, v202
	v_add_f32_e32 v201, v201, v203
	v_add_f32_e32 v200, v200, v204
	v_add_f32_e32 v201, v201, v205
	v_add_f32_e32 v200, v200, v206
	v_add_f32_e32 v201, v201, v207
	global_store_dwordx2 v250, v[200:201], s[72:73]
	v_mfma_f32_32x32x16_f16 v[32:47], a[116:119], v[184:187], v[32:47]
	ds_read_b128 v[184:187], v193 offset:63488
	v_mfma_f32_32x32x16_f16 v[48:63], a[116:119], v[188:191], v[48:63]
	ds_read_b128 v[188:191], v193 offset:64512
	s_barrier
	v_mfma_f32_32x32x16_f16 v[0:15], a[120:123], v[160:163], v[0:15]
	ds_read_b128 v[160:163], v192 offset:0
	v_mfma_f32_32x32x16_f16 v[16:31], a[120:123], v[164:167], v[16:31]
	ds_read_b128 v[164:167], v192 offset:1024
	global_load_lds_dwordx4 v192, s[44:45] offset:3072 sc1
	v_mfma_f32_32x32x16_f16 v[32:47], a[120:123], v[168:171], v[32:47]
	ds_read_b128 v[168:171], v192 offset:2048
	s_waitcnt lgkmcnt(7)
	v_mfma_f32_32x32x16_f16 v[48:63], a[120:123], v[172:175], v[48:63]
	ds_read_b128 v[172:175], v192 offset:3072
	s_waitcnt lgkmcnt(7)
	v_mfma_f32_32x32x16_f16 v[0:15], a[124:127], v[176:179], v[0:15]
	ds_read_b128 v[176:179], v192 offset:4096
	s_waitcnt lgkmcnt(7)
	v_mfma_f32_32x32x16_f16 v[16:31], a[124:127], v[180:183], v[16:31]
	ds_read_b128 v[180:183], v192 offset:5120
	s_add_u32 s44, s34, 0x30000
	s_addc_u32 s45, s35, 0
	s_mov_b32 m0, s56
	s_nop 0
	global_load_lds_dwordx4 v192, s[44:45] sc1
	s_waitcnt lgkmcnt(7)
	v_mfma_f32_32x32x16_f16 v[32:47], a[124:127], v[184:187], v[32:47]
	ds_read_b128 v[184:187], v192 offset:6144
	s_waitcnt lgkmcnt(7)
	v_mfma_f32_32x32x16_f16 v[48:63], a[124:127], v[188:191], v[48:63]
	ds_read_b128 v[188:191], v192 offset:7168
	s_waitcnt lgkmcnt(7)
	v_mfma_f32_32x32x16_f16 v[0:15], a[128:131], v[160:163], v[0:15]
	ds_read_b128 v[160:163], v192 offset:8192
	s_waitcnt lgkmcnt(7)
	v_mfma_f32_32x32x16_f16 v[16:31], a[128:131], v[164:167], v[16:31]
	ds_read_b128 v[164:167], v192 offset:9216
	global_load_lds_dwordx4 v192, s[44:45] offset:1024 sc1
	s_waitcnt lgkmcnt(7)
	v_mfma_f32_32x32x16_f16 v[32:47], a[128:131], v[168:171], v[32:47]
	ds_read_b128 v[168:171], v192 offset:10240
	s_waitcnt lgkmcnt(7)
	v_mfma_f32_32x32x16_f16 v[48:63], a[128:131], v[172:175], v[48:63]
	ds_read_b128 v[172:175], v192 offset:11264
	s_waitcnt lgkmcnt(7)
	v_mfma_f32_32x32x16_f16 v[0:15], a[132:135], v[176:179], v[0:15]
	ds_read_b128 v[176:179], v192 offset:12288
	s_waitcnt lgkmcnt(7)
	v_mfma_f32_32x32x16_f16 v[16:31], a[132:135], v[180:183], v[16:31]
	ds_read_b128 v[180:183], v192 offset:13312
	global_load_lds_dwordx4 v192, s[44:45] offset:2048 sc1
	s_waitcnt lgkmcnt(7)
	v_mfma_f32_32x32x16_f16 v[32:47], a[132:135], v[184:187], v[32:47]
	ds_read_b128 v[184:187], v192 offset:14336
	s_waitcnt lgkmcnt(7)
	v_mfma_f32_32x32x16_f16 v[48:63], a[132:135], v[188:191], v[48:63]
	ds_read_b128 v[188:191], v192 offset:15360
	s_waitcnt lgkmcnt(7)
	v_mfma_f32_32x32x16_f16 v[0:15], a[136:139], v[160:163], v[0:15]
	ds_read_b128 v[160:163], v192 offset:16384
	s_waitcnt lgkmcnt(7)
	v_mfma_f32_32x32x16_f16 v[16:31], a[136:139], v[164:167], v[16:31]
	ds_read_b128 v[164:167], v192 offset:17408
	global_load_lds_dwordx4 v192, s[44:45] offset:3072 sc1
	s_waitcnt lgkmcnt(7)
	v_mfma_f32_32x32x16_f16 v[32:47], a[136:139], v[168:171], v[32:47]
	ds_read_b128 v[168:171], v192 offset:18432
	s_waitcnt lgkmcnt(7)
	v_mfma_f32_32x32x16_f16 v[48:63], a[136:139], v[172:175], v[48:63]
	ds_read_b128 v[172:175], v192 offset:19456
	s_waitcnt lgkmcnt(7)
	v_mfma_f32_32x32x16_f16 v[0:15], a[140:143], v[176:179], v[0:15]
	ds_read_b128 v[176:179], v192 offset:20480
	s_waitcnt lgkmcnt(7)
	v_mfma_f32_32x32x16_f16 v[16:31], a[140:143], v[180:183], v[16:31]
	ds_read_b128 v[180:183], v192 offset:21504
	s_add_u32 s44, s34, 0x31000
	s_addc_u32 s45, s35, 0
	s_mov_b32 m0, s57
	s_nop 0
	global_load_lds_dwordx4 v192, s[44:45] sc1
	s_waitcnt lgkmcnt(7)
	v_mfma_f32_32x32x16_f16 v[32:47], a[140:143], v[184:187], v[32:47]
	ds_read_b128 v[184:187], v192 offset:22528
	s_waitcnt lgkmcnt(7)
	v_mfma_f32_32x32x16_f16 v[48:63], a[140:143], v[188:191], v[48:63]
	ds_read_b128 v[188:191], v192 offset:23552
	s_waitcnt lgkmcnt(7)
	v_mfma_f32_32x32x16_f16 v[0:15], a[144:147], v[160:163], v[0:15]
	ds_read_b128 v[160:163], v192 offset:24576
	s_waitcnt lgkmcnt(7)
	v_mfma_f32_32x32x16_f16 v[16:31], a[144:147], v[164:167], v[16:31]
	ds_read_b128 v[164:167], v192 offset:25600
	global_load_lds_dwordx4 v192, s[44:45] offset:1024 sc1
	s_waitcnt lgkmcnt(7)
	v_mfma_f32_32x32x16_f16 v[32:47], a[144:147], v[168:171], v[32:47]
	ds_read_b128 v[168:171], v192 offset:26624
	s_waitcnt lgkmcnt(7)
	v_mfma_f32_32x32x16_f16 v[48:63], a[144:147], v[172:175], v[48:63]
	ds_read_b128 v[172:175], v192 offset:27648
	s_waitcnt lgkmcnt(7)
	v_mfma_f32_32x32x16_f16 v[0:15], a[148:151], v[176:179], v[0:15]
	ds_read_b128 v[176:179], v192 offset:28672
	s_waitcnt lgkmcnt(7)
	v_mfma_f32_32x32x16_f16 v[16:31], a[148:151], v[180:183], v[16:31]
	ds_read_b128 v[180:183], v192 offset:29696
	global_load_lds_dwordx4 v192, s[44:45] offset:2048 sc1
	s_waitcnt lgkmcnt(7)
	v_mfma_f32_32x32x16_f16 v[32:47], a[148:151], v[184:187], v[32:47]
	ds_read_b128 v[184:187], v192 offset:30720
	s_waitcnt lgkmcnt(7)
	v_mfma_f32_32x32x16_f16 v[48:63], a[148:151], v[188:191], v[48:63]
	ds_read_b128 v[188:191], v192 offset:31744
	s_waitcnt vmcnt(7)
	s_barrier
	s_waitcnt lgkmcnt(7)
	v_mfma_f32_32x32x16_f16 v[0:15], a[152:155], v[160:163], v[0:15]
	ds_read_b128 v[160:163], v192 offset:32768
	s_waitcnt lgkmcnt(7)
	v_mfma_f32_32x32x16_f16 v[16:31], a[152:155], v[164:167], v[16:31]
	ds_read_b128 v[164:167], v192 offset:33792
	global_load_lds_dwordx4 v192, s[44:45] offset:3072 sc1
	s_waitcnt lgkmcnt(7)
	v_mfma_f32_32x32x16_f16 v[32:47], a[152:155], v[168:171], v[32:47]
	ds_read_b128 v[168:171], v192 offset:34816
	s_waitcnt lgkmcnt(7)
	v_mfma_f32_32x32x16_f16 v[48:63], a[152:155], v[172:175], v[48:63]
	ds_read_b128 v[172:175], v192 offset:35840
	s_waitcnt lgkmcnt(7)
	v_mfma_f32_32x32x16_f16 v[0:15], a[156:159], v[176:179], v[0:15]
	ds_read_b128 v[176:179], v192 offset:36864
	s_waitcnt lgkmcnt(7)
	v_mfma_f32_32x32x16_f16 v[16:31], a[156:159], v[180:183], v[16:31]
	ds_read_b128 v[180:183], v192 offset:37888
	s_add_u32 s44, s34, 0x38000
	s_addc_u32 s45, s35, 0
	s_mov_b32 m0, s58
	s_nop 0
	global_load_lds_dwordx4 v192, s[44:45] sc1
	s_waitcnt lgkmcnt(7)
	v_mfma_f32_32x32x16_f16 v[32:47], a[156:159], v[184:187], v[32:47]
	ds_read_b128 v[184:187], v192 offset:38912
	s_waitcnt lgkmcnt(7)
	v_mfma_f32_32x32x16_f16 v[48:63], a[156:159], v[188:191], v[48:63]
	ds_read_b128 v[188:191], v192 offset:39936
	s_lshl_b32 s64, s71, 3
	s_add_u32 s64, s64, s29
	s_lshl_b32 s64, s64, 7
	s_add_u32 s38, s8, s64
	s_addc_u32 s39, s9, 0
	global_load_dword v251, v196, s[38:39] sc1
	s_waitcnt lgkmcnt(7)
	v_mfma_f32_32x32x16_f16 v[0:15], a[160:163], v[160:163], v[0:15]
	ds_read_b128 v[160:163], v192 offset:40960
	s_waitcnt lgkmcnt(7)
	v_mfma_f32_32x32x16_f16 v[16:31], a[160:163], v[164:167], v[16:31]
	ds_read_b128 v[164:167], v192 offset:41984
	global_load_lds_dwordx4 v192, s[44:45] offset:1024 sc1
	s_waitcnt lgkmcnt(7)
	v_mfma_f32_32x32x16_f16 v[32:47], a[160:163], v[168:171], v[32:47]
	ds_read_b128 v[168:171], v192 offset:43008
	s_waitcnt lgkmcnt(7)
	v_mfma_f32_32x32x16_f16 v[48:63], a[160:163], v[172:175], v[48:63]
	ds_read_b128 v[172:175], v192 offset:44032
	s_waitcnt lgkmcnt(7)
	v_mfma_f32_32x32x16_f16 v[0:15], a[164:167], v[176:179], v[0:15]
	ds_read_b128 v[176:179], v192 offset:45056
	s_waitcnt lgkmcnt(7)
	v_mfma_f32_32x32x16_f16 v[16:31], a[164:167], v[180:183], v[16:31]
	ds_read_b128 v[180:183], v192 offset:46080
	global_load_lds_dwordx4 v192, s[44:45] offset:2048 sc1
	s_waitcnt lgkmcnt(7)
	v_mfma_f32_32x32x16_f16 v[32:47], a[164:167], v[184:187], v[32:47]
	ds_read_b128 v[184:187], v192 offset:47104
	s_waitcnt lgkmcnt(7)
	v_mfma_f32_32x32x16_f16 v[48:63], a[164:167], v[188:191], v[48:63]
	ds_read_b128 v[188:191], v192 offset:48128
	s_waitcnt lgkmcnt(7)
	v_mfma_f32_32x32x16_f16 v[0:15], a[168:171], v[160:163], v[0:15]
	ds_read_b128 v[160:163], v192 offset:49152
	s_waitcnt lgkmcnt(7)
	v_mfma_f32_32x32x16_f16 v[16:31], a[168:171], v[164:167], v[16:31]
	ds_read_b128 v[164:167], v192 offset:50176
	global_load_lds_dwordx4 v192, s[44:45] offset:3072 sc1
	s_waitcnt lgkmcnt(7)
	v_mfma_f32_32x32x16_f16 v[32:47], a[168:171], v[168:171], v[32:47]
	ds_read_b128 v[168:171], v192 offset:51200
	s_waitcnt lgkmcnt(7)
	v_mfma_f32_32x32x16_f16 v[48:63], a[168:171], v[172:175], v[48:63]
	ds_read_b128 v[172:175], v192 offset:52224
	s_waitcnt lgkmcnt(7)
	v_mfma_f32_32x32x16_f16 v[0:15], a[172:175], v[176:179], v[0:15]
	ds_read_b128 v[176:179], v192 offset:53248
	s_waitcnt lgkmcnt(7)
	v_mfma_f32_32x32x16_f16 v[16:31], a[172:175], v[180:183], v[16:31]
	ds_read_b128 v[180:183], v192 offset:54272
	s_add_u32 s44, s34, 0x39000
	s_addc_u32 s45, s35, 0
	s_mov_b32 m0, s59
	s_nop 0
	global_load_lds_dwordx4 v192, s[44:45] sc1
	s_waitcnt lgkmcnt(7)
	v_mfma_f32_32x32x16_f16 v[32:47], a[172:175], v[184:187], v[32:47]
	ds_read_b128 v[184:187], v192 offset:55296
	s_waitcnt lgkmcnt(7)
	v_mfma_f32_32x32x16_f16 v[48:63], a[172:175], v[188:191], v[48:63]
	ds_read_b128 v[188:191], v192 offset:56320
	s_waitcnt lgkmcnt(7)
	v_mfma_f32_32x32x16_f16 v[0:15], a[176:179], v[160:163], v[0:15]
	ds_read_b128 v[160:163], v192 offset:57344
	s_waitcnt lgkmcnt(7)
	v_mfma_f32_32x32x16_f16 v[16:31], a[176:179], v[164:167], v[16:31]
	ds_read_b128 v[164:167], v192 offset:58368
	global_load_lds_dwordx4 v192, s[44:45] offset:1024 sc1
	s_waitcnt lgkmcnt(7)
	v_mfma_f32_32x32x16_f16 v[32:47], a[176:179], v[168:171], v[32:47]
	ds_read_b128 v[168:171], v192 offset:59392
	s_waitcnt lgkmcnt(7)
	v_mfma_f32_32x32x16_f16 v[48:63], a[176:179], v[172:175], v[48:63]
	ds_read_b128 v[172:175], v192 offset:60416
	s_waitcnt lgkmcnt(7)
	v_mfma_f32_32x32x16_f16 v[0:15], a[180:183], v[176:179], v[0:15]
	ds_read_b128 v[176:179], v192 offset:61440
	s_waitcnt lgkmcnt(7)
	v_mfma_f32_32x32x16_f16 v[16:31], a[180:183], v[180:183], v[16:31]
	ds_read_b128 v[180:183], v192 offset:62464
	global_load_lds_dwordx4 v192, s[44:45] offset:2048 sc1
	s_waitcnt lgkmcnt(7)
	v_mfma_f32_32x32x16_f16 v[32:47], a[180:183], v[184:187], v[32:47]
	ds_read_b128 v[184:187], v192 offset:63488
	s_waitcnt lgkmcnt(7)
	v_mfma_f32_32x32x16_f16 v[48:63], a[180:183], v[188:191], v[48:63]
	ds_read_b128 v[188:191], v192 offset:64512
	s_waitcnt vmcnt(8)
	s_barrier
	s_waitcnt lgkmcnt(7)
	v_mfma_f32_32x32x16_f16 v[0:15], a[184:187], v[160:163], v[0:15]
	ds_read_b128 v[160:163], v193 offset:0
	s_waitcnt lgkmcnt(7)
	v_mfma_f32_32x32x16_f16 v[16:31], a[184:187], v[164:167], v[16:31]
	ds_read_b128 v[164:167], v193 offset:1024
	global_load_lds_dwordx4 v192, s[44:45] offset:3072 sc1
	s_waitcnt lgkmcnt(7)
	v_mfma_f32_32x32x16_f16 v[32:47], a[184:187], v[168:171], v[32:47]
	ds_read_b128 v[168:171], v193 offset:2048
	s_waitcnt lgkmcnt(7)
	v_mfma_f32_32x32x16_f16 v[48:63], a[184:187], v[172:175], v[48:63]
	ds_read_b128 v[172:175], v193 offset:3072
	s_waitcnt lgkmcnt(7)
	v_mfma_f32_32x32x16_f16 v[0:15], a[188:191], v[176:179], v[0:15]
	ds_read_b128 v[176:179], v193 offset:4096
	s_waitcnt lgkmcnt(7)
	v_mfma_f32_32x32x16_f16 v[16:31], a[188:191], v[180:183], v[16:31]
	ds_read_b128 v[180:183], v193 offset:5120
	s_waitcnt vmcnt(7)
	v_cmp_gt_u32_e32 vcc, 2, v251
	s_cbranch_vccz .LD_tok20

.LD_tok20:
	s_and_b32 s64, s71, 1
	s_lshl_b32 s64, s64, 22
	s_add_u32 s64, s64, s49
	s_add_u32 s64, s64, 0x40000
	s_add_u32 s34, s6, s64
	s_addc_u32 s35, s7, 0
	s_add_u32 s44, s34, 0x0
	s_addc_u32 s45, s35, 0
	s_mov_b32 m0, s52
	s_nop 0
	global_load_lds_dwordx4 v192, s[44:45] sc1
	s_waitcnt lgkmcnt(7)
	v_mfma_f32_32x32x16_f16 v[32:47], a[188:191], v[184:187], v[32:47]
	ds_read_b128 v[184:187], v193 offset:6144
	s_waitcnt lgkmcnt(7)
	v_mfma_f32_32x32x16_f16 v[48:63], a[188:191], v[188:191], v[48:63]
	ds_read_b128 v[188:191], v193 offset:7168
	s_waitcnt lgkmcnt(7)
	v_mfma_f32_32x32x16_f16 v[0:15], a[192:195], v[160:163], v[0:15]
	ds_read_b128 v[160:163], v193 offset:8192
	s_waitcnt lgkmcnt(7)
	v_mfma_f32_32x32x16_f16 v[16:31], a[192:195], v[164:167], v[16:31]
	ds_read_b128 v[164:167], v193 offset:9216
	global_load_lds_dwordx4 v192, s[44:45] offset:1024 sc1
	s_waitcnt lgkmcnt(7)
	v_mfma_f32_32x32x16_f16 v[32:47], a[192:195], v[168:171], v[32:47]
	ds_read_b128 v[168:171], v193 offset:10240
	s_waitcnt lgkmcnt(7)
	v_mfma_f32_32x32x16_f16 v[48:63], a[192:195], v[172:175], v[48:63]
	ds_read_b128 v[172:175], v193 offset:11264
	s_waitcnt lgkmcnt(7)
	v_mfma_f32_32x32x16_f16 v[0:15], a[196:199], v[176:179], v[0:15]
	ds_read_b128 v[176:179], v193 offset:12288
	s_waitcnt lgkmcnt(7)
	v_mfma_f32_32x32x16_f16 v[16:31], a[196:199], v[180:183], v[16:31]
	ds_read_b128 v[180:183], v193 offset:13312
	global_load_lds_dwordx4 v192, s[44:45] offset:2048 sc1
	s_waitcnt lgkmcnt(7)
	v_mfma_f32_32x32x16_f16 v[32:47], a[196:199], v[184:187], v[32:47]
	ds_read_b128 v[184:187], v193 offset:14336
	s_waitcnt lgkmcnt(7)
	v_mfma_f32_32x32x16_f16 v[48:63], a[196:199], v[188:191], v[48:63]
	ds_read_b128 v[188:191], v193 offset:15360
	s_waitcnt lgkmcnt(7)
	v_mfma_f32_32x32x16_f16 v[0:15], a[200:203], v[160:163], v[0:15]
	ds_read_b128 v[160:163], v193 offset:16384
	s_waitcnt lgkmcnt(7)
	v_mfma_f32_32x32x16_f16 v[16:31], a[200:203], v[164:167], v[16:31]
	ds_read_b128 v[164:167], v193 offset:17408
	global_load_lds_dwordx4 v192, s[44:45] offset:3072 sc1
	s_waitcnt lgkmcnt(7)
	v_mfma_f32_32x32x16_f16 v[32:47], a[200:203], v[168:171], v[32:47]
	ds_read_b128 v[168:171], v193 offset:18432
	s_waitcnt lgkmcnt(7)
	v_mfma_f32_32x32x16_f16 v[48:63], a[200:203], v[172:175], v[48:63]
	ds_read_b128 v[172:175], v193 offset:19456
	s_waitcnt lgkmcnt(7)
	v_mfma_f32_32x32x16_f16 v[0:15], a[204:207], v[176:179], v[0:15]
	ds_read_b128 v[176:179], v193 offset:20480
	s_waitcnt lgkmcnt(7)
	v_mfma_f32_32x32x16_f16 v[16:31], a[204:207], v[180:183], v[16:31]
	ds_read_b128 v[180:183], v193 offset:21504
	s_add_u32 s44, s34, 0x1000
	s_addc_u32 s45, s35, 0
	s_mov_b32 m0, s53
	s_nop 0
	global_load_lds_dwordx4 v192, s[44:45] sc1
	s_waitcnt lgkmcnt(7)
	v_mfma_f32_32x32x16_f16 v[32:47], a[204:207], v[184:187], v[32:47]
	ds_read_b128 v[184:187], v193 offset:22528
	s_waitcnt lgkmcnt(7)
	v_mfma_f32_32x32x16_f16 v[48:63], a[204:207], v[188:191], v[48:63]
	ds_read_b128 v[188:191], v193 offset:23552
	s_waitcnt lgkmcnt(7)
	v_mfma_f32_32x32x16_f16 v[0:15], a[208:211], v[160:163], v[0:15]
	ds_read_b128 v[160:163], v193 offset:24576
	s_waitcnt lgkmcnt(7)
	v_mfma_f32_32x32x16_f16 v[16:31], a[208:211], v[164:167], v[16:31]
	ds_read_b128 v[164:167], v193 offset:25600
	global_load_lds_dwordx4 v192, s[44:45] offset:1024 sc1
	s_waitcnt lgkmcnt(7)
	v_mfma_f32_32x32x16_f16 v[32:47], a[208:211], v[168:171], v[32:47]
	ds_read_b128 v[168:171], v193 offset:26624
	s_waitcnt lgkmcnt(7)
	v_mfma_f32_32x32x16_f16 v[48:63], a[208:211], v[172:175], v[48:63]
	ds_read_b128 v[172:175], v193 offset:27648
	s_waitcnt lgkmcnt(7)
	v_mfma_f32_32x32x16_f16 v[0:15], a[212:215], v[176:179], v[0:15]
	ds_read_b128 v[176:179], v193 offset:28672
	s_waitcnt lgkmcnt(7)
	v_mfma_f32_32x32x16_f16 v[16:31], a[212:215], v[180:183], v[16:31]
	ds_read_b128 v[180:183], v193 offset:29696
	global_load_lds_dwordx4 v192, s[44:45] offset:2048 sc1
	s_waitcnt lgkmcnt(7)
	v_mfma_f32_32x32x16_f16 v[32:47], a[212:215], v[184:187], v[32:47]
	ds_read_b128 v[184:187], v193 offset:30720
	s_waitcnt lgkmcnt(7)
	v_mfma_f32_32x32x16_f16 v[48:63], a[212:215], v[188:191], v[48:63]
	ds_read_b128 v[188:191], v193 offset:31744
	s_waitcnt vmcnt(7)
	s_barrier
	s_waitcnt lgkmcnt(7)
	v_mfma_f32_32x32x16_f16 v[0:15], a[216:219], v[160:163], v[0:15]
	ds_read_b128 v[160:163], v193 offset:32768
	s_waitcnt lgkmcnt(7)
	v_mfma_f32_32x32x16_f16 v[16:31], a[216:219], v[164:167], v[16:31]
	ds_read_b128 v[164:167], v193 offset:33792
	global_load_lds_dwordx4 v192, s[44:45] offset:3072 sc1
	s_waitcnt lgkmcnt(7)
	v_mfma_f32_32x32x16_f16 v[32:47], a[216:219], v[168:171], v[32:47]
	ds_read_b128 v[168:171], v193 offset:34816
	s_waitcnt lgkmcnt(7)
	v_mfma_f32_32x32x16_f16 v[48:63], a[216:219], v[172:175], v[48:63]
	ds_read_b128 v[172:175], v193 offset:35840
	s_waitcnt lgkmcnt(7)
	v_mfma_f32_32x32x16_f16 v[0:15], a[220:223], v[176:179], v[0:15]
	ds_read_b128 v[176:179], v193 offset:36864
	s_waitcnt lgkmcnt(7)
	v_mfma_f32_32x32x16_f16 v[16:31], a[220:223], v[180:183], v[16:31]
	ds_read_b128 v[180:183], v193 offset:37888
	s_add_u32 s44, s34, 0x8000
	s_addc_u32 s45, s35, 0
	s_mov_b32 m0, s54
	s_nop 0
	global_load_lds_dwordx4 v192, s[44:45] sc1
	s_waitcnt lgkmcnt(7)
	v_mfma_f32_32x32x16_f16 v[32:47], a[220:223], v[184:187], v[32:47]
	ds_read_b128 v[184:187], v193 offset:38912
	s_waitcnt lgkmcnt(7)
	v_mfma_f32_32x32x16_f16 v[48:63], a[220:223], v[188:191], v[48:63]
	ds_read_b128 v[188:191], v193 offset:39936
	s_waitcnt lgkmcnt(7)
	v_mfma_f32_32x32x16_f16 v[0:15], a[224:227], v[160:163], v[0:15]
	ds_read_b128 v[160:163], v193 offset:40960
	s_waitcnt lgkmcnt(7)
	v_mfma_f32_32x32x16_f16 v[16:31], a[224:227], v[164:167], v[16:31]
	ds_read_b128 v[164:167], v193 offset:41984
	global_load_lds_dwordx4 v192, s[44:45] offset:1024 sc1
	s_waitcnt lgkmcnt(7)
	v_mfma_f32_32x32x16_f16 v[32:47], a[224:227], v[168:171], v[32:47]
	ds_read_b128 v[168:171], v193 offset:43008
	s_waitcnt lgkmcnt(7)
	v_mfma_f32_32x32x16_f16 v[48:63], a[224:227], v[172:175], v[48:63]
	ds_read_b128 v[172:175], v193 offset:44032
	s_waitcnt lgkmcnt(7)
	v_mfma_f32_32x32x16_f16 v[0:15], a[228:231], v[176:179], v[0:15]
	ds_read_b128 v[176:179], v193 offset:45056
	s_waitcnt lgkmcnt(7)
	v_mfma_f32_32x32x16_f16 v[16:31], a[228:231], v[180:183], v[16:31]
	ds_read_b128 v[180:183], v193 offset:46080
	global_load_lds_dwordx4 v192, s[44:45] offset:2048 sc1
	s_waitcnt lgkmcnt(7)
	v_mfma_f32_32x32x16_f16 v[32:47], a[228:231], v[184:187], v[32:47]
	ds_read_b128 v[184:187], v193 offset:47104
	s_waitcnt lgkmcnt(7)
	v_mfma_f32_32x32x16_f16 v[48:63], a[228:231], v[188:191], v[48:63]
	ds_read_b128 v[188:191], v193 offset:48128
	s_waitcnt lgkmcnt(7)
	v_mfma_f32_32x32x16_f16 v[0:15], a[232:235], v[160:163], v[0:15]
	ds_read_b128 v[160:163], v193 offset:49152
	s_waitcnt lgkmcnt(7)
	v_mfma_f32_32x32x16_f16 v[16:31], a[232:235], v[164:167], v[16:31]
	ds_read_b128 v[164:167], v193 offset:50176
	global_load_lds_dwordx4 v192, s[44:45] offset:3072 sc1
	s_waitcnt lgkmcnt(7)
	v_mfma_f32_32x32x16_f16 v[32:47], a[232:235], v[168:171], v[32:47]
	ds_read_b128 v[168:171], v193 offset:51200
	s_waitcnt lgkmcnt(7)
	v_mfma_f32_32x32x16_f16 v[48:63], a[232:235], v[172:175], v[48:63]
	ds_read_b128 v[172:175], v193 offset:52224
	s_waitcnt lgkmcnt(7)
	v_mfma_f32_32x32x16_f16 v[0:15], a[236:239], v[176:179], v[0:15]
	ds_read_b128 v[176:179], v193 offset:53248
	s_waitcnt lgkmcnt(7)
	v_mfma_f32_32x32x16_f16 v[16:31], a[236:239], v[180:183], v[16:31]
	ds_read_b128 v[180:183], v193 offset:54272
	s_add_u32 s44, s34, 0x9000
	s_addc_u32 s45, s35, 0
	s_mov_b32 m0, s55
	s_nop 0
	global_load_lds_dwordx4 v192, s[44:45] sc1
	s_waitcnt lgkmcnt(7)
	v_mfma_f32_32x32x16_f16 v[32:47], a[236:239], v[184:187], v[32:47]
	ds_read_b128 v[184:187], v193 offset:55296
	s_waitcnt lgkmcnt(7)
	v_mfma_f32_32x32x16_f16 v[48:63], a[236:239], v[188:191], v[48:63]
	ds_read_b128 v[188:191], v193 offset:56320
	s_waitcnt lgkmcnt(7)
	v_mfma_f32_32x32x16_f16 v[0:15], a[240:243], v[160:163], v[0:15]
	ds_read_b128 v[160:163], v193 offset:57344
	s_waitcnt lgkmcnt(7)
	v_mfma_f32_32x32x16_f16 v[16:31], a[240:243], v[164:167], v[16:31]
	ds_read_b128 v[164:167], v193 offset:58368
	global_load_lds_dwordx4 v192, s[44:45] offset:1024 sc1
	s_waitcnt lgkmcnt(7)
	v_mfma_f32_32x32x16_f16 v[32:47], a[240:243], v[168:171], v[32:47]
	ds_read_b128 v[168:171], v193 offset:59392
	s_waitcnt lgkmcnt(7)
	v_mfma_f32_32x32x16_f16 v[48:63], a[240:243], v[172:175], v[48:63]
	ds_read_b128 v[172:175], v193 offset:60416
	s_waitcnt lgkmcnt(7)
	v_mfma_f32_32x32x16_f16 v[0:15], a[244:247], v[176:179], v[0:15]
	ds_read_b128 v[176:179], v193 offset:61440
	s_waitcnt lgkmcnt(7)
	v_mfma_f32_32x32x16_f16 v[16:31], a[244:247], v[180:183], v[16:31]
	ds_read_b128 v[180:183], v193 offset:62464
	global_load_lds_dwordx4 v192, s[44:45] offset:2048 sc1
	s_waitcnt lgkmcnt(7)
	v_mfma_f32_32x32x16_f16 v[32:47], a[244:247], v[184:187], v[32:47]
	ds_read_b128 v[184:187], v193 offset:63488
	s_waitcnt lgkmcnt(7)
	v_mfma_f32_32x32x16_f16 v[48:63], a[244:247], v[188:191], v[48:63]
	ds_read_b128 v[188:191], v193 offset:64512
	s_waitcnt vmcnt(7)
	s_barrier
	s_waitcnt lgkmcnt(7)
	v_mfma_f32_32x32x16_f16 v[0:15], a[248:251], v[160:163], v[0:15]
	ds_read_b128 v[160:163], v192 offset:0
	s_waitcnt lgkmcnt(7)
	v_mfma_f32_32x32x16_f16 v[16:31], a[248:251], v[164:167], v[16:31]
	ds_read_b128 v[164:167], v192 offset:1024
	global_load_lds_dwordx4 v192, s[44:45] offset:3072 sc1
	s_waitcnt lgkmcnt(7)
	v_mfma_f32_32x32x16_f16 v[32:47], a[248:251], v[168:171], v[32:47]
	ds_read_b128 v[168:171], v192 offset:2048
	s_waitcnt lgkmcnt(7)
	v_mfma_f32_32x32x16_f16 v[48:63], a[248:251], v[172:175], v[48:63]
	ds_read_b128 v[172:175], v192 offset:3072
	s_waitcnt lgkmcnt(7)
	v_mfma_f32_32x32x16_f16 v[0:15], a[252:255], v[176:179], v[0:15]
	ds_read_b128 v[176:179], v192 offset:4096
	s_waitcnt lgkmcnt(7)
	v_mfma_f32_32x32x16_f16 v[16:31], a[252:255], v[180:183], v[16:31]
	ds_read_b128 v[180:183], v192 offset:5120
	s_add_u32 s44, s34, 0x10000
	s_addc_u32 s45, s35, 0
	s_mov_b32 m0, s56
	s_nop 0
	global_load_lds_dwordx4 v192, s[44:45] sc1
	s_waitcnt lgkmcnt(7)
	v_mfma_f32_32x32x16_f16 v[32:47], a[252:255], v[184:187], v[32:47]
	ds_read_b128 v[184:187], v192 offset:6144
	s_waitcnt lgkmcnt(7)
	v_mfma_f32_32x32x16_f16 v[48:63], a[252:255], v[188:191], v[48:63]
	ds_read_b128 v[188:191], v192 offset:7168
	s_and_b32 s64, s33, 1
	s_lshl_b32 s64, s64, 22
	s_add_u32 s64, s64, s50
	s_add_u32 s36, s6, s64
	s_addc_u32 s37, s7, 0
	s_lshl_b32 s64, s33, 3
	s_add_u32 s64, s64, s29
	s_lshl_b32 s64, s64, 5
	s_add_u32 s64, s64, s30
	s_lshl_b32 s64, s64, 2
	s_add_u32 s40, s8, s64
	s_addc_u32 s41, s9, 0
	s_add_u32 s61, s33, 1
	s_min_u32 s61, s61, s60
	s_lshl_b32 s64, s33, 19
	s_add_u32 s72, s62, s64
	s_addc_u32 s73, s63, 0
	s_nop 11
	v_exp_f32_e32 v200, v0
	v_exp_f32_e32 v201, v1
	v_exp_f32_e32 v202, v2
	v_exp_f32_e32 v203, v3
	v_exp_f32_e32 v204, v4
	v_exp_f32_e32 v205, v5
	v_exp_f32_e32 v206, v6
	v_exp_f32_e32 v207, v7
	v_exp_f32_e32 v208, v8
	v_exp_f32_e32 v209, v9
	v_exp_f32_e32 v210, v10
	v_exp_f32_e32 v211, v11
	v_exp_f32_e32 v212, v12
	v_exp_f32_e32 v213, v13
	v_exp_f32_e32 v214, v14
	v_exp_f32_e32 v215, v15
	v_add_f32_e32 v200, 1.0, v200
	v_add_f32_e32 v201, 1.0, v201
	v_add_f32_e32 v202, 1.0, v202
	v_add_f32_e32 v203, 1.0, v203
	v_add_f32_e32 v204, 1.0, v204
	v_add_f32_e32 v205, 1.0, v205
	v_add_f32_e32 v206, 1.0, v206
	v_add_f32_e32 v207, 1.0, v207
	v_add_f32_e32 v208, 1.0, v208
	v_add_f32_e32 v209, 1.0, v209
	v_add_f32_e32 v210, 1.0, v210
	v_add_f32_e32 v211, 1.0, v211
	v_add_f32_e32 v212, 1.0, v212
	v_add_f32_e32 v213, 1.0, v213
	v_add_f32_e32 v214, 1.0, v214
	v_add_f32_e32 v215, 1.0, v215
	v_rcp_f32_e32 v200, v200
	v_rcp_f32_e32 v201, v201
	v_rcp_f32_e32 v202, v202
	v_rcp_f32_e32 v203, v203
	v_rcp_f32_e32 v204, v204
	v_rcp_f32_e32 v205, v205
	v_rcp_f32_e32 v206, v206
	v_rcp_f32_e32 v207, v207
	v_rcp_f32_e32 v208, v208
	v_rcp_f32_e32 v209, v209
	v_rcp_f32_e32 v210, v210
	v_rcp_f32_e32 v211, v211
	v_rcp_f32_e32 v212, v212
	v_rcp_f32_e32 v213, v213
	v_rcp_f32_e32 v214, v214
	v_rcp_f32_e32 v215, v215
	v_fmamk_f32 v208, v208, 0xc0b8aa3b, v198
	v_fmamk_f32 v209, v209, 0xc0b8aa3b, v198
	v_fmamk_f32 v210, v210, 0xc0b8aa3b, v198
	v_fmamk_f32 v211, v211, 0xc0b8aa3b, v198
	v_mul_f32_e32 v204, v204, v128
	v_mul_f32_e32 v205, v205, v129
	v_mul_f32_e32 v206, v206, v130
	v_mul_f32_e32 v207, v207, v131
	v_fma_f32 v128, v200, v208, v204
	v_fma_f32 v129, v201, v209, v205
	v_fma_f32 v130, v202, v210, v206
	v_fma_f32 v131, v203, v211, v207
	v_exp_f32_e32 v200, v128
	v_exp_f32_e32 v201, v129
	v_exp_f32_e32 v202, v130
	v_exp_f32_e32 v203, v131
	s_waitcnt lgkmcnt(7)
	v_mfma_f32_32x32x16_f16 v[64:79], a[0:3], v[160:163], v[64:79]
	ds_read_b128 v[160:163], v192 offset:8192
	v_add_f32_e32 v200, 1.0, v200
	v_add_f32_e32 v201, 1.0, v201
	v_add_f32_e32 v202, 1.0, v202
	v_add_f32_e32 v203, 1.0, v203
	s_waitcnt lgkmcnt(7)
	v_mfma_f32_32x32x16_f16 v[80:95], a[0:3], v[164:167], v[80:95]
	ds_read_b128 v[164:167], v192 offset:9216
	global_load_lds_dwordx4 v192, s[44:45] offset:1024 sc1
	v_rcp_f32_e32 v200, v200
	v_rcp_f32_e32 v201, v201
	s_waitcnt lgkmcnt(7)
	v_mfma_f32_32x32x16_f16 v[96:111], a[0:3], v[168:171], v[96:111]
	ds_read_b128 v[168:171], v192 offset:10240
	v_rcp_f32_e32 v202, v202
	v_rcp_f32_e32 v203, v203
	v_fma_f32 v200, v200, 2.0, -1.0
	s_waitcnt lgkmcnt(7)
	v_mfma_f32_32x32x16_f16 v[112:127], a[0:3], v[172:175], v[112:127]
	ds_read_b128 v[172:175], v192 offset:11264
	v_fma_f32 v201, v201, 2.0, -1.0
	v_fma_f32 v202, v202, 2.0, -1.0
	v_fma_f32 v203, v203, 2.0, -1.0
	v_mul_f32_e32 v216, v212, v200
	v_mul_f32_e32 v217, v213, v201
	s_waitcnt lgkmcnt(7)
	v_mfma_f32_32x32x16_f16 v[64:79], a[4:7], v[176:179], v[64:79]
	ds_read_b128 v[176:179], v192 offset:12288
	v_mul_f32_e32 v218, v214, v202
	v_mul_f32_e32 v219, v215, v203
	v_mul_f32_e32 v236, v216, v228
	v_mul_f32_e32 v237, v216, v232
	v_fmac_f32_e32 v236, v217, v229
	s_waitcnt lgkmcnt(7)
	v_mfma_f32_32x32x16_f16 v[80:95], a[4:7], v[180:183], v[80:95]
	ds_read_b128 v[180:183], v192 offset:13312
	global_load_lds_dwordx4 v192, s[44:45] offset:2048 sc1
	v_fmac_f32_e32 v237, v217, v233
	v_fmac_f32_e32 v236, v218, v230
	v_fmac_f32_e32 v237, v218, v234
	v_fmac_f32_e32 v236, v219, v231
	v_fmac_f32_e32 v237, v219, v235
	s_waitcnt lgkmcnt(7)
	v_mfma_f32_32x32x16_f16 v[96:111], a[4:7], v[184:187], v[96:111]
	ds_read_b128 v[184:187], v192 offset:14336
	v_mov_b32_e32 v238, v236
	v_mov_b32_e32 v239, v236
	v_mov_b32_e32 v240, v237
	v_mov_b32_e32 v241, v237
	s_waitcnt lgkmcnt(7)
	v_mfma_f32_32x32x16_f16 v[112:127], a[4:7], v[188:191], v[112:127]
	ds_read_b128 v[188:191], v192 offset:15360
	s_nop 1
	v_permlane32_swap_b32_e32 v238, v239
	v_permlane32_swap_b32_e32 v240, v241
	v_add_f32_e32 v238, v238, v239
	v_add_f32_e32 v239, v240, v241
	ds_write_b64 v248, v[238:239] offset:0
	s_waitcnt lgkmcnt(8)
	v_mfma_f32_32x32x16_f16 v[64:79], a[8:11], v[160:163], v[64:79]
	ds_read_b128 v[160:163], v192 offset:16384
	v_cvt_pk_f16_f32 v220, v216, v217
	v_cvt_pk_f16_f32 v221, v218, v219
	v_exp_f32_e32 v200, v16
	s_waitcnt lgkmcnt(8)
	v_mfma_f32_32x32x16_f16 v[80:95], a[8:11], v[164:167], v[80:95]
	ds_read_b128 v[164:167], v192 offset:17408
	global_load_lds_dwordx4 v192, s[44:45] offset:3072 sc1
	v_exp_f32_e32 v201, v17
	v_exp_f32_e32 v202, v18
	s_waitcnt lgkmcnt(8)
	v_mfma_f32_32x32x16_f16 v[96:111], a[8:11], v[168:171], v[96:111]
	ds_read_b128 v[168:171], v192 offset:18432
	v_exp_f32_e32 v203, v19
	v_exp_f32_e32 v204, v20
	s_waitcnt lgkmcnt(8)
	v_mfma_f32_32x32x16_f16 v[112:127], a[8:11], v[172:175], v[112:127]
	ds_read_b128 v[172:175], v192 offset:19456
	v_exp_f32_e32 v205, v21
	v_exp_f32_e32 v206, v22
	s_waitcnt lgkmcnt(8)
	v_mfma_f32_32x32x16_f16 v[64:79], a[12:15], v[176:179], v[64:79]
	ds_read_b128 v[176:179], v192 offset:20480
	v_exp_f32_e32 v207, v23
	v_exp_f32_e32 v208, v24
	s_waitcnt lgkmcnt(8)
	v_mfma_f32_32x32x16_f16 v[80:95], a[12:15], v[180:183], v[80:95]
	ds_read_b128 v[180:183], v192 offset:21504
	s_add_u32 s44, s34, 0x11000
	s_addc_u32 s45, s35, 0
	s_mov_b32 m0, s57
	s_nop 0
	global_load_lds_dwordx4 v192, s[44:45] sc1
	v_exp_f32_e32 v209, v25
	v_exp_f32_e32 v210, v26
	s_waitcnt lgkmcnt(8)
	v_mfma_f32_32x32x16_f16 v[96:111], a[12:15], v[184:187], v[96:111]
	ds_read_b128 v[184:187], v192 offset:22528
	v_exp_f32_e32 v211, v27
	v_exp_f32_e32 v212, v28
	s_waitcnt lgkmcnt(8)
	v_mfma_f32_32x32x16_f16 v[112:127], a[12:15], v[188:191], v[112:127]
	ds_read_b128 v[188:191], v192 offset:23552
	v_exp_f32_e32 v213, v29
	v_exp_f32_e32 v214, v30
	s_waitcnt lgkmcnt(7)
	v_mfma_f32_32x32x16_f16 v[64:79], a[16:19], v[160:163], v[64:79]
	ds_read_b128 v[160:163], v192 offset:24576
	v_exp_f32_e32 v215, v31
	v_add_f32_e32 v200, 1.0, v200
	v_add_f32_e32 v201, 1.0, v201
	v_add_f32_e32 v202, 1.0, v202
	s_waitcnt lgkmcnt(7)
	v_mfma_f32_32x32x16_f16 v[80:95], a[16:19], v[164:167], v[80:95]
	ds_read_b128 v[164:167], v192 offset:25600
	global_load_lds_dwordx4 v192, s[44:45] offset:1024 sc1
	v_add_f32_e32 v203, 1.0, v203
	v_add_f32_e32 v204, 1.0, v204
	v_add_f32_e32 v205, 1.0, v205
	v_add_f32_e32 v206, 1.0, v206
	v_add_f32_e32 v207, 1.0, v207
	s_waitcnt lgkmcnt(7)
	v_mfma_f32_32x32x16_f16 v[96:111], a[16:19], v[168:171], v[96:111]
	ds_read_b128 v[168:171], v192 offset:26624
	v_add_f32_e32 v208, 1.0, v208
	v_add_f32_e32 v209, 1.0, v209
	v_add_f32_e32 v210, 1.0, v210
	v_add_f32_e32 v211, 1.0, v211
	v_add_f32_e32 v212, 1.0, v212
	s_waitcnt lgkmcnt(7)
	v_mfma_f32_32x32x16_f16 v[112:127], a[16:19], v[172:175], v[112:127]
	ds_read_b128 v[172:175], v192 offset:27648
	v_add_f32_e32 v213, 1.0, v213
	v_add_f32_e32 v214, 1.0, v214
	v_add_f32_e32 v215, 1.0, v215
	v_rcp_f32_e32 v200, v200
	s_waitcnt lgkmcnt(7)
	v_mfma_f32_32x32x16_f16 v[64:79], a[20:23], v[176:179], v[64:79]
	ds_read_b128 v[176:179], v192 offset:28672
	v_rcp_f32_e32 v201, v201
	v_rcp_f32_e32 v202, v202
	s_waitcnt lgkmcnt(7)
	v_mfma_f32_32x32x16_f16 v[80:95], a[20:23], v[180:183], v[80:95]
	ds_read_b128 v[180:183], v192 offset:29696
	global_load_lds_dwordx4 v192, s[44:45] offset:2048 sc1
	v_rcp_f32_e32 v203, v203
	v_rcp_f32_e32 v204, v204
	s_waitcnt lgkmcnt(7)
	v_mfma_f32_32x32x16_f16 v[96:111], a[20:23], v[184:187], v[96:111]
	ds_read_b128 v[184:187], v192 offset:30720
	v_rcp_f32_e32 v205, v205
	v_rcp_f32_e32 v206, v206
	s_waitcnt lgkmcnt(7)
	v_mfma_f32_32x32x16_f16 v[112:127], a[20:23], v[188:191], v[112:127]
	ds_read_b128 v[188:191], v192 offset:31744
	v_rcp_f32_e32 v207, v207
	v_rcp_f32_e32 v208, v208
	s_waitcnt vmcnt(7)
	s_barrier
	s_waitcnt lgkmcnt(7)
	v_mfma_f32_32x32x16_f16 v[64:79], a[24:27], v[160:163], v[64:79]
	ds_read_b128 v[160:163], v192 offset:32768
	v_rcp_f32_e32 v209, v209
	v_rcp_f32_e32 v210, v210
	s_waitcnt lgkmcnt(7)
	v_mfma_f32_32x32x16_f16 v[80:95], a[24:27], v[164:167], v[80:95]
	ds_read_b128 v[164:167], v192 offset:33792
	global_load_lds_dwordx4 v192, s[44:45] offset:3072 sc1
	v_rcp_f32_e32 v211, v211
	v_rcp_f32_e32 v212, v212
	s_waitcnt lgkmcnt(7)
	v_mfma_f32_32x32x16_f16 v[96:111], a[24:27], v[168:171], v[96:111]
	ds_read_b128 v[168:171], v192 offset:34816
	v_rcp_f32_e32 v213, v213
	v_rcp_f32_e32 v214, v214
	s_waitcnt lgkmcnt(7)
	v_mfma_f32_32x32x16_f16 v[112:127], a[24:27], v[172:175], v[112:127]
	ds_read_b128 v[172:175], v192 offset:35840
	v_rcp_f32_e32 v215, v215
	v_fmamk_f32 v208, v208, 0xc0b8aa3b, v198
	v_fmamk_f32 v209, v209, 0xc0b8aa3b, v198
	v_fmamk_f32 v210, v210, 0xc0b8aa3b, v198
	s_waitcnt lgkmcnt(7)
	v_mfma_f32_32x32x16_f16 v[64:79], a[28:31], v[176:179], v[64:79]
	ds_read_b128 v[176:179], v192 offset:36864
	v_fmamk_f32 v211, v211, 0xc0b8aa3b, v198
	v_mul_f32_e32 v204, v204, v132
	v_mul_f32_e32 v205, v205, v133
	v_mul_f32_e32 v206, v206, v134
	v_mul_f32_e32 v207, v207, v135
	s_waitcnt lgkmcnt(7)
	v_mfma_f32_32x32x16_f16 v[80:95], a[28:31], v[180:183], v[80:95]
	ds_read_b128 v[180:183], v192 offset:37888
	s_add_u32 s44, s34, 0x18000
	s_addc_u32 s45, s35, 0
	s_mov_b32 m0, s58
	s_nop 0
	global_load_lds_dwordx4 v192, s[44:45] sc1
	v_fma_f32 v132, v200, v208, v204
	v_fma_f32 v133, v201, v209, v205
	v_fma_f32 v134, v202, v210, v206
	v_fma_f32 v135, v203, v211, v207
	s_waitcnt lgkmcnt(7)
	v_mfma_f32_32x32x16_f16 v[96:111], a[28:31], v[184:187], v[96:111]
	ds_read_b128 v[184:187], v192 offset:38912
	v_exp_f32_e32 v200, v132
	v_exp_f32_e32 v201, v133
	s_waitcnt lgkmcnt(7)
	v_mfma_f32_32x32x16_f16 v[112:127], a[28:31], v[188:191], v[112:127]
	ds_read_b128 v[188:191], v192 offset:39936
	v_exp_f32_e32 v202, v134
	v_exp_f32_e32 v203, v135
	v_add_f32_e32 v200, 1.0, v200
	s_waitcnt lgkmcnt(7)
	v_mfma_f32_32x32x16_f16 v[64:79], a[32:35], v[160:163], v[64:79]
	ds_read_b128 v[160:163], v192 offset:40960
	v_add_f32_e32 v201, 1.0, v201
	v_add_f32_e32 v202, 1.0, v202
	v_add_f32_e32 v203, 1.0, v203
	v_rcp_f32_e32 v200, v200
	s_waitcnt lgkmcnt(7)
	v_mfma_f32_32x32x16_f16 v[80:95], a[32:35], v[164:167], v[80:95]
	ds_read_b128 v[164:167], v192 offset:41984
	global_load_lds_dwordx4 v192, s[44:45] offset:1024 sc1
	v_rcp_f32_e32 v201, v201
	v_rcp_f32_e32 v202, v202
	s_waitcnt lgkmcnt(7)
	v_mfma_f32_32x32x16_f16 v[96:111], a[32:35], v[168:171], v[96:111]
	ds_read_b128 v[168:171], v192 offset:43008
	v_rcp_f32_e32 v203, v203
	v_fma_f32 v200, v200, 2.0, -1.0
	v_fma_f32 v201, v201, 2.0, -1.0
	v_fma_f32 v202, v202, 2.0, -1.0
	s_waitcnt lgkmcnt(7)
	v_mfma_f32_32x32x16_f16 v[112:127], a[32:35], v[172:175], v[112:127]
	ds_read_b128 v[172:175], v192 offset:44032
	v_fma_f32 v203, v203, 2.0, -1.0
	v_mul_f32_e32 v216, v212, v200
	v_mul_f32_e32 v217, v213, v201
	v_mul_f32_e32 v218, v214, v202
	v_mul_f32_e32 v219, v215, v203
	s_waitcnt lgkmcnt(7)
	v_mfma_f32_32x32x16_f16 v[64:79], a[36:39], v[176:179], v[64:79]
	ds_read_b128 v[176:179], v192 offset:45056
	v_mul_f32_e32 v236, v216, v228
	v_mul_f32_e32 v237, v216, v232
	v_fmac_f32_e32 v236, v217, v229
	v_fmac_f32_e32 v237, v217, v233
	v_fmac_f32_e32 v236, v218, v230
	s_waitcnt lgkmcnt(7)
	v_mfma_f32_32x32x16_f16 v[80:95], a[36:39], v[180:183], v[80:95]
	ds_read_b128 v[180:183], v192 offset:46080
	global_load_lds_dwordx4 v192, s[44:45] offset:2048 sc1
	v_fmac_f32_e32 v237, v218, v234
	v_fmac_f32_e32 v236, v219, v231
	v_fmac_f32_e32 v237, v219, v235
	v_mov_b32_e32 v238, v236
	v_mov_b32_e32 v239, v236
	s_waitcnt lgkmcnt(7)
	v_mfma_f32_32x32x16_f16 v[96:111], a[36:39], v[184:187], v[96:111]
	ds_read_b128 v[184:187], v192 offset:47104
	v_mov_b32_e32 v240, v237
	v_mov_b32_e32 v241, v237
	s_waitcnt lgkmcnt(7)
	v_mfma_f32_32x32x16_f16 v[112:127], a[36:39], v[188:191], v[112:127]
	ds_read_b128 v[188:191], v192 offset:48128
	s_nop 1
	v_permlane32_swap_b32_e32 v238, v239
	v_permlane32_swap_b32_e32 v240, v241
	v_add_f32_e32 v238, v238, v239
	v_add_f32_e32 v239, v240, v241
	ds_write_b64 v248, v[238:239] offset:256
	s_waitcnt lgkmcnt(8)
	v_mfma_f32_32x32x16_f16 v[64:79], a[40:43], v[160:163], v[64:79]
	ds_read_b128 v[160:163], v192 offset:49152
	v_cvt_pk_f16_f32 v222, v216, v217
	v_cvt_pk_f16_f32 v223, v218, v219
	s_waitcnt lgkmcnt(8)
	v_mfma_f32_32x32x16_f16 v[80:95], a[40:43], v[164:167], v[80:95]
	ds_read_b128 v[164:167], v192 offset:50176
	global_load_lds_dwordx4 v192, s[44:45] offset:3072 sc1
	s_nop 1
	v_permlane32_swap_b32_e32 v220, v222
	v_permlane32_swap_b32_e32 v221, v223
	s_cmp_eq_u32 s31, 0
	s_cbranch_scc1 .LD_slow22
	global_store_dwordx4 v195, v[220:223], s[36:37] offset:0
	s_branch .LD_join23

.LD_join23:
	s_waitcnt lgkmcnt(8)
	v_mfma_f32_32x32x16_f16 v[96:111], a[40:43], v[168:171], v[96:111]
	ds_read_b128 v[168:171], v192 offset:51200
	v_exp_f32_e32 v200, v32
	v_exp_f32_e32 v201, v33
	s_waitcnt lgkmcnt(8)
	v_mfma_f32_32x32x16_f16 v[112:127], a[40:43], v[172:175], v[112:127]
	ds_read_b128 v[172:175], v192 offset:52224
	v_exp_f32_e32 v202, v34
	v_exp_f32_e32 v203, v35
	s_waitcnt lgkmcnt(8)
	v_mfma_f32_32x32x16_f16 v[64:79], a[44:47], v[176:179], v[64:79]
	ds_read_b128 v[176:179], v192 offset:53248
	v_exp_f32_e32 v204, v36
	v_exp_f32_e32 v205, v37
	s_waitcnt lgkmcnt(8)
	v_mfma_f32_32x32x16_f16 v[80:95], a[44:47], v[180:183], v[80:95]
	ds_read_b128 v[180:183], v192 offset:54272
	s_add_u32 s44, s34, 0x19000
	s_addc_u32 s45, s35, 0
	s_mov_b32 m0, s59
	s_nop 0
	global_load_lds_dwordx4 v192, s[44:45] sc1
	v_exp_f32_e32 v206, v38
	v_exp_f32_e32 v207, v39
	s_waitcnt lgkmcnt(8)
	v_mfma_f32_32x32x16_f16 v[96:111], a[44:47], v[184:187], v[96:111]
	ds_read_b128 v[184:187], v192 offset:55296
	v_exp_f32_e32 v208, v40
	v_exp_f32_e32 v209, v41
	s_waitcnt lgkmcnt(8)
	v_mfma_f32_32x32x16_f16 v[112:127], a[44:47], v[188:191], v[112:127]
	ds_read_b128 v[188:191], v192 offset:56320
	v_exp_f32_e32 v210, v42
	v_exp_f32_e32 v211, v43
	s_waitcnt lgkmcnt(7)
	v_mfma_f32_32x32x16_f16 v[64:79], a[48:51], v[160:163], v[64:79]
	ds_read_b128 v[160:163], v192 offset:57344
	v_exp_f32_e32 v212, v44
	v_exp_f32_e32 v213, v45
	s_waitcnt lgkmcnt(7)
	v_mfma_f32_32x32x16_f16 v[80:95], a[48:51], v[164:167], v[80:95]
	ds_read_b128 v[164:167], v192 offset:58368
	global_load_lds_dwordx4 v192, s[44:45] offset:1024 sc1
	v_exp_f32_e32 v214, v46
	v_exp_f32_e32 v215, v47
	v_add_f32_e32 v200, 1.0, v200
	s_waitcnt lgkmcnt(7)
	v_mfma_f32_32x32x16_f16 v[96:111], a[48:51], v[168:171], v[96:111]
	ds_read_b128 v[168:171], v192 offset:59392
	v_add_f32_e32 v201, 1.0, v201
	v_add_f32_e32 v202, 1.0, v202
	v_add_f32_e32 v203, 1.0, v203
	v_add_f32_e32 v204, 1.0, v204
	v_add_f32_e32 v205, 1.0, v205
	s_waitcnt lgkmcnt(7)
	v_mfma_f32_32x32x16_f16 v[112:127], a[48:51], v[172:175], v[112:127]
	ds_read_b128 v[172:175], v192 offset:60416
	v_add_f32_e32 v206, 1.0, v206
	v_add_f32_e32 v207, 1.0, v207
	v_add_f32_e32 v208, 1.0, v208
	v_add_f32_e32 v209, 1.0, v209
	v_add_f32_e32 v210, 1.0, v210
	s_waitcnt lgkmcnt(7)
	v_mfma_f32_32x32x16_f16 v[64:79], a[52:55], v[176:179], v[64:79]
	ds_read_b128 v[176:179], v192 offset:61440
	v_add_f32_e32 v211, 1.0, v211
	v_add_f32_e32 v212, 1.0, v212
	v_add_f32_e32 v213, 1.0, v213
	v_add_f32_e32 v214, 1.0, v214
	v_add_f32_e32 v215, 1.0, v215
	s_waitcnt lgkmcnt(7)
	v_mfma_f32_32x32x16_f16 v[80:95], a[52:55], v[180:183], v[80:95]
	ds_read_b128 v[180:183], v192 offset:62464
	global_load_lds_dwordx4 v192, s[44:45] offset:2048 sc1
	v_rcp_f32_e32 v200, v200
	v_rcp_f32_e32 v201, v201
	s_waitcnt lgkmcnt(7)
	v_mfma_f32_32x32x16_f16 v[96:111], a[52:55], v[184:187], v[96:111]
	ds_read_b128 v[184:187], v192 offset:63488
	v_rcp_f32_e32 v202, v202
	v_rcp_f32_e32 v203, v203
	s_waitcnt lgkmcnt(7)
	v_mfma_f32_32x32x16_f16 v[112:127], a[52:55], v[188:191], v[112:127]
	ds_read_b128 v[188:191], v192 offset:64512
	v_rcp_f32_e32 v204, v204
	v_rcp_f32_e32 v205, v205
	s_waitcnt vmcnt(8)
	s_barrier
	s_waitcnt lgkmcnt(7)
	v_mfma_f32_32x32x16_f16 v[64:79], a[56:59], v[160:163], v[64:79]
	ds_read_b128 v[160:163], v193 offset:0
	v_rcp_f32_e32 v206, v206
	v_rcp_f32_e32 v207, v207
	s_waitcnt lgkmcnt(7)
	v_mfma_f32_32x32x16_f16 v[80:95], a[56:59], v[164:167], v[80:95]
	ds_read_b128 v[164:167], v193 offset:1024
	global_load_lds_dwordx4 v192, s[44:45] offset:3072 sc1
	v_rcp_f32_e32 v208, v208
	v_rcp_f32_e32 v209, v209
	s_waitcnt lgkmcnt(7)
	v_mfma_f32_32x32x16_f16 v[96:111], a[56:59], v[168:171], v[96:111]
	ds_read_b128 v[168:171], v193 offset:2048
	v_rcp_f32_e32 v210, v210
	v_rcp_f32_e32 v211, v211
	s_waitcnt lgkmcnt(7)
	v_mfma_f32_32x32x16_f16 v[112:127], a[56:59], v[172:175], v[112:127]
	ds_read_b128 v[172:175], v193 offset:3072
	v_rcp_f32_e32 v212, v212
	v_rcp_f32_e32 v213, v213
	s_waitcnt lgkmcnt(7)
	v_mfma_f32_32x32x16_f16 v[64:79], a[60:63], v[176:179], v[64:79]
	ds_read_b128 v[176:179], v193 offset:4096
	v_rcp_f32_e32 v214, v214
	v_rcp_f32_e32 v215, v215
	v_fmamk_f32 v208, v208, 0xc0b8aa3b, v198
	s_waitcnt lgkmcnt(7)
	v_mfma_f32_32x32x16_f16 v[80:95], a[60:63], v[180:183], v[80:95]
	ds_read_b128 v[180:183], v193 offset:5120
	s_add_u32 s44, s34, 0x20000
	s_addc_u32 s45, s35, 0
	s_mov_b32 m0, s52
	s_nop 0
	global_load_lds_dwordx4 v192, s[44:45] sc1
	v_fmamk_f32 v209, v209, 0xc0b8aa3b, v198
	v_fmamk_f32 v210, v210, 0xc0b8aa3b, v198
	v_fmamk_f32 v211, v211, 0xc0b8aa3b, v198
	v_mul_f32_e32 v204, v204, v136
	v_mul_f32_e32 v205, v205, v137
	s_waitcnt lgkmcnt(7)
	v_mfma_f32_32x32x16_f16 v[96:111], a[60:63], v[184:187], v[96:111]
	ds_read_b128 v[184:187], v193 offset:6144
	v_mul_f32_e32 v206, v206, v138
	v_mul_f32_e32 v207, v207, v139
	v_fma_f32 v136, v200, v208, v204
	v_fma_f32 v137, v201, v209, v205
	v_fma_f32 v138, v202, v210, v206
	s_waitcnt lgkmcnt(7)
	v_mfma_f32_32x32x16_f16 v[112:127], a[60:63], v[188:191], v[112:127]
	ds_read_b128 v[188:191], v193 offset:7168
	v_fma_f32 v139, v203, v211, v207
	v_exp_f32_e32 v200, v136
	v_exp_f32_e32 v201, v137
	s_waitcnt lgkmcnt(7)
	v_mfma_f32_32x32x16_f16 v[64:79], a[64:67], v[160:163], v[64:79]
	ds_read_b128 v[160:163], v193 offset:8192
	v_exp_f32_e32 v202, v138
	v_exp_f32_e32 v203, v139
	v_add_f32_e32 v200, 1.0, v200
	s_waitcnt lgkmcnt(7)
	v_mfma_f32_32x32x16_f16 v[80:95], a[64:67], v[164:167], v[80:95]
	ds_read_b128 v[164:167], v193 offset:9216
	global_load_lds_dwordx4 v192, s[44:45] offset:1024 sc1
	v_add_f32_e32 v201, 1.0, v201
	v_add_f32_e32 v202, 1.0, v202
	v_add_f32_e32 v203, 1.0, v203
	v_rcp_f32_e32 v200, v200
	s_waitcnt lgkmcnt(7)
	v_mfma_f32_32x32x16_f16 v[96:111], a[64:67], v[168:171], v[96:111]
	ds_read_b128 v[168:171], v193 offset:10240
	v_rcp_f32_e32 v201, v201
	v_rcp_f32_e32 v202, v202
	s_waitcnt lgkmcnt(7)
	v_mfma_f32_32x32x16_f16 v[112:127], a[64:67], v[172:175], v[112:127]
	ds_read_b128 v[172:175], v193 offset:11264
	v_rcp_f32_e32 v203, v203
	v_fma_f32 v200, v200, 2.0, -1.0
	v_fma_f32 v201, v201, 2.0, -1.0
	v_fma_f32 v202, v202, 2.0, -1.0
	s_waitcnt lgkmcnt(7)
	v_mfma_f32_32x32x16_f16 v[64:79], a[68:71], v[176:179], v[64:79]
	ds_read_b128 v[176:179], v193 offset:12288
	v_fma_f32 v203, v203, 2.0, -1.0
	v_mul_f32_e32 v216, v212, v200
	v_mul_f32_e32 v217, v213, v201
	v_mul_f32_e32 v218, v214, v202
	v_mul_f32_e32 v219, v215, v203
	s_waitcnt lgkmcnt(7)
	v_mfma_f32_32x32x16_f16 v[80:95], a[68:71], v[180:183], v[80:95]
	ds_read_b128 v[180:183], v193 offset:13312
	global_load_lds_dwordx4 v192, s[44:45] offset:2048 sc1
	v_mul_f32_e32 v236, v216, v228
	v_mul_f32_e32 v237, v216, v232
	v_fmac_f32_e32 v236, v217, v229
	v_fmac_f32_e32 v237, v217, v233
	v_fmac_f32_e32 v236, v218, v230
	s_waitcnt lgkmcnt(7)
	v_mfma_f32_32x32x16_f16 v[96:111], a[68:71], v[184:187], v[96:111]
	ds_read_b128 v[184:187], v193 offset:14336
	v_fmac_f32_e32 v237, v218, v234
	v_fmac_f32_e32 v236, v219, v231
	v_fmac_f32_e32 v237, v219, v235
	v_mov_b32_e32 v238, v236
	v_mov_b32_e32 v239, v236
	s_waitcnt lgkmcnt(7)
	v_mfma_f32_32x32x16_f16 v[112:127], a[68:71], v[188:191], v[112:127]
	ds_read_b128 v[188:191], v193 offset:15360
	v_mov_b32_e32 v240, v237
	v_mov_b32_e32 v241, v237
	s_waitcnt lgkmcnt(7)
	v_mfma_f32_32x32x16_f16 v[64:79], a[72:75], v[160:163], v[64:79]
	ds_read_b128 v[160:163], v193 offset:16384
	s_nop 1
	v_permlane32_swap_b32_e32 v238, v239
	v_permlane32_swap_b32_e32 v240, v241
	v_add_f32_e32 v238, v238, v239
	v_add_f32_e32 v239, v240, v241
	ds_write_b64 v248, v[238:239] offset:512
	s_waitcnt lgkmcnt(8)
	v_mfma_f32_32x32x16_f16 v[80:95], a[72:75], v[164:167], v[80:95]
	ds_read_b128 v[164:167], v193 offset:17408
	global_load_lds_dwordx4 v192, s[44:45] offset:3072 sc1
	v_cvt_pk_f16_f32 v224, v216, v217
	v_cvt_pk_f16_f32 v225, v218, v219
	v_exp_f32_e32 v200, v48
	s_waitcnt lgkmcnt(8)
	v_mfma_f32_32x32x16_f16 v[96:111], a[72:75], v[168:171], v[96:111]
	ds_read_b128 v[168:171], v193 offset:18432
	v_exp_f32_e32 v201, v49
	v_exp_f32_e32 v202, v50
	s_waitcnt lgkmcnt(8)
	v_mfma_f32_32x32x16_f16 v[112:127], a[72:75], v[172:175], v[112:127]
	ds_read_b128 v[172:175], v193 offset:19456
	v_exp_f32_e32 v203, v51
	v_exp_f32_e32 v204, v52
	s_waitcnt lgkmcnt(8)
	v_mfma_f32_32x32x16_f16 v[64:79], a[76:79], v[176:179], v[64:79]
	ds_read_b128 v[176:179], v193 offset:20480
	v_exp_f32_e32 v205, v53
	v_exp_f32_e32 v206, v54
	s_waitcnt lgkmcnt(8)
	v_mfma_f32_32x32x16_f16 v[80:95], a[76:79], v[180:183], v[80:95]
	ds_read_b128 v[180:183], v193 offset:21504
	s_add_u32 s44, s34, 0x21000
	s_addc_u32 s45, s35, 0
	s_mov_b32 m0, s53
	s_nop 0
	global_load_lds_dwordx4 v192, s[44:45] sc1
	v_exp_f32_e32 v207, v55
	v_exp_f32_e32 v208, v56
	s_waitcnt lgkmcnt(8)
	v_mfma_f32_32x32x16_f16 v[96:111], a[76:79], v[184:187], v[96:111]
	ds_read_b128 v[184:187], v193 offset:22528
	v_exp_f32_e32 v209, v57
	v_exp_f32_e32 v210, v58
	s_waitcnt lgkmcnt(8)
	v_mfma_f32_32x32x16_f16 v[112:127], a[76:79], v[188:191], v[112:127]
	ds_read_b128 v[188:191], v193 offset:23552
	v_exp_f32_e32 v211, v59
	v_exp_f32_e32 v212, v60
	s_waitcnt lgkmcnt(8)
	v_mfma_f32_32x32x16_f16 v[64:79], a[80:83], v[160:163], v[64:79]
	ds_read_b128 v[160:163], v193 offset:24576
	v_exp_f32_e32 v213, v61
	v_exp_f32_e32 v214, v62
	s_waitcnt lgkmcnt(7)
	v_mfma_f32_32x32x16_f16 v[80:95], a[80:83], v[164:167], v[80:95]
	ds_read_b128 v[164:167], v193 offset:25600
	global_load_lds_dwordx4 v192, s[44:45] offset:1024 sc1
	v_exp_f32_e32 v215, v63
	v_add_f32_e32 v200, 1.0, v200
	v_add_f32_e32 v201, 1.0, v201
	v_add_f32_e32 v202, 1.0, v202
	s_waitcnt lgkmcnt(7)
	v_mfma_f32_32x32x16_f16 v[96:111], a[80:83], v[168:171], v[96:111]
	ds_read_b128 v[168:171], v193 offset:26624
	v_add_f32_e32 v203, 1.0, v203
	v_add_f32_e32 v204, 1.0, v204
	v_add_f32_e32 v205, 1.0, v205
	v_add_f32_e32 v206, 1.0, v206
	v_add_f32_e32 v207, 1.0, v207
	s_waitcnt lgkmcnt(7)
	v_mfma_f32_32x32x16_f16 v[112:127], a[80:83], v[172:175], v[112:127]
	ds_read_b128 v[172:175], v193 offset:27648
	v_add_f32_e32 v208, 1.0, v208
	v_add_f32_e32 v209, 1.0, v209
	v_add_f32_e32 v210, 1.0, v210
	v_add_f32_e32 v211, 1.0, v211
	v_add_f32_e32 v212, 1.0, v212
	s_waitcnt lgkmcnt(7)
	v_mfma_f32_32x32x16_f16 v[64:79], a[84:87], v[176:179], v[64:79]
	ds_read_b128 v[176:179], v193 offset:28672
	v_add_f32_e32 v213, 1.0, v213
	v_add_f32_e32 v214, 1.0, v214
	v_add_f32_e32 v215, 1.0, v215
	v_rcp_f32_e32 v200, v200
	s_waitcnt lgkmcnt(7)
	v_mfma_f32_32x32x16_f16 v[80:95], a[84:87], v[180:183], v[80:95]
	ds_read_b128 v[180:183], v193 offset:29696
	global_load_lds_dwordx4 v192, s[44:45] offset:2048 sc1
	v_rcp_f32_e32 v201, v201
	v_rcp_f32_e32 v202, v202
	s_waitcnt lgkmcnt(7)
	v_mfma_f32_32x32x16_f16 v[96:111], a[84:87], v[184:187], v[96:111]
	ds_read_b128 v[184:187], v193 offset:30720
	v_rcp_f32_e32 v203, v203
	v_rcp_f32_e32 v204, v204
	s_waitcnt lgkmcnt(7)
	v_mfma_f32_32x32x16_f16 v[112:127], a[84:87], v[188:191], v[112:127]
	ds_read_b128 v[188:191], v193 offset:31744
	v_rcp_f32_e32 v205, v205
	v_rcp_f32_e32 v206, v206
	s_waitcnt vmcnt(7)
	s_barrier
	s_waitcnt lgkmcnt(7)
	v_mfma_f32_32x32x16_f16 v[64:79], a[88:91], v[160:163], v[64:79]
	ds_read_b128 v[160:163], v193 offset:32768
	v_rcp_f32_e32 v207, v207
	v_rcp_f32_e32 v208, v208
	s_waitcnt lgkmcnt(7)
	v_mfma_f32_32x32x16_f16 v[80:95], a[88:91], v[164:167], v[80:95]
	ds_read_b128 v[164:167], v193 offset:33792
	global_load_lds_dwordx4 v192, s[44:45] offset:3072 sc1
	v_rcp_f32_e32 v209, v209
	v_rcp_f32_e32 v210, v210
	s_waitcnt lgkmcnt(7)
	v_mfma_f32_32x32x16_f16 v[96:111], a[88:91], v[168:171], v[96:111]
	ds_read_b128 v[168:171], v193 offset:34816
	v_rcp_f32_e32 v211, v211
	v_rcp_f32_e32 v212, v212
	s_waitcnt lgkmcnt(7)
	v_mfma_f32_32x32x16_f16 v[112:127], a[88:91], v[172:175], v[112:127]
	ds_read_b128 v[172:175], v193 offset:35840
	v_rcp_f32_e32 v213, v213
	v_rcp_f32_e32 v214, v214
	s_waitcnt lgkmcnt(7)
	v_mfma_f32_32x32x16_f16 v[64:79], a[92:95], v[176:179], v[64:79]
	ds_read_b128 v[176:179], v193 offset:36864
	v_rcp_f32_e32 v215, v215
	v_fmamk_f32 v208, v208, 0xc0b8aa3b, v198
	v_fmamk_f32 v209, v209, 0xc0b8aa3b, v198
	v_fmamk_f32 v210, v210, 0xc0b8aa3b, v198
	s_waitcnt lgkmcnt(7)
	v_mfma_f32_32x32x16_f16 v[80:95], a[92:95], v[180:183], v[80:95]
	ds_read_b128 v[180:183], v193 offset:37888
	s_add_u32 s44, s34, 0x28000
	s_addc_u32 s45, s35, 0
	s_mov_b32 m0, s54
	s_nop 0
	global_load_lds_dwordx4 v192, s[44:45] sc1
	v_fmamk_f32 v211, v211, 0xc0b8aa3b, v198
	v_mul_f32_e32 v204, v204, v140
	v_mul_f32_e32 v205, v205, v141
	v_mul_f32_e32 v206, v206, v142
	v_mul_f32_e32 v207, v207, v143
	s_waitcnt lgkmcnt(7)
	v_mfma_f32_32x32x16_f16 v[96:111], a[92:95], v[184:187], v[96:111]
	ds_read_b128 v[184:187], v193 offset:38912
	v_fma_f32 v140, v200, v208, v204
	v_fma_f32 v141, v201, v209, v205
	v_fma_f32 v142, v202, v210, v206
	v_fma_f32 v143, v203, v211, v207
	s_waitcnt lgkmcnt(7)
	v_mfma_f32_32x32x16_f16 v[112:127], a[92:95], v[188:191], v[112:127]
	ds_read_b128 v[188:191], v193 offset:39936
	v_exp_f32_e32 v200, v140
	v_exp_f32_e32 v201, v141
	s_waitcnt lgkmcnt(7)
	v_mfma_f32_32x32x16_f16 v[64:79], a[96:99], v[160:163], v[64:79]
	ds_read_b128 v[160:163], v193 offset:40960
	v_exp_f32_e32 v202, v142
	v_exp_f32_e32 v203, v143
	v_add_f32_e32 v200, 1.0, v200
	s_waitcnt lgkmcnt(7)
	v_mfma_f32_32x32x16_f16 v[80:95], a[96:99], v[164:167], v[80:95]
	ds_read_b128 v[164:167], v193 offset:41984
	global_load_lds_dwordx4 v192, s[44:45] offset:1024 sc1
	v_add_f32_e32 v201, 1.0, v201
	v_add_f32_e32 v202, 1.0, v202
	v_add_f32_e32 v203, 1.0, v203
	v_rcp_f32_e32 v200, v200
	s_waitcnt lgkmcnt(7)
	v_mfma_f32_32x32x16_f16 v[96:111], a[96:99], v[168:171], v[96:111]
	ds_read_b128 v[168:171], v193 offset:43008
	v_rcp_f32_e32 v201, v201
	v_rcp_f32_e32 v202, v202
	s_waitcnt lgkmcnt(7)
	v_mfma_f32_32x32x16_f16 v[112:127], a[96:99], v[172:175], v[112:127]
	ds_read_b128 v[172:175], v193 offset:44032
	v_rcp_f32_e32 v203, v203
	v_fma_f32 v200, v200, 2.0, -1.0
	v_fma_f32 v201, v201, 2.0, -1.0
	v_fma_f32 v202, v202, 2.0, -1.0
	s_waitcnt lgkmcnt(7)
	v_mfma_f32_32x32x16_f16 v[64:79], a[100:103], v[176:179], v[64:79]
	ds_read_b128 v[176:179], v193 offset:45056
	v_fma_f32 v203, v203, 2.0, -1.0
	v_mul_f32_e32 v216, v212, v200
	v_mul_f32_e32 v217, v213, v201
	v_mul_f32_e32 v218, v214, v202
	v_mul_f32_e32 v219, v215, v203
	s_waitcnt lgkmcnt(7)
	v_mfma_f32_32x32x16_f16 v[80:95], a[100:103], v[180:183], v[80:95]
	ds_read_b128 v[180:183], v193 offset:46080
	global_load_lds_dwordx4 v192, s[44:45] offset:2048 sc1
	v_mul_f32_e32 v236, v216, v228
	v_mul_f32_e32 v237, v216, v232
	v_fmac_f32_e32 v236, v217, v229
	v_fmac_f32_e32 v237, v217, v233
	v_fmac_f32_e32 v236, v218, v230
	s_waitcnt lgkmcnt(7)
	v_mfma_f32_32x32x16_f16 v[96:111], a[100:103], v[184:187], v[96:111]
	ds_read_b128 v[184:187], v193 offset:47104
	v_fmac_f32_e32 v237, v218, v234
	v_fmac_f32_e32 v236, v219, v231
	v_fmac_f32_e32 v237, v219, v235
	v_mov_b32_e32 v238, v236
	v_mov_b32_e32 v239, v236
	s_waitcnt lgkmcnt(7)
	v_mfma_f32_32x32x16_f16 v[112:127], a[100:103], v[188:191], v[112:127]
	ds_read_b128 v[188:191], v193 offset:48128
	v_mov_b32_e32 v240, v237
	v_mov_b32_e32 v241, v237
	s_waitcnt lgkmcnt(7)
	v_mfma_f32_32x32x16_f16 v[64:79], a[104:107], v[160:163], v[64:79]
	ds_read_b128 v[160:163], v193 offset:49152
	s_nop 1
	v_permlane32_swap_b32_e32 v238, v239
	v_permlane32_swap_b32_e32 v240, v241
	v_add_f32_e32 v238, v238, v239
	v_add_f32_e32 v239, v240, v241
	ds_write_b64 v248, v[238:239] offset:768
	s_waitcnt lgkmcnt(8)
	v_mfma_f32_32x32x16_f16 v[80:95], a[104:107], v[164:167], v[80:95]
	ds_read_b128 v[164:167], v193 offset:50176
	global_load_lds_dwordx4 v192, s[44:45] offset:3072 sc1
	v_cvt_pk_f16_f32 v226, v216, v217
	v_cvt_pk_f16_f32 v227, v218, v219
	s_waitcnt lgkmcnt(8)
	v_mfma_f32_32x32x16_f16 v[96:111], a[104:107], v[168:171], v[96:111]
	ds_read_b128 v[168:171], v193 offset:51200
	s_nop 1
	v_permlane32_swap_b32_e32 v224, v226
	v_permlane32_swap_b32_e32 v225, v227
	s_cmp_eq_u32 s31, 0
	s_cbranch_scc1 .LD_slow24
	global_store_dwordx4 v195, v[224:227], s[36:37] offset:2048
	s_branch .LD_join25

.LD_join25:
	s_waitcnt lgkmcnt(8)
	v_mfma_f32_32x32x16_f16 v[112:127], a[104:107], v[172:175], v[112:127]
	ds_read_b128 v[172:175], v193 offset:52224
	s_add_u32 s46, s42, 0x0
	s_addc_u32 s47, s43, 0
	global_load_dwordx4 v[0:3], v192, s[46:47] offset:0
	global_load_dwordx4 v[4:7], v192, s[46:47] offset:1024
	s_waitcnt lgkmcnt(8)
	v_mfma_f32_32x32x16_f16 v[64:79], a[108:111], v[176:179], v[64:79]
	ds_read_b128 v[176:179], v193 offset:53248
	global_load_dwordx4 v[8:11], v192, s[46:47] offset:2048
	global_load_dwordx4 v[12:15], v192, s[46:47] offset:3072
	s_add_u32 s46, s42, 0x1000
	s_addc_u32 s47, s43, 0
	s_waitcnt lgkmcnt(8)
	v_mfma_f32_32x32x16_f16 v[80:95], a[108:111], v[180:183], v[80:95]
	ds_read_b128 v[180:183], v193 offset:54272
	s_add_u32 s44, s34, 0x29000
	s_addc_u32 s45, s35, 0
	s_mov_b32 m0, s55
	s_nop 0
	global_load_lds_dwordx4 v192, s[44:45] sc1
	global_load_dwordx4 v[16:19], v192, s[46:47] offset:0
	global_load_dwordx4 v[20:23], v192, s[46:47] offset:1024
	global_load_dwordx4 v[24:27], v192, s[46:47] offset:2048
	s_waitcnt lgkmcnt(8)
	v_mfma_f32_32x32x16_f16 v[96:111], a[108:111], v[184:187], v[96:111]
	ds_read_b128 v[184:187], v193 offset:55296
	global_load_dwordx4 v[28:31], v192, s[46:47] offset:3072
	s_add_u32 s46, s42, 0x2000
	s_addc_u32 s47, s43, 0
	global_load_dwordx4 v[32:35], v192, s[46:47] offset:0
	s_waitcnt lgkmcnt(8)
	v_mfma_f32_32x32x16_f16 v[112:127], a[108:111], v[188:191], v[112:127]
	ds_read_b128 v[188:191], v193 offset:56320
	global_load_dwordx4 v[36:39], v192, s[46:47] offset:1024
	global_load_dwordx4 v[40:43], v192, s[46:47] offset:2048
	global_load_dwordx4 v[44:47], v192, s[46:47] offset:3072
	s_waitcnt lgkmcnt(8)
	v_mfma_f32_32x32x16_f16 v[64:79], a[112:115], v[160:163], v[64:79]
	ds_read_b128 v[160:163], v193 offset:57344
	s_add_u32 s46, s42, 0x3000
	s_addc_u32 s47, s43, 0
	global_load_dwordx4 v[48:51], v192, s[46:47] offset:0
	global_load_dwordx4 v[52:55], v192, s[46:47] offset:1024
	s_waitcnt lgkmcnt(7)
	v_mfma_f32_32x32x16_f16 v[80:95], a[112:115], v[164:167], v[80:95]
	ds_read_b128 v[164:167], v193 offset:58368
	global_load_lds_dwordx4 v192, s[44:45] offset:1024 sc1
	global_load_dwordx4 v[56:59], v192, s[46:47] offset:2048
	global_load_dwordx4 v[60:63], v192, s[46:47] offset:3072
	s_waitcnt lgkmcnt(7)
	v_mfma_f32_32x32x16_f16 v[96:111], a[112:115], v[168:171], v[96:111]
	ds_read_b128 v[168:171], v193 offset:59392
	s_waitcnt vmcnt(18)
	s_barrier
	v_mov_b32_e32 v199, 1
	s_cmp_eq_u32 s31, 0
	s_cbranch_scc1 .LD_slow26
	global_store_dword v197, v199, s[40:41]
	s_branch .LD_join27

.LD_join27:
	ds_read_b64 v[200:201], v249 offset:0
	ds_read_b64 v[202:203], v249 offset:2048
	ds_read_b64 v[204:205], v249 offset:4096
	ds_read_b64 v[206:207], v249 offset:6144
	s_waitcnt lgkmcnt(11)
	v_mfma_f32_32x32x16_f16 v[112:127], a[112:115], v[172:175], v[112:127]
	ds_read_b128 v[172:175], v193 offset:60416
	s_waitcnt lgkmcnt(11)
	v_mfma_f32_32x32x16_f16 v[64:79], a[116:119], v[176:179], v[64:79]
	ds_read_b128 v[176:179], v193 offset:61440
	s_waitcnt lgkmcnt(11)
	v_mfma_f32_32x32x16_f16 v[80:95], a[116:119], v[180:183], v[80:95]
	ds_read_b128 v[180:183], v193 offset:62464
	global_load_lds_dwordx4 v192, s[44:45] offset:2048 sc1
	s_waitcnt lgkmcnt(3)
	v_add_f32_e32 v200, v200, v202
	v_add_f32_e32 v201, v201, v203
	v_add_f32_e32 v200, v200, v204
	v_add_f32_e32 v201, v201, v205
	v_add_f32_e32 v200, v200, v206
	v_add_f32_e32 v201, v201, v207
	global_store_dwordx2 v250, v[200:201], s[72:73]
	v_mfma_f32_32x32x16_f16 v[96:111], a[116:119], v[184:187], v[96:111]
	ds_read_b128 v[184:187], v193 offset:63488
	v_mfma_f32_32x32x16_f16 v[112:127], a[116:119], v[188:191], v[112:127]
	ds_read_b128 v[188:191], v193 offset:64512
	s_barrier
	v_mfma_f32_32x32x16_f16 v[64:79], a[120:123], v[160:163], v[64:79]
	ds_read_b128 v[160:163], v192 offset:0
	v_mfma_f32_32x32x16_f16 v[80:95], a[120:123], v[164:167], v[80:95]
	ds_read_b128 v[164:167], v192 offset:1024
	global_load_lds_dwordx4 v192, s[44:45] offset:3072 sc1
	v_mfma_f32_32x32x16_f16 v[96:111], a[120:123], v[168:171], v[96:111]
	ds_read_b128 v[168:171], v192 offset:2048
	s_waitcnt lgkmcnt(7)
	v_mfma_f32_32x32x16_f16 v[112:127], a[120:123], v[172:175], v[112:127]
	ds_read_b128 v[172:175], v192 offset:3072
	s_waitcnt lgkmcnt(7)
	v_mfma_f32_32x32x16_f16 v[64:79], a[124:127], v[176:179], v[64:79]
	ds_read_b128 v[176:179], v192 offset:4096
	s_waitcnt lgkmcnt(7)
	v_mfma_f32_32x32x16_f16 v[80:95], a[124:127], v[180:183], v[80:95]
	ds_read_b128 v[180:183], v192 offset:5120
	s_add_u32 s44, s34, 0x30000
	s_addc_u32 s45, s35, 0
	s_mov_b32 m0, s56
	s_nop 0
	global_load_lds_dwordx4 v192, s[44:45] sc1
	s_waitcnt lgkmcnt(7)
	v_mfma_f32_32x32x16_f16 v[96:111], a[124:127], v[184:187], v[96:111]
	ds_read_b128 v[184:187], v192 offset:6144
	s_waitcnt lgkmcnt(7)
	v_mfma_f32_32x32x16_f16 v[112:127], a[124:127], v[188:191], v[112:127]
	ds_read_b128 v[188:191], v192 offset:7168
	s_waitcnt lgkmcnt(7)
	v_mfma_f32_32x32x16_f16 v[64:79], a[128:131], v[160:163], v[64:79]
	ds_read_b128 v[160:163], v192 offset:8192
	s_waitcnt lgkmcnt(7)
	v_mfma_f32_32x32x16_f16 v[80:95], a[128:131], v[164:167], v[80:95]
	ds_read_b128 v[164:167], v192 offset:9216
	global_load_lds_dwordx4 v192, s[44:45] offset:1024 sc1
	s_waitcnt lgkmcnt(7)
	v_mfma_f32_32x32x16_f16 v[96:111], a[128:131], v[168:171], v[96:111]
	ds_read_b128 v[168:171], v192 offset:10240
	s_waitcnt lgkmcnt(7)
	v_mfma_f32_32x32x16_f16 v[112:127], a[128:131], v[172:175], v[112:127]
	ds_read_b128 v[172:175], v192 offset:11264
	s_waitcnt lgkmcnt(7)
	v_mfma_f32_32x32x16_f16 v[64:79], a[132:135], v[176:179], v[64:79]
	ds_read_b128 v[176:179], v192 offset:12288
	s_waitcnt lgkmcnt(7)
	v_mfma_f32_32x32x16_f16 v[80:95], a[132:135], v[180:183], v[80:95]
	ds_read_b128 v[180:183], v192 offset:13312
	global_load_lds_dwordx4 v192, s[44:45] offset:2048 sc1
	s_waitcnt lgkmcnt(7)
	v_mfma_f32_32x32x16_f16 v[96:111], a[132:135], v[184:187], v[96:111]
	ds_read_b128 v[184:187], v192 offset:14336
	s_waitcnt lgkmcnt(7)
	v_mfma_f32_32x32x16_f16 v[112:127], a[132:135], v[188:191], v[112:127]
	ds_read_b128 v[188:191], v192 offset:15360
	s_waitcnt lgkmcnt(7)
	v_mfma_f32_32x32x16_f16 v[64:79], a[136:139], v[160:163], v[64:79]
	ds_read_b128 v[160:163], v192 offset:16384
	s_waitcnt lgkmcnt(7)
	v_mfma_f32_32x32x16_f16 v[80:95], a[136:139], v[164:167], v[80:95]
	ds_read_b128 v[164:167], v192 offset:17408
	global_load_lds_dwordx4 v192, s[44:45] offset:3072 sc1
	s_waitcnt lgkmcnt(7)
	v_mfma_f32_32x32x16_f16 v[96:111], a[136:139], v[168:171], v[96:111]
	ds_read_b128 v[168:171], v192 offset:18432
	s_waitcnt lgkmcnt(7)
	v_mfma_f32_32x32x16_f16 v[112:127], a[136:139], v[172:175], v[112:127]
	ds_read_b128 v[172:175], v192 offset:19456
	s_waitcnt lgkmcnt(7)
	v_mfma_f32_32x32x16_f16 v[64:79], a[140:143], v[176:179], v[64:79]
	ds_read_b128 v[176:179], v192 offset:20480
	s_waitcnt lgkmcnt(7)
	v_mfma_f32_32x32x16_f16 v[80:95], a[140:143], v[180:183], v[80:95]
	ds_read_b128 v[180:183], v192 offset:21504
	s_add_u32 s44, s34, 0x31000
	s_addc_u32 s45, s35, 0
	s_mov_b32 m0, s57
	s_nop 0
	global_load_lds_dwordx4 v192, s[44:45] sc1
	s_waitcnt lgkmcnt(7)
	v_mfma_f32_32x32x16_f16 v[96:111], a[140:143], v[184:187], v[96:111]
	ds_read_b128 v[184:187], v192 offset:22528
	s_waitcnt lgkmcnt(7)
	v_mfma_f32_32x32x16_f16 v[112:127], a[140:143], v[188:191], v[112:127]
	ds_read_b128 v[188:191], v192 offset:23552
	s_waitcnt lgkmcnt(7)
	v_mfma_f32_32x32x16_f16 v[64:79], a[144:147], v[160:163], v[64:79]
	ds_read_b128 v[160:163], v192 offset:24576
	s_waitcnt lgkmcnt(7)
	v_mfma_f32_32x32x16_f16 v[80:95], a[144:147], v[164:167], v[80:95]
	ds_read_b128 v[164:167], v192 offset:25600
	global_load_lds_dwordx4 v192, s[44:45] offset:1024 sc1
	s_waitcnt lgkmcnt(7)
	v_mfma_f32_32x32x16_f16 v[96:111], a[144:147], v[168:171], v[96:111]
	ds_read_b128 v[168:171], v192 offset:26624
	s_waitcnt lgkmcnt(7)
	v_mfma_f32_32x32x16_f16 v[112:127], a[144:147], v[172:175], v[112:127]
	ds_read_b128 v[172:175], v192 offset:27648
	s_waitcnt lgkmcnt(7)
	v_mfma_f32_32x32x16_f16 v[64:79], a[148:151], v[176:179], v[64:79]
	ds_read_b128 v[176:179], v192 offset:28672
	s_waitcnt lgkmcnt(7)
	v_mfma_f32_32x32x16_f16 v[80:95], a[148:151], v[180:183], v[80:95]
	ds_read_b128 v[180:183], v192 offset:29696
	global_load_lds_dwordx4 v192, s[44:45] offset:2048 sc1
	s_waitcnt lgkmcnt(7)
	v_mfma_f32_32x32x16_f16 v[96:111], a[148:151], v[184:187], v[96:111]
	ds_read_b128 v[184:187], v192 offset:30720
	s_waitcnt lgkmcnt(7)
	v_mfma_f32_32x32x16_f16 v[112:127], a[148:151], v[188:191], v[112:127]
	ds_read_b128 v[188:191], v192 offset:31744
	s_waitcnt vmcnt(7)
	s_barrier
	s_waitcnt lgkmcnt(7)
	v_mfma_f32_32x32x16_f16 v[64:79], a[152:155], v[160:163], v[64:79]
	ds_read_b128 v[160:163], v192 offset:32768
	s_waitcnt lgkmcnt(7)
	v_mfma_f32_32x32x16_f16 v[80:95], a[152:155], v[164:167], v[80:95]
	ds_read_b128 v[164:167], v192 offset:33792
	global_load_lds_dwordx4 v192, s[44:45] offset:3072 sc1
	s_waitcnt lgkmcnt(7)
	v_mfma_f32_32x32x16_f16 v[96:111], a[152:155], v[168:171], v[96:111]
	ds_read_b128 v[168:171], v192 offset:34816
	s_waitcnt lgkmcnt(7)
	v_mfma_f32_32x32x16_f16 v[112:127], a[152:155], v[172:175], v[112:127]
	ds_read_b128 v[172:175], v192 offset:35840
	s_waitcnt lgkmcnt(7)
	v_mfma_f32_32x32x16_f16 v[64:79], a[156:159], v[176:179], v[64:79]
	ds_read_b128 v[176:179], v192 offset:36864
	s_waitcnt lgkmcnt(7)
	v_mfma_f32_32x32x16_f16 v[80:95], a[156:159], v[180:183], v[80:95]
	ds_read_b128 v[180:183], v192 offset:37888
	s_add_u32 s44, s34, 0x38000
	s_addc_u32 s45, s35, 0
	s_mov_b32 m0, s58
	s_nop 0
	global_load_lds_dwordx4 v192, s[44:45] sc1
	s_waitcnt lgkmcnt(7)
	v_mfma_f32_32x32x16_f16 v[96:111], a[156:159], v[184:187], v[96:111]
	ds_read_b128 v[184:187], v192 offset:38912
	s_waitcnt lgkmcnt(7)
	v_mfma_f32_32x32x16_f16 v[112:127], a[156:159], v[188:191], v[112:127]
	ds_read_b128 v[188:191], v192 offset:39936
	s_lshl_b32 s64, s33, 3
	s_add_u32 s64, s64, s29
	s_lshl_b32 s64, s64, 7
	s_add_u32 s38, s8, s64
	s_addc_u32 s39, s9, 0
	global_load_dword v251, v196, s[38:39] sc1
	s_waitcnt lgkmcnt(7)
	v_mfma_f32_32x32x16_f16 v[64:79], a[160:163], v[160:163], v[64:79]
	ds_read_b128 v[160:163], v192 offset:40960
	s_waitcnt lgkmcnt(7)
	v_mfma_f32_32x32x16_f16 v[80:95], a[160:163], v[164:167], v[80:95]
	ds_read_b128 v[164:167], v192 offset:41984
	global_load_lds_dwordx4 v192, s[44:45] offset:1024 sc1
	s_waitcnt lgkmcnt(7)
	v_mfma_f32_32x32x16_f16 v[96:111], a[160:163], v[168:171], v[96:111]
	ds_read_b128 v[168:171], v192 offset:43008
	s_waitcnt lgkmcnt(7)
	v_mfma_f32_32x32x16_f16 v[112:127], a[160:163], v[172:175], v[112:127]
	ds_read_b128 v[172:175], v192 offset:44032
	s_waitcnt lgkmcnt(7)
	v_mfma_f32_32x32x16_f16 v[64:79], a[164:167], v[176:179], v[64:79]
	ds_read_b128 v[176:179], v192 offset:45056
	s_waitcnt lgkmcnt(7)
	v_mfma_f32_32x32x16_f16 v[80:95], a[164:167], v[180:183], v[80:95]
	ds_read_b128 v[180:183], v192 offset:46080
	global_load_lds_dwordx4 v192, s[44:45] offset:2048 sc1
	s_waitcnt lgkmcnt(7)
	v_mfma_f32_32x32x16_f16 v[96:111], a[164:167], v[184:187], v[96:111]
	ds_read_b128 v[184:187], v192 offset:47104
	s_waitcnt lgkmcnt(7)
	v_mfma_f32_32x32x16_f16 v[112:127], a[164:167], v[188:191], v[112:127]
	ds_read_b128 v[188:191], v192 offset:48128
	s_waitcnt lgkmcnt(7)
	v_mfma_f32_32x32x16_f16 v[64:79], a[168:171], v[160:163], v[64:79]
	ds_read_b128 v[160:163], v192 offset:49152
	s_waitcnt lgkmcnt(7)
	v_mfma_f32_32x32x16_f16 v[80:95], a[168:171], v[164:167], v[80:95]
	ds_read_b128 v[164:167], v192 offset:50176
	global_load_lds_dwordx4 v192, s[44:45] offset:3072 sc1
	s_waitcnt lgkmcnt(7)
	v_mfma_f32_32x32x16_f16 v[96:111], a[168:171], v[168:171], v[96:111]
	ds_read_b128 v[168:171], v192 offset:51200
	s_waitcnt lgkmcnt(7)
	v_mfma_f32_32x32x16_f16 v[112:127], a[168:171], v[172:175], v[112:127]
	ds_read_b128 v[172:175], v192 offset:52224
	s_waitcnt lgkmcnt(7)
	v_mfma_f32_32x32x16_f16 v[64:79], a[172:175], v[176:179], v[64:79]
	ds_read_b128 v[176:179], v192 offset:53248
	s_waitcnt lgkmcnt(7)
	v_mfma_f32_32x32x16_f16 v[80:95], a[172:175], v[180:183], v[80:95]
	ds_read_b128 v[180:183], v192 offset:54272
	s_add_u32 s44, s34, 0x39000
	s_addc_u32 s45, s35, 0
	s_mov_b32 m0, s59
	s_nop 0
	global_load_lds_dwordx4 v192, s[44:45] sc1
	s_waitcnt lgkmcnt(7)
	v_mfma_f32_32x32x16_f16 v[96:111], a[172:175], v[184:187], v[96:111]
	ds_read_b128 v[184:187], v192 offset:55296
	s_waitcnt lgkmcnt(7)
	v_mfma_f32_32x32x16_f16 v[112:127], a[172:175], v[188:191], v[112:127]
	ds_read_b128 v[188:191], v192 offset:56320
	s_waitcnt lgkmcnt(7)
	v_mfma_f32_32x32x16_f16 v[64:79], a[176:179], v[160:163], v[64:79]
	ds_read_b128 v[160:163], v192 offset:57344
	s_waitcnt lgkmcnt(7)
	v_mfma_f32_32x32x16_f16 v[80:95], a[176:179], v[164:167], v[80:95]
	ds_read_b128 v[164:167], v192 offset:58368
	global_load_lds_dwordx4 v192, s[44:45] offset:1024 sc1
	s_waitcnt lgkmcnt(7)
	v_mfma_f32_32x32x16_f16 v[96:111], a[176:179], v[168:171], v[96:111]
	ds_read_b128 v[168:171], v192 offset:59392
	s_waitcnt lgkmcnt(7)
	v_mfma_f32_32x32x16_f16 v[112:127], a[176:179], v[172:175], v[112:127]
	ds_read_b128 v[172:175], v192 offset:60416
	s_waitcnt lgkmcnt(7)
	v_mfma_f32_32x32x16_f16 v[64:79], a[180:183], v[176:179], v[64:79]
	ds_read_b128 v[176:179], v192 offset:61440
	s_waitcnt lgkmcnt(7)
	v_mfma_f32_32x32x16_f16 v[80:95], a[180:183], v[180:183], v[80:95]
	ds_read_b128 v[180:183], v192 offset:62464
	global_load_lds_dwordx4 v192, s[44:45] offset:2048 sc1
	s_waitcnt lgkmcnt(7)
	v_mfma_f32_32x32x16_f16 v[96:111], a[180:183], v[184:187], v[96:111]
	ds_read_b128 v[184:187], v192 offset:63488
	s_waitcnt lgkmcnt(7)
	v_mfma_f32_32x32x16_f16 v[112:127], a[180:183], v[188:191], v[112:127]
	ds_read_b128 v[188:191], v192 offset:64512
	s_waitcnt vmcnt(8)
	s_barrier
	s_waitcnt lgkmcnt(7)
	v_mfma_f32_32x32x16_f16 v[64:79], a[184:187], v[160:163], v[64:79]
	ds_read_b128 v[160:163], v193 offset:0
	s_waitcnt lgkmcnt(7)
	v_mfma_f32_32x32x16_f16 v[80:95], a[184:187], v[164:167], v[80:95]
	ds_read_b128 v[164:167], v193 offset:1024
	global_load_lds_dwordx4 v192, s[44:45] offset:3072 sc1
	s_waitcnt lgkmcnt(7)
	v_mfma_f32_32x32x16_f16 v[96:111], a[184:187], v[168:171], v[96:111]
	ds_read_b128 v[168:171], v193 offset:2048
	s_waitcnt lgkmcnt(7)
	v_mfma_f32_32x32x16_f16 v[112:127], a[184:187], v[172:175], v[112:127]
	ds_read_b128 v[172:175], v193 offset:3072
	s_waitcnt lgkmcnt(7)
	v_mfma_f32_32x32x16_f16 v[64:79], a[188:191], v[176:179], v[64:79]
	ds_read_b128 v[176:179], v193 offset:4096
	s_waitcnt lgkmcnt(7)
	v_mfma_f32_32x32x16_f16 v[80:95], a[188:191], v[180:183], v[80:95]
	ds_read_b128 v[180:183], v193 offset:5120
	s_waitcnt vmcnt(7)
	v_cmp_gt_u32_e32 vcc, 1, v251
	s_cbranch_vccz .LD_tok28

.LD_end11:
	s_nop 15
	s_nop 3
	s_sub_u32 s71, s33, 1
	s_and_b32 s64, s71, 1
	s_lshl_b32 s64, s64, 22
	s_add_u32 s64, s64, s50
	s_add_u32 s64, s64, 0x40000
	s_add_u32 s36, s6, s64
	s_addc_u32 s37, s7, 0
	s_lshl_b32 s64, s71, 3
	s_add_u32 s64, s64, s29
	s_lshl_b32 s64, s64, 5
	s_add_u32 s64, s64, s30
	s_lshl_b32 s64, s64, 2
	s_add_u32 s40, s8, s64
	s_addc_u32 s41, s9, 0
	s_lshl_b32 s64, s71, 19
	s_add_u32 s64, s64, 0x400
	s_add_u32 s72, s62, s64
	s_addc_u32 s73, s63, 0
	v_exp_f32_e32 v200, v64
	v_exp_f32_e32 v201, v65
	v_exp_f32_e32 v202, v66
	v_exp_f32_e32 v203, v67
	v_exp_f32_e32 v204, v68
	v_exp_f32_e32 v205, v69
	v_exp_f32_e32 v206, v70
	v_exp_f32_e32 v207, v71
	v_exp_f32_e32 v208, v72
	v_exp_f32_e32 v209, v73
	v_exp_f32_e32 v210, v74
	v_exp_f32_e32 v211, v75
	v_exp_f32_e32 v212, v76
	v_exp_f32_e32 v213, v77
	v_exp_f32_e32 v214, v78
	v_exp_f32_e32 v215, v79
	v_add_f32_e32 v200, 1.0, v200
	v_add_f32_e32 v201, 1.0, v201
	v_add_f32_e32 v202, 1.0, v202
	v_add_f32_e32 v203, 1.0, v203
	v_add_f32_e32 v204, 1.0, v204
	v_add_f32_e32 v205, 1.0, v205
	v_add_f32_e32 v206, 1.0, v206
	v_add_f32_e32 v207, 1.0, v207
	v_add_f32_e32 v208, 1.0, v208
	v_add_f32_e32 v209, 1.0, v209
	v_add_f32_e32 v210, 1.0, v210
	v_add_f32_e32 v211, 1.0, v211
	v_add_f32_e32 v212, 1.0, v212
	v_add_f32_e32 v213, 1.0, v213
	v_add_f32_e32 v214, 1.0, v214
	v_add_f32_e32 v215, 1.0, v215
	v_rcp_f32_e32 v200, v200
	v_rcp_f32_e32 v201, v201
	v_rcp_f32_e32 v202, v202
	v_rcp_f32_e32 v203, v203
	v_rcp_f32_e32 v204, v204
	v_rcp_f32_e32 v205, v205
	v_rcp_f32_e32 v206, v206
	v_rcp_f32_e32 v207, v207
	v_rcp_f32_e32 v208, v208
	v_rcp_f32_e32 v209, v209
	v_rcp_f32_e32 v210, v210
	v_rcp_f32_e32 v211, v211
	v_rcp_f32_e32 v212, v212
	v_rcp_f32_e32 v213, v213
	v_rcp_f32_e32 v214, v214
	v_rcp_f32_e32 v215, v215
	v_fmamk_f32 v208, v208, 0xc0b8aa3b, v198
	v_fmamk_f32 v209, v209, 0xc0b8aa3b, v198
	v_fmamk_f32 v210, v210, 0xc0b8aa3b, v198
	v_fmamk_f32 v211, v211, 0xc0b8aa3b, v198
	v_mul_f32_e32 v204, v204, v144
	v_mul_f32_e32 v205, v205, v145
	v_mul_f32_e32 v206, v206, v146
	v_mul_f32_e32 v207, v207, v147
	v_fma_f32 v144, v200, v208, v204
	v_fma_f32 v145, v201, v209, v205
	v_fma_f32 v146, v202, v210, v206
	v_fma_f32 v147, v203, v211, v207
	v_exp_f32_e32 v200, v144
	v_exp_f32_e32 v201, v145
	v_exp_f32_e32 v202, v146
	v_exp_f32_e32 v203, v147
	v_add_f32_e32 v200, 1.0, v200
	v_add_f32_e32 v201, 1.0, v201
	v_add_f32_e32 v202, 1.0, v202
	v_add_f32_e32 v203, 1.0, v203
	v_rcp_f32_e32 v200, v200
	v_rcp_f32_e32 v201, v201
	v_rcp_f32_e32 v202, v202
	v_rcp_f32_e32 v203, v203
	v_fma_f32 v200, v200, 2.0, -1.0
	v_fma_f32 v201, v201, 2.0, -1.0
	v_fma_f32 v202, v202, 2.0, -1.0
	v_fma_f32 v203, v203, 2.0, -1.0
	v_mul_f32_e32 v216, v212, v200
	v_mul_f32_e32 v217, v213, v201
	v_mul_f32_e32 v218, v214, v202
	v_mul_f32_e32 v219, v215, v203
	v_mul_f32_e32 v236, v216, v228
	v_mul_f32_e32 v237, v216, v232
	v_fmac_f32_e32 v236, v217, v229
	v_fmac_f32_e32 v237, v217, v233
	v_fmac_f32_e32 v236, v218, v230
	v_fmac_f32_e32 v237, v218, v234
	v_fmac_f32_e32 v236, v219, v231
	v_fmac_f32_e32 v237, v219, v235
	v_mov_b32_e32 v238, v236
	v_mov_b32_e32 v239, v236
	v_mov_b32_e32 v240, v237
	v_mov_b32_e32 v241, v237
	s_nop 1
	v_permlane32_swap_b32_e32 v238, v239
	v_permlane32_swap_b32_e32 v240, v241
	v_add_f32_e32 v238, v238, v239
	v_add_f32_e32 v239, v240, v241
	ds_write_b64 v248, v[238:239] offset:1024
	v_cvt_pk_f16_f32 v220, v216, v217
	v_cvt_pk_f16_f32 v221, v218, v219
	v_exp_f32_e32 v200, v80
	v_exp_f32_e32 v201, v81
	v_exp_f32_e32 v202, v82
	v_exp_f32_e32 v203, v83
	v_exp_f32_e32 v204, v84
	v_exp_f32_e32 v205, v85
	v_exp_f32_e32 v206, v86
	v_exp_f32_e32 v207, v87
	v_exp_f32_e32 v208, v88
	v_exp_f32_e32 v209, v89
	v_exp_f32_e32 v210, v90
	v_exp_f32_e32 v211, v91
	v_exp_f32_e32 v212, v92
	v_exp_f32_e32 v213, v93
	v_exp_f32_e32 v214, v94
	v_exp_f32_e32 v215, v95
	v_add_f32_e32 v200, 1.0, v200
	v_add_f32_e32 v201, 1.0, v201
	v_add_f32_e32 v202, 1.0, v202
	v_add_f32_e32 v203, 1.0, v203
	v_add_f32_e32 v204, 1.0, v204
	v_add_f32_e32 v205, 1.0, v205
	v_add_f32_e32 v206, 1.0, v206
	v_add_f32_e32 v207, 1.0, v207
	v_add_f32_e32 v208, 1.0, v208
	v_add_f32_e32 v209, 1.0, v209
	v_add_f32_e32 v210, 1.0, v210
	v_add_f32_e32 v211, 1.0, v211
	v_add_f32_e32 v212, 1.0, v212
	v_add_f32_e32 v213, 1.0, v213
	v_add_f32_e32 v214, 1.0, v214
	v_add_f32_e32 v215, 1.0, v215
	v_rcp_f32_e32 v200, v200
	v_rcp_f32_e32 v201, v201
	v_rcp_f32_e32 v202, v202
	v_rcp_f32_e32 v203, v203
	v_rcp_f32_e32 v204, v204
	v_rcp_f32_e32 v205, v205
	v_rcp_f32_e32 v206, v206
	v_rcp_f32_e32 v207, v207
	v_rcp_f32_e32 v208, v208
	v_rcp_f32_e32 v209, v209
	v_rcp_f32_e32 v210, v210
	v_rcp_f32_e32 v211, v211
	v_rcp_f32_e32 v212, v212
	v_rcp_f32_e32 v213, v213
	v_rcp_f32_e32 v214, v214
	v_rcp_f32_e32 v215, v215
	v_fmamk_f32 v208, v208, 0xc0b8aa3b, v198
	v_fmamk_f32 v209, v209, 0xc0b8aa3b, v198
	v_fmamk_f32 v210, v210, 0xc0b8aa3b, v198
	v_fmamk_f32 v211, v211, 0xc0b8aa3b, v198
	v_mul_f32_e32 v204, v204, v148
	v_mul_f32_e32 v205, v205, v149
	v_mul_f32_e32 v206, v206, v150
	v_mul_f32_e32 v207, v207, v151
	v_fma_f32 v148, v200, v208, v204
	v_fma_f32 v149, v201, v209, v205
	v_fma_f32 v150, v202, v210, v206
	v_fma_f32 v151, v203, v211, v207
	v_exp_f32_e32 v200, v148
	v_exp_f32_e32 v201, v149
	v_exp_f32_e32 v202, v150
	v_exp_f32_e32 v203, v151
	v_add_f32_e32 v200, 1.0, v200
	v_add_f32_e32 v201, 1.0, v201
	v_add_f32_e32 v202, 1.0, v202
	v_add_f32_e32 v203, 1.0, v203
	v_rcp_f32_e32 v200, v200
	v_rcp_f32_e32 v201, v201
	v_rcp_f32_e32 v202, v202
	v_rcp_f32_e32 v203, v203
	v_fma_f32 v200, v200, 2.0, -1.0
	v_fma_f32 v201, v201, 2.0, -1.0
	v_fma_f32 v202, v202, 2.0, -1.0
	v_fma_f32 v203, v203, 2.0, -1.0
	v_mul_f32_e32 v216, v212, v200
	v_mul_f32_e32 v217, v213, v201
	v_mul_f32_e32 v218, v214, v202
	v_mul_f32_e32 v219, v215, v203
	v_mul_f32_e32 v236, v216, v228
	v_mul_f32_e32 v237, v216, v232
	v_fmac_f32_e32 v236, v217, v229
	v_fmac_f32_e32 v237, v217, v233
	v_fmac_f32_e32 v236, v218, v230
	v_fmac_f32_e32 v237, v218, v234
	v_fmac_f32_e32 v236, v219, v231
	v_fmac_f32_e32 v237, v219, v235
	v_mov_b32_e32 v238, v236
	v_mov_b32_e32 v239, v236
	v_mov_b32_e32 v240, v237
	v_mov_b32_e32 v241, v237
	s_nop 1
	v_permlane32_swap_b32_e32 v238, v239
	v_permlane32_swap_b32_e32 v240, v241
	v_add_f32_e32 v238, v238, v239
	v_add_f32_e32 v239, v240, v241
	ds_write_b64 v248, v[238:239] offset:1280
	v_cvt_pk_f16_f32 v222, v216, v217
	v_cvt_pk_f16_f32 v223, v218, v219
	s_nop 1
	v_permlane32_swap_b32_e32 v220, v222
	v_permlane32_swap_b32_e32 v221, v223
	s_cmp_eq_u32 s31, 0
	s_cbranch_scc1 .LD_slow30
	global_store_dwordx4 v195, v[220:223], s[36:37] offset:0
	s_branch .LD_join31

.LD_join31:
	v_exp_f32_e32 v200, v96
	v_exp_f32_e32 v201, v97
	v_exp_f32_e32 v202, v98
	v_exp_f32_e32 v203, v99
	v_exp_f32_e32 v204, v100
	v_exp_f32_e32 v205, v101
	v_exp_f32_e32 v206, v102
	v_exp_f32_e32 v207, v103
	v_exp_f32_e32 v208, v104
	v_exp_f32_e32 v209, v105
	v_exp_f32_e32 v210, v106
	v_exp_f32_e32 v211, v107
	v_exp_f32_e32 v212, v108
	v_exp_f32_e32 v213, v109
	v_exp_f32_e32 v214, v110
	v_exp_f32_e32 v215, v111
	v_add_f32_e32 v200, 1.0, v200
	v_add_f32_e32 v201, 1.0, v201
	v_add_f32_e32 v202, 1.0, v202
	v_add_f32_e32 v203, 1.0, v203
	v_add_f32_e32 v204, 1.0, v204
	v_add_f32_e32 v205, 1.0, v205
	v_add_f32_e32 v206, 1.0, v206
	v_add_f32_e32 v207, 1.0, v207
	v_add_f32_e32 v208, 1.0, v208
	v_add_f32_e32 v209, 1.0, v209
	v_add_f32_e32 v210, 1.0, v210
	v_add_f32_e32 v211, 1.0, v211
	v_add_f32_e32 v212, 1.0, v212
	v_add_f32_e32 v213, 1.0, v213
	v_add_f32_e32 v214, 1.0, v214
	v_add_f32_e32 v215, 1.0, v215
	v_rcp_f32_e32 v200, v200
	v_rcp_f32_e32 v201, v201
	v_rcp_f32_e32 v202, v202
	v_rcp_f32_e32 v203, v203
	v_rcp_f32_e32 v204, v204
	v_rcp_f32_e32 v205, v205
	v_rcp_f32_e32 v206, v206
	v_rcp_f32_e32 v207, v207
	v_rcp_f32_e32 v208, v208
	v_rcp_f32_e32 v209, v209
	v_rcp_f32_e32 v210, v210
	v_rcp_f32_e32 v211, v211
	v_rcp_f32_e32 v212, v212
	v_rcp_f32_e32 v213, v213
	v_rcp_f32_e32 v214, v214
	v_rcp_f32_e32 v215, v215
	v_fmamk_f32 v208, v208, 0xc0b8aa3b, v198
	v_fmamk_f32 v209, v209, 0xc0b8aa3b, v198
	v_fmamk_f32 v210, v210, 0xc0b8aa3b, v198
	v_fmamk_f32 v211, v211, 0xc0b8aa3b, v198
	v_mul_f32_e32 v204, v204, v152
	v_mul_f32_e32 v205, v205, v153
	v_mul_f32_e32 v206, v206, v154
	v_mul_f32_e32 v207, v207, v155
	v_fma_f32 v152, v200, v208, v204
	v_fma_f32 v153, v201, v209, v205
	v_fma_f32 v154, v202, v210, v206
	v_fma_f32 v155, v203, v211, v207
	v_exp_f32_e32 v200, v152
	v_exp_f32_e32 v201, v153
	v_exp_f32_e32 v202, v154
	v_exp_f32_e32 v203, v155
	v_add_f32_e32 v200, 1.0, v200
	v_add_f32_e32 v201, 1.0, v201
	v_add_f32_e32 v202, 1.0, v202
	v_add_f32_e32 v203, 1.0, v203
	v_rcp_f32_e32 v200, v200
	v_rcp_f32_e32 v201, v201
	v_rcp_f32_e32 v202, v202
	v_rcp_f32_e32 v203, v203
	v_fma_f32 v200, v200, 2.0, -1.0
	v_fma_f32 v201, v201, 2.0, -1.0
	v_fma_f32 v202, v202, 2.0, -1.0
	v_fma_f32 v203, v203, 2.0, -1.0
	v_mul_f32_e32 v216, v212, v200
	v_mul_f32_e32 v217, v213, v201
	v_mul_f32_e32 v218, v214, v202
	v_mul_f32_e32 v219, v215, v203
	v_mul_f32_e32 v236, v216, v228
	v_mul_f32_e32 v237, v216, v232
	v_fmac_f32_e32 v236, v217, v229
	v_fmac_f32_e32 v237, v217, v233
	v_fmac_f32_e32 v236, v218, v230
	v_fmac_f32_e32 v237, v218, v234
	v_fmac_f32_e32 v236, v219, v231
	v_fmac_f32_e32 v237, v219, v235
	v_mov_b32_e32 v238, v236
	v_mov_b32_e32 v239, v236
	v_mov_b32_e32 v240, v237
	v_mov_b32_e32 v241, v237
	s_nop 1
	v_permlane32_swap_b32_e32 v238, v239
	v_permlane32_swap_b32_e32 v240, v241
	v_add_f32_e32 v238, v238, v239
	v_add_f32_e32 v239, v240, v241
	ds_write_b64 v248, v[238:239] offset:1536
	v_cvt_pk_f16_f32 v224, v216, v217
	v_cvt_pk_f16_f32 v225, v218, v219
	v_exp_f32_e32 v200, v112
	v_exp_f32_e32 v201, v113
	v_exp_f32_e32 v202, v114
	v_exp_f32_e32 v203, v115
	v_exp_f32_e32 v204, v116
	v_exp_f32_e32 v205, v117
	v_exp_f32_e32 v206, v118
	v_exp_f32_e32 v207, v119
	v_exp_f32_e32 v208, v120
	v_exp_f32_e32 v209, v121
	v_exp_f32_e32 v210, v122
	v_exp_f32_e32 v211, v123
	v_exp_f32_e32 v212, v124
	v_exp_f32_e32 v213, v125
	v_exp_f32_e32 v214, v126
	v_exp_f32_e32 v215, v127
	v_add_f32_e32 v200, 1.0, v200
	v_add_f32_e32 v201, 1.0, v201
	v_add_f32_e32 v202, 1.0, v202
	v_add_f32_e32 v203, 1.0, v203
	v_add_f32_e32 v204, 1.0, v204
	v_add_f32_e32 v205, 1.0, v205
	v_add_f32_e32 v206, 1.0, v206
	v_add_f32_e32 v207, 1.0, v207
	v_add_f32_e32 v208, 1.0, v208
	v_add_f32_e32 v209, 1.0, v209
	v_add_f32_e32 v210, 1.0, v210
	v_add_f32_e32 v211, 1.0, v211
	v_add_f32_e32 v212, 1.0, v212
	v_add_f32_e32 v213, 1.0, v213
	v_add_f32_e32 v214, 1.0, v214
	v_add_f32_e32 v215, 1.0, v215
	v_rcp_f32_e32 v200, v200
	v_rcp_f32_e32 v201, v201
	v_rcp_f32_e32 v202, v202
	v_rcp_f32_e32 v203, v203
	v_rcp_f32_e32 v204, v204
	v_rcp_f32_e32 v205, v205
	v_rcp_f32_e32 v206, v206
	v_rcp_f32_e32 v207, v207
	v_rcp_f32_e32 v208, v208
	v_rcp_f32_e32 v209, v209
	v_rcp_f32_e32 v210, v210
	v_rcp_f32_e32 v211, v211
	v_rcp_f32_e32 v212, v212
	v_rcp_f32_e32 v213, v213
	v_rcp_f32_e32 v214, v214
	v_rcp_f32_e32 v215, v215
	v_fmamk_f32 v208, v208, 0xc0b8aa3b, v198
	v_fmamk_f32 v209, v209, 0xc0b8aa3b, v198
	v_fmamk_f32 v210, v210, 0xc0b8aa3b, v198
	v_fmamk_f32 v211, v211, 0xc0b8aa3b, v198
	v_mul_f32_e32 v204, v204, v156
	v_mul_f32_e32 v205, v205, v157
	v_mul_f32_e32 v206, v206, v158
	v_mul_f32_e32 v207, v207, v159
	v_fma_f32 v156, v200, v208, v204
	v_fma_f32 v157, v201, v209, v205
	v_fma_f32 v158, v202, v210, v206
	v_fma_f32 v159, v203, v211, v207
	v_exp_f32_e32 v200, v156
	v_exp_f32_e32 v201, v157
	v_exp_f32_e32 v202, v158
	v_exp_f32_e32 v203, v159
	v_add_f32_e32 v200, 1.0, v200
	v_add_f32_e32 v201, 1.0, v201
	v_add_f32_e32 v202, 1.0, v202
	v_add_f32_e32 v203, 1.0, v203
	v_rcp_f32_e32 v200, v200
	v_rcp_f32_e32 v201, v201
	v_rcp_f32_e32 v202, v202
	v_rcp_f32_e32 v203, v203
	v_fma_f32 v200, v200, 2.0, -1.0
	v_fma_f32 v201, v201, 2.0, -1.0
	v_fma_f32 v202, v202, 2.0, -1.0
	v_fma_f32 v203, v203, 2.0, -1.0
	v_mul_f32_e32 v216, v212, v200
	v_mul_f32_e32 v217, v213, v201
	v_mul_f32_e32 v218, v214, v202
	v_mul_f32_e32 v219, v215, v203
	v_mul_f32_e32 v236, v216, v228
	v_mul_f32_e32 v237, v216, v232
	v_fmac_f32_e32 v236, v217, v229
	v_fmac_f32_e32 v237, v217, v233
	v_fmac_f32_e32 v236, v218, v230
	v_fmac_f32_e32 v237, v218, v234
	v_fmac_f32_e32 v236, v219, v231
	v_fmac_f32_e32 v237, v219, v235
	v_mov_b32_e32 v238, v236
	v_mov_b32_e32 v239, v236
	v_mov_b32_e32 v240, v237
	v_mov_b32_e32 v241, v237
	s_nop 1
	v_permlane32_swap_b32_e32 v238, v239
	v_permlane32_swap_b32_e32 v240, v241
	v_add_f32_e32 v238, v238, v239
	v_add_f32_e32 v239, v240, v241
	ds_write_b64 v248, v[238:239] offset:1792
	v_cvt_pk_f16_f32 v226, v216, v217
	v_cvt_pk_f16_f32 v227, v218, v219
	s_nop 1
	v_permlane32_swap_b32_e32 v224, v226
	v_permlane32_swap_b32_e32 v225, v227
	s_cmp_eq_u32 s31, 0
	s_cbranch_scc1 .LD_slow32
	global_store_dwordx4 v195, v[224:227], s[36:37] offset:2048
	s_branch .LD_join33

.LD_join33:
	s_waitcnt vmcnt(1)
	s_waitcnt vmcnt(0)
	s_waitcnt lgkmcnt(0)
	s_barrier
	v_mov_b32_e32 v199, 2
	s_cmp_eq_u32 s31, 0
	s_cbranch_scc1 .LD_slow34
	global_store_dword v197, v199, s[40:41]
	s_branch .LD_join35

.LD_join35:
	ds_read_b64 v[200:201], v249 offset:1024
	ds_read_b64 v[202:203], v249 offset:3072
	ds_read_b64 v[204:205], v249 offset:5120
	ds_read_b64 v[206:207], v249 offset:7168
	s_waitcnt lgkmcnt(0)
	v_add_f32_e32 v200, v200, v202
	v_add_f32_e32 v201, v201, v203
	v_add_f32_e32 v200, v200, v204
	v_add_f32_e32 v201, v201, v205
	v_add_f32_e32 v200, v200, v206
	v_add_f32_e32 v201, v201, v207
	global_store_dwordx2 v250, v[200:201], s[72:73]
	s_waitcnt vmcnt(0) lgkmcnt(0)
	s_endpgm
	.p2align 8

	.amdhsa_kernel _Z12lstm_persistILi0EEvPKDv8_DF16_PhPjS4_PKfS6_S6_PKDv4_DF16_S9_S6_PfSA_i
		.amdhsa_group_segment_fixed_size 0
		.amdhsa_private_segment_fixed_size 0
		.amdhsa_kernarg_size 100
		.amdhsa_user_sgpr_count 2
		.amdhsa_user_sgpr_dispatch_ptr 0
		.amdhsa_user_sgpr_queue_ptr 0
		.amdhsa_user_sgpr_kernarg_segment_ptr 1
		.amdhsa_user_sgpr_dispatch_id 0
		.amdhsa_user_sgpr_kernarg_preload_length 0
		.amdhsa_user_sgpr_kernarg_preload_offset 0
		.amdhsa_user_sgpr_private_segment_size 0
		.amdhsa_uses_dynamic_stack 0
		.amdhsa_enable_private_segment 0
		.amdhsa_system_sgpr_workgroup_id_x 1
		.amdhsa_system_sgpr_workgroup_id_y 0
		.amdhsa_system_sgpr_workgroup_id_z 0
		.amdhsa_system_sgpr_workgroup_info 0
		.amdhsa_system_vgpr_workitem_id 0
		.amdhsa_next_free_vgpr 512
		.amdhsa_next_free_sgpr 80
		.amdhsa_accum_offset 256
		.amdhsa_reserve_vcc 1
		.amdhsa_float_round_mode_32 0
		.amdhsa_float_round_mode_16_64 0
		.amdhsa_float_denorm_mode_32 3
		.amdhsa_float_denorm_mode_16_64 3
		.amdhsa_dx10_clamp 1
		.amdhsa_ieee_mode 1
		.amdhsa_fp16_overflow 0
		.amdhsa_tg_split 0
		.amdhsa_exception_fp_ieee_invalid_op 0
		.amdhsa_exception_fp_denorm_src 0
		.amdhsa_exception_fp_ieee_div_zero 0
		.amdhsa_exception_fp_ieee_overflow 0
		.amdhsa_exception_fp_ieee_underflow 0
		.amdhsa_exception_fp_ieee_inexact 0
		.amdhsa_exception_int_div_zero 0
	.end_amdhsa_kernel

amdhsa.kernels:
  - .agpr_count:     0
    .args:
      - .actual_access:  read_only
        .address_space:  global
        .offset:         0
        .size:           8
        .value_kind:     global_buffer
      - .actual_access:  read_only
        .address_space:  global
        .offset:         8
        .size:           8
        .value_kind:     global_buffer
      - .actual_access:  write_only
        .address_space:  global
        .offset:         16
        .size:           8
        .value_kind:     global_buffer
      - .offset:         24
        .size:           4
        .value_kind:     hidden_block_count_x
      - .offset:         28
        .size:           4
        .value_kind:     hidden_block_count_y
      - .offset:         32
        .size:           4
        .value_kind:     hidden_block_count_z
      - .offset:         36
        .size:           2
        .value_kind:     hidden_group_size_x
      - .offset:         38
        .size:           2
        .value_kind:     hidden_group_size_y
      - .offset:         40
        .size:           2
        .value_kind:     hidden_group_size_z
      - .offset:         42
        .size:           2
        .value_kind:     hidden_remainder_x
      - .offset:         44
        .size:           2
        .value_kind:     hidden_remainder_y
      - .offset:         46
        .size:           2
        .value_kind:     hidden_remainder_z
      - .offset:         64
        .size:           8
        .value_kind:     hidden_global_offset_x
      - .offset:         72
        .size:           8
        .value_kind:     hidden_global_offset_y
      - .offset:         80
        .size:           8
        .value_kind:     hidden_global_offset_z
      - .offset:         88
        .size:           2
        .value_kind:     hidden_grid_dims
    .group_segment_fixed_size: 0
    .kernarg_segment_align: 8
    .kernarg_segment_size: 280
    .language:       OpenCL C
    .language_version:
      - 2
      - 0
    .max_flat_workgroup_size: 1024
    .name:           _Z14seq_out_kernelPKfS0_Pf
    .private_segment_fixed_size: 0
    .sgpr_count:     16
    .sgpr_spill_count: 0
    .symbol:         _Z14seq_out_kernelPKfS0_Pf.kd
    .uniform_work_group_size: 1
    .uses_dynamic_stack: false
    .vgpr_count:     25
    .vgpr_spill_count: 0
    .wavefront_size: 64
  - .agpr_count:     16
    .args:
      - .actual_access:  read_only
        .address_space:  global
        .offset:         0
        .size:           8
        .value_kind:     global_buffer
      - .actual_access:  read_only
        .address_space:  global
        .offset:         8
        .size:           8
        .value_kind:     global_buffer
      - .actual_access:  read_only
        .address_space:  global
        .offset:         16
        .size:           8
        .value_kind:     global_buffer
      - .actual_access:  write_only
        .address_space:  global
        .offset:         24
        .size:           8
        .value_kind:     global_buffer
      - .offset:         32
        .size:           4
        .value_kind:     by_value
      - .offset:         36
        .size:           4
        .value_kind:     by_value
      - .offset:         40
        .size:           4
        .value_kind:     by_value
      - .offset:         48
        .size:           4
        .value_kind:     hidden_block_count_x
      - .offset:         52
        .size:           4
        .value_kind:     hidden_block_count_y
      - .offset:         56
        .size:           4
        .value_kind:     hidden_block_count_z
      - .offset:         60
        .size:           2
        .value_kind:     hidden_group_size_x
      - .offset:         62
        .size:           2
        .value_kind:     hidden_group_size_y
      - .offset:         64
        .size:           2
        .value_kind:     hidden_group_size_z
      - .offset:         66
        .size:           2
        .value_kind:     hidden_remainder_x
      - .offset:         68
        .size:           2
        .value_kind:     hidden_remainder_y
      - .offset:         70
        .size:           2
        .value_kind:     hidden_remainder_z
      - .offset:         88
        .size:           8
        .value_kind:     hidden_global_offset_x
      - .offset:         96
        .size:           8
        .value_kind:     hidden_global_offset_y
      - .offset:         104
        .size:           8
        .value_kind:     hidden_global_offset_z
      - .offset:         112
        .size:           2
        .value_kind:     hidden_grid_dims
    .group_segment_fixed_size: 17408
    .kernarg_segment_align: 8
    .kernarg_segment_size: 304
    .language:       OpenCL C
    .language_version:
      - 2
      - 0
    .max_flat_workgroup_size: 256
    .name:           _Z14gemm_nt_mfma32PKfS0_S0_Pfiii
    .private_segment_fixed_size: 0
    .sgpr_count:     26
    .sgpr_spill_count: 0
    .symbol:         _Z14gemm_nt_mfma32PKfS0_S0_Pfiii.kd
    .uniform_work_group_size: 1
    .uses_dynamic_stack: false
    .vgpr_count:     44
    .vgpr_spill_count: 0
    .wavefront_size: 64
  - .agpr_count:     16
    .args:
      - .actual_access:  read_only
        .address_space:  global
        .offset:         0
        .size:           8
        .value_kind:     global_buffer
      - .actual_access:  read_only
        .address_space:  global
        .offset:         8
        .size:           8
        .value_kind:     global_buffer
      - .actual_access:  read_only
        .address_space:  global
        .offset:         16
        .size:           8
        .value_kind:     global_buffer
      - .actual_access:  write_only
        .address_space:  global
        .offset:         24
        .size:           8
        .value_kind:     global_buffer
      - .actual_access:  write_only
        .address_space:  global
        .offset:         32
        .size:           8
        .value_kind:     global_buffer
    .group_segment_fixed_size: 10880
    .kernarg_segment_align: 8
    .kernarg_segment_size: 40
    .language:       OpenCL C
    .language_version:
      - 2
      - 0
    .max_flat_workgroup_size: 256
    .name:           _Z12pre_d_kernelPKfS0_S0_PDv4_DF16_S2_
    .private_segment_fixed_size: 0
    .sgpr_count:     18
    .sgpr_spill_count: 0
    .symbol:         _Z12pre_d_kernelPKfS0_S0_PDv4_DF16_S2_.kd
    .uniform_work_group_size: 1
    .uses_dynamic_stack: false
    .vgpr_count:     64
    .vgpr_spill_count: 0
    .wavefront_size: 64
  - .agpr_count:     0
    .args:
      - .actual_access:  read_only
        .address_space:  global
        .offset:         0
        .size:           8
        .value_kind:     global_buffer
      - .actual_access:  write_only
        .address_space:  global
        .offset:         8
        .size:           8
        .value_kind:     global_buffer
      - .actual_access:  read_only
        .address_space:  global
        .offset:         16
        .size:           8
        .value_kind:     global_buffer
      - .actual_access:  write_only
        .address_space:  global
        .offset:         24
        .size:           8
        .value_kind:     global_buffer
      - .actual_access:  read_only
        .address_space:  global
        .offset:         32
        .size:           8
        .value_kind:     global_buffer
      - .actual_access:  write_only
        .address_space:  global
        .offset:         40
        .size:           8
        .value_kind:     global_buffer
      - .actual_access:  read_only
        .address_space:  global
        .offset:         48
        .size:           8
        .value_kind:     global_buffer
      - .actual_access:  read_only
        .address_space:  global
        .offset:         56
        .size:           8
        .value_kind:     global_buffer
      - .actual_access:  read_only
        .address_space:  global
        .offset:         64
        .size:           8
        .value_kind:     global_buffer
      - .actual_access:  write_only
        .address_space:  global
        .offset:         72
        .size:           8
        .value_kind:     global_buffer
      - .actual_access:  write_only
        .address_space:  global
        .offset:         80
        .size:           8
        .value_kind:     global_buffer
    .group_segment_fixed_size: 8320
    .kernarg_segment_align: 8
    .kernarg_segment_size: 88
    .language:       OpenCL C
    .language_version:
      - 2
      - 0
    .max_flat_workgroup_size: 256
    .name:           _Z11prep_kernelPKfPDv8_DF16_S0_S2_S0_P15HIP_vector_typeIfLj2EES0_S0_S0_PfPj
    .private_segment_fixed_size: 0
    .sgpr_count:     23
    .sgpr_spill_count: 0
    .symbol:         _Z11prep_kernelPKfPDv8_DF16_S0_S2_S0_P15HIP_vector_typeIfLj2EES0_S0_S0_PfPj.kd
    .uniform_work_group_size: 1
    .uses_dynamic_stack: false
    .vgpr_count:     96
    .vgpr_spill_count: 0
    .wavefront_size: 64
  - .agpr_count:     0
    .args:
      - .actual_access:  read_only
        .address_space:  global
        .offset:         0
        .size:           8
        .value_kind:     global_buffer
      - .actual_access:  read_only
        .address_space:  global
        .offset:         8
        .size:           8
        .value_kind:     global_buffer
      - .actual_access:  write_only
        .address_space:  global
        .offset:         16
        .size:           8
        .value_kind:     global_buffer
      - .offset:         24
        .size:           4
        .value_kind:     hidden_block_count_x
      - .offset:         28
        .size:           4
        .value_kind:     hidden_block_count_y
      - .offset:         32
        .size:           4
        .value_kind:     hidden_block_count_z
      - .offset:         36
        .size:           2
        .value_kind:     hidden_group_size_x
      - .offset:         38
        .size:           2
        .value_kind:     hidden_group_size_y
      - .offset:         40
        .size:           2
        .value_kind:     hidden_group_size_z
      - .offset:         42
        .size:           2
        .value_kind:     hidden_remainder_x
      - .offset:         44
        .size:           2
        .value_kind:     hidden_remainder_y
      - .offset:         46
        .size:           2
        .value_kind:     hidden_remainder_z
      - .offset:         64
        .size:           8
        .value_kind:     hidden_global_offset_x
      - .offset:         72
        .size:           8
        .value_kind:     hidden_global_offset_y
      - .offset:         80
        .size:           8
        .value_kind:     hidden_global_offset_z
      - .offset:         88
        .size:           2
        .value_kind:     hidden_grid_dims
    .group_segment_fixed_size: 0
    .kernarg_segment_align: 8
    .kernarg_segment_size: 280
    .language:       OpenCL C
    .language_version:
      - 2
      - 0
    .max_flat_workgroup_size: 1024
    .name:           _Z12x_out_kernelPKfS0_Pf
    .private_segment_fixed_size: 0
    .sgpr_count:     22
    .sgpr_spill_count: 0
    .symbol:         _Z12x_out_kernelPKfS0_Pf.kd
    .uniform_work_group_size: 1
    .uses_dynamic_stack: false
    .vgpr_count:     66
    .vgpr_spill_count: 0
    .wavefront_size: 64
  - .agpr_count:     256
    .args:
      - .actual_access:  read_only
        .address_space:  global
        .offset:         0
        .size:           8
        .value_kind:     global_buffer
      - .address_space:  global
        .offset:         8
        .size:           8
        .value_kind:     global_buffer
      - .address_space:  global
        .offset:         16
        .size:           8
        .value_kind:     global_buffer
      - .address_space:  global
        .offset:         24
        .size:           8
        .value_kind:     global_buffer
      - .address_space:  global
        .offset:         32
        .size:           8
        .value_kind:     global_buffer
      - .address_space:  global
        .offset:         40
        .size:           8
        .value_kind:     global_buffer
      - .address_space:  global
        .offset:         48
        .size:           8
        .value_kind:     global_buffer
      - .actual_access:  read_only
        .address_space:  global
        .offset:         56
        .size:           8
        .value_kind:     global_buffer
      - .actual_access:  read_only
        .address_space:  global
        .offset:         64
        .size:           8
        .value_kind:     global_buffer
      - .actual_access:  read_only
        .address_space:  global
        .offset:         72
        .size:           8
        .value_kind:     global_buffer
      - .actual_access:  read_only
        .address_space:  global
        .offset:         80
        .size:           8
        .value_kind:     global_buffer
      - .address_space:  global
        .offset:         88
        .size:           8
        .value_kind:     global_buffer
      - .offset:         96
        .size:           4
        .value_kind:     by_value
    .group_segment_fixed_size: 0
    .kernarg_segment_align: 8
    .kernarg_segment_size: 100
    .language:       OpenCL C
    .language_version:
      - 2
      - 0
    .max_flat_workgroup_size: 256
    .name:           _Z12lstm_persistILi1EEvPKDv8_DF16_PhPjS4_PKfS6_S6_PKDv4_DF16_S9_S6_PfSA_i
    .private_segment_fixed_size: 0
    .sgpr_count:     86
    .sgpr_spill_count: 0
    .symbol:         _Z12lstm_persistILi1EEvPKDv8_DF16_PhPjS4_PKfS6_S6_PKDv4_DF16_S9_S6_PfSA_i.kd
    .uniform_work_group_size: 1
    .uses_dynamic_stack: false
    .vgpr_count:     512
    .vgpr_spill_count: 0
    .wavefront_size: 64
  - .agpr_count:     256
    .args:
      - .actual_access:  read_only
        .address_space:  global
        .offset:         0
        .size:           8
        .value_kind:     global_buffer
      - .address_space:  global
        .offset:         8
        .size:           8
        .value_kind:     global_buffer
      - .address_space:  global
        .offset:         16
        .size:           8
        .value_kind:     global_buffer
      - .address_space:  global
        .offset:         24
        .size:           8
        .value_kind:     global_buffer
      - .actual_access:  read_only
        .address_space:  global
        .offset:         32
        .size:           8
        .value_kind:     global_buffer
      - .actual_access:  read_only
        .address_space:  global
        .offset:         40
        .size:           8
        .value_kind:     global_buffer
      - .actual_access:  read_only
        .address_space:  global
        .offset:         48
        .size:           8
        .value_kind:     global_buffer
      - .actual_access:  read_only
        .address_space:  global
        .offset:         56
        .size:           8
        .value_kind:     global_buffer
      - .address_space:  global
        .offset:         64
        .size:           8
        .value_kind:     global_buffer
      - .actual_access:  read_only
        .address_space:  global
        .offset:         72
        .size:           8
        .value_kind:     global_buffer
      - .actual_access:  write_only
        .address_space:  global
        .offset:         80
        .size:           8
        .value_kind:     global_buffer
      - .actual_access:  read_only
        .address_space:  global
        .offset:         88
        .size:           8
        .value_kind:     global_buffer
      - .offset:         96
        .size:           4
        .value_kind:     by_value
    .group_segment_fixed_size: 0
    .kernarg_segment_align: 8
    .kernarg_segment_size: 100
    .language:       OpenCL C
    .language_version:
      - 2
      - 0
    .max_flat_workgroup_size: 256
    .name:           _Z12lstm_persistILi0EEvPKDv8_DF16_PhPjS4_PKfS6_S6_PKDv4_DF16_S9_S6_PfSA_i
    .private_segment_fixed_size: 0
    .sgpr_count:     86
    .sgpr_spill_count: 0
    .symbol:         _Z12lstm_persistILi0EEvPKDv8_DF16_PhPjS4_PKfS6_S6_PKDv4_DF16_S9_S6_PfSA_i.kd
    .uniform_work_group_size: 1
    .uses_dynamic_stack: false
    .vgpr_count:     512
    .vgpr_spill_count: 0
    .wavefront_size: 64
